# Y carry scan: per-stream (b_last,a_max) pairs loaded once and broadcast with v_readlane instead of a dependent global load + vmcnt(0) per step
# speedup vs baseline: 1.0206x; 1.0012x over previous
; __device__ __forceinline__ int cslot(int bh, int c) { return (c + bh) & 31; }
; template <int GRP>
; __device__ __forceinline__ void y_phase(Frame& F, const MW& W) {
;     ...
;         const int bh = base >> 11, g = (base & 2047) + F.tid, e = g >> 4, d8 = (g & 15) * 8;
;         const float* sc = W.SC + (size_t)bh * 64;
;         const size_t off = (size_t)bh * 32 * 16384 + (size_t)e * 128 + d8;
;         u32x2 v[32];
; #pragma unroll
;     ...
;         const bool nsc = (g < 32);
;         f32x4 nv[32];
;         if (nsc) {
; #pragma unroll
;             for (int c = 0; c < 32; ++c) nv[c] = *(const f32x4*)(W.NC + ((size_t)bh * 32 + c) * 128 + g * 4); }
;         float C[8];
; #pragma unroll
;         for (int i = 0; i < 8; ++i) C[i] = 0.f;
;         float m = 0.f;
; #pragma unroll
;         for (int c = 0; c < 32; ++c) {
;             u32x2 o; o.x = pg8::pack_fp8x4(C[0], C[1], C[2], C[3]); o.y = pg8::pack_fp8x4(C[4], C[5], C[6], C[7]); *(u32x2*)(W.CP + off + (size_t)cslot(bh, c) * 16384) = o;
;             const float bl = sc[2 * c], am = sc[2 * c + 1], mn = fmaxf(bl + m, am), dec = __expf(bl + m - mn), inj = __expf(am - mn);
;             const auto x0 = __builtin_amdgcn_cvt_pk_f32_fp8((int)v[c].x, false), x1 = __builtin_amdgcn_cvt_pk_f32_fp8((int)v[c].x, true), x2 = __builtin_amdgcn_cvt_pk_f32_fp8((int)v[c].y, false), x3 = __builtin_amdgcn_cvt_pk_f32_fp8((int)v[c].y, true);
;             C[0] = C[0] * dec + x0[0] * inj; C[1] = C[1] * dec + x0[1] * inj; C[2] = C[2] * dec + x1[0] * inj; C[3] = C[3] * dec + x1[1] * inj;
;             C[4] = C[4] * dec + x2[0] * inj; C[5] = C[5] * dec + x2[1] * inj; C[6] = C[6] * dec + x3[0] * inj; C[7] = C[7] * dec + x3[1] * inj; m = mn; }
.LBB0_364:
	s_or_b64 exec, exec, s[22:23]
	v_mov_b32_e32 v210, v137
	v_cvt_pk_fp8_f32 v210, 0, 0
	v_readlane_b32 vcc_lo, v255, 21
	v_readlane_b32 vcc_hi, v255, 22
	s_lshl_b64 s[22:23], s[24:25], 8
	v_cvt_pk_fp8_f32 v210, 0, 0 op_sel:[0,0,1]
	v_readlane_b32 s25, v255, 19
	v_lshl_add_u64 v[126:127], vcc, 0, v[126:127]
	s_add_u32 s22, s25, s22
	v_readlane_b32 s25, v255, 20
	v_mov_b32_e32 v211, v210
	v_lshl_add_u64 v[212:213], v[126:127], 0, s[70:71]
	s_addc_u32 s23, s25, s23
	global_store_dwordx2 v[212:213], v[210:211], off
	v_and_b32_e32 v254, 31, v194
	v_lshlrev_b32_e32 v254, 3, v254
	global_load_dwordx2 v[252:253], v254, s[22:23]
	global_load_dwordx2 v[210:211], v137, s[22:23]
	s_waitcnt vmcnt(32)
	v_cvt_pk_f32_fp8_sdwa v[218:219], v208 src0_sel:WORD_1
	v_cvt_pk_f32_fp8_e32 v[220:221], v209
	v_mov_b32_e32 v242, v137
	s_waitcnt vmcnt(31)
	v_cvt_pk_f32_fp8_sdwa v[244:245], v206 src0_sel:WORD_1
	v_cvt_pk_f32_fp8_e32 v[246:247], v207
	v_cvt_pk_f32_fp8_sdwa v[248:249], v207 src0_sel:WORD_1
	s_add_i32 s13, s13, 0x7c000
	s_and_b32 s70, s13, 0x7c000
	s_waitcnt vmcnt(0)
	v_add_f32_e32 v1, 0, v210
	v_max_f32_e32 v195, v211, v211
	v_max_f32_e32 v195, v1, v195
	v_sub_f32_e32 v1, v1, v195
	v_mul_f32_e32 v1, 0x3fb8aa3b, v1
	v_exp_f32_e32 v240, v1
	v_sub_f32_e32 v1, v211, v195
	v_mul_f32_e32 v1, 0x3fb8aa3b, v1
	v_cvt_pk_f32_fp8_e32 v[210:211], v208
	v_cvt_pk_f32_fp8_sdwa v[208:209], v209 src0_sel:WORD_1
	v_exp_f32_e32 v241, v1
	v_mov_b32_e32 v243, v208
	v_pk_mul_f32 v[216:217], v[240:241], v[242:243]
	s_nop 0
	v_fma_f32 v214, v210, v241, v216
	v_fma_f32 v212, v211, v241, v216
	v_fma_f32 v210, v218, v241, v216
	v_fma_f32 v208, v219, v241, v216
	v_fma_f32 v222, v241, v220, v216
	v_fma_f32 v220, v241, v221, v216
	v_pk_fma_f32 v[218:219], v[240:241], v[242:243], v[216:217] op_sel:[0,0,1] op_sel_hi:[1,1,0]
	v_fmac_f32_e32 v216, v241, v209
	v_med3_f32 v1, v214, s17, v231
	v_med3_f32 v209, v212, s17, v231
	v_mov_b32_e32 v240, v137
	v_cvt_pk_fp8_f32 v240, v1, v209
	v_med3_f32 v1, v222, s17, v231
	v_med3_f32 v209, v220, s17, v231
	v_mov_b32_e32 v241, v137
	v_cvt_pk_fp8_f32 v241, v1, v209
	v_med3_f32 v211, v210, s17, v231
	v_med3_f32 v213, v208, s17, v231
	v_cvt_pk_fp8_f32 v240, v211, v213 op_sel:[0,0,1]
	v_med3_f32 v211, v218, s17, v231
	v_med3_f32 v213, v216, s17, v231
	v_cvt_pk_fp8_f32 v241, v211, v213 op_sel:[0,0,1]
	v_lshl_add_u64 v[242:243], v[126:127], 0, s[52:53]
	v_mov_b32_e32 v211, v244
	v_mov_b32_e32 v209, v245
	global_store_dwordx2 v[242:243], v[240:241], off
	v_readlane_b32 s100, v252, 1
	s_nop 1
	v_mov_b32_e32 v240, s100
	v_readlane_b32 s100, v253, 1
	s_nop 1
	v_mov_b32_e32 v241, s100
	v_cvt_pk_f32_fp8_e32 v[242:243], v206
	v_mov_b32_e32 v215, v242
	v_mov_b32_e32 v213, v243
	v_add_f32_e32 v1, v195, v240
	v_max_f32_e32 v195, v241, v241
	v_max_f32_e32 v195, v1, v195
	v_sub_f32_e32 v1, v1, v195
	v_mul_f32_e32 v1, 0x3fb8aa3b, v1
	v_exp_f32_e32 v240, v1
	v_sub_f32_e32 v1, v241, v195
	v_mul_f32_e32 v1, 0x3fb8aa3b, v1
	v_exp_f32_e32 v241, v1
	s_nop 0
	v_mul_f32_e32 v206, v242, v241
	v_pk_fma_f32 v[214:215], v[214:215], v[240:241], v[206:207] op_sel_hi:[1,1,0]
	v_mul_f32_e32 v206, v243, v241
	v_pk_fma_f32 v[212:213], v[212:213], v[240:241], v[206:207] op_sel_hi:[1,1,0]
	v_mul_f32_e32 v206, v244, v241
	v_pk_fma_f32 v[210:211], v[210:211], v[240:241], v[206:207] op_sel_hi:[1,1,0]
	v_mul_f32_e32 v206, v245, v241
	v_pk_fma_f32 v[208:209], v[208:209], v[240:241], v[206:207] op_sel_hi:[1,1,0]
	v_mov_b32_e32 v223, v241
	v_mov_b32_e32 v206, v240
	v_mov_b32_e32 v207, v246
	v_mul_f32_e32 v242, v241, v246
	v_pk_fma_f32 v[206:207], v[222:223], v[206:207], v[242:243] op_sel_hi:[1,1,0]
	v_mov_b32_e32 v221, v241
	v_mov_b32_e32 v246, v240
	v_mul_f32_e32 v222, v241, v247
	v_pk_fma_f32 v[220:221], v[220:221], v[246:247], v[222:223] op_sel_hi:[1,1,0]
	v_mov_b32_e32 v219, v241
	v_mov_b32_e32 v222, v240
	v_mov_b32_e32 v223, v248
	v_mul_f32_e32 v242, v241, v248
	v_pk_fma_f32 v[218:219], v[218:219], v[222:223], v[242:243] op_sel_hi:[1,1,0]
	v_mov_b32_e32 v217, v241
	v_mov_b32_e32 v248, v240
	v_mul_f32_e32 v222, v241, v249
	v_pk_fma_f32 v[216:217], v[216:217], v[248:249], v[222:223] op_sel_hi:[1,1,0]
	v_med3_f32 v1, v214, s17, v231
	v_med3_f32 v207, v212, s17, v231
	v_mov_b32_e32 v222, v137
	v_cvt_pk_fp8_f32 v222, v1, v207
	v_med3_f32 v1, v206, s17, v231
	v_med3_f32 v207, v220, s17, v231
	v_mov_b32_e32 v223, v137
	v_cvt_pk_fp8_f32 v223, v1, v207
	v_med3_f32 v209, v210, s17, v231
	v_med3_f32 v211, v208, s17, v231
	v_cvt_pk_fp8_f32 v222, v209, v211 op_sel:[0,0,1]
	v_med3_f32 v209, v218, s17, v231
	v_med3_f32 v211, v216, s17, v231
	v_cvt_pk_fp8_f32 v223, v209, v211 op_sel:[0,0,1]
	v_lshl_add_u64 v[240:241], v[126:127], 0, s[68:69]
	v_cvt_pk_f32_fp8_sdwa v[242:243], v204 src0_sel:WORD_1
	v_cvt_pk_f32_fp8_e32 v[244:245], v205
	global_store_dwordx2 v[240:241], v[222:223], off
	v_readlane_b32 s100, v252, 2
	s_nop 1
	v_mov_b32_e32 v222, s100
	v_readlane_b32 s100, v253, 2
	s_nop 1
	v_mov_b32_e32 v223, s100
	v_cvt_pk_f32_fp8_e32 v[240:241], v204
	v_cvt_pk_f32_fp8_sdwa v[246:247], v205 src0_sel:WORD_1
	v_mov_b32_e32 v211, v242
	v_mov_b32_e32 v209, v243
	v_mov_b32_e32 v215, v240
	v_mov_b32_e32 v213, v241
	v_add_f32_e32 v1, v195, v222
	v_max_f32_e32 v195, v223, v223
	v_max_f32_e32 v195, v1, v195
	v_sub_f32_e32 v1, v1, v195
	v_mul_f32_e32 v1, 0x3fb8aa3b, v1
	v_exp_f32_e32 v222, v1
	v_sub_f32_e32 v1, v223, v195
	v_mul_f32_e32 v1, 0x3fb8aa3b, v1
	v_exp_f32_e32 v223, v1
	s_nop 0
	v_mul_f32_e32 v204, v240, v223
	v_pk_fma_f32 v[214:215], v[214:215], v[222:223], v[204:205] op_sel_hi:[1,1,0]
	v_mul_f32_e32 v204, v241, v223
	v_pk_fma_f32 v[212:213], v[212:213], v[222:223], v[204:205] op_sel_hi:[1,1,0]
; __device__ __forceinline__ int cslot(int bh, int c) { return (c + bh) & 31; }
; template <int GRP>
; __device__ __forceinline__ void y_phase(Frame& F, const MW& W) {
;     ...
;         for (int c = 0; c < 32; ++c) {
;             u32x2 o; o.x = pg8::pack_fp8x4(C[0], C[1], C[2], C[3]); o.y = pg8::pack_fp8x4(C[4], C[5], C[6], C[7]); *(u32x2*)(W.CP + off + (size_t)cslot(bh, c) * 16384) = o;
;             const float bl = sc[2 * c], am = sc[2 * c + 1], mn = fmaxf(bl + m, am), dec = __expf(bl + m - mn), inj = __expf(am - mn);
;             const auto x0 = __builtin_amdgcn_cvt_pk_f32_fp8((int)v[c].x, false), x1 = __builtin_amdgcn_cvt_pk_f32_fp8((int)v[c].x, true), x2 = __builtin_amdgcn_cvt_pk_f32_fp8((int)v[c].y, false), x3 = __builtin_amdgcn_cvt_pk_f32_fp8((int)v[c].y, true);
;             C[0] = C[0] * dec + x0[0] * inj; C[1] = C[1] * dec + x0[1] * inj; C[2] = C[2] * dec + x1[0] * inj; C[3] = C[3] * dec + x1[1] * inj;
;             C[4] = C[4] * dec + x2[0] * inj; C[5] = C[5] * dec + x2[1] * inj; C[6] = C[6] * dec + x3[0] * inj; C[7] = C[7] * dec + x3[1] * inj; m = mn; }
	v_mul_f32_e32 v204, v242, v223
	v_pk_fma_f32 v[210:211], v[210:211], v[222:223], v[204:205] op_sel_hi:[1,1,0]
	v_mul_f32_e32 v204, v243, v223
	v_pk_fma_f32 v[208:209], v[208:209], v[222:223], v[204:205] op_sel_hi:[1,1,0]
	v_mov_b32_e32 v207, v223
	v_mov_b32_e32 v204, v222
	v_mov_b32_e32 v205, v244
	v_mul_f32_e32 v240, v223, v244
	v_pk_fma_f32 v[206:207], v[206:207], v[204:205], v[240:241] op_sel_hi:[1,1,0]
	v_mov_b32_e32 v221, v223
	v_mov_b32_e32 v244, v222
	v_mul_f32_e32 v204, v223, v245
	v_pk_fma_f32 v[204:205], v[220:221], v[244:245], v[204:205] op_sel_hi:[1,1,0]
	v_mov_b32_e32 v219, v223
	v_mov_b32_e32 v220, v222
	v_mov_b32_e32 v221, v246
	v_mul_f32_e32 v240, v223, v246
	v_pk_fma_f32 v[218:219], v[218:219], v[220:221], v[240:241] op_sel_hi:[1,1,0]
	v_mov_b32_e32 v217, v223
	v_mov_b32_e32 v246, v222
	v_mul_f32_e32 v220, v223, v247
	v_pk_fma_f32 v[216:217], v[216:217], v[246:247], v[220:221] op_sel_hi:[1,1,0]
	v_med3_f32 v1, v214, s17, v231
	v_med3_f32 v205, v212, s17, v231
	v_mov_b32_e32 v220, v137
	v_cvt_pk_fp8_f32 v220, v1, v205
	v_med3_f32 v1, v206, s17, v231
	v_med3_f32 v205, v204, s17, v231
	v_mov_b32_e32 v221, v137
	v_cvt_pk_fp8_f32 v221, v1, v205
	v_med3_f32 v207, v210, s17, v231
	v_med3_f32 v209, v208, s17, v231
	v_cvt_pk_fp8_f32 v220, v207, v209 op_sel:[0,0,1]
	v_med3_f32 v207, v218, s17, v231
	v_med3_f32 v209, v216, s17, v231
	v_cvt_pk_fp8_f32 v221, v207, v209 op_sel:[0,0,1]
	v_lshl_add_u64 v[222:223], v[126:127], 0, s[54:55]
	v_cvt_pk_f32_fp8_sdwa v[240:241], v202 src0_sel:WORD_1
	v_cvt_pk_f32_fp8_e32 v[242:243], v203
	global_store_dwordx2 v[222:223], v[220:221], off
	v_readlane_b32 s100, v252, 3
	s_nop 1
	v_mov_b32_e32 v220, s100
	v_readlane_b32 s100, v253, 3
	s_nop 1
	v_mov_b32_e32 v221, s100
	v_cvt_pk_f32_fp8_e32 v[222:223], v202
	v_cvt_pk_f32_fp8_sdwa v[244:245], v203 src0_sel:WORD_1
	v_mov_b32_e32 v211, v240
	v_mov_b32_e32 v209, v241
	v_mov_b32_e32 v215, v222
	v_mov_b32_e32 v213, v223
	v_add_f32_e32 v1, v195, v220
	v_max_f32_e32 v195, v221, v221
	v_max_f32_e32 v195, v1, v195
	v_sub_f32_e32 v1, v1, v195
	v_mul_f32_e32 v1, 0x3fb8aa3b, v1
	v_exp_f32_e32 v220, v1
	v_sub_f32_e32 v1, v221, v195
	v_mul_f32_e32 v1, 0x3fb8aa3b, v1
	v_exp_f32_e32 v221, v1
	s_nop 0
	v_mul_f32_e32 v202, v222, v221
	v_pk_fma_f32 v[214:215], v[214:215], v[220:221], v[202:203] op_sel_hi:[1,1,0]
	v_mul_f32_e32 v202, v223, v221
	v_pk_fma_f32 v[212:213], v[212:213], v[220:221], v[202:203] op_sel_hi:[1,1,0]
	v_mul_f32_e32 v202, v240, v221
	v_pk_fma_f32 v[210:211], v[210:211], v[220:221], v[202:203] op_sel_hi:[1,1,0]
	v_mul_f32_e32 v202, v241, v221
	v_pk_fma_f32 v[208:209], v[208:209], v[220:221], v[202:203] op_sel_hi:[1,1,0]
	v_mov_b32_e32 v207, v221
	v_mov_b32_e32 v202, v220
	v_mov_b32_e32 v203, v242
	v_mul_f32_e32 v222, v221, v242
	v_pk_fma_f32 v[206:207], v[206:207], v[202:203], v[222:223] op_sel_hi:[1,1,0]
	v_mov_b32_e32 v205, v221
	v_mov_b32_e32 v242, v220
	v_mul_f32_e32 v202, v221, v243
	v_pk_fma_f32 v[204:205], v[204:205], v[242:243], v[202:203] op_sel_hi:[1,1,0]
	v_mov_b32_e32 v219, v221
	v_mov_b32_e32 v202, v220
	v_mov_b32_e32 v203, v244
	v_mul_f32_e32 v222, v221, v244
	v_pk_fma_f32 v[202:203], v[218:219], v[202:203], v[222:223] op_sel_hi:[1,1,0]
	v_mov_b32_e32 v217, v221
	v_mov_b32_e32 v244, v220
	v_mul_f32_e32 v218, v221, v245
	v_pk_fma_f32 v[216:217], v[216:217], v[244:245], v[218:219] op_sel_hi:[1,1,0]
	v_med3_f32 v1, v214, s17, v231
	v_med3_f32 v203, v212, s17, v231
	v_mov_b32_e32 v218, v137
	v_cvt_pk_fp8_f32 v218, v1, v203
	v_med3_f32 v1, v206, s17, v231
	v_med3_f32 v203, v204, s17, v231
	v_mov_b32_e32 v219, v137
	v_cvt_pk_fp8_f32 v219, v1, v203
	v_med3_f32 v205, v210, s17, v231
	v_med3_f32 v207, v208, s17, v231
	v_cvt_pk_fp8_f32 v218, v205, v207 op_sel:[0,0,1]
	v_med3_f32 v205, v202, s17, v231
	v_med3_f32 v207, v216, s17, v231
	v_cvt_pk_fp8_f32 v219, v205, v207 op_sel:[0,0,1]
	v_lshl_add_u64 v[220:221], v[126:127], 0, s[14:15]
	v_cvt_pk_f32_fp8_sdwa v[222:223], v200 src0_sel:WORD_1
	v_cvt_pk_f32_fp8_e32 v[240:241], v201
	global_store_dwordx2 v[220:221], v[218:219], off
	v_readlane_b32 s100, v252, 4
	s_nop 1
	v_mov_b32_e32 v218, s100
	v_readlane_b32 s100, v253, 4
	s_nop 1
	v_mov_b32_e32 v219, s100
	v_cvt_pk_f32_fp8_e32 v[220:221], v200
	v_cvt_pk_f32_fp8_sdwa v[200:201], v201 src0_sel:WORD_1
	v_mov_b32_e32 v211, v222
	v_mov_b32_e32 v209, v223
	v_mov_b32_e32 v215, v220
	v_mov_b32_e32 v213, v221
	v_add_f32_e32 v1, v195, v218
	v_max_f32_e32 v195, v219, v219
	v_max_f32_e32 v195, v1, v195
	v_sub_f32_e32 v1, v1, v195
	v_mul_f32_e32 v1, 0x3fb8aa3b, v1
	v_exp_f32_e32 v218, v1
	v_sub_f32_e32 v1, v219, v195
	v_mul_f32_e32 v1, 0x3fb8aa3b, v1
	v_exp_f32_e32 v219, v1
	s_nop 0
	v_mul_f32_e32 v220, v220, v219
	v_pk_fma_f32 v[214:215], v[214:215], v[218:219], v[220:221] op_sel_hi:[1,1,0]
	v_mul_f32_e32 v220, v221, v219
	v_pk_fma_f32 v[212:213], v[212:213], v[218:219], v[220:221] op_sel_hi:[1,1,0]
	v_mul_f32_e32 v220, v222, v219
	v_pk_fma_f32 v[210:211], v[210:211], v[218:219], v[220:221] op_sel_hi:[1,1,0]
	v_mul_f32_e32 v220, v223, v219
	v_pk_fma_f32 v[208:209], v[208:209], v[218:219], v[220:221] op_sel_hi:[1,1,0]
	v_mov_b32_e32 v207, v219
	v_mov_b32_e32 v220, v218
	v_mov_b32_e32 v221, v240
	v_mul_f32_e32 v222, v219, v240
	v_pk_fma_f32 v[206:207], v[206:207], v[220:221], v[222:223] op_sel_hi:[1,1,0]
	v_mov_b32_e32 v205, v219
	v_mov_b32_e32 v240, v218
	v_mul_f32_e32 v220, v219, v241
	v_pk_fma_f32 v[204:205], v[204:205], v[240:241], v[220:221] op_sel_hi:[1,1,0]
	v_mov_b32_e32 v203, v219
	v_mov_b32_e32 v220, v218
	v_mov_b32_e32 v221, v200
	v_mul_f32_e32 v200, v219, v200
	v_pk_fma_f32 v[202:203], v[202:203], v[220:221], v[200:201] op_sel_hi:[1,1,0]
; __device__ __forceinline__ int cslot(int bh, int c) { return (c + bh) & 31; }
; template <int GRP>
; __device__ __forceinline__ void y_phase(Frame& F, const MW& W) {
;     ...
;         for (int c = 0; c < 32; ++c) {
;             u32x2 o; o.x = pg8::pack_fp8x4(C[0], C[1], C[2], C[3]); o.y = pg8::pack_fp8x4(C[4], C[5], C[6], C[7]); *(u32x2*)(W.CP + off + (size_t)cslot(bh, c) * 16384) = o;
;             const float bl = sc[2 * c], am = sc[2 * c + 1], mn = fmaxf(bl + m, am), dec = __expf(bl + m - mn), inj = __expf(am - mn);
;             const auto x0 = __builtin_amdgcn_cvt_pk_f32_fp8((int)v[c].x, false), x1 = __builtin_amdgcn_cvt_pk_f32_fp8((int)v[c].x, true), x2 = __builtin_amdgcn_cvt_pk_f32_fp8((int)v[c].y, false), x3 = __builtin_amdgcn_cvt_pk_f32_fp8((int)v[c].y, true);
;             C[0] = C[0] * dec + x0[0] * inj; C[1] = C[1] * dec + x0[1] * inj; C[2] = C[2] * dec + x1[0] * inj; C[3] = C[3] * dec + x1[1] * inj;
;             C[4] = C[4] * dec + x2[0] * inj; C[5] = C[5] * dec + x2[1] * inj; C[6] = C[6] * dec + x3[0] * inj; C[7] = C[7] * dec + x3[1] * inj; m = mn; }
	v_mov_b32_e32 v217, v219
	v_mov_b32_e32 v200, v218
	v_mul_f32_e32 v218, v219, v201
	v_pk_fma_f32 v[200:201], v[216:217], v[200:201], v[218:219] op_sel_hi:[1,1,0]
	v_med3_f32 v1, v214, s17, v231
	v_med3_f32 v201, v212, s17, v231
	v_mov_b32_e32 v216, v137
	v_cvt_pk_fp8_f32 v216, v1, v201
	v_med3_f32 v1, v206, s17, v231
	v_med3_f32 v201, v204, s17, v231
	v_mov_b32_e32 v217, v137
	v_cvt_pk_fp8_f32 v217, v1, v201
	v_med3_f32 v203, v210, s17, v231
	v_med3_f32 v205, v208, s17, v231
	v_cvt_pk_fp8_f32 v216, v203, v205 op_sel:[0,0,1]
	v_med3_f32 v203, v202, s17, v231
	v_med3_f32 v205, v200, s17, v231
	v_cvt_pk_fp8_f32 v217, v203, v205 op_sel:[0,0,1]
	v_lshl_add_u64 v[218:219], v[126:127], 0, s[62:63]
	v_cvt_pk_f32_fp8_sdwa v[220:221], v198 src0_sel:WORD_1
	v_cvt_pk_f32_fp8_e32 v[222:223], v199
	global_store_dwordx2 v[218:219], v[216:217], off
	v_readlane_b32 s100, v252, 5
	s_nop 1
	v_mov_b32_e32 v216, s100
	v_readlane_b32 s100, v253, 5
	s_nop 1
	v_mov_b32_e32 v217, s100
	v_cvt_pk_f32_fp8_e32 v[218:219], v198
	v_cvt_pk_f32_fp8_sdwa v[240:241], v199 src0_sel:WORD_1
	v_mov_b32_e32 v211, v220
	v_mov_b32_e32 v209, v221
	v_mov_b32_e32 v215, v218
	v_mov_b32_e32 v213, v219
	v_add_f32_e32 v1, v195, v216
	v_max_f32_e32 v195, v217, v217
	v_max_f32_e32 v195, v1, v195
	v_sub_f32_e32 v1, v1, v195
	v_mul_f32_e32 v1, 0x3fb8aa3b, v1
	v_exp_f32_e32 v216, v1
	v_sub_f32_e32 v1, v217, v195
	v_mul_f32_e32 v1, 0x3fb8aa3b, v1
	v_exp_f32_e32 v217, v1
	s_nop 0
	v_mul_f32_e32 v198, v218, v217
	v_pk_fma_f32 v[198:199], v[214:215], v[216:217], v[198:199] op_sel_hi:[1,1,0]
	v_mul_f32_e32 v214, v219, v217
	v_pk_fma_f32 v[212:213], v[212:213], v[216:217], v[214:215] op_sel_hi:[1,1,0]
	v_mul_f32_e32 v214, v220, v217
	v_pk_fma_f32 v[210:211], v[210:211], v[216:217], v[214:215] op_sel_hi:[1,1,0]
	v_mul_f32_e32 v214, v221, v217
	v_pk_fma_f32 v[208:209], v[208:209], v[216:217], v[214:215] op_sel_hi:[1,1,0]
	v_mov_b32_e32 v207, v217
	v_mov_b32_e32 v214, v216
	v_mov_b32_e32 v215, v222
	v_mul_f32_e32 v218, v217, v222
	v_pk_fma_f32 v[206:207], v[206:207], v[214:215], v[218:219] op_sel_hi:[1,1,0]
	v_mov_b32_e32 v205, v217
	v_mov_b32_e32 v222, v216
	v_mul_f32_e32 v214, v217, v223
	v_pk_fma_f32 v[204:205], v[204:205], v[222:223], v[214:215] op_sel_hi:[1,1,0]
	v_mov_b32_e32 v203, v217
	v_mov_b32_e32 v214, v216
	v_mov_b32_e32 v215, v240
	v_mul_f32_e32 v218, v217, v240
	v_pk_fma_f32 v[202:203], v[202:203], v[214:215], v[218:219] op_sel_hi:[1,1,0]
	v_mov_b32_e32 v201, v217
	v_mov_b32_e32 v240, v216
	v_mul_f32_e32 v214, v217, v241
	v_pk_fma_f32 v[200:201], v[200:201], v[240:241], v[214:215] op_sel_hi:[1,1,0]
	v_med3_f32 v1, v198, s17, v231
	v_med3_f32 v199, v212, s17, v231
	v_mov_b32_e32 v214, v137
	v_cvt_pk_fp8_f32 v214, v1, v199
	v_med3_f32 v1, v206, s17, v231
	v_med3_f32 v199, v204, s17, v231
	v_mov_b32_e32 v215, v137
	v_cvt_pk_fp8_f32 v215, v1, v199
	v_med3_f32 v201, v210, s17, v231
	v_med3_f32 v203, v208, s17, v231
	v_cvt_pk_fp8_f32 v214, v201, v203 op_sel:[0,0,1]
	v_med3_f32 v201, v202, s17, v231
	v_med3_f32 v203, v200, s17, v231
	v_cvt_pk_fp8_f32 v215, v201, v203 op_sel:[0,0,1]
	v_lshl_add_u64 v[216:217], v[126:127], 0, s[72:73]
	v_cvt_pk_f32_fp8_sdwa v[218:219], v196 src0_sel:WORD_1
	v_cvt_pk_f32_fp8_e32 v[220:221], v197
	global_store_dwordx2 v[216:217], v[214:215], off
	v_readlane_b32 s100, v252, 6
	s_nop 1
	v_mov_b32_e32 v214, s100
	v_readlane_b32 s100, v253, 6
	s_nop 1
	v_mov_b32_e32 v215, s100
	v_cvt_pk_f32_fp8_e32 v[216:217], v196
	v_cvt_pk_f32_fp8_sdwa v[222:223], v197 src0_sel:WORD_1
	v_mov_b32_e32 v211, v218
	v_mov_b32_e32 v209, v219
	v_mov_b32_e32 v199, v216
	v_mov_b32_e32 v213, v217
	v_add_f32_e32 v1, v195, v214
	v_max_f32_e32 v195, v215, v215
	v_max_f32_e32 v195, v1, v195
	v_sub_f32_e32 v1, v1, v195
	v_mul_f32_e32 v1, 0x3fb8aa3b, v1
	v_exp_f32_e32 v214, v1
	v_sub_f32_e32 v1, v215, v195
	v_mul_f32_e32 v1, 0x3fb8aa3b, v1
	v_exp_f32_e32 v215, v1
	s_nop 0
	v_mul_f32_e32 v196, v216, v215
	v_pk_fma_f32 v[198:199], v[198:199], v[214:215], v[196:197] op_sel_hi:[1,1,0]
	v_mul_f32_e32 v196, v217, v215
	v_pk_fma_f32 v[196:197], v[212:213], v[214:215], v[196:197] op_sel_hi:[1,1,0]
	v_mul_f32_e32 v212, v218, v215
	v_pk_fma_f32 v[210:211], v[210:211], v[214:215], v[212:213] op_sel_hi:[1,1,0]
	v_mul_f32_e32 v212, v219, v215
	v_pk_fma_f32 v[208:209], v[208:209], v[214:215], v[212:213] op_sel_hi:[1,1,0]
	v_mov_b32_e32 v207, v215
	v_mov_b32_e32 v212, v214
	v_mov_b32_e32 v213, v220
	v_mul_f32_e32 v216, v215, v220
	v_pk_fma_f32 v[206:207], v[206:207], v[212:213], v[216:217] op_sel_hi:[1,1,0]
	v_mov_b32_e32 v205, v215
	v_mov_b32_e32 v220, v214
	v_mul_f32_e32 v212, v215, v221
	v_pk_fma_f32 v[204:205], v[204:205], v[220:221], v[212:213] op_sel_hi:[1,1,0]
	v_mov_b32_e32 v203, v215
	v_mov_b32_e32 v212, v214
	v_mov_b32_e32 v213, v222
	v_mul_f32_e32 v216, v215, v222
	v_pk_fma_f32 v[202:203], v[202:203], v[212:213], v[216:217] op_sel_hi:[1,1,0]
	v_mov_b32_e32 v201, v215
	v_mov_b32_e32 v222, v214
	v_mul_f32_e32 v212, v215, v223
	v_pk_fma_f32 v[200:201], v[200:201], v[222:223], v[212:213] op_sel_hi:[1,1,0]
	v_med3_f32 v1, v198, s17, v231
	v_med3_f32 v197, v196, s17, v231
	v_mov_b32_e32 v212, v137
	v_cvt_pk_fp8_f32 v212, v1, v197
	v_med3_f32 v1, v206, s17, v231
	v_med3_f32 v197, v204, s17, v231
	v_mov_b32_e32 v213, v137
	v_cvt_pk_fp8_f32 v213, v1, v197
	v_med3_f32 v199, v210, s17, v231
	v_med3_f32 v201, v208, s17, v231
	v_cvt_pk_fp8_f32 v212, v199, v201 op_sel:[0,0,1]
	v_med3_f32 v199, v202, s17, v231
	v_med3_f32 v201, v200, s17, v231
	v_cvt_pk_fp8_f32 v213, v199, v201 op_sel:[0,0,1]
	v_lshl_add_u64 v[214:215], v[126:127], 0, s[0:1]
	v_cvt_pk_f32_fp8_sdwa v[216:217], v192 src0_sel:WORD_1
; __device__ __forceinline__ int cslot(int bh, int c) { return (c + bh) & 31; }
; template <int GRP>
; __device__ __forceinline__ void y_phase(Frame& F, const MW& W) {
;     ...
;         for (int c = 0; c < 32; ++c) {
;             u32x2 o; o.x = pg8::pack_fp8x4(C[0], C[1], C[2], C[3]); o.y = pg8::pack_fp8x4(C[4], C[5], C[6], C[7]); *(u32x2*)(W.CP + off + (size_t)cslot(bh, c) * 16384) = o;
;             const float bl = sc[2 * c], am = sc[2 * c + 1], mn = fmaxf(bl + m, am), dec = __expf(bl + m - mn), inj = __expf(am - mn);
;             const auto x0 = __builtin_amdgcn_cvt_pk_f32_fp8((int)v[c].x, false), x1 = __builtin_amdgcn_cvt_pk_f32_fp8((int)v[c].x, true), x2 = __builtin_amdgcn_cvt_pk_f32_fp8((int)v[c].y, false), x3 = __builtin_amdgcn_cvt_pk_f32_fp8((int)v[c].y, true);
;             C[0] = C[0] * dec + x0[0] * inj; C[1] = C[1] * dec + x0[1] * inj; C[2] = C[2] * dec + x1[0] * inj; C[3] = C[3] * dec + x1[1] * inj;
;             C[4] = C[4] * dec + x2[0] * inj; C[5] = C[5] * dec + x2[1] * inj; C[6] = C[6] * dec + x3[0] * inj; C[7] = C[7] * dec + x3[1] * inj; m = mn; }
	v_cvt_pk_f32_fp8_e32 v[218:219], v193
	global_store_dwordx2 v[214:215], v[212:213], off
	v_readlane_b32 s100, v252, 7
	s_nop 1
	v_mov_b32_e32 v212, s100
	v_readlane_b32 s100, v253, 7
	s_nop 1
	v_mov_b32_e32 v213, s100
	v_cvt_pk_f32_fp8_e32 v[214:215], v192
	v_cvt_pk_f32_fp8_sdwa v[220:221], v193 src0_sel:WORD_1
	v_mov_b32_e32 v211, v216
	v_mov_b32_e32 v209, v217
	v_mov_b32_e32 v199, v214
	v_mov_b32_e32 v197, v215
	v_add_f32_e32 v1, v195, v212
	v_max_f32_e32 v195, v213, v213
	v_max_f32_e32 v195, v1, v195
	v_sub_f32_e32 v1, v1, v195
	v_mul_f32_e32 v1, 0x3fb8aa3b, v1
	v_exp_f32_e32 v212, v1
	v_sub_f32_e32 v1, v213, v195
	v_mul_f32_e32 v1, 0x3fb8aa3b, v1
	v_exp_f32_e32 v213, v1
	s_nop 0
	v_mul_f32_e32 v192, v214, v213
	v_pk_fma_f32 v[198:199], v[198:199], v[212:213], v[192:193] op_sel_hi:[1,1,0]
	v_mul_f32_e32 v192, v215, v213
	v_pk_fma_f32 v[196:197], v[196:197], v[212:213], v[192:193] op_sel_hi:[1,1,0]
	v_mul_f32_e32 v192, v216, v213
	v_pk_fma_f32 v[192:193], v[210:211], v[212:213], v[192:193] op_sel_hi:[1,1,0]
	v_mul_f32_e32 v210, v217, v213
	v_pk_fma_f32 v[208:209], v[208:209], v[212:213], v[210:211] op_sel_hi:[1,1,0]
	v_mov_b32_e32 v207, v213
	v_mov_b32_e32 v210, v212
	v_mov_b32_e32 v211, v218
	v_mul_f32_e32 v214, v213, v218
	v_pk_fma_f32 v[206:207], v[206:207], v[210:211], v[214:215] op_sel_hi:[1,1,0]
	v_mov_b32_e32 v205, v213
	v_mov_b32_e32 v218, v212
	v_mul_f32_e32 v210, v213, v219
	v_pk_fma_f32 v[204:205], v[204:205], v[218:219], v[210:211] op_sel_hi:[1,1,0]
	v_mov_b32_e32 v203, v213
	v_mov_b32_e32 v210, v212
	v_mov_b32_e32 v211, v220
	v_mul_f32_e32 v214, v213, v220
	v_pk_fma_f32 v[202:203], v[202:203], v[210:211], v[214:215] op_sel_hi:[1,1,0]
	v_mov_b32_e32 v201, v213
	v_mov_b32_e32 v220, v212
	v_mul_f32_e32 v210, v213, v221
	v_pk_fma_f32 v[200:201], v[200:201], v[220:221], v[210:211] op_sel_hi:[1,1,0]
	v_med3_f32 v1, v198, s17, v231
	v_med3_f32 v193, v196, s17, v231
	v_mov_b32_e32 v210, v137
	v_cvt_pk_fp8_f32 v210, v1, v193
	v_med3_f32 v1, v206, s17, v231
	v_med3_f32 v193, v204, s17, v231
	v_mov_b32_e32 v211, v137
	v_cvt_pk_fp8_f32 v211, v1, v193
	v_med3_f32 v197, v192, s17, v231
	v_med3_f32 v199, v208, s17, v231
	v_cvt_pk_fp8_f32 v210, v197, v199 op_sel:[0,0,1]
	v_med3_f32 v197, v202, s17, v231
	v_med3_f32 v199, v200, s17, v231
	v_cvt_pk_fp8_f32 v211, v197, v199 op_sel:[0,0,1]
	v_lshl_add_u64 v[212:213], v[126:127], 0, s[74:75]
	v_cvt_pk_f32_fp8_sdwa v[214:215], v190 src0_sel:WORD_1
	v_cvt_pk_f32_fp8_e32 v[216:217], v191
	global_store_dwordx2 v[212:213], v[210:211], off
	v_readlane_b32 s100, v252, 8
	s_nop 1
	v_mov_b32_e32 v210, s100
	v_readlane_b32 s100, v253, 8
	s_nop 1
	v_mov_b32_e32 v211, s100
	v_cvt_pk_f32_fp8_e32 v[212:213], v190
	v_cvt_pk_f32_fp8_sdwa v[218:219], v191 src0_sel:WORD_1
	v_mov_b32_e32 v209, v215
	v_mov_b32_e32 v199, v212
	v_mov_b32_e32 v197, v213
	v_add_f32_e32 v1, v195, v210
	v_max_f32_e32 v193, v211, v211
	v_max_f32_e32 v195, v1, v193
	v_sub_f32_e32 v1, v1, v195
	v_mul_f32_e32 v1, 0x3fb8aa3b, v1
	v_exp_f32_e32 v210, v1
	v_sub_f32_e32 v1, v211, v195
	v_mul_f32_e32 v1, 0x3fb8aa3b, v1
	v_exp_f32_e32 v211, v1
	v_mov_b32_e32 v193, v214
	v_mul_f32_e32 v190, v212, v211
	v_pk_fma_f32 v[198:199], v[198:199], v[210:211], v[190:191] op_sel_hi:[1,1,0]
	v_mul_f32_e32 v190, v213, v211
	v_pk_fma_f32 v[196:197], v[196:197], v[210:211], v[190:191] op_sel_hi:[1,1,0]
	v_mul_f32_e32 v190, v214, v211
	v_pk_fma_f32 v[192:193], v[192:193], v[210:211], v[190:191] op_sel_hi:[1,1,0]
	v_mul_f32_e32 v190, v215, v211
	v_pk_fma_f32 v[190:191], v[208:209], v[210:211], v[190:191] op_sel_hi:[1,1,0]
	v_mov_b32_e32 v207, v211
	v_mov_b32_e32 v208, v210
	v_mov_b32_e32 v209, v216
	v_mul_f32_e32 v212, v211, v216
	v_pk_fma_f32 v[206:207], v[206:207], v[208:209], v[212:213] op_sel_hi:[1,1,0]
	v_mov_b32_e32 v205, v211
	v_mov_b32_e32 v216, v210
	v_mul_f32_e32 v208, v211, v217
	v_pk_fma_f32 v[204:205], v[204:205], v[216:217], v[208:209] op_sel_hi:[1,1,0]
	v_mov_b32_e32 v203, v211
	v_mov_b32_e32 v208, v210
	v_mov_b32_e32 v209, v218
	v_mul_f32_e32 v212, v211, v218
	v_pk_fma_f32 v[202:203], v[202:203], v[208:209], v[212:213] op_sel_hi:[1,1,0]
	v_mov_b32_e32 v201, v211
	v_mov_b32_e32 v218, v210
	v_mul_f32_e32 v208, v211, v219
	v_pk_fma_f32 v[200:201], v[200:201], v[218:219], v[208:209] op_sel_hi:[1,1,0]
	v_med3_f32 v1, v198, s17, v231
	v_med3_f32 v191, v196, s17, v231
	v_mov_b32_e32 v208, v137
	v_cvt_pk_fp8_f32 v208, v1, v191
	v_med3_f32 v1, v206, s17, v231
	v_med3_f32 v191, v204, s17, v231
	v_mov_b32_e32 v209, v137
	v_cvt_pk_fp8_f32 v209, v1, v191
	v_med3_f32 v193, v192, s17, v231
	v_med3_f32 v197, v190, s17, v231
	v_cvt_pk_fp8_f32 v208, v193, v197 op_sel:[0,0,1]
	v_med3_f32 v193, v202, s17, v231
	v_med3_f32 v197, v200, s17, v231
	v_cvt_pk_fp8_f32 v209, v193, v197 op_sel:[0,0,1]
	v_lshl_add_u64 v[210:211], v[126:127], 0, s[56:57]
	v_cvt_pk_f32_fp8_sdwa v[212:213], v188 src0_sel:WORD_1
	v_cvt_pk_f32_fp8_e32 v[214:215], v189
	global_store_dwordx2 v[210:211], v[208:209], off
	v_readlane_b32 s100, v252, 9
	s_nop 1
	v_mov_b32_e32 v208, s100
	v_readlane_b32 s100, v253, 9
	s_nop 1
	v_mov_b32_e32 v209, s100
	v_cvt_pk_f32_fp8_e32 v[210:211], v188
	v_cvt_pk_f32_fp8_sdwa v[216:217], v189 src0_sel:WORD_1
	v_mov_b32_e32 v193, v212
	v_mov_b32_e32 v199, v210
	v_mov_b32_e32 v197, v211
	v_add_f32_e32 v1, v195, v208
	v_max_f32_e32 v191, v209, v209
	v_max_f32_e32 v195, v1, v191
	v_sub_f32_e32 v1, v1, v195
	v_mul_f32_e32 v1, 0x3fb8aa3b, v1
	v_exp_f32_e32 v208, v1
	v_sub_f32_e32 v1, v209, v195
	v_mul_f32_e32 v1, 0x3fb8aa3b, v1
	v_exp_f32_e32 v209, v1
	v_mov_b32_e32 v191, v213
	v_mul_f32_e32 v188, v210, v209
	v_pk_fma_f32 v[198:199], v[198:199], v[208:209], v[188:189] op_sel_hi:[1,1,0]
; __device__ __forceinline__ int cslot(int bh, int c) { return (c + bh) & 31; }
; template <int GRP>
; __device__ __forceinline__ void y_phase(Frame& F, const MW& W) {
;     ...
;         for (int c = 0; c < 32; ++c) {
;             u32x2 o; o.x = pg8::pack_fp8x4(C[0], C[1], C[2], C[3]); o.y = pg8::pack_fp8x4(C[4], C[5], C[6], C[7]); *(u32x2*)(W.CP + off + (size_t)cslot(bh, c) * 16384) = o;
;             const float bl = sc[2 * c], am = sc[2 * c + 1], mn = fmaxf(bl + m, am), dec = __expf(bl + m - mn), inj = __expf(am - mn);
;             const auto x0 = __builtin_amdgcn_cvt_pk_f32_fp8((int)v[c].x, false), x1 = __builtin_amdgcn_cvt_pk_f32_fp8((int)v[c].x, true), x2 = __builtin_amdgcn_cvt_pk_f32_fp8((int)v[c].y, false), x3 = __builtin_amdgcn_cvt_pk_f32_fp8((int)v[c].y, true);
;             C[0] = C[0] * dec + x0[0] * inj; C[1] = C[1] * dec + x0[1] * inj; C[2] = C[2] * dec + x1[0] * inj; C[3] = C[3] * dec + x1[1] * inj;
;             C[4] = C[4] * dec + x2[0] * inj; C[5] = C[5] * dec + x2[1] * inj; C[6] = C[6] * dec + x3[0] * inj; C[7] = C[7] * dec + x3[1] * inj; m = mn; }
	v_mul_f32_e32 v188, v211, v209
	v_pk_fma_f32 v[196:197], v[196:197], v[208:209], v[188:189] op_sel_hi:[1,1,0]
	v_mul_f32_e32 v188, v212, v209
	v_pk_fma_f32 v[192:193], v[192:193], v[208:209], v[188:189] op_sel_hi:[1,1,0]
	v_mul_f32_e32 v188, v213, v209
	v_pk_fma_f32 v[190:191], v[190:191], v[208:209], v[188:189] op_sel_hi:[1,1,0]
	v_mov_b32_e32 v207, v209
	v_mov_b32_e32 v188, v208
	v_mov_b32_e32 v189, v214
	v_mul_f32_e32 v210, v209, v214
	v_pk_fma_f32 v[188:189], v[206:207], v[188:189], v[210:211] op_sel_hi:[1,1,0]
	v_mov_b32_e32 v205, v209
	v_mov_b32_e32 v214, v208
	v_mul_f32_e32 v206, v209, v215
	v_pk_fma_f32 v[204:205], v[204:205], v[214:215], v[206:207] op_sel_hi:[1,1,0]
	v_mov_b32_e32 v203, v209
	v_mov_b32_e32 v206, v208
	v_mov_b32_e32 v207, v216
	v_mul_f32_e32 v210, v209, v216
	v_pk_fma_f32 v[202:203], v[202:203], v[206:207], v[210:211] op_sel_hi:[1,1,0]
	v_mov_b32_e32 v201, v209
	v_mov_b32_e32 v216, v208
	v_mul_f32_e32 v206, v209, v217
	v_pk_fma_f32 v[200:201], v[200:201], v[216:217], v[206:207] op_sel_hi:[1,1,0]
	v_med3_f32 v1, v198, s17, v231
	v_med3_f32 v189, v196, s17, v231
	v_mov_b32_e32 v206, v137
	v_cvt_pk_fp8_f32 v206, v1, v189
	v_med3_f32 v1, v188, s17, v231
	v_med3_f32 v189, v204, s17, v231
	v_mov_b32_e32 v207, v137
	v_cvt_pk_fp8_f32 v207, v1, v189
	v_med3_f32 v191, v192, s17, v231
	v_med3_f32 v193, v190, s17, v231
	v_cvt_pk_fp8_f32 v206, v191, v193 op_sel:[0,0,1]
	v_med3_f32 v191, v202, s17, v231
	v_med3_f32 v193, v200, s17, v231
	v_cvt_pk_fp8_f32 v207, v191, v193 op_sel:[0,0,1]
	v_lshl_add_u64 v[208:209], v[126:127], 0, s[66:67]
	v_cvt_pk_f32_fp8_sdwa v[210:211], v186 src0_sel:WORD_1
	v_cvt_pk_f32_fp8_e32 v[212:213], v187
	global_store_dwordx2 v[208:209], v[206:207], off
	v_readlane_b32 s100, v252, 10
	s_nop 1
	v_mov_b32_e32 v206, s100
	v_readlane_b32 s100, v253, 10
	s_nop 1
	v_mov_b32_e32 v207, s100
	v_cvt_pk_f32_fp8_e32 v[208:209], v186
	v_cvt_pk_f32_fp8_sdwa v[214:215], v187 src0_sel:WORD_1
	v_mov_b32_e32 v193, v210
	v_mov_b32_e32 v191, v211
	v_mov_b32_e32 v199, v208
	v_mov_b32_e32 v197, v209
	v_add_f32_e32 v1, v195, v206
	v_max_f32_e32 v189, v207, v207
	v_max_f32_e32 v195, v1, v189
	v_sub_f32_e32 v1, v1, v195
	v_mul_f32_e32 v1, 0x3fb8aa3b, v1
	v_exp_f32_e32 v206, v1
	v_sub_f32_e32 v1, v207, v195
	v_mul_f32_e32 v1, 0x3fb8aa3b, v1
	v_exp_f32_e32 v207, v1
	s_nop 0
	v_mul_f32_e32 v186, v208, v207
	v_pk_fma_f32 v[198:199], v[198:199], v[206:207], v[186:187] op_sel_hi:[1,1,0]
	v_mul_f32_e32 v186, v209, v207
	v_pk_fma_f32 v[196:197], v[196:197], v[206:207], v[186:187] op_sel_hi:[1,1,0]
	v_mul_f32_e32 v186, v210, v207
	v_pk_fma_f32 v[192:193], v[192:193], v[206:207], v[186:187] op_sel_hi:[1,1,0]
	v_mul_f32_e32 v186, v211, v207
	v_pk_fma_f32 v[190:191], v[190:191], v[206:207], v[186:187] op_sel_hi:[1,1,0]
	v_mov_b32_e32 v189, v207
	v_mov_b32_e32 v186, v206
	v_mov_b32_e32 v187, v212
	v_mul_f32_e32 v208, v207, v212
	v_pk_fma_f32 v[188:189], v[188:189], v[186:187], v[208:209] op_sel_hi:[1,1,0]
	v_mov_b32_e32 v205, v207
	v_mov_b32_e32 v212, v206
	v_mul_f32_e32 v186, v207, v213
	v_pk_fma_f32 v[186:187], v[204:205], v[212:213], v[186:187] op_sel_hi:[1,1,0]
	v_mov_b32_e32 v203, v207
	v_mov_b32_e32 v204, v206
	v_mov_b32_e32 v205, v214
	v_mul_f32_e32 v208, v207, v214
	v_pk_fma_f32 v[202:203], v[202:203], v[204:205], v[208:209] op_sel_hi:[1,1,0]
	v_mov_b32_e32 v201, v207
	v_mov_b32_e32 v214, v206
	v_mul_f32_e32 v204, v207, v215
	v_pk_fma_f32 v[200:201], v[200:201], v[214:215], v[204:205] op_sel_hi:[1,1,0]
	v_med3_f32 v1, v198, s17, v231
	v_med3_f32 v187, v196, s17, v231
	v_mov_b32_e32 v204, v137
	v_cvt_pk_fp8_f32 v204, v1, v187
	v_med3_f32 v1, v188, s17, v231
	v_med3_f32 v187, v186, s17, v231
	v_mov_b32_e32 v205, v137
	v_cvt_pk_fp8_f32 v205, v1, v187
	v_med3_f32 v189, v192, s17, v231
	v_med3_f32 v191, v190, s17, v231
	v_cvt_pk_fp8_f32 v204, v189, v191 op_sel:[0,0,1]
	v_med3_f32 v189, v202, s17, v231
	v_med3_f32 v191, v200, s17, v231
	v_cvt_pk_fp8_f32 v205, v189, v191 op_sel:[0,0,1]
	v_lshl_add_u64 v[206:207], v[126:127], 0, s[96:97]
	v_cvt_pk_f32_fp8_sdwa v[208:209], v184 src0_sel:WORD_1
	v_cvt_pk_f32_fp8_e32 v[210:211], v185
	global_store_dwordx2 v[206:207], v[204:205], off
	v_readlane_b32 s100, v252, 11
	s_nop 1
	v_mov_b32_e32 v204, s100
	v_readlane_b32 s100, v253, 11
	s_nop 1
	v_mov_b32_e32 v205, s100
	v_cvt_pk_f32_fp8_e32 v[206:207], v184
	v_cvt_pk_f32_fp8_sdwa v[212:213], v185 src0_sel:WORD_1
	v_mov_b32_e32 v193, v208
	v_mov_b32_e32 v191, v209
	v_mov_b32_e32 v199, v206
	v_mov_b32_e32 v197, v207
	v_add_f32_e32 v1, v195, v204
	v_max_f32_e32 v187, v205, v205
	v_max_f32_e32 v195, v1, v187
	v_sub_f32_e32 v1, v1, v195
	v_mul_f32_e32 v1, 0x3fb8aa3b, v1
	v_exp_f32_e32 v204, v1
	v_sub_f32_e32 v1, v205, v195
	v_mul_f32_e32 v1, 0x3fb8aa3b, v1
	v_exp_f32_e32 v205, v1
	s_nop 0
	v_mul_f32_e32 v184, v206, v205
	v_pk_fma_f32 v[198:199], v[198:199], v[204:205], v[184:185] op_sel_hi:[1,1,0]
	v_mul_f32_e32 v184, v207, v205
	v_pk_fma_f32 v[196:197], v[196:197], v[204:205], v[184:185] op_sel_hi:[1,1,0]
	v_mul_f32_e32 v184, v208, v205
	v_pk_fma_f32 v[192:193], v[192:193], v[204:205], v[184:185] op_sel_hi:[1,1,0]
	v_mul_f32_e32 v184, v209, v205
	v_pk_fma_f32 v[190:191], v[190:191], v[204:205], v[184:185] op_sel_hi:[1,1,0]
	v_mov_b32_e32 v189, v205
	v_mov_b32_e32 v184, v204
	v_mov_b32_e32 v185, v210
	v_mul_f32_e32 v206, v205, v210
	v_pk_fma_f32 v[188:189], v[188:189], v[184:185], v[206:207] op_sel_hi:[1,1,0]
	v_mov_b32_e32 v187, v205
	v_mov_b32_e32 v210, v204
	v_mul_f32_e32 v184, v205, v211
	v_pk_fma_f32 v[186:187], v[186:187], v[210:211], v[184:185] op_sel_hi:[1,1,0]
	v_mov_b32_e32 v203, v205
	v_mov_b32_e32 v184, v204
	v_mov_b32_e32 v185, v212
; __device__ __forceinline__ int cslot(int bh, int c) { return (c + bh) & 31; }
; template <int GRP>
; __device__ __forceinline__ void y_phase(Frame& F, const MW& W) {
;     ...
;         for (int c = 0; c < 32; ++c) {
;             u32x2 o; o.x = pg8::pack_fp8x4(C[0], C[1], C[2], C[3]); o.y = pg8::pack_fp8x4(C[4], C[5], C[6], C[7]); *(u32x2*)(W.CP + off + (size_t)cslot(bh, c) * 16384) = o;
;             const float bl = sc[2 * c], am = sc[2 * c + 1], mn = fmaxf(bl + m, am), dec = __expf(bl + m - mn), inj = __expf(am - mn);
;             const auto x0 = __builtin_amdgcn_cvt_pk_f32_fp8((int)v[c].x, false), x1 = __builtin_amdgcn_cvt_pk_f32_fp8((int)v[c].x, true), x2 = __builtin_amdgcn_cvt_pk_f32_fp8((int)v[c].y, false), x3 = __builtin_amdgcn_cvt_pk_f32_fp8((int)v[c].y, true);
;             C[0] = C[0] * dec + x0[0] * inj; C[1] = C[1] * dec + x0[1] * inj; C[2] = C[2] * dec + x1[0] * inj; C[3] = C[3] * dec + x1[1] * inj;
;             C[4] = C[4] * dec + x2[0] * inj; C[5] = C[5] * dec + x2[1] * inj; C[6] = C[6] * dec + x3[0] * inj; C[7] = C[7] * dec + x3[1] * inj; m = mn; }
	v_mul_f32_e32 v206, v205, v212
	v_pk_fma_f32 v[184:185], v[202:203], v[184:185], v[206:207] op_sel_hi:[1,1,0]
	v_mov_b32_e32 v201, v205
	v_mov_b32_e32 v212, v204
	v_mul_f32_e32 v202, v205, v213
	v_pk_fma_f32 v[200:201], v[200:201], v[212:213], v[202:203] op_sel_hi:[1,1,0]
	v_med3_f32 v1, v198, s17, v231
	v_med3_f32 v185, v196, s17, v231
	v_mov_b32_e32 v202, v137
	v_cvt_pk_fp8_f32 v202, v1, v185
	v_med3_f32 v1, v188, s17, v231
	v_med3_f32 v185, v186, s17, v231
	v_mov_b32_e32 v203, v137
	v_cvt_pk_fp8_f32 v203, v1, v185
	v_med3_f32 v187, v192, s17, v231
	v_med3_f32 v189, v190, s17, v231
	v_cvt_pk_fp8_f32 v202, v187, v189 op_sel:[0,0,1]
	v_med3_f32 v187, v184, s17, v231
	v_med3_f32 v189, v200, s17, v231
	v_cvt_pk_fp8_f32 v203, v187, v189 op_sel:[0,0,1]
	v_lshl_add_u64 v[204:205], v[126:127], 0, s[94:95]
	v_cvt_pk_f32_fp8_sdwa v[206:207], v182 src0_sel:WORD_1
	v_cvt_pk_f32_fp8_e32 v[208:209], v183
	global_store_dwordx2 v[204:205], v[202:203], off
	v_readlane_b32 s100, v252, 12
	s_nop 1
	v_mov_b32_e32 v202, s100
	v_readlane_b32 s100, v253, 12
	s_nop 1
	v_mov_b32_e32 v203, s100
	v_cvt_pk_f32_fp8_e32 v[204:205], v182
	v_cvt_pk_f32_fp8_sdwa v[182:183], v183 src0_sel:WORD_1
	v_mov_b32_e32 v193, v206
	v_mov_b32_e32 v191, v207
	v_mov_b32_e32 v199, v204
	v_mov_b32_e32 v197, v205
	v_add_f32_e32 v1, v195, v202
	v_max_f32_e32 v185, v203, v203
	v_max_f32_e32 v195, v1, v185
	v_sub_f32_e32 v1, v1, v195
	v_mul_f32_e32 v1, 0x3fb8aa3b, v1
	v_exp_f32_e32 v202, v1
	v_sub_f32_e32 v1, v203, v195
	v_mul_f32_e32 v1, 0x3fb8aa3b, v1
	v_exp_f32_e32 v203, v1
	s_nop 0
	v_mul_f32_e32 v204, v204, v203
	v_pk_fma_f32 v[198:199], v[198:199], v[202:203], v[204:205] op_sel_hi:[1,1,0]
	v_mul_f32_e32 v204, v205, v203
	v_pk_fma_f32 v[196:197], v[196:197], v[202:203], v[204:205] op_sel_hi:[1,1,0]
	v_mul_f32_e32 v204, v206, v203
	v_pk_fma_f32 v[192:193], v[192:193], v[202:203], v[204:205] op_sel_hi:[1,1,0]
	v_mul_f32_e32 v204, v207, v203
	v_pk_fma_f32 v[190:191], v[190:191], v[202:203], v[204:205] op_sel_hi:[1,1,0]
	v_mov_b32_e32 v189, v203
	v_mov_b32_e32 v204, v202
	v_mov_b32_e32 v205, v208
	v_mul_f32_e32 v206, v203, v208
	v_pk_fma_f32 v[188:189], v[188:189], v[204:205], v[206:207] op_sel_hi:[1,1,0]
	v_mov_b32_e32 v187, v203
	v_mov_b32_e32 v208, v202
	v_mul_f32_e32 v204, v203, v209
	v_pk_fma_f32 v[186:187], v[186:187], v[208:209], v[204:205] op_sel_hi:[1,1,0]
	v_mov_b32_e32 v185, v203
	v_mov_b32_e32 v204, v202
	v_mov_b32_e32 v205, v182
	v_mul_f32_e32 v182, v203, v182
	v_pk_fma_f32 v[184:185], v[184:185], v[204:205], v[182:183] op_sel_hi:[1,1,0]
	v_mov_b32_e32 v201, v203
	v_mov_b32_e32 v182, v202
	v_mul_f32_e32 v202, v203, v183
	v_pk_fma_f32 v[182:183], v[200:201], v[182:183], v[202:203] op_sel_hi:[1,1,0]
	v_med3_f32 v1, v198, s17, v231
	v_med3_f32 v183, v196, s17, v231
	v_mov_b32_e32 v200, v137
	v_cvt_pk_fp8_f32 v200, v1, v183
	v_med3_f32 v1, v188, s17, v231
	v_med3_f32 v183, v186, s17, v231
	v_mov_b32_e32 v201, v137
	v_cvt_pk_fp8_f32 v201, v1, v183
	v_med3_f32 v185, v192, s17, v231
	v_med3_f32 v187, v190, s17, v231
	v_cvt_pk_fp8_f32 v200, v185, v187 op_sel:[0,0,1]
	v_med3_f32 v185, v184, s17, v231
	v_med3_f32 v187, v182, s17, v231
	v_cvt_pk_fp8_f32 v201, v185, v187 op_sel:[0,0,1]
	v_lshl_add_u64 v[202:203], v[126:127], 0, s[92:93]
	v_cvt_pk_f32_fp8_sdwa v[204:205], v180 src0_sel:WORD_1
	v_cvt_pk_f32_fp8_e32 v[206:207], v181
	global_store_dwordx2 v[202:203], v[200:201], off
	v_readlane_b32 s100, v252, 13
	s_nop 1
	v_mov_b32_e32 v200, s100
	v_readlane_b32 s100, v253, 13
	s_nop 1
	v_mov_b32_e32 v201, s100
	v_cvt_pk_f32_fp8_e32 v[202:203], v180
	v_cvt_pk_f32_fp8_sdwa v[208:209], v181 src0_sel:WORD_1
	v_mov_b32_e32 v193, v204
	v_mov_b32_e32 v191, v205
	v_mov_b32_e32 v199, v202
	v_mov_b32_e32 v197, v203
	v_add_f32_e32 v1, v195, v200
	v_max_f32_e32 v183, v201, v201
	v_max_f32_e32 v195, v1, v183
	v_sub_f32_e32 v1, v1, v195
	v_mul_f32_e32 v1, 0x3fb8aa3b, v1
	v_exp_f32_e32 v200, v1
	v_sub_f32_e32 v1, v201, v195
	v_mul_f32_e32 v1, 0x3fb8aa3b, v1
	v_exp_f32_e32 v201, v1
	s_nop 0
	v_mul_f32_e32 v180, v202, v201
	v_pk_fma_f32 v[180:181], v[198:199], v[200:201], v[180:181] op_sel_hi:[1,1,0]
	v_mul_f32_e32 v198, v203, v201
	v_pk_fma_f32 v[196:197], v[196:197], v[200:201], v[198:199] op_sel_hi:[1,1,0]
	v_mul_f32_e32 v198, v204, v201
	v_pk_fma_f32 v[192:193], v[192:193], v[200:201], v[198:199] op_sel_hi:[1,1,0]
	v_mul_f32_e32 v198, v205, v201
	v_pk_fma_f32 v[190:191], v[190:191], v[200:201], v[198:199] op_sel_hi:[1,1,0]
	v_mov_b32_e32 v189, v201
	v_mov_b32_e32 v198, v200
	v_mov_b32_e32 v199, v206
	v_mul_f32_e32 v202, v201, v206
	v_pk_fma_f32 v[188:189], v[188:189], v[198:199], v[202:203] op_sel_hi:[1,1,0]
	v_mov_b32_e32 v187, v201
	v_mov_b32_e32 v206, v200
	v_mul_f32_e32 v198, v201, v207
	v_pk_fma_f32 v[186:187], v[186:187], v[206:207], v[198:199] op_sel_hi:[1,1,0]
	v_mov_b32_e32 v185, v201
	v_mov_b32_e32 v198, v200
	v_mov_b32_e32 v199, v208
	v_mul_f32_e32 v202, v201, v208
	v_pk_fma_f32 v[184:185], v[184:185], v[198:199], v[202:203] op_sel_hi:[1,1,0]
	v_mov_b32_e32 v183, v201
	v_mov_b32_e32 v208, v200
	v_mul_f32_e32 v198, v201, v209
	v_pk_fma_f32 v[182:183], v[182:183], v[208:209], v[198:199] op_sel_hi:[1,1,0]
	v_med3_f32 v1, v180, s17, v231
	v_med3_f32 v181, v196, s17, v231
	v_mov_b32_e32 v198, v137
	v_cvt_pk_fp8_f32 v198, v1, v181
	v_med3_f32 v1, v188, s17, v231
	v_med3_f32 v181, v186, s17, v231
	v_mov_b32_e32 v199, v137
	v_cvt_pk_fp8_f32 v199, v1, v181
	v_med3_f32 v183, v192, s17, v231
	v_med3_f32 v185, v190, s17, v231
	v_cvt_pk_fp8_f32 v198, v183, v185 op_sel:[0,0,1]
	v_med3_f32 v183, v184, s17, v231
	v_med3_f32 v185, v182, s17, v231
	v_cvt_pk_fp8_f32 v199, v183, v185 op_sel:[0,0,1]
; __device__ __forceinline__ int cslot(int bh, int c) { return (c + bh) & 31; }
; template <int GRP>
; __device__ __forceinline__ void y_phase(Frame& F, const MW& W) {
;     ...
;         for (int c = 0; c < 32; ++c) {
;             u32x2 o; o.x = pg8::pack_fp8x4(C[0], C[1], C[2], C[3]); o.y = pg8::pack_fp8x4(C[4], C[5], C[6], C[7]); *(u32x2*)(W.CP + off + (size_t)cslot(bh, c) * 16384) = o;
;             const float bl = sc[2 * c], am = sc[2 * c + 1], mn = fmaxf(bl + m, am), dec = __expf(bl + m - mn), inj = __expf(am - mn);
;             const auto x0 = __builtin_amdgcn_cvt_pk_f32_fp8((int)v[c].x, false), x1 = __builtin_amdgcn_cvt_pk_f32_fp8((int)v[c].x, true), x2 = __builtin_amdgcn_cvt_pk_f32_fp8((int)v[c].y, false), x3 = __builtin_amdgcn_cvt_pk_f32_fp8((int)v[c].y, true);
;             C[0] = C[0] * dec + x0[0] * inj; C[1] = C[1] * dec + x0[1] * inj; C[2] = C[2] * dec + x1[0] * inj; C[3] = C[3] * dec + x1[1] * inj;
;             C[4] = C[4] * dec + x2[0] * inj; C[5] = C[5] * dec + x2[1] * inj; C[6] = C[6] * dec + x3[0] * inj; C[7] = C[7] * dec + x3[1] * inj; m = mn; }
	v_lshl_add_u64 v[200:201], v[126:127], 0, s[90:91]
	v_cvt_pk_f32_fp8_sdwa v[202:203], v178 src0_sel:WORD_1
	v_cvt_pk_f32_fp8_e32 v[204:205], v179
	global_store_dwordx2 v[200:201], v[198:199], off
	v_readlane_b32 s100, v252, 14
	s_nop 1
	v_mov_b32_e32 v198, s100
	v_readlane_b32 s100, v253, 14
	s_nop 1
	v_mov_b32_e32 v199, s100
	v_cvt_pk_f32_fp8_e32 v[200:201], v178
	v_cvt_pk_f32_fp8_sdwa v[206:207], v179 src0_sel:WORD_1
	v_mov_b32_e32 v193, v202
	v_mov_b32_e32 v191, v203
	v_mov_b32_e32 v197, v201
	v_add_f32_e32 v1, v195, v198
	v_max_f32_e32 v181, v199, v199
	v_max_f32_e32 v195, v1, v181
	v_sub_f32_e32 v1, v1, v195
	v_mul_f32_e32 v1, 0x3fb8aa3b, v1
	v_exp_f32_e32 v198, v1
	v_sub_f32_e32 v1, v199, v195
	v_mul_f32_e32 v1, 0x3fb8aa3b, v1
	v_exp_f32_e32 v199, v1
	v_mov_b32_e32 v181, v200
	v_mul_f32_e32 v178, v200, v199
	v_pk_fma_f32 v[180:181], v[180:181], v[198:199], v[178:179] op_sel_hi:[1,1,0]
	v_mul_f32_e32 v178, v201, v199
	v_pk_fma_f32 v[178:179], v[196:197], v[198:199], v[178:179] op_sel_hi:[1,1,0]
	v_mul_f32_e32 v196, v202, v199
	v_pk_fma_f32 v[192:193], v[192:193], v[198:199], v[196:197] op_sel_hi:[1,1,0]
	v_mul_f32_e32 v196, v203, v199
	v_pk_fma_f32 v[190:191], v[190:191], v[198:199], v[196:197] op_sel_hi:[1,1,0]
	v_mov_b32_e32 v189, v199
	v_mov_b32_e32 v196, v198
	v_mov_b32_e32 v197, v204
	v_mul_f32_e32 v200, v199, v204
	v_pk_fma_f32 v[188:189], v[188:189], v[196:197], v[200:201] op_sel_hi:[1,1,0]
	v_mov_b32_e32 v187, v199
	v_mov_b32_e32 v204, v198
	v_mul_f32_e32 v196, v199, v205
	v_pk_fma_f32 v[186:187], v[186:187], v[204:205], v[196:197] op_sel_hi:[1,1,0]
	v_mov_b32_e32 v185, v199
	v_mov_b32_e32 v196, v198
	v_mov_b32_e32 v197, v206
	v_mul_f32_e32 v200, v199, v206
	v_pk_fma_f32 v[184:185], v[184:185], v[196:197], v[200:201] op_sel_hi:[1,1,0]
	v_mov_b32_e32 v183, v199
	v_mov_b32_e32 v206, v198
	v_mul_f32_e32 v196, v199, v207
	v_pk_fma_f32 v[182:183], v[182:183], v[206:207], v[196:197] op_sel_hi:[1,1,0]
	v_med3_f32 v1, v180, s17, v231
	v_med3_f32 v179, v178, s17, v231
	v_mov_b32_e32 v196, v137
	v_cvt_pk_fp8_f32 v196, v1, v179
	v_med3_f32 v1, v188, s17, v231
	v_med3_f32 v179, v186, s17, v231
	v_mov_b32_e32 v197, v137
	v_cvt_pk_fp8_f32 v197, v1, v179
	v_med3_f32 v181, v192, s17, v231
	v_med3_f32 v183, v190, s17, v231
	v_cvt_pk_fp8_f32 v196, v181, v183 op_sel:[0,0,1]
	v_med3_f32 v181, v184, s17, v231
	v_med3_f32 v183, v182, s17, v231
	v_cvt_pk_fp8_f32 v197, v181, v183 op_sel:[0,0,1]
	v_lshl_add_u64 v[198:199], v[126:127], 0, s[88:89]
	v_cvt_pk_f32_fp8_sdwa v[200:201], v176 src0_sel:WORD_1
	v_cvt_pk_f32_fp8_e32 v[202:203], v177
	global_store_dwordx2 v[198:199], v[196:197], off
	v_readlane_b32 s100, v252, 15
	s_nop 1
	v_mov_b32_e32 v196, s100
	v_readlane_b32 s100, v253, 15
	s_nop 1
	v_mov_b32_e32 v197, s100
	v_cvt_pk_f32_fp8_e32 v[198:199], v176
	v_cvt_pk_f32_fp8_sdwa v[204:205], v177 src0_sel:WORD_1
	v_mov_b32_e32 v193, v200
	v_mov_b32_e32 v191, v201
	v_mov_b32_e32 v181, v198
	v_add_f32_e32 v1, v195, v196
	v_max_f32_e32 v179, v197, v197
	v_max_f32_e32 v195, v1, v179
	v_sub_f32_e32 v1, v1, v195
	v_mul_f32_e32 v1, 0x3fb8aa3b, v1
	v_exp_f32_e32 v196, v1
	v_sub_f32_e32 v1, v197, v195
	v_mul_f32_e32 v1, 0x3fb8aa3b, v1
	v_exp_f32_e32 v197, v1
	v_mov_b32_e32 v179, v199
	v_mul_f32_e32 v176, v198, v197
	v_pk_fma_f32 v[180:181], v[180:181], v[196:197], v[176:177] op_sel_hi:[1,1,0]
	v_mul_f32_e32 v176, v199, v197
	v_pk_fma_f32 v[178:179], v[178:179], v[196:197], v[176:177] op_sel_hi:[1,1,0]
	v_mul_f32_e32 v176, v200, v197
	v_pk_fma_f32 v[176:177], v[192:193], v[196:197], v[176:177] op_sel_hi:[1,1,0]
	v_mul_f32_e32 v192, v201, v197
	v_pk_fma_f32 v[190:191], v[190:191], v[196:197], v[192:193] op_sel_hi:[1,1,0]
	v_mov_b32_e32 v189, v197
	v_mov_b32_e32 v192, v196
	v_mov_b32_e32 v193, v202
	v_mul_f32_e32 v198, v197, v202
	v_pk_fma_f32 v[188:189], v[188:189], v[192:193], v[198:199] op_sel_hi:[1,1,0]
	v_mov_b32_e32 v187, v197
	v_mov_b32_e32 v202, v196
	v_mul_f32_e32 v192, v197, v203
	v_pk_fma_f32 v[186:187], v[186:187], v[202:203], v[192:193] op_sel_hi:[1,1,0]
	v_mov_b32_e32 v185, v197
	v_mov_b32_e32 v192, v196
	v_mov_b32_e32 v193, v204
	v_mul_f32_e32 v198, v197, v204
	v_pk_fma_f32 v[184:185], v[184:185], v[192:193], v[198:199] op_sel_hi:[1,1,0]
	v_mov_b32_e32 v183, v197
	v_mov_b32_e32 v204, v196
	v_mul_f32_e32 v192, v197, v205
	v_pk_fma_f32 v[182:183], v[182:183], v[204:205], v[192:193] op_sel_hi:[1,1,0]
	v_med3_f32 v1, v180, s17, v231
	v_med3_f32 v177, v178, s17, v231
	v_mov_b32_e32 v192, v137
	v_cvt_pk_fp8_f32 v192, v1, v177
	v_med3_f32 v1, v188, s17, v231
	v_med3_f32 v177, v186, s17, v231
	v_mov_b32_e32 v193, v137
	v_cvt_pk_fp8_f32 v193, v1, v177
	v_med3_f32 v179, v176, s17, v231
	v_med3_f32 v181, v190, s17, v231
	v_cvt_pk_fp8_f32 v192, v179, v181 op_sel:[0,0,1]
	v_med3_f32 v179, v184, s17, v231
	v_med3_f32 v181, v182, s17, v231
	v_cvt_pk_fp8_f32 v193, v179, v181 op_sel:[0,0,1]
	v_lshl_add_u64 v[196:197], v[126:127], 0, s[86:87]
	v_cvt_pk_f32_fp8_sdwa v[198:199], v174 src0_sel:WORD_1
	v_cvt_pk_f32_fp8_e32 v[200:201], v175
	global_store_dwordx2 v[196:197], v[192:193], off
	v_readlane_b32 s100, v252, 16
	s_nop 1
	v_mov_b32_e32 v192, s100
	v_readlane_b32 s100, v253, 16
	s_nop 1
	v_mov_b32_e32 v193, s100
	v_cvt_pk_f32_fp8_e32 v[196:197], v174
	v_cvt_pk_f32_fp8_sdwa v[202:203], v175 src0_sel:WORD_1
	v_mov_b32_e32 v191, v199
	v_mov_b32_e32 v181, v196
	v_mov_b32_e32 v179, v197
	v_add_f32_e32 v1, v195, v192
	v_max_f32_e32 v177, v193, v193
	v_max_f32_e32 v195, v1, v177
	v_sub_f32_e32 v1, v1, v195
	v_mul_f32_e32 v1, 0x3fb8aa3b, v1
	v_exp_f32_e32 v192, v1
	v_sub_f32_e32 v1, v193, v195
	v_mul_f32_e32 v1, 0x3fb8aa3b, v1
	v_exp_f32_e32 v193, v1
	v_mov_b32_e32 v177, v198
; __device__ __forceinline__ int cslot(int bh, int c) { return (c + bh) & 31; }
; template <int GRP>
; __device__ __forceinline__ void y_phase(Frame& F, const MW& W) {
;     ...
;         for (int c = 0; c < 32; ++c) {
;             u32x2 o; o.x = pg8::pack_fp8x4(C[0], C[1], C[2], C[3]); o.y = pg8::pack_fp8x4(C[4], C[5], C[6], C[7]); *(u32x2*)(W.CP + off + (size_t)cslot(bh, c) * 16384) = o;
;             const float bl = sc[2 * c], am = sc[2 * c + 1], mn = fmaxf(bl + m, am), dec = __expf(bl + m - mn), inj = __expf(am - mn);
;             const auto x0 = __builtin_amdgcn_cvt_pk_f32_fp8((int)v[c].x, false), x1 = __builtin_amdgcn_cvt_pk_f32_fp8((int)v[c].x, true), x2 = __builtin_amdgcn_cvt_pk_f32_fp8((int)v[c].y, false), x3 = __builtin_amdgcn_cvt_pk_f32_fp8((int)v[c].y, true);
;             C[0] = C[0] * dec + x0[0] * inj; C[1] = C[1] * dec + x0[1] * inj; C[2] = C[2] * dec + x1[0] * inj; C[3] = C[3] * dec + x1[1] * inj;
;             C[4] = C[4] * dec + x2[0] * inj; C[5] = C[5] * dec + x2[1] * inj; C[6] = C[6] * dec + x3[0] * inj; C[7] = C[7] * dec + x3[1] * inj; m = mn; }
	v_mul_f32_e32 v174, v196, v193
	v_pk_fma_f32 v[180:181], v[180:181], v[192:193], v[174:175] op_sel_hi:[1,1,0]
	v_mul_f32_e32 v174, v197, v193
	v_pk_fma_f32 v[178:179], v[178:179], v[192:193], v[174:175] op_sel_hi:[1,1,0]
	v_mul_f32_e32 v174, v198, v193
	v_pk_fma_f32 v[176:177], v[176:177], v[192:193], v[174:175] op_sel_hi:[1,1,0]
	v_mul_f32_e32 v174, v199, v193
	v_pk_fma_f32 v[174:175], v[190:191], v[192:193], v[174:175] op_sel_hi:[1,1,0]
	v_mov_b32_e32 v189, v193
	v_mov_b32_e32 v190, v192
	v_mov_b32_e32 v191, v200
	v_mul_f32_e32 v196, v193, v200
	v_pk_fma_f32 v[188:189], v[188:189], v[190:191], v[196:197] op_sel_hi:[1,1,0]
	v_mov_b32_e32 v187, v193
	v_mov_b32_e32 v200, v192
	v_mul_f32_e32 v190, v193, v201
	v_pk_fma_f32 v[186:187], v[186:187], v[200:201], v[190:191] op_sel_hi:[1,1,0]
	v_mov_b32_e32 v185, v193
	v_mov_b32_e32 v190, v192
	v_mov_b32_e32 v191, v202
	v_mul_f32_e32 v196, v193, v202
	v_pk_fma_f32 v[184:185], v[184:185], v[190:191], v[196:197] op_sel_hi:[1,1,0]
	v_mov_b32_e32 v183, v193
	v_mov_b32_e32 v202, v192
	v_mul_f32_e32 v190, v193, v203
	v_pk_fma_f32 v[182:183], v[182:183], v[202:203], v[190:191] op_sel_hi:[1,1,0]
	v_med3_f32 v1, v180, s17, v231
	v_med3_f32 v175, v178, s17, v231
	v_mov_b32_e32 v190, v137
	v_cvt_pk_fp8_f32 v190, v1, v175
	v_med3_f32 v1, v188, s17, v231
	v_med3_f32 v175, v186, s17, v231
	v_mov_b32_e32 v191, v137
	v_cvt_pk_fp8_f32 v191, v1, v175
	v_med3_f32 v177, v176, s17, v231
	v_med3_f32 v179, v174, s17, v231
	v_cvt_pk_fp8_f32 v190, v177, v179 op_sel:[0,0,1]
	v_med3_f32 v177, v184, s17, v231
	v_med3_f32 v179, v182, s17, v231
	v_cvt_pk_fp8_f32 v191, v177, v179 op_sel:[0,0,1]
	v_lshl_add_u64 v[192:193], v[126:127], 0, s[84:85]
	v_cvt_pk_f32_fp8_sdwa v[196:197], v172 src0_sel:WORD_1
	v_cvt_pk_f32_fp8_e32 v[198:199], v173
	global_store_dwordx2 v[192:193], v[190:191], off
	v_readlane_b32 s100, v252, 17
	s_nop 1
	v_mov_b32_e32 v190, s100
	v_readlane_b32 s100, v253, 17
	s_nop 1
	v_mov_b32_e32 v191, s100
	v_cvt_pk_f32_fp8_e32 v[192:193], v172
	v_cvt_pk_f32_fp8_sdwa v[200:201], v173 src0_sel:WORD_1
	v_mov_b32_e32 v177, v196
	v_mov_b32_e32 v181, v192
	v_mov_b32_e32 v179, v193
	v_add_f32_e32 v1, v195, v190
	v_max_f32_e32 v175, v191, v191
	v_max_f32_e32 v195, v1, v175
	v_sub_f32_e32 v1, v1, v195
	v_mul_f32_e32 v1, 0x3fb8aa3b, v1
	v_exp_f32_e32 v190, v1
	v_sub_f32_e32 v1, v191, v195
	v_mul_f32_e32 v1, 0x3fb8aa3b, v1
	v_exp_f32_e32 v191, v1
	v_mov_b32_e32 v175, v197
	v_mul_f32_e32 v172, v192, v191
	v_pk_fma_f32 v[180:181], v[180:181], v[190:191], v[172:173] op_sel_hi:[1,1,0]
	v_mul_f32_e32 v172, v193, v191
	v_pk_fma_f32 v[178:179], v[178:179], v[190:191], v[172:173] op_sel_hi:[1,1,0]
	v_mul_f32_e32 v172, v196, v191
	v_pk_fma_f32 v[176:177], v[176:177], v[190:191], v[172:173] op_sel_hi:[1,1,0]
	v_mul_f32_e32 v172, v197, v191
	v_pk_fma_f32 v[174:175], v[174:175], v[190:191], v[172:173] op_sel_hi:[1,1,0]
	v_mov_b32_e32 v189, v191
	v_mov_b32_e32 v172, v190
	v_mov_b32_e32 v173, v198
	v_mul_f32_e32 v192, v191, v198
	v_pk_fma_f32 v[172:173], v[188:189], v[172:173], v[192:193] op_sel_hi:[1,1,0]
	v_mov_b32_e32 v187, v191
	v_mov_b32_e32 v198, v190
	v_mul_f32_e32 v188, v191, v199
	v_pk_fma_f32 v[186:187], v[186:187], v[198:199], v[188:189] op_sel_hi:[1,1,0]
	v_mov_b32_e32 v185, v191
	v_mov_b32_e32 v188, v190
	v_mov_b32_e32 v189, v200
	v_mul_f32_e32 v192, v191, v200
	v_pk_fma_f32 v[184:185], v[184:185], v[188:189], v[192:193] op_sel_hi:[1,1,0]
	v_mov_b32_e32 v183, v191
	v_mov_b32_e32 v200, v190
	v_mul_f32_e32 v188, v191, v201
	v_pk_fma_f32 v[182:183], v[182:183], v[200:201], v[188:189] op_sel_hi:[1,1,0]
	v_med3_f32 v1, v180, s17, v231
	v_med3_f32 v173, v178, s17, v231
	v_mov_b32_e32 v188, v137
	v_cvt_pk_fp8_f32 v188, v1, v173
	v_med3_f32 v1, v172, s17, v231
	v_med3_f32 v173, v186, s17, v231
	v_mov_b32_e32 v189, v137
	v_cvt_pk_fp8_f32 v189, v1, v173
	v_med3_f32 v175, v176, s17, v231
	v_med3_f32 v177, v174, s17, v231
	v_cvt_pk_fp8_f32 v188, v175, v177 op_sel:[0,0,1]
	v_med3_f32 v175, v184, s17, v231
	v_med3_f32 v177, v182, s17, v231
	v_cvt_pk_fp8_f32 v189, v175, v177 op_sel:[0,0,1]
	v_lshl_add_u64 v[190:191], v[126:127], 0, s[82:83]
	v_cvt_pk_f32_fp8_sdwa v[192:193], v170 src0_sel:WORD_1
	v_cvt_pk_f32_fp8_e32 v[196:197], v171
	global_store_dwordx2 v[190:191], v[188:189], off
	v_readlane_b32 s100, v252, 18
	s_nop 1
	v_mov_b32_e32 v188, s100
	v_readlane_b32 s100, v253, 18
	s_nop 1
	v_mov_b32_e32 v189, s100
	v_cvt_pk_f32_fp8_e32 v[190:191], v170
	v_cvt_pk_f32_fp8_sdwa v[198:199], v171 src0_sel:WORD_1
	v_mov_b32_e32 v177, v192
	v_mov_b32_e32 v175, v193
	v_mov_b32_e32 v181, v190
	v_mov_b32_e32 v179, v191
	v_add_f32_e32 v1, v195, v188
	v_max_f32_e32 v173, v189, v189
	v_max_f32_e32 v195, v1, v173
	v_sub_f32_e32 v1, v1, v195
	v_mul_f32_e32 v1, 0x3fb8aa3b, v1
	v_exp_f32_e32 v188, v1
	v_sub_f32_e32 v1, v189, v195
	v_mul_f32_e32 v1, 0x3fb8aa3b, v1
	v_exp_f32_e32 v189, v1
	s_nop 0
	v_mul_f32_e32 v170, v190, v189
	v_pk_fma_f32 v[180:181], v[180:181], v[188:189], v[170:171] op_sel_hi:[1,1,0]
	v_mul_f32_e32 v170, v191, v189
	v_pk_fma_f32 v[178:179], v[178:179], v[188:189], v[170:171] op_sel_hi:[1,1,0]
	v_mul_f32_e32 v170, v192, v189
	v_pk_fma_f32 v[176:177], v[176:177], v[188:189], v[170:171] op_sel_hi:[1,1,0]
	v_mul_f32_e32 v170, v193, v189
	v_pk_fma_f32 v[174:175], v[174:175], v[188:189], v[170:171] op_sel_hi:[1,1,0]
	v_mov_b32_e32 v173, v189
	v_mov_b32_e32 v170, v188
	v_mov_b32_e32 v171, v196
	v_mul_f32_e32 v190, v189, v196
	v_pk_fma_f32 v[172:173], v[172:173], v[170:171], v[190:191] op_sel_hi:[1,1,0]
	v_mov_b32_e32 v187, v189
	v_mov_b32_e32 v196, v188
	v_mul_f32_e32 v170, v189, v197
	v_pk_fma_f32 v[170:171], v[186:187], v[196:197], v[170:171] op_sel_hi:[1,1,0]
; __device__ __forceinline__ int cslot(int bh, int c) { return (c + bh) & 31; }
; template <int GRP>
; __device__ __forceinline__ void y_phase(Frame& F, const MW& W) {
;     ...
;         for (int c = 0; c < 32; ++c) {
;             u32x2 o; o.x = pg8::pack_fp8x4(C[0], C[1], C[2], C[3]); o.y = pg8::pack_fp8x4(C[4], C[5], C[6], C[7]); *(u32x2*)(W.CP + off + (size_t)cslot(bh, c) * 16384) = o;
;             const float bl = sc[2 * c], am = sc[2 * c + 1], mn = fmaxf(bl + m, am), dec = __expf(bl + m - mn), inj = __expf(am - mn);
;             const auto x0 = __builtin_amdgcn_cvt_pk_f32_fp8((int)v[c].x, false), x1 = __builtin_amdgcn_cvt_pk_f32_fp8((int)v[c].x, true), x2 = __builtin_amdgcn_cvt_pk_f32_fp8((int)v[c].y, false), x3 = __builtin_amdgcn_cvt_pk_f32_fp8((int)v[c].y, true);
;             C[0] = C[0] * dec + x0[0] * inj; C[1] = C[1] * dec + x0[1] * inj; C[2] = C[2] * dec + x1[0] * inj; C[3] = C[3] * dec + x1[1] * inj;
;             C[4] = C[4] * dec + x2[0] * inj; C[5] = C[5] * dec + x2[1] * inj; C[6] = C[6] * dec + x3[0] * inj; C[7] = C[7] * dec + x3[1] * inj; m = mn; }
	v_mov_b32_e32 v185, v189
	v_mov_b32_e32 v186, v188
	v_mov_b32_e32 v187, v198
	v_mul_f32_e32 v190, v189, v198
	v_pk_fma_f32 v[184:185], v[184:185], v[186:187], v[190:191] op_sel_hi:[1,1,0]
	v_mov_b32_e32 v183, v189
	v_mov_b32_e32 v198, v188
	v_mul_f32_e32 v186, v189, v199
	v_pk_fma_f32 v[182:183], v[182:183], v[198:199], v[186:187] op_sel_hi:[1,1,0]
	v_med3_f32 v1, v180, s17, v231
	v_med3_f32 v171, v178, s17, v231
	v_mov_b32_e32 v186, v137
	v_cvt_pk_fp8_f32 v186, v1, v171
	v_med3_f32 v1, v172, s17, v231
	v_med3_f32 v171, v170, s17, v231
	v_mov_b32_e32 v187, v137
	v_cvt_pk_fp8_f32 v187, v1, v171
	v_med3_f32 v173, v176, s17, v231
	v_med3_f32 v175, v174, s17, v231
	v_cvt_pk_fp8_f32 v186, v173, v175 op_sel:[0,0,1]
	v_med3_f32 v173, v184, s17, v231
	v_med3_f32 v175, v182, s17, v231
	v_cvt_pk_fp8_f32 v187, v173, v175 op_sel:[0,0,1]
	v_lshl_add_u64 v[188:189], v[126:127], 0, s[80:81]
	v_cvt_pk_f32_fp8_sdwa v[190:191], v168 src0_sel:WORD_1
	v_cvt_pk_f32_fp8_e32 v[192:193], v169
	global_store_dwordx2 v[188:189], v[186:187], off
	v_readlane_b32 s100, v252, 19
	s_nop 1
	v_mov_b32_e32 v186, s100
	v_readlane_b32 s100, v253, 19
	s_nop 1
	v_mov_b32_e32 v187, s100
	v_cvt_pk_f32_fp8_e32 v[188:189], v168
	v_cvt_pk_f32_fp8_sdwa v[196:197], v169 src0_sel:WORD_1
	v_mov_b32_e32 v177, v190
	v_mov_b32_e32 v175, v191
	v_mov_b32_e32 v181, v188
	v_mov_b32_e32 v179, v189
	v_add_f32_e32 v1, v195, v186
	v_max_f32_e32 v171, v187, v187
	v_max_f32_e32 v195, v1, v171
	v_sub_f32_e32 v1, v1, v195
	v_mul_f32_e32 v1, 0x3fb8aa3b, v1
	v_exp_f32_e32 v186, v1
	v_sub_f32_e32 v1, v187, v195
	v_mul_f32_e32 v1, 0x3fb8aa3b, v1
	v_exp_f32_e32 v187, v1
	s_nop 0
	v_mul_f32_e32 v168, v188, v187
	v_pk_fma_f32 v[180:181], v[180:181], v[186:187], v[168:169] op_sel_hi:[1,1,0]
	v_mul_f32_e32 v168, v189, v187
	v_pk_fma_f32 v[178:179], v[178:179], v[186:187], v[168:169] op_sel_hi:[1,1,0]
	v_mul_f32_e32 v168, v190, v187
	v_pk_fma_f32 v[176:177], v[176:177], v[186:187], v[168:169] op_sel_hi:[1,1,0]
	v_mul_f32_e32 v168, v191, v187
	v_pk_fma_f32 v[174:175], v[174:175], v[186:187], v[168:169] op_sel_hi:[1,1,0]
	v_mov_b32_e32 v173, v187
	v_mov_b32_e32 v168, v186
	v_mov_b32_e32 v169, v192
	v_mul_f32_e32 v188, v187, v192
	v_pk_fma_f32 v[172:173], v[172:173], v[168:169], v[188:189] op_sel_hi:[1,1,0]
	v_mov_b32_e32 v171, v187
	v_mov_b32_e32 v192, v186
	v_mul_f32_e32 v168, v187, v193
	v_pk_fma_f32 v[170:171], v[170:171], v[192:193], v[168:169] op_sel_hi:[1,1,0]
	v_mov_b32_e32 v185, v187
	v_mov_b32_e32 v168, v186
	v_mov_b32_e32 v169, v196
	v_mul_f32_e32 v188, v187, v196
	v_pk_fma_f32 v[168:169], v[184:185], v[168:169], v[188:189] op_sel_hi:[1,1,0]
	v_mov_b32_e32 v183, v187
	v_mov_b32_e32 v196, v186
	v_mul_f32_e32 v184, v187, v197
	v_pk_fma_f32 v[182:183], v[182:183], v[196:197], v[184:185] op_sel_hi:[1,1,0]
	v_med3_f32 v1, v180, s17, v231
	v_med3_f32 v169, v178, s17, v231
	v_mov_b32_e32 v184, v137
	v_cvt_pk_fp8_f32 v184, v1, v169
	v_med3_f32 v1, v172, s17, v231
	v_med3_f32 v169, v170, s17, v231
	v_mov_b32_e32 v185, v137
	v_cvt_pk_fp8_f32 v185, v1, v169
	v_med3_f32 v171, v176, s17, v231
	v_med3_f32 v173, v174, s17, v231
	v_cvt_pk_fp8_f32 v184, v171, v173 op_sel:[0,0,1]
	v_med3_f32 v171, v168, s17, v231
	v_med3_f32 v173, v182, s17, v231
	v_cvt_pk_fp8_f32 v185, v171, v173 op_sel:[0,0,1]
	v_lshl_add_u64 v[186:187], v[126:127], 0, s[78:79]
	v_cvt_pk_f32_fp8_sdwa v[188:189], v166 src0_sel:WORD_1
	v_cvt_pk_f32_fp8_e32 v[190:191], v167
	global_store_dwordx2 v[186:187], v[184:185], off
	v_readlane_b32 s100, v252, 20
	s_nop 1
	v_mov_b32_e32 v184, s100
	v_readlane_b32 s100, v253, 20
	s_nop 1
	v_mov_b32_e32 v185, s100
	v_cvt_pk_f32_fp8_e32 v[186:187], v166
	v_cvt_pk_f32_fp8_sdwa v[166:167], v167 src0_sel:WORD_1
	v_mov_b32_e32 v177, v188
	v_mov_b32_e32 v175, v189
	v_mov_b32_e32 v181, v186
	v_mov_b32_e32 v179, v187
	v_add_f32_e32 v1, v195, v184
	v_max_f32_e32 v169, v185, v185
	v_max_f32_e32 v192, v1, v169
	v_sub_f32_e32 v1, v1, v192
	v_mul_f32_e32 v1, 0x3fb8aa3b, v1
	v_exp_f32_e32 v184, v1
	v_sub_f32_e32 v1, v185, v192
	v_mul_f32_e32 v1, 0x3fb8aa3b, v1
	v_exp_f32_e32 v185, v1
	s_nop 0
	v_mul_f32_e32 v186, v186, v185
	v_pk_fma_f32 v[180:181], v[180:181], v[184:185], v[186:187] op_sel_hi:[1,1,0]
	v_mul_f32_e32 v186, v187, v185
	v_pk_fma_f32 v[178:179], v[178:179], v[184:185], v[186:187] op_sel_hi:[1,1,0]
	v_mul_f32_e32 v186, v188, v185
	v_pk_fma_f32 v[176:177], v[176:177], v[184:185], v[186:187] op_sel_hi:[1,1,0]
	v_mul_f32_e32 v186, v189, v185
	v_pk_fma_f32 v[174:175], v[174:175], v[184:185], v[186:187] op_sel_hi:[1,1,0]
	v_mov_b32_e32 v173, v185
	v_mov_b32_e32 v186, v184
	v_mov_b32_e32 v187, v190
	v_mul_f32_e32 v188, v185, v190
	v_pk_fma_f32 v[172:173], v[172:173], v[186:187], v[188:189] op_sel_hi:[1,1,0]
	v_mov_b32_e32 v171, v185
	v_mov_b32_e32 v190, v184
	v_mul_f32_e32 v186, v185, v191
	v_pk_fma_f32 v[170:171], v[170:171], v[190:191], v[186:187] op_sel_hi:[1,1,0]
	v_mov_b32_e32 v169, v185
	v_mov_b32_e32 v186, v184
	v_mov_b32_e32 v187, v166
	v_mul_f32_e32 v166, v185, v166
	v_pk_fma_f32 v[168:169], v[168:169], v[186:187], v[166:167] op_sel_hi:[1,1,0]
	v_mov_b32_e32 v183, v185
	v_mov_b32_e32 v166, v184
	v_mul_f32_e32 v184, v185, v167
	v_pk_fma_f32 v[166:167], v[182:183], v[166:167], v[184:185] op_sel_hi:[1,1,0]
	v_med3_f32 v1, v180, s17, v231
	v_med3_f32 v167, v178, s17, v231
	v_mov_b32_e32 v182, v137
	v_cvt_pk_fp8_f32 v182, v1, v167
	v_med3_f32 v1, v172, s17, v231
	v_med3_f32 v167, v170, s17, v231
	v_mov_b32_e32 v183, v137
	v_cvt_pk_fp8_f32 v183, v1, v167
	v_med3_f32 v169, v176, s17, v231
	v_med3_f32 v171, v174, s17, v231
	v_cvt_pk_fp8_f32 v182, v169, v171 op_sel:[0,0,1]
	v_med3_f32 v169, v168, s17, v231
; __device__ __forceinline__ int cslot(int bh, int c) { return (c + bh) & 31; }
; template <int GRP>
; __device__ __forceinline__ void y_phase(Frame& F, const MW& W) {
;     ...
;         for (int c = 0; c < 32; ++c) {
;             u32x2 o; o.x = pg8::pack_fp8x4(C[0], C[1], C[2], C[3]); o.y = pg8::pack_fp8x4(C[4], C[5], C[6], C[7]); *(u32x2*)(W.CP + off + (size_t)cslot(bh, c) * 16384) = o;
;             const float bl = sc[2 * c], am = sc[2 * c + 1], mn = fmaxf(bl + m, am), dec = __expf(bl + m - mn), inj = __expf(am - mn);
;             const auto x0 = __builtin_amdgcn_cvt_pk_f32_fp8((int)v[c].x, false), x1 = __builtin_amdgcn_cvt_pk_f32_fp8((int)v[c].x, true), x2 = __builtin_amdgcn_cvt_pk_f32_fp8((int)v[c].y, false), x3 = __builtin_amdgcn_cvt_pk_f32_fp8((int)v[c].y, true);
;             C[0] = C[0] * dec + x0[0] * inj; C[1] = C[1] * dec + x0[1] * inj; C[2] = C[2] * dec + x1[0] * inj; C[3] = C[3] * dec + x1[1] * inj;
;             C[4] = C[4] * dec + x2[0] * inj; C[5] = C[5] * dec + x2[1] * inj; C[6] = C[6] * dec + x3[0] * inj; C[7] = C[7] * dec + x3[1] * inj; m = mn; }
	v_med3_f32 v171, v166, s17, v231
	v_cvt_pk_fp8_f32 v183, v169, v171 op_sel:[0,0,1]
	v_lshl_add_u64 v[184:185], v[126:127], 0, s[76:77]
	v_cvt_pk_f32_fp8_sdwa v[186:187], v164 src0_sel:WORD_1
	v_cvt_pk_f32_fp8_e32 v[188:189], v165
	global_store_dwordx2 v[184:185], v[182:183], off
	v_readlane_b32 s100, v252, 21
	s_nop 1
	v_mov_b32_e32 v182, s100
	v_readlane_b32 s100, v253, 21
	s_nop 1
	v_mov_b32_e32 v183, s100
	v_cvt_pk_f32_fp8_e32 v[184:185], v164
	v_cvt_pk_f32_fp8_sdwa v[190:191], v165 src0_sel:WORD_1
	v_mov_b32_e32 v177, v186
	v_mov_b32_e32 v175, v187
	v_mov_b32_e32 v181, v184
	v_mov_b32_e32 v179, v185
	v_add_f32_e32 v1, v192, v182
	v_max_f32_e32 v167, v183, v183
	v_max_f32_e32 v192, v1, v167
	v_sub_f32_e32 v1, v1, v192
	v_mul_f32_e32 v1, 0x3fb8aa3b, v1
	v_exp_f32_e32 v182, v1
	v_sub_f32_e32 v1, v183, v192
	v_mul_f32_e32 v1, 0x3fb8aa3b, v1
	v_exp_f32_e32 v183, v1
	s_nop 0
	v_mul_f32_e32 v164, v184, v183
	v_pk_fma_f32 v[164:165], v[180:181], v[182:183], v[164:165] op_sel_hi:[1,1,0]
	v_mul_f32_e32 v180, v185, v183
	v_pk_fma_f32 v[178:179], v[178:179], v[182:183], v[180:181] op_sel_hi:[1,1,0]
	v_mul_f32_e32 v180, v186, v183
	v_pk_fma_f32 v[176:177], v[176:177], v[182:183], v[180:181] op_sel_hi:[1,1,0]
	v_mul_f32_e32 v180, v187, v183
	v_pk_fma_f32 v[174:175], v[174:175], v[182:183], v[180:181] op_sel_hi:[1,1,0]
	v_mov_b32_e32 v173, v183
	v_mov_b32_e32 v180, v182
	v_mov_b32_e32 v181, v188
	v_mul_f32_e32 v184, v183, v188
	v_pk_fma_f32 v[172:173], v[172:173], v[180:181], v[184:185] op_sel_hi:[1,1,0]
	v_mov_b32_e32 v171, v183
	v_mov_b32_e32 v188, v182
	v_mul_f32_e32 v180, v183, v189
	v_pk_fma_f32 v[170:171], v[170:171], v[188:189], v[180:181] op_sel_hi:[1,1,0]
	v_mov_b32_e32 v169, v183
	v_mov_b32_e32 v180, v182
	v_mov_b32_e32 v181, v190
	v_mul_f32_e32 v184, v183, v190
	v_pk_fma_f32 v[168:169], v[168:169], v[180:181], v[184:185] op_sel_hi:[1,1,0]
	v_mov_b32_e32 v167, v183
	v_mov_b32_e32 v190, v182
	v_mul_f32_e32 v180, v183, v191
	v_pk_fma_f32 v[166:167], v[166:167], v[190:191], v[180:181] op_sel_hi:[1,1,0]
	v_med3_f32 v1, v164, s17, v231
	v_med3_f32 v165, v178, s17, v231
	v_mov_b32_e32 v180, v137
	v_cvt_pk_fp8_f32 v180, v1, v165
	v_med3_f32 v1, v172, s17, v231
	v_med3_f32 v165, v170, s17, v231
	v_mov_b32_e32 v181, v137
	v_cvt_pk_fp8_f32 v181, v1, v165
	v_med3_f32 v167, v176, s17, v231
	v_med3_f32 v169, v174, s17, v231
	v_cvt_pk_fp8_f32 v180, v167, v169 op_sel:[0,0,1]
	v_med3_f32 v167, v168, s17, v231
	v_med3_f32 v169, v166, s17, v231
	v_cvt_pk_fp8_f32 v181, v167, v169 op_sel:[0,0,1]
	v_lshl_add_u64 v[182:183], v[126:127], 0, s[46:47]
	v_cvt_pk_f32_fp8_sdwa v[184:185], v162 src0_sel:WORD_1
	v_cvt_pk_f32_fp8_e32 v[186:187], v163
	global_store_dwordx2 v[182:183], v[180:181], off
	v_readlane_b32 s100, v252, 22
	s_nop 1
	v_mov_b32_e32 v180, s100
	v_readlane_b32 s100, v253, 22
	s_nop 1
	v_mov_b32_e32 v181, s100
	v_cvt_pk_f32_fp8_e32 v[182:183], v162
	v_cvt_pk_f32_fp8_sdwa v[188:189], v163 src0_sel:WORD_1
	v_mov_b32_e32 v177, v184
	v_mov_b32_e32 v175, v185
	v_mov_b32_e32 v179, v183
	v_add_f32_e32 v1, v192, v180
	v_max_f32_e32 v165, v181, v181
	v_max_f32_e32 v190, v1, v165
	v_sub_f32_e32 v1, v1, v190
	v_mul_f32_e32 v1, 0x3fb8aa3b, v1
	v_exp_f32_e32 v180, v1
	v_sub_f32_e32 v1, v181, v190
	v_mul_f32_e32 v1, 0x3fb8aa3b, v1
	v_exp_f32_e32 v181, v1
	v_mov_b32_e32 v165, v182
	v_mul_f32_e32 v162, v182, v181
	v_pk_fma_f32 v[164:165], v[164:165], v[180:181], v[162:163] op_sel_hi:[1,1,0]
	v_mul_f32_e32 v162, v183, v181
	v_pk_fma_f32 v[162:163], v[178:179], v[180:181], v[162:163] op_sel_hi:[1,1,0]
	v_mul_f32_e32 v178, v184, v181
	v_pk_fma_f32 v[176:177], v[176:177], v[180:181], v[178:179] op_sel_hi:[1,1,0]
	v_mul_f32_e32 v178, v185, v181
	v_pk_fma_f32 v[174:175], v[174:175], v[180:181], v[178:179] op_sel_hi:[1,1,0]
	v_mov_b32_e32 v173, v181
	v_mov_b32_e32 v178, v180
	v_mov_b32_e32 v179, v186
	v_mul_f32_e32 v182, v181, v186
	v_pk_fma_f32 v[172:173], v[172:173], v[178:179], v[182:183] op_sel_hi:[1,1,0]
	v_mov_b32_e32 v171, v181
	v_mov_b32_e32 v186, v180
	v_mul_f32_e32 v178, v181, v187
	v_pk_fma_f32 v[170:171], v[170:171], v[186:187], v[178:179] op_sel_hi:[1,1,0]
	v_mov_b32_e32 v169, v181
	v_mov_b32_e32 v178, v180
	v_mov_b32_e32 v179, v188
	v_mul_f32_e32 v182, v181, v188
	v_pk_fma_f32 v[168:169], v[168:169], v[178:179], v[182:183] op_sel_hi:[1,1,0]
	v_mov_b32_e32 v167, v181
	v_mov_b32_e32 v188, v180
	v_mul_f32_e32 v178, v181, v189
	v_pk_fma_f32 v[166:167], v[166:167], v[188:189], v[178:179] op_sel_hi:[1,1,0]
	v_med3_f32 v1, v164, s17, v231
	v_med3_f32 v163, v162, s17, v231
	v_mov_b32_e32 v178, v137
	v_cvt_pk_fp8_f32 v178, v1, v163
	v_med3_f32 v1, v172, s17, v231
	v_med3_f32 v163, v170, s17, v231
	v_mov_b32_e32 v179, v137
	v_cvt_pk_fp8_f32 v179, v1, v163
	v_med3_f32 v165, v176, s17, v231
	v_med3_f32 v167, v174, s17, v231
	v_cvt_pk_fp8_f32 v178, v165, v167 op_sel:[0,0,1]
	v_med3_f32 v165, v168, s17, v231
	v_med3_f32 v167, v166, s17, v231
	v_cvt_pk_fp8_f32 v179, v165, v167 op_sel:[0,0,1]
	v_lshl_add_u64 v[180:181], v[126:127], 0, s[44:45]
	v_cvt_pk_f32_fp8_sdwa v[182:183], v160 src0_sel:WORD_1
	v_cvt_pk_f32_fp8_e32 v[184:185], v161
	global_store_dwordx2 v[180:181], v[178:179], off
	v_readlane_b32 s100, v252, 23
	s_nop 1
	v_mov_b32_e32 v178, s100
	v_readlane_b32 s100, v253, 23
	s_nop 1
	v_mov_b32_e32 v179, s100
	v_cvt_pk_f32_fp8_e32 v[180:181], v160
	v_cvt_pk_f32_fp8_sdwa v[186:187], v161 src0_sel:WORD_1
	v_mov_b32_e32 v177, v182
	v_mov_b32_e32 v175, v183
	v_mov_b32_e32 v165, v180
	v_add_f32_e32 v1, v190, v178
	v_max_f32_e32 v163, v179, v179
	v_max_f32_e32 v188, v1, v163
	v_sub_f32_e32 v1, v1, v188
	v_mul_f32_e32 v1, 0x3fb8aa3b, v1
	v_exp_f32_e32 v178, v1
; __device__ __forceinline__ int cslot(int bh, int c) { return (c + bh) & 31; }
; template <int GRP>
; __device__ __forceinline__ void y_phase(Frame& F, const MW& W) {
;     ...
;         for (int c = 0; c < 32; ++c) {
;             u32x2 o; o.x = pg8::pack_fp8x4(C[0], C[1], C[2], C[3]); o.y = pg8::pack_fp8x4(C[4], C[5], C[6], C[7]); *(u32x2*)(W.CP + off + (size_t)cslot(bh, c) * 16384) = o;
;             const float bl = sc[2 * c], am = sc[2 * c + 1], mn = fmaxf(bl + m, am), dec = __expf(bl + m - mn), inj = __expf(am - mn);
;             const auto x0 = __builtin_amdgcn_cvt_pk_f32_fp8((int)v[c].x, false), x1 = __builtin_amdgcn_cvt_pk_f32_fp8((int)v[c].x, true), x2 = __builtin_amdgcn_cvt_pk_f32_fp8((int)v[c].y, false), x3 = __builtin_amdgcn_cvt_pk_f32_fp8((int)v[c].y, true);
;             C[0] = C[0] * dec + x0[0] * inj; C[1] = C[1] * dec + x0[1] * inj; C[2] = C[2] * dec + x1[0] * inj; C[3] = C[3] * dec + x1[1] * inj;
;             C[4] = C[4] * dec + x2[0] * inj; C[5] = C[5] * dec + x2[1] * inj; C[6] = C[6] * dec + x3[0] * inj; C[7] = C[7] * dec + x3[1] * inj; m = mn; }
	v_sub_f32_e32 v1, v179, v188
	v_mul_f32_e32 v1, 0x3fb8aa3b, v1
	v_exp_f32_e32 v179, v1
	v_mov_b32_e32 v163, v181
	v_mul_f32_e32 v160, v180, v179
	v_pk_fma_f32 v[164:165], v[164:165], v[178:179], v[160:161] op_sel_hi:[1,1,0]
	v_mul_f32_e32 v160, v181, v179
	v_pk_fma_f32 v[162:163], v[162:163], v[178:179], v[160:161] op_sel_hi:[1,1,0]
	v_mul_f32_e32 v160, v182, v179
	v_pk_fma_f32 v[160:161], v[176:177], v[178:179], v[160:161] op_sel_hi:[1,1,0]
	v_mul_f32_e32 v176, v183, v179
	v_pk_fma_f32 v[174:175], v[174:175], v[178:179], v[176:177] op_sel_hi:[1,1,0]
	v_mov_b32_e32 v173, v179
	v_mov_b32_e32 v176, v178
	v_mov_b32_e32 v177, v184
	v_mul_f32_e32 v180, v179, v184
	v_pk_fma_f32 v[172:173], v[172:173], v[176:177], v[180:181] op_sel_hi:[1,1,0]
	v_mov_b32_e32 v171, v179
	v_mov_b32_e32 v184, v178
	v_mul_f32_e32 v176, v179, v185
	v_pk_fma_f32 v[170:171], v[170:171], v[184:185], v[176:177] op_sel_hi:[1,1,0]
	v_mov_b32_e32 v169, v179
	v_mov_b32_e32 v176, v178
	v_mov_b32_e32 v177, v186
	v_mul_f32_e32 v180, v179, v186
	v_pk_fma_f32 v[168:169], v[168:169], v[176:177], v[180:181] op_sel_hi:[1,1,0]
	v_mov_b32_e32 v167, v179
	v_mov_b32_e32 v186, v178
	v_mul_f32_e32 v176, v179, v187
	v_pk_fma_f32 v[166:167], v[166:167], v[186:187], v[176:177] op_sel_hi:[1,1,0]
	v_med3_f32 v1, v164, s17, v231
	v_med3_f32 v161, v162, s17, v231
	v_mov_b32_e32 v176, v137
	v_cvt_pk_fp8_f32 v176, v1, v161
	v_med3_f32 v1, v172, s17, v231
	v_med3_f32 v161, v170, s17, v231
	v_mov_b32_e32 v177, v137
	v_cvt_pk_fp8_f32 v177, v1, v161
	v_med3_f32 v163, v160, s17, v231
	v_med3_f32 v165, v174, s17, v231
	v_cvt_pk_fp8_f32 v176, v163, v165 op_sel:[0,0,1]
	v_med3_f32 v163, v168, s17, v231
	v_med3_f32 v165, v166, s17, v231
	v_cvt_pk_fp8_f32 v177, v163, v165 op_sel:[0,0,1]
	v_lshl_add_u64 v[178:179], v[126:127], 0, s[42:43]
	v_cvt_pk_f32_fp8_sdwa v[180:181], v158 src0_sel:WORD_1
	v_cvt_pk_f32_fp8_e32 v[182:183], v159
	global_store_dwordx2 v[178:179], v[176:177], off
	v_readlane_b32 s100, v252, 24
	s_nop 1
	v_mov_b32_e32 v176, s100
	v_readlane_b32 s100, v253, 24
	s_nop 1
	v_mov_b32_e32 v177, s100
	v_cvt_pk_f32_fp8_e32 v[178:179], v158
	v_cvt_pk_f32_fp8_sdwa v[184:185], v159 src0_sel:WORD_1
	v_mov_b32_e32 v175, v181
	v_mov_b32_e32 v165, v178
	v_mov_b32_e32 v163, v179
	v_add_f32_e32 v1, v188, v176
	v_max_f32_e32 v161, v177, v177
	v_max_f32_e32 v186, v1, v161
	v_sub_f32_e32 v1, v1, v186
	v_mul_f32_e32 v1, 0x3fb8aa3b, v1
	v_exp_f32_e32 v176, v1
	v_sub_f32_e32 v1, v177, v186
	v_mul_f32_e32 v1, 0x3fb8aa3b, v1
	v_exp_f32_e32 v177, v1
	v_mov_b32_e32 v161, v180
	v_mul_f32_e32 v158, v178, v177
	v_pk_fma_f32 v[164:165], v[164:165], v[176:177], v[158:159] op_sel_hi:[1,1,0]
	v_mul_f32_e32 v158, v179, v177
	v_pk_fma_f32 v[162:163], v[162:163], v[176:177], v[158:159] op_sel_hi:[1,1,0]
	v_mul_f32_e32 v158, v180, v177
	v_pk_fma_f32 v[160:161], v[160:161], v[176:177], v[158:159] op_sel_hi:[1,1,0]
	v_mul_f32_e32 v158, v181, v177
	v_pk_fma_f32 v[158:159], v[174:175], v[176:177], v[158:159] op_sel_hi:[1,1,0]
	v_mov_b32_e32 v173, v177
	v_mov_b32_e32 v174, v176
	v_mov_b32_e32 v175, v182
	v_mul_f32_e32 v178, v177, v182
	v_pk_fma_f32 v[172:173], v[172:173], v[174:175], v[178:179] op_sel_hi:[1,1,0]
	v_mov_b32_e32 v171, v177
	v_mov_b32_e32 v182, v176
	v_mul_f32_e32 v174, v177, v183
	v_pk_fma_f32 v[170:171], v[170:171], v[182:183], v[174:175] op_sel_hi:[1,1,0]
	v_mov_b32_e32 v169, v177
	v_mov_b32_e32 v174, v176
	v_mov_b32_e32 v175, v184
	v_mul_f32_e32 v178, v177, v184
	v_pk_fma_f32 v[168:169], v[168:169], v[174:175], v[178:179] op_sel_hi:[1,1,0]
	v_mov_b32_e32 v167, v177
	v_mov_b32_e32 v184, v176
	v_mul_f32_e32 v174, v177, v185
	v_pk_fma_f32 v[166:167], v[166:167], v[184:185], v[174:175] op_sel_hi:[1,1,0]
	v_med3_f32 v1, v164, s17, v231
	v_med3_f32 v159, v162, s17, v231
	v_mov_b32_e32 v174, v137
	v_cvt_pk_fp8_f32 v174, v1, v159
	v_med3_f32 v1, v172, s17, v231
	v_med3_f32 v159, v170, s17, v231
	v_mov_b32_e32 v175, v137
	v_cvt_pk_fp8_f32 v175, v1, v159
	v_med3_f32 v161, v160, s17, v231
	v_med3_f32 v163, v158, s17, v231
	v_cvt_pk_fp8_f32 v174, v161, v163 op_sel:[0,0,1]
	v_med3_f32 v161, v168, s17, v231
	v_med3_f32 v163, v166, s17, v231
	v_cvt_pk_fp8_f32 v175, v161, v163 op_sel:[0,0,1]
	v_lshl_add_u64 v[176:177], v[126:127], 0, s[40:41]
	v_cvt_pk_f32_fp8_sdwa v[178:179], v156 src0_sel:WORD_1
	v_cvt_pk_f32_fp8_e32 v[180:181], v157
	global_store_dwordx2 v[176:177], v[174:175], off
	v_readlane_b32 s100, v252, 25
	s_nop 1
	v_mov_b32_e32 v174, s100
	v_readlane_b32 s100, v253, 25
	s_nop 1
	v_mov_b32_e32 v175, s100
	v_cvt_pk_f32_fp8_e32 v[176:177], v156
	v_cvt_pk_f32_fp8_sdwa v[182:183], v157 src0_sel:WORD_1
	v_mov_b32_e32 v161, v178
	v_mov_b32_e32 v165, v176
	v_mov_b32_e32 v163, v177
	v_add_f32_e32 v1, v186, v174
	v_max_f32_e32 v159, v175, v175
	v_max_f32_e32 v184, v1, v159
	v_sub_f32_e32 v1, v1, v184
	v_mul_f32_e32 v1, 0x3fb8aa3b, v1
	v_exp_f32_e32 v174, v1
	v_sub_f32_e32 v1, v175, v184
	v_mul_f32_e32 v1, 0x3fb8aa3b, v1
	v_exp_f32_e32 v175, v1
	v_mov_b32_e32 v159, v179
	v_mul_f32_e32 v156, v176, v175
	v_pk_fma_f32 v[164:165], v[164:165], v[174:175], v[156:157] op_sel_hi:[1,1,0]
	v_mul_f32_e32 v156, v177, v175
	v_pk_fma_f32 v[162:163], v[162:163], v[174:175], v[156:157] op_sel_hi:[1,1,0]
	v_mul_f32_e32 v156, v178, v175
	v_pk_fma_f32 v[160:161], v[160:161], v[174:175], v[156:157] op_sel_hi:[1,1,0]
	v_mul_f32_e32 v156, v179, v175
	v_pk_fma_f32 v[158:159], v[158:159], v[174:175], v[156:157] op_sel_hi:[1,1,0]
	v_mov_b32_e32 v173, v175
	v_mov_b32_e32 v156, v174
	v_mov_b32_e32 v157, v180
	v_mul_f32_e32 v176, v175, v180
	v_pk_fma_f32 v[156:157], v[172:173], v[156:157], v[176:177] op_sel_hi:[1,1,0]
	v_mov_b32_e32 v171, v175
; __device__ __forceinline__ int cslot(int bh, int c) { return (c + bh) & 31; }
; template <int GRP>
; __device__ __forceinline__ void y_phase(Frame& F, const MW& W) {
;     ...
;         for (int c = 0; c < 32; ++c) {
;             u32x2 o; o.x = pg8::pack_fp8x4(C[0], C[1], C[2], C[3]); o.y = pg8::pack_fp8x4(C[4], C[5], C[6], C[7]); *(u32x2*)(W.CP + off + (size_t)cslot(bh, c) * 16384) = o;
;             const float bl = sc[2 * c], am = sc[2 * c + 1], mn = fmaxf(bl + m, am), dec = __expf(bl + m - mn), inj = __expf(am - mn);
;             const auto x0 = __builtin_amdgcn_cvt_pk_f32_fp8((int)v[c].x, false), x1 = __builtin_amdgcn_cvt_pk_f32_fp8((int)v[c].x, true), x2 = __builtin_amdgcn_cvt_pk_f32_fp8((int)v[c].y, false), x3 = __builtin_amdgcn_cvt_pk_f32_fp8((int)v[c].y, true);
;             C[0] = C[0] * dec + x0[0] * inj; C[1] = C[1] * dec + x0[1] * inj; C[2] = C[2] * dec + x1[0] * inj; C[3] = C[3] * dec + x1[1] * inj;
;             C[4] = C[4] * dec + x2[0] * inj; C[5] = C[5] * dec + x2[1] * inj; C[6] = C[6] * dec + x3[0] * inj; C[7] = C[7] * dec + x3[1] * inj; m = mn; }
	v_mov_b32_e32 v180, v174
	v_mul_f32_e32 v172, v175, v181
	v_pk_fma_f32 v[170:171], v[170:171], v[180:181], v[172:173] op_sel_hi:[1,1,0]
	v_mov_b32_e32 v169, v175
	v_mov_b32_e32 v172, v174
	v_mov_b32_e32 v173, v182
	v_mul_f32_e32 v176, v175, v182
	v_pk_fma_f32 v[168:169], v[168:169], v[172:173], v[176:177] op_sel_hi:[1,1,0]
	v_mov_b32_e32 v167, v175
	v_mov_b32_e32 v182, v174
	v_mul_f32_e32 v172, v175, v183
	v_pk_fma_f32 v[166:167], v[166:167], v[182:183], v[172:173] op_sel_hi:[1,1,0]
	v_med3_f32 v1, v164, s17, v231
	v_med3_f32 v157, v162, s17, v231
	v_mov_b32_e32 v172, v137
	v_cvt_pk_fp8_f32 v172, v1, v157
	v_med3_f32 v1, v156, s17, v231
	v_med3_f32 v157, v170, s17, v231
	v_mov_b32_e32 v173, v137
	v_cvt_pk_fp8_f32 v173, v1, v157
	v_med3_f32 v159, v160, s17, v231
	v_med3_f32 v161, v158, s17, v231
	v_cvt_pk_fp8_f32 v172, v159, v161 op_sel:[0,0,1]
	v_med3_f32 v159, v168, s17, v231
	v_med3_f32 v161, v166, s17, v231
	v_cvt_pk_fp8_f32 v173, v159, v161 op_sel:[0,0,1]
	v_lshl_add_u64 v[174:175], v[126:127], 0, s[38:39]
	v_cvt_pk_f32_fp8_sdwa v[176:177], v154 src0_sel:WORD_1
	v_cvt_pk_f32_fp8_e32 v[178:179], v155
	global_store_dwordx2 v[174:175], v[172:173], off
	v_readlane_b32 s100, v252, 26
	s_nop 1
	v_mov_b32_e32 v172, s100
	v_readlane_b32 s100, v253, 26
	s_nop 1
	v_mov_b32_e32 v173, s100
	v_cvt_pk_f32_fp8_e32 v[174:175], v154
	v_cvt_pk_f32_fp8_sdwa v[180:181], v155 src0_sel:WORD_1
	v_mov_b32_e32 v161, v176
	v_mov_b32_e32 v159, v177
	v_mov_b32_e32 v165, v174
	v_mov_b32_e32 v163, v175
	v_add_f32_e32 v1, v184, v172
	v_max_f32_e32 v157, v173, v173
	v_max_f32_e32 v182, v1, v157
	v_sub_f32_e32 v1, v1, v182
	v_mul_f32_e32 v1, 0x3fb8aa3b, v1
	v_exp_f32_e32 v172, v1
	v_sub_f32_e32 v1, v173, v182
	v_mul_f32_e32 v1, 0x3fb8aa3b, v1
	v_exp_f32_e32 v173, v1
	s_nop 0
	v_mul_f32_e32 v154, v174, v173
	v_pk_fma_f32 v[164:165], v[164:165], v[172:173], v[154:155] op_sel_hi:[1,1,0]
	v_mul_f32_e32 v154, v175, v173
	v_pk_fma_f32 v[162:163], v[162:163], v[172:173], v[154:155] op_sel_hi:[1,1,0]
	v_mul_f32_e32 v154, v176, v173
	v_pk_fma_f32 v[160:161], v[160:161], v[172:173], v[154:155] op_sel_hi:[1,1,0]
	v_mul_f32_e32 v154, v177, v173
	v_pk_fma_f32 v[158:159], v[158:159], v[172:173], v[154:155] op_sel_hi:[1,1,0]
	v_mov_b32_e32 v157, v173
	v_mov_b32_e32 v154, v172
	v_mov_b32_e32 v155, v178
	v_mul_f32_e32 v174, v173, v178
	v_pk_fma_f32 v[156:157], v[156:157], v[154:155], v[174:175] op_sel_hi:[1,1,0]
	v_mov_b32_e32 v171, v173
	v_mov_b32_e32 v178, v172
	v_mul_f32_e32 v154, v173, v179
	v_pk_fma_f32 v[154:155], v[170:171], v[178:179], v[154:155] op_sel_hi:[1,1,0]
	v_mov_b32_e32 v169, v173
	v_mov_b32_e32 v170, v172
	v_mov_b32_e32 v171, v180
	v_mul_f32_e32 v174, v173, v180
	v_pk_fma_f32 v[168:169], v[168:169], v[170:171], v[174:175] op_sel_hi:[1,1,0]
	v_mov_b32_e32 v167, v173
	v_mov_b32_e32 v180, v172
	v_mul_f32_e32 v170, v173, v181
	v_pk_fma_f32 v[166:167], v[166:167], v[180:181], v[170:171] op_sel_hi:[1,1,0]
	v_med3_f32 v1, v164, s17, v231
	v_med3_f32 v155, v162, s17, v231
	v_mov_b32_e32 v170, v137
	v_cvt_pk_fp8_f32 v170, v1, v155
	v_med3_f32 v1, v156, s17, v231
	v_med3_f32 v155, v154, s17, v231
	v_mov_b32_e32 v171, v137
	v_cvt_pk_fp8_f32 v171, v1, v155
	v_med3_f32 v157, v160, s17, v231
	v_med3_f32 v159, v158, s17, v231
	v_cvt_pk_fp8_f32 v170, v157, v159 op_sel:[0,0,1]
	v_med3_f32 v157, v168, s17, v231
	v_med3_f32 v159, v166, s17, v231
	v_cvt_pk_fp8_f32 v171, v157, v159 op_sel:[0,0,1]
	v_lshl_add_u64 v[172:173], v[126:127], 0, s[36:37]
	v_cvt_pk_f32_fp8_sdwa v[174:175], v152 src0_sel:WORD_1
	v_cvt_pk_f32_fp8_e32 v[176:177], v153
	global_store_dwordx2 v[172:173], v[170:171], off
	v_readlane_b32 s100, v252, 27
	s_nop 1
	v_mov_b32_e32 v170, s100
	v_readlane_b32 s100, v253, 27
	s_nop 1
	v_mov_b32_e32 v171, s100
	v_cvt_pk_f32_fp8_e32 v[172:173], v152
	v_cvt_pk_f32_fp8_sdwa v[178:179], v153 src0_sel:WORD_1
	v_mov_b32_e32 v161, v174
	v_mov_b32_e32 v159, v175
	v_mov_b32_e32 v165, v172
	v_mov_b32_e32 v163, v173
	v_add_f32_e32 v1, v182, v170
	v_max_f32_e32 v155, v171, v171
	v_max_f32_e32 v180, v1, v155
	v_sub_f32_e32 v1, v1, v180
	v_mul_f32_e32 v1, 0x3fb8aa3b, v1
	v_exp_f32_e32 v170, v1
	v_sub_f32_e32 v1, v171, v180
	v_mul_f32_e32 v1, 0x3fb8aa3b, v1
	v_exp_f32_e32 v171, v1
	s_nop 0
	v_mul_f32_e32 v152, v172, v171
	v_pk_fma_f32 v[164:165], v[164:165], v[170:171], v[152:153] op_sel_hi:[1,1,0]
	v_mul_f32_e32 v152, v173, v171
	v_pk_fma_f32 v[162:163], v[162:163], v[170:171], v[152:153] op_sel_hi:[1,1,0]
	v_mul_f32_e32 v152, v174, v171
	v_pk_fma_f32 v[160:161], v[160:161], v[170:171], v[152:153] op_sel_hi:[1,1,0]
	v_mul_f32_e32 v152, v175, v171
	v_pk_fma_f32 v[158:159], v[158:159], v[170:171], v[152:153] op_sel_hi:[1,1,0]
	v_mov_b32_e32 v157, v171
	v_mov_b32_e32 v152, v170
	v_mov_b32_e32 v153, v176
	v_mul_f32_e32 v172, v171, v176
	v_pk_fma_f32 v[156:157], v[156:157], v[152:153], v[172:173] op_sel_hi:[1,1,0]
	v_mov_b32_e32 v155, v171
	v_mov_b32_e32 v176, v170
	v_mul_f32_e32 v152, v171, v177
	v_pk_fma_f32 v[154:155], v[154:155], v[176:177], v[152:153] op_sel_hi:[1,1,0]
	v_mov_b32_e32 v169, v171
	v_mov_b32_e32 v152, v170
	v_mov_b32_e32 v153, v178
	v_mul_f32_e32 v172, v171, v178
	v_pk_fma_f32 v[152:153], v[168:169], v[152:153], v[172:173] op_sel_hi:[1,1,0]
	v_mov_b32_e32 v167, v171
	v_mov_b32_e32 v178, v170
	v_mul_f32_e32 v168, v171, v179
	v_pk_fma_f32 v[166:167], v[166:167], v[178:179], v[168:169] op_sel_hi:[1,1,0]
	v_med3_f32 v1, v164, s17, v231
	v_med3_f32 v153, v162, s17, v231
	v_mov_b32_e32 v168, v137
	v_cvt_pk_fp8_f32 v168, v1, v153
	v_med3_f32 v1, v156, s17, v231
	v_med3_f32 v153, v154, s17, v231
	v_mov_b32_e32 v169, v137
	v_cvt_pk_fp8_f32 v169, v1, v153
	v_med3_f32 v155, v160, s17, v231
; __device__ __forceinline__ int cslot(int bh, int c) { return (c + bh) & 31; }
; template <int GRP>
; __device__ __forceinline__ void y_phase(Frame& F, const MW& W) {
;     ...
;         for (int c = 0; c < 32; ++c) {
;             u32x2 o; o.x = pg8::pack_fp8x4(C[0], C[1], C[2], C[3]); o.y = pg8::pack_fp8x4(C[4], C[5], C[6], C[7]); *(u32x2*)(W.CP + off + (size_t)cslot(bh, c) * 16384) = o;
;             const float bl = sc[2 * c], am = sc[2 * c + 1], mn = fmaxf(bl + m, am), dec = __expf(bl + m - mn), inj = __expf(am - mn);
;             const auto x0 = __builtin_amdgcn_cvt_pk_f32_fp8((int)v[c].x, false), x1 = __builtin_amdgcn_cvt_pk_f32_fp8((int)v[c].x, true), x2 = __builtin_amdgcn_cvt_pk_f32_fp8((int)v[c].y, false), x3 = __builtin_amdgcn_cvt_pk_f32_fp8((int)v[c].y, true);
;             C[0] = C[0] * dec + x0[0] * inj; C[1] = C[1] * dec + x0[1] * inj; C[2] = C[2] * dec + x1[0] * inj; C[3] = C[3] * dec + x1[1] * inj;
;             C[4] = C[4] * dec + x2[0] * inj; C[5] = C[5] * dec + x2[1] * inj; C[6] = C[6] * dec + x3[0] * inj; C[7] = C[7] * dec + x3[1] * inj; m = mn; }
	v_med3_f32 v157, v158, s17, v231
	v_cvt_pk_fp8_f32 v168, v155, v157 op_sel:[0,0,1]
	v_med3_f32 v155, v152, s17, v231
	v_med3_f32 v157, v166, s17, v231
	v_cvt_pk_fp8_f32 v169, v155, v157 op_sel:[0,0,1]
	v_lshl_add_u64 v[170:171], v[126:127], 0, s[34:35]
	v_cvt_pk_f32_fp8_sdwa v[172:173], v132 src0_sel:WORD_1
	v_cvt_pk_f32_fp8_e32 v[174:175], v133
	global_store_dwordx2 v[170:171], v[168:169], off
	v_readlane_b32 s100, v252, 28
	s_nop 1
	v_mov_b32_e32 v168, s100
	v_readlane_b32 s100, v253, 28
	s_nop 1
	v_mov_b32_e32 v169, s100
	v_cvt_pk_f32_fp8_e32 v[170:171], v132
	v_cvt_pk_f32_fp8_sdwa v[132:133], v133 src0_sel:WORD_1
	v_mov_b32_e32 v161, v172
	v_mov_b32_e32 v159, v173
	v_mov_b32_e32 v165, v170
	v_mov_b32_e32 v163, v171
	v_add_f32_e32 v1, v180, v168
	v_max_f32_e32 v153, v169, v169
	v_max_f32_e32 v176, v1, v153
	v_sub_f32_e32 v1, v1, v176
	v_mul_f32_e32 v1, 0x3fb8aa3b, v1
	v_exp_f32_e32 v168, v1
	v_sub_f32_e32 v1, v169, v176
	v_mul_f32_e32 v1, 0x3fb8aa3b, v1
	v_exp_f32_e32 v169, v1
	s_nop 0
	v_mul_f32_e32 v170, v170, v169
	v_pk_fma_f32 v[164:165], v[164:165], v[168:169], v[170:171] op_sel_hi:[1,1,0]
	v_mul_f32_e32 v170, v171, v169
	v_pk_fma_f32 v[162:163], v[162:163], v[168:169], v[170:171] op_sel_hi:[1,1,0]
	v_mul_f32_e32 v170, v172, v169
	v_pk_fma_f32 v[160:161], v[160:161], v[168:169], v[170:171] op_sel_hi:[1,1,0]
	v_mul_f32_e32 v170, v173, v169
	v_pk_fma_f32 v[158:159], v[158:159], v[168:169], v[170:171] op_sel_hi:[1,1,0]
	v_mov_b32_e32 v157, v169
	v_mov_b32_e32 v170, v168
	v_mov_b32_e32 v171, v174
	v_mul_f32_e32 v172, v169, v174
	v_pk_fma_f32 v[156:157], v[156:157], v[170:171], v[172:173] op_sel_hi:[1,1,0]
	v_mov_b32_e32 v155, v169
	v_mov_b32_e32 v174, v168
	v_mul_f32_e32 v170, v169, v175
	v_pk_fma_f32 v[154:155], v[154:155], v[174:175], v[170:171] op_sel_hi:[1,1,0]
	v_mov_b32_e32 v153, v169
	v_mov_b32_e32 v170, v168
	v_mov_b32_e32 v171, v132
	v_mul_f32_e32 v132, v169, v132
	v_pk_fma_f32 v[152:153], v[152:153], v[170:171], v[132:133] op_sel_hi:[1,1,0]
	v_mov_b32_e32 v167, v169
	v_mov_b32_e32 v132, v168
	v_mul_f32_e32 v168, v169, v133
	v_pk_fma_f32 v[132:133], v[166:167], v[132:133], v[168:169] op_sel_hi:[1,1,0]
	v_med3_f32 v1, v164, s17, v231
	v_med3_f32 v133, v162, s17, v231
	v_mov_b32_e32 v166, v137
	v_cvt_pk_fp8_f32 v166, v1, v133
	v_med3_f32 v1, v156, s17, v231
	v_med3_f32 v133, v154, s17, v231
	v_mov_b32_e32 v167, v137
	v_cvt_pk_fp8_f32 v167, v1, v133
	v_med3_f32 v153, v160, s17, v231
	v_med3_f32 v155, v158, s17, v231
	v_cvt_pk_fp8_f32 v166, v153, v155 op_sel:[0,0,1]
	v_med3_f32 v153, v152, s17, v231
	v_med3_f32 v155, v132, s17, v231
	v_cvt_pk_fp8_f32 v167, v153, v155 op_sel:[0,0,1]
	v_lshl_add_u64 v[168:169], v[126:127], 0, s[30:31]
	v_cvt_pk_f32_fp8_sdwa v[170:171], v130 src0_sel:WORD_1
	v_cvt_pk_f32_fp8_e32 v[172:173], v131
	global_store_dwordx2 v[168:169], v[166:167], off
	v_readlane_b32 s100, v252, 29
	s_nop 1
	v_mov_b32_e32 v166, s100
	v_readlane_b32 s100, v253, 29
	s_nop 1
	v_mov_b32_e32 v167, s100
	v_cvt_pk_f32_fp8_e32 v[168:169], v130
	v_cvt_pk_f32_fp8_sdwa v[130:131], v131 src0_sel:WORD_1
	v_mov_b32_e32 v161, v170
	v_mov_b32_e32 v159, v171
	v_mov_b32_e32 v165, v168
	v_mov_b32_e32 v163, v169
	v_add_f32_e32 v1, v176, v166
	v_max_f32_e32 v133, v167, v167
	v_max_f32_e32 v174, v1, v133
	v_sub_f32_e32 v1, v1, v174
	v_mul_f32_e32 v1, 0x3fb8aa3b, v1
	v_exp_f32_e32 v166, v1
	v_sub_f32_e32 v1, v167, v174
	v_mul_f32_e32 v1, 0x3fb8aa3b, v1
	v_exp_f32_e32 v167, v1
	s_nop 0
	v_mul_f32_e32 v168, v168, v167
	v_pk_fma_f32 v[164:165], v[164:165], v[166:167], v[168:169] op_sel_hi:[1,1,0]
	v_mul_f32_e32 v168, v169, v167
	v_pk_fma_f32 v[162:163], v[162:163], v[166:167], v[168:169] op_sel_hi:[1,1,0]
	v_mul_f32_e32 v168, v170, v167
	v_pk_fma_f32 v[160:161], v[160:161], v[166:167], v[168:169] op_sel_hi:[1,1,0]
	v_mul_f32_e32 v168, v171, v167
	v_pk_fma_f32 v[158:159], v[158:159], v[166:167], v[168:169] op_sel_hi:[1,1,0]
	v_mov_b32_e32 v157, v167
	v_mov_b32_e32 v168, v166
	v_mov_b32_e32 v169, v172
	v_mul_f32_e32 v170, v167, v172
	v_pk_fma_f32 v[156:157], v[156:157], v[168:169], v[170:171] op_sel_hi:[1,1,0]
	v_mov_b32_e32 v155, v167
	v_mov_b32_e32 v172, v166
	v_mul_f32_e32 v168, v167, v173
	v_pk_fma_f32 v[154:155], v[154:155], v[172:173], v[168:169] op_sel_hi:[1,1,0]
	v_mov_b32_e32 v153, v167
	v_mov_b32_e32 v168, v166
	v_mov_b32_e32 v169, v130
	v_mul_f32_e32 v130, v167, v130
	v_pk_fma_f32 v[152:153], v[152:153], v[168:169], v[130:131] op_sel_hi:[1,1,0]
	v_mov_b32_e32 v133, v167
	v_mov_b32_e32 v130, v166
	v_mul_f32_e32 v166, v167, v131
	v_pk_fma_f32 v[130:131], v[132:133], v[130:131], v[166:167] op_sel_hi:[1,1,0]
	v_med3_f32 v1, v164, s17, v231
	v_med3_f32 v131, v162, s17, v231
	v_mov_b32_e32 v132, v137
	v_cvt_pk_fp8_f32 v132, v1, v131
	v_med3_f32 v133, v160, s17, v231
	v_med3_f32 v153, v158, s17, v231
	v_med3_f32 v1, v156, s17, v231
	v_cvt_pk_fp8_f32 v132, v133, v153 op_sel:[0,0,1]
	v_med3_f32 v131, v154, s17, v231
	v_mov_b32_e32 v133, v137
	v_cvt_pk_fp8_f32 v133, v1, v131
	v_med3_f32 v153, v152, s17, v231
	v_med3_f32 v155, v130, s17, v231
	v_lshl_add_u64 v[166:167], v[126:127], 0, s[28:29]
	v_cvt_pk_fp8_f32 v133, v153, v155 op_sel:[0,0,1]
	v_cvt_pk_f32_fp8_sdwa v[168:169], v128 src0_sel:WORD_1
	v_cvt_pk_f32_fp8_e32 v[170:171], v129
	v_lshl_add_u64 v[126:127], v[126:127], 0, s[70:71]
	global_store_dwordx2 v[166:167], v[132:133], off
	v_readlane_b32 s100, v252, 30
	s_nop 1
	v_mov_b32_e32 v132, s100
	v_readlane_b32 s100, v253, 30
	s_nop 1
	v_mov_b32_e32 v133, s100
	v_cvt_pk_f32_fp8_e32 v[166:167], v128
	v_cvt_pk_f32_fp8_sdwa v[128:129], v129 src0_sel:WORD_1
	v_mov_b32_e32 v161, v168
	v_mov_b32_e32 v159, v169
	v_mov_b32_e32 v165, v166
; __device__ __forceinline__ int cslot(int bh, int c) { return (c + bh) & 31; }
; template <int GRP>
; __device__ __forceinline__ void y_phase(Frame& F, const MW& W) {
;     ...
;         for (int c = 0; c < 32; ++c) {
;             u32x2 o; o.x = pg8::pack_fp8x4(C[0], C[1], C[2], C[3]); o.y = pg8::pack_fp8x4(C[4], C[5], C[6], C[7]); *(u32x2*)(W.CP + off + (size_t)cslot(bh, c) * 16384) = o;
;             const float bl = sc[2 * c], am = sc[2 * c + 1], mn = fmaxf(bl + m, am), dec = __expf(bl + m - mn), inj = __expf(am - mn);
;             const auto x0 = __builtin_amdgcn_cvt_pk_f32_fp8((int)v[c].x, false), x1 = __builtin_amdgcn_cvt_pk_f32_fp8((int)v[c].x, true), x2 = __builtin_amdgcn_cvt_pk_f32_fp8((int)v[c].y, false), x3 = __builtin_amdgcn_cvt_pk_f32_fp8((int)v[c].y, true);
;             C[0] = C[0] * dec + x0[0] * inj; C[1] = C[1] * dec + x0[1] * inj; C[2] = C[2] * dec + x1[0] * inj; C[3] = C[3] * dec + x1[1] * inj;
;             C[4] = C[4] * dec + x2[0] * inj; C[5] = C[5] * dec + x2[1] * inj; C[6] = C[6] * dec + x3[0] * inj; C[7] = C[7] * dec + x3[1] * inj; m = mn; }
;         if (nsc) {
;             f32x4 N = (f32x4){0.f, 0.f, 0.f, 0.f}; float mm = 0.f;
; #pragma unroll
;             for (int c = 0; c < 32; ++c) {
;                 *(f32x4*)(W.NP + ((size_t)bh * 32 + c) * 128 + g * 4) = N; if (g == 0) W.MP[bh * 32 + c] = mm;
;                 const float bl = sc[2 * c], am = sc[2 * c + 1], mn = fmaxf(bl + mm, am), dec = __expf(bl + mm - mn), inj = __expf(am - mn);
;                 N = N * dec + nv[c] * inj; mm = mn; }
	v_mov_b32_e32 v163, v167
	v_add_f32_e32 v1, v174, v132
	v_max_f32_e32 v131, v133, v133
	v_max_f32_e32 v131, v1, v131
	v_sub_f32_e32 v1, v1, v131
	v_mul_f32_e32 v1, 0x3fb8aa3b, v1
	v_exp_f32_e32 v132, v1
	v_sub_f32_e32 v1, v133, v131
	v_mul_f32_e32 v1, 0x3fb8aa3b, v1
	v_exp_f32_e32 v133, v1
	s_nop 0
	v_pk_mul_f32 v[160:161], v[160:161], v[132:133]
	v_pk_mul_f32 v[158:159], v[158:159], v[132:133]
	v_add_f32_e32 v160, v160, v161
	v_add_f32_e32 v161, v158, v159
	v_mov_b32_e32 v157, v133
	v_mov_b32_e32 v158, v132
	v_mov_b32_e32 v159, v170
	v_mov_b32_e32 v155, v133
	v_mov_b32_e32 v170, v132
	v_pk_mul_f32 v[164:165], v[164:165], v[132:133]
	v_pk_mul_f32 v[162:163], v[162:163], v[132:133]
	v_pk_mul_f32 v[156:157], v[156:157], v[158:159]
	v_pk_mul_f32 v[154:155], v[154:155], v[170:171]
	v_mov_b32_e32 v153, v133
	v_mov_b32_e32 v131, v133
	v_mov_b32_e32 v133, v129
	v_add_f32_e32 v1, v164, v165
	v_add_f32_e32 v162, v162, v163
	v_add_f32_e32 v156, v156, v157
	v_add_f32_e32 v157, v154, v155
	v_mov_b32_e32 v155, v128
	v_pk_mul_f32 v[128:129], v[130:131], v[132:133]
	v_med3_f32 v1, v1, s17, v231
	v_add_f32_e32 v129, v128, v129
	v_med3_f32 v130, v162, s17, v231
	v_mov_b32_e32 v128, v137
	v_cvt_pk_fp8_f32 v128, v1, v130
	v_mov_b32_e32 v154, v132
	v_med3_f32 v131, v160, s17, v231
	v_med3_f32 v132, v161, s17, v231
	v_cvt_pk_fp8_f32 v128, v131, v132 op_sel:[0,0,1]
	v_med3_f32 v1, v156, s17, v231
	v_med3_f32 v130, v157, s17, v231
	v_med3_f32 v132, v129, s17, v231
	v_mov_b32_e32 v129, v137
	v_cvt_pk_fp8_f32 v129, v1, v130
	v_pk_mul_f32 v[152:153], v[152:153], v[154:155]
	s_nop 0
	v_add_f32_e32 v152, v152, v153
	v_med3_f32 v131, v152, s17, v231
	v_cvt_pk_fp8_f32 v129, v131, v132 op_sel:[0,0,1]
	global_store_dwordx2 v[126:127], v[128:129], off
	s_and_saveexec_b64 s[0:1], s[10:11]
	s_cbranch_execz .LBB0_429
	s_lshl_b32 s24, s24, 5
	v_readlane_b32 s14, v255, 25
	v_readlane_b32 s15, v255, 26
	s_add_u32 s26, s14, s26
	v_cmp_eq_u32_e64 s[10:11], 0, v136
	s_addc_u32 s27, s15, s27
	v_lshlrev_b32_e32 v136, 2, v138
	global_store_dwordx4 v136, v[236:239], s[26:27]
	s_and_saveexec_b64 s[14:15], s[10:11]
	s_cbranch_execz .LBB0_367
	s_ashr_i32 s25, s24, 31
	s_lshl_b64 s[28:29], s[24:25], 2
	s_add_u32 s28, s64, s28
	s_addc_u32 s29, s65, s29
	global_store_dword v137, v137, s[28:29]
.LBB0_367:
	s_or_b64 exec, exec, s[14:15]
	v_readlane_b32 s100, v252, 0
	s_nop 1
	v_mov_b32_e32 v126, s100
	v_readlane_b32 s100, v253, 0
	s_nop 1
	v_mov_b32_e32 v127, s100
	v_lshl_add_u64 v[130:131], s[26:27], 0, v[136:137]
	v_add_f32_e32 v126, 0, v126
	v_max_f32_e32 v1, v127, v127
	v_max_f32_e32 v1, v126, v1
	v_sub_f32_e32 v126, v126, v1
	v_sub_f32_e32 v127, v127, v1
	v_mul_f32_e32 v126, 0x3fb8aa3b, v126
	v_mul_f32_e32 v127, 0x3fb8aa3b, v127
	v_exp_f32_e32 v128, v126
	v_exp_f32_e32 v126, v127
	v_mul_f32_e32 v132, 0, v128
	v_pk_fma_f32 v[128:129], v[32:33], v[126:127], v[132:133] op_sel_hi:[1,0,0]
	v_pk_fma_f32 v[126:127], v[30:31], v[126:127], v[132:133] op_sel_hi:[1,0,0]
	global_store_dwordx4 v[130:131], v[126:129], off offset:512
	s_and_saveexec_b64 s[14:15], s[10:11]
	s_cbranch_execz .LBB0_369
	s_ashr_i32 s25, s24, 31
	s_lshl_b64 s[28:29], s[24:25], 2
	s_add_u32 s28, s64, s28
	s_addc_u32 s29, s65, s29
	global_store_dword v137, v1, s[28:29] offset:4
.LBB0_369:
	s_or_b64 exec, exec, s[14:15]
	v_readlane_b32 s100, v252, 1
	s_nop 1
	v_mov_b32_e32 v132, s100
	v_readlane_b32 s100, v253, 1
	s_nop 1
	v_mov_b32_e32 v133, s100
	v_add_f32_e32 v132, v1, v132
	v_max_f32_e32 v1, v133, v133
	v_max_f32_e32 v1, v132, v1
	v_sub_f32_e32 v152, v132, v1
	v_sub_f32_e32 v132, v133, v1
	v_mul_f32_e32 v132, 0x3fb8aa3b, v132
	v_exp_f32_e32 v132, v132
	v_mul_f32_e32 v133, 0x3fb8aa3b, v152
	v_exp_f32_e32 v152, v133
	v_pk_mul_f32 v[154:155], v[26:27], v[132:133] op_sel_hi:[1,0]
	v_pk_mul_f32 v[132:133], v[28:29], v[132:133] op_sel_hi:[1,0]
	v_pk_fma_f32 v[126:127], v[126:127], v[152:153], v[154:155] op_sel_hi:[1,0,1]
	v_pk_fma_f32 v[128:129], v[128:129], v[152:153], v[132:133] op_sel_hi:[1,0,1]
	global_store_dwordx4 v[130:131], v[126:129], off offset:1024
	s_and_saveexec_b64 s[14:15], s[10:11]
	s_cbranch_execz .LBB0_371
	s_ashr_i32 s25, s24, 31
	s_lshl_b64 s[28:29], s[24:25], 2
	s_add_u32 s28, s64, s28
	s_addc_u32 s29, s65, s29
	global_store_dword v137, v1, s[28:29] offset:8
.LBB0_371:
	s_or_b64 exec, exec, s[14:15]
	v_readlane_b32 s100, v252, 2
	s_nop 1
	v_mov_b32_e32 v132, s100
	v_readlane_b32 s100, v253, 2
	s_nop 1
	v_mov_b32_e32 v133, s100
	v_add_f32_e32 v132, v1, v132
	v_max_f32_e32 v1, v133, v133
	v_max_f32_e32 v1, v132, v1
	v_sub_f32_e32 v152, v132, v1
	v_sub_f32_e32 v132, v133, v1
	v_mul_f32_e32 v132, 0x3fb8aa3b, v132
	v_exp_f32_e32 v132, v132
	v_mul_f32_e32 v133, 0x3fb8aa3b, v152
	v_exp_f32_e32 v152, v133
	v_pk_mul_f32 v[154:155], v[22:23], v[132:133] op_sel_hi:[1,0]
	v_pk_mul_f32 v[132:133], v[24:25], v[132:133] op_sel_hi:[1,0]
	v_pk_fma_f32 v[126:127], v[126:127], v[152:153], v[154:155] op_sel_hi:[1,0,1]
	v_pk_fma_f32 v[128:129], v[128:129], v[152:153], v[132:133] op_sel_hi:[1,0,1]
	global_store_dwordx4 v[130:131], v[126:129], off offset:1536
	s_and_saveexec_b64 s[14:15], s[10:11]
	s_cbranch_execz .LBB0_373
	s_ashr_i32 s25, s24, 31
	s_lshl_b64 s[28:29], s[24:25], 2
	s_add_u32 s28, s64, s28
	s_addc_u32 s29, s65, s29
	global_store_dword v137, v1, s[28:29] offset:12
; template <int GRP>
; __device__ __forceinline__ void y_phase(Frame& F, const MW& W) {
;     ...
;         if (nsc) {
;             f32x4 N = (f32x4){0.f, 0.f, 0.f, 0.f}; float mm = 0.f;
; #pragma unroll
;             for (int c = 0; c < 32; ++c) {
;                 *(f32x4*)(W.NP + ((size_t)bh * 32 + c) * 128 + g * 4) = N; if (g == 0) W.MP[bh * 32 + c] = mm;
;                 const float bl = sc[2 * c], am = sc[2 * c + 1], mn = fmaxf(bl + mm, am), dec = __expf(bl + mm - mn), inj = __expf(am - mn);
;                 N = N * dec + nv[c] * inj; mm = mn; }
.LBB0_373:
	s_or_b64 exec, exec, s[14:15]
	v_readlane_b32 s100, v252, 3
	s_nop 1
	v_mov_b32_e32 v132, s100
	v_readlane_b32 s100, v253, 3
	s_nop 1
	v_mov_b32_e32 v133, s100
	v_add_f32_e32 v132, v1, v132
	v_max_f32_e32 v1, v133, v133
	v_max_f32_e32 v1, v132, v1
	v_sub_f32_e32 v152, v132, v1
	v_sub_f32_e32 v132, v133, v1
	v_mul_f32_e32 v132, 0x3fb8aa3b, v132
	v_exp_f32_e32 v132, v132
	v_mul_f32_e32 v133, 0x3fb8aa3b, v152
	v_exp_f32_e32 v152, v133
	v_pk_mul_f32 v[154:155], v[18:19], v[132:133] op_sel_hi:[1,0]
	v_pk_mul_f32 v[132:133], v[20:21], v[132:133] op_sel_hi:[1,0]
	v_pk_fma_f32 v[126:127], v[126:127], v[152:153], v[154:155] op_sel_hi:[1,0,1]
	v_pk_fma_f32 v[128:129], v[128:129], v[152:153], v[132:133] op_sel_hi:[1,0,1]
	global_store_dwordx4 v[130:131], v[126:129], off offset:2048
	s_and_saveexec_b64 s[14:15], s[10:11]
	s_cbranch_execz .LBB0_375
	s_ashr_i32 s25, s24, 31
	s_lshl_b64 s[28:29], s[24:25], 2
	s_add_u32 s28, s64, s28
	s_addc_u32 s29, s65, s29
	global_store_dword v137, v1, s[28:29] offset:16
.LBB0_375:
	s_or_b64 exec, exec, s[14:15]
	v_readlane_b32 s100, v252, 4
	s_nop 1
	v_mov_b32_e32 v132, s100
	v_readlane_b32 s100, v253, 4
	s_nop 1
	v_mov_b32_e32 v133, s100
	v_add_f32_e32 v132, v1, v132
	v_max_f32_e32 v1, v133, v133
	v_max_f32_e32 v1, v132, v1
	v_sub_f32_e32 v152, v132, v1
	v_sub_f32_e32 v132, v133, v1
	v_mul_f32_e32 v132, 0x3fb8aa3b, v132
	v_exp_f32_e32 v132, v132
	v_mul_f32_e32 v133, 0x3fb8aa3b, v152
	v_exp_f32_e32 v152, v133
	v_pk_mul_f32 v[154:155], v[14:15], v[132:133] op_sel_hi:[1,0]
	v_pk_mul_f32 v[132:133], v[16:17], v[132:133] op_sel_hi:[1,0]
	v_pk_fma_f32 v[126:127], v[126:127], v[152:153], v[154:155] op_sel_hi:[1,0,1]
	v_pk_fma_f32 v[128:129], v[128:129], v[152:153], v[132:133] op_sel_hi:[1,0,1]
	global_store_dwordx4 v[130:131], v[126:129], off offset:2560
	s_and_saveexec_b64 s[14:15], s[10:11]
	s_cbranch_execz .LBB0_377
	s_ashr_i32 s25, s24, 31
	s_lshl_b64 s[28:29], s[24:25], 2
	s_add_u32 s28, s64, s28
	s_addc_u32 s29, s65, s29
	global_store_dword v137, v1, s[28:29] offset:20
.LBB0_377:
	s_or_b64 exec, exec, s[14:15]
	v_readlane_b32 s100, v252, 5
	s_nop 1
	v_mov_b32_e32 v132, s100
	v_readlane_b32 s100, v253, 5
	s_nop 1
	v_mov_b32_e32 v133, s100
	v_add_f32_e32 v132, v1, v132
	v_max_f32_e32 v1, v133, v133
	v_max_f32_e32 v1, v132, v1
	v_sub_f32_e32 v152, v132, v1
	v_sub_f32_e32 v132, v133, v1
	v_mul_f32_e32 v132, 0x3fb8aa3b, v132
	v_exp_f32_e32 v132, v132
	v_mul_f32_e32 v133, 0x3fb8aa3b, v152
	v_exp_f32_e32 v152, v133
	v_pk_mul_f32 v[154:155], v[10:11], v[132:133] op_sel_hi:[1,0]
	v_pk_mul_f32 v[132:133], v[12:13], v[132:133] op_sel_hi:[1,0]
	v_pk_fma_f32 v[126:127], v[126:127], v[152:153], v[154:155] op_sel_hi:[1,0,1]
	v_pk_fma_f32 v[128:129], v[128:129], v[152:153], v[132:133] op_sel_hi:[1,0,1]
	global_store_dwordx4 v[130:131], v[126:129], off offset:3072
	s_and_saveexec_b64 s[14:15], s[10:11]
	s_cbranch_execz .LBB0_379
	s_ashr_i32 s25, s24, 31
	s_lshl_b64 s[28:29], s[24:25], 2
	s_add_u32 s28, s64, s28
	s_addc_u32 s29, s65, s29
	global_store_dword v137, v1, s[28:29] offset:24
.LBB0_379:
	s_or_b64 exec, exec, s[14:15]
	v_readlane_b32 s100, v252, 6
	s_nop 1
	v_mov_b32_e32 v132, s100
	v_readlane_b32 s100, v253, 6
	s_nop 1
	v_mov_b32_e32 v133, s100
	v_add_f32_e32 v132, v1, v132
	v_max_f32_e32 v1, v133, v133
	v_max_f32_e32 v1, v132, v1
	v_sub_f32_e32 v152, v132, v1
	v_sub_f32_e32 v132, v133, v1
	v_mul_f32_e32 v132, 0x3fb8aa3b, v132
	v_exp_f32_e32 v132, v132
	v_mul_f32_e32 v133, 0x3fb8aa3b, v152
	v_exp_f32_e32 v152, v133
	s_waitcnt lgkmcnt(1)
	v_pk_mul_f32 v[154:155], v[6:7], v[132:133] op_sel_hi:[1,0]
	s_waitcnt lgkmcnt(0)
	v_pk_mul_f32 v[132:133], v[8:9], v[132:133] op_sel_hi:[1,0]
	v_pk_fma_f32 v[126:127], v[126:127], v[152:153], v[154:155] op_sel_hi:[1,0,1]
	v_pk_fma_f32 v[128:129], v[128:129], v[152:153], v[132:133] op_sel_hi:[1,0,1]
	global_store_dwordx4 v[130:131], v[126:129], off offset:3584
	s_and_saveexec_b64 s[14:15], s[10:11]
	s_cbranch_execz .LBB0_381
	s_ashr_i32 s25, s24, 31
	s_lshl_b64 s[28:29], s[24:25], 2
	s_add_u32 s28, s64, s28
	s_addc_u32 s29, s65, s29
	global_store_dword v137, v1, s[28:29] offset:28
.LBB0_381:
	s_or_b64 exec, exec, s[14:15]
	v_readlane_b32 s100, v252, 7
	s_nop 1
	v_mov_b32_e32 v132, s100
	v_readlane_b32 s100, v253, 7
	s_nop 1
	v_mov_b32_e32 v133, s100
	v_lshl_add_u64 v[130:131], s[26:27], 0, v[136:137]
	v_add_co_u32_e32 v154, vcc, 0x1000, v130
	v_add_f32_e32 v132, v1, v132
	v_max_f32_e32 v1, v133, v133
	v_max_f32_e32 v1, v132, v1
	v_sub_f32_e32 v132, v132, v1
	v_sub_f32_e32 v133, v133, v1
	v_mul_f32_e32 v152, 0x3fb8aa3b, v132
	v_mul_f32_e32 v132, 0x3fb8aa3b, v133
	v_exp_f32_e32 v132, v132
	v_exp_f32_e32 v152, v152
	v_addc_co_u32_e32 v155, vcc, 0, v131, vcc
	v_pk_mul_f32 v[156:157], v[2:3], v[132:133] op_sel_hi:[1,0]
	v_pk_mul_f32 v[132:133], v[4:5], v[132:133] op_sel_hi:[1,0]
	v_pk_fma_f32 v[126:127], v[126:127], v[152:153], v[156:157] op_sel_hi:[1,0,1]
	v_pk_fma_f32 v[128:129], v[128:129], v[152:153], v[132:133] op_sel_hi:[1,0,1]
	global_store_dwordx4 v[154:155], v[126:129], off
	s_and_saveexec_b64 s[14:15], s[10:11]
	s_cbranch_execz .LBB0_383
	s_ashr_i32 s25, s24, 31
	s_lshl_b64 s[28:29], s[24:25], 2
	s_add_u32 s28, s64, s28
	s_addc_u32 s29, s65, s29
	global_store_dword v137, v1, s[28:29] offset:32
; template <int GRP>
; __device__ __forceinline__ void y_phase(Frame& F, const MW& W) {
;     ...
;         if (nsc) {
;             f32x4 N = (f32x4){0.f, 0.f, 0.f, 0.f}; float mm = 0.f;
; #pragma unroll
;             for (int c = 0; c < 32; ++c) {
;                 *(f32x4*)(W.NP + ((size_t)bh * 32 + c) * 128 + g * 4) = N; if (g == 0) W.MP[bh * 32 + c] = mm;
;                 const float bl = sc[2 * c], am = sc[2 * c + 1], mn = fmaxf(bl + mm, am), dec = __expf(bl + mm - mn), inj = __expf(am - mn);
;                 N = N * dec + nv[c] * inj; mm = mn; }
.LBB0_383:
	s_or_b64 exec, exec, s[14:15]
	v_readlane_b32 s100, v252, 8
	s_nop 1
	v_mov_b32_e32 v132, s100
	v_readlane_b32 s100, v253, 8
	s_nop 1
	v_mov_b32_e32 v133, s100
	v_add_co_u32_e32 v130, vcc, 0x1000, v130
	v_add_f32_e32 v132, v1, v132
	v_max_f32_e32 v1, v133, v133
	v_max_f32_e32 v1, v132, v1
	v_sub_f32_e32 v132, v132, v1
	v_sub_f32_e32 v133, v133, v1
	v_mul_f32_e32 v152, 0x3fb8aa3b, v132
	v_mul_f32_e32 v132, 0x3fb8aa3b, v133
	v_exp_f32_e32 v132, v132
	v_exp_f32_e32 v152, v152
	v_addc_co_u32_e32 v131, vcc, 0, v131, vcc
	v_pk_mul_f32 v[154:155], v[62:63], v[132:133] op_sel_hi:[1,0]
	v_pk_mul_f32 v[132:133], v[64:65], v[132:133] op_sel_hi:[1,0]
	v_pk_fma_f32 v[126:127], v[126:127], v[152:153], v[154:155] op_sel_hi:[1,0,1]
	v_pk_fma_f32 v[128:129], v[128:129], v[152:153], v[132:133] op_sel_hi:[1,0,1]
	global_store_dwordx4 v[130:131], v[126:129], off offset:512
	s_and_saveexec_b64 s[14:15], s[10:11]
	s_cbranch_execz .LBB0_385
	s_ashr_i32 s25, s24, 31
	s_lshl_b64 s[28:29], s[24:25], 2
	s_add_u32 s28, s64, s28
	s_addc_u32 s29, s65, s29
	global_store_dword v137, v1, s[28:29] offset:36
.LBB0_385:
	s_or_b64 exec, exec, s[14:15]
	v_readlane_b32 s100, v252, 9
	s_nop 1
	v_mov_b32_e32 v132, s100
	v_readlane_b32 s100, v253, 9
	s_nop 1
	v_mov_b32_e32 v133, s100
	v_lshl_add_u64 v[130:131], s[26:27], 0, v[136:137]
	v_add_co_u32_e32 v154, vcc, 0x1000, v130
	v_add_f32_e32 v132, v1, v132
	v_max_f32_e32 v1, v133, v133
	v_max_f32_e32 v1, v132, v1
	v_sub_f32_e32 v132, v132, v1
	v_sub_f32_e32 v133, v133, v1
	v_mul_f32_e32 v152, 0x3fb8aa3b, v132
	v_mul_f32_e32 v132, 0x3fb8aa3b, v133
	v_exp_f32_e32 v132, v132
	v_exp_f32_e32 v152, v152
	v_addc_co_u32_e32 v155, vcc, 0, v131, vcc
	v_pk_mul_f32 v[156:157], v[58:59], v[132:133] op_sel_hi:[1,0]
	v_pk_mul_f32 v[132:133], v[60:61], v[132:133] op_sel_hi:[1,0]
	v_pk_fma_f32 v[126:127], v[126:127], v[152:153], v[156:157] op_sel_hi:[1,0,1]
	v_pk_fma_f32 v[128:129], v[128:129], v[152:153], v[132:133] op_sel_hi:[1,0,1]
	global_store_dwordx4 v[154:155], v[126:129], off offset:1024
	s_and_saveexec_b64 s[14:15], s[10:11]
	s_cbranch_execz .LBB0_387
	s_ashr_i32 s25, s24, 31
	s_lshl_b64 s[28:29], s[24:25], 2
	s_add_u32 s28, s64, s28
	s_addc_u32 s29, s65, s29
	global_store_dword v137, v1, s[28:29] offset:40
.LBB0_387:
	s_or_b64 exec, exec, s[14:15]
	v_readlane_b32 s100, v252, 10
	s_nop 1
	v_mov_b32_e32 v132, s100
	v_readlane_b32 s100, v253, 10
	s_nop 1
	v_mov_b32_e32 v133, s100
	v_add_co_u32_e32 v130, vcc, 0x1000, v130
	v_add_f32_e32 v132, v1, v132
	v_max_f32_e32 v1, v133, v133
	v_max_f32_e32 v1, v132, v1
	v_sub_f32_e32 v132, v132, v1
	v_sub_f32_e32 v133, v133, v1
	v_mul_f32_e32 v152, 0x3fb8aa3b, v132
	v_mul_f32_e32 v132, 0x3fb8aa3b, v133
	v_exp_f32_e32 v132, v132
	v_exp_f32_e32 v152, v152
	v_addc_co_u32_e32 v131, vcc, 0, v131, vcc
	v_pk_mul_f32 v[154:155], v[54:55], v[132:133] op_sel_hi:[1,0]
	v_pk_mul_f32 v[132:133], v[56:57], v[132:133] op_sel_hi:[1,0]
	v_pk_fma_f32 v[126:127], v[126:127], v[152:153], v[154:155] op_sel_hi:[1,0,1]
	v_pk_fma_f32 v[128:129], v[128:129], v[152:153], v[132:133] op_sel_hi:[1,0,1]
	global_store_dwordx4 v[130:131], v[126:129], off offset:1536
	s_and_saveexec_b64 s[14:15], s[10:11]
	s_cbranch_execz .LBB0_389
	s_ashr_i32 s25, s24, 31
	s_lshl_b64 s[28:29], s[24:25], 2
	s_add_u32 s28, s64, s28
	s_addc_u32 s29, s65, s29
	global_store_dword v137, v1, s[28:29] offset:44
.LBB0_389:
	s_or_b64 exec, exec, s[14:15]
	v_readlane_b32 s100, v252, 11
	s_nop 1
	v_mov_b32_e32 v132, s100
	v_readlane_b32 s100, v253, 11
	s_nop 1
	v_mov_b32_e32 v133, s100
	v_lshl_add_u64 v[130:131], s[26:27], 0, v[136:137]
	v_add_co_u32_e32 v154, vcc, 0x1000, v130
	v_add_f32_e32 v132, v1, v132
	v_max_f32_e32 v1, v133, v133
	v_max_f32_e32 v1, v132, v1
	v_sub_f32_e32 v132, v132, v1
	v_sub_f32_e32 v133, v133, v1
	v_mul_f32_e32 v152, 0x3fb8aa3b, v132
	v_mul_f32_e32 v132, 0x3fb8aa3b, v133
	v_exp_f32_e32 v132, v132
	v_exp_f32_e32 v152, v152
	v_addc_co_u32_e32 v155, vcc, 0, v131, vcc
	v_pk_mul_f32 v[156:157], v[50:51], v[132:133] op_sel_hi:[1,0]
	v_pk_mul_f32 v[132:133], v[52:53], v[132:133] op_sel_hi:[1,0]
	v_pk_fma_f32 v[126:127], v[126:127], v[152:153], v[156:157] op_sel_hi:[1,0,1]
	v_pk_fma_f32 v[128:129], v[128:129], v[152:153], v[132:133] op_sel_hi:[1,0,1]
	global_store_dwordx4 v[154:155], v[126:129], off offset:2048
	s_and_saveexec_b64 s[14:15], s[10:11]
	s_cbranch_execz .LBB0_391
	s_ashr_i32 s25, s24, 31
	s_lshl_b64 s[28:29], s[24:25], 2
	s_add_u32 s28, s64, s28
	s_addc_u32 s29, s65, s29
	global_store_dword v137, v1, s[28:29] offset:48
.LBB0_391:
	s_or_b64 exec, exec, s[14:15]
	v_readlane_b32 s100, v252, 12
	s_nop 1
	v_mov_b32_e32 v132, s100
	v_readlane_b32 s100, v253, 12
	s_nop 1
	v_mov_b32_e32 v133, s100
	v_add_co_u32_e32 v130, vcc, 0x1000, v130
	v_add_f32_e32 v132, v1, v132
	v_max_f32_e32 v1, v133, v133
	v_max_f32_e32 v1, v132, v1
	v_sub_f32_e32 v132, v132, v1
	v_sub_f32_e32 v133, v133, v1
	v_mul_f32_e32 v152, 0x3fb8aa3b, v132
	v_mul_f32_e32 v132, 0x3fb8aa3b, v133
	v_exp_f32_e32 v132, v132
	v_exp_f32_e32 v152, v152
	v_addc_co_u32_e32 v131, vcc, 0, v131, vcc
	v_pk_mul_f32 v[154:155], v[46:47], v[132:133] op_sel_hi:[1,0]
	v_pk_mul_f32 v[132:133], v[48:49], v[132:133] op_sel_hi:[1,0]
	v_pk_fma_f32 v[126:127], v[126:127], v[152:153], v[154:155] op_sel_hi:[1,0,1]
	v_pk_fma_f32 v[128:129], v[128:129], v[152:153], v[132:133] op_sel_hi:[1,0,1]
	global_store_dwordx4 v[130:131], v[126:129], off offset:2560
	s_and_saveexec_b64 s[14:15], s[10:11]
	s_cbranch_execz .LBB0_393
	s_ashr_i32 s25, s24, 31
	s_lshl_b64 s[28:29], s[24:25], 2
	s_add_u32 s28, s64, s28
	s_addc_u32 s29, s65, s29
	global_store_dword v137, v1, s[28:29] offset:52
; template <int GRP>
; __device__ __forceinline__ void y_phase(Frame& F, const MW& W) {
;     ...
;         if (nsc) {
;             f32x4 N = (f32x4){0.f, 0.f, 0.f, 0.f}; float mm = 0.f;
; #pragma unroll
;             for (int c = 0; c < 32; ++c) {
;                 *(f32x4*)(W.NP + ((size_t)bh * 32 + c) * 128 + g * 4) = N; if (g == 0) W.MP[bh * 32 + c] = mm;
;                 const float bl = sc[2 * c], am = sc[2 * c + 1], mn = fmaxf(bl + mm, am), dec = __expf(bl + mm - mn), inj = __expf(am - mn);
;                 N = N * dec + nv[c] * inj; mm = mn; }
.LBB0_393:
	s_or_b64 exec, exec, s[14:15]
	v_readlane_b32 s100, v252, 13
	s_nop 1
	v_mov_b32_e32 v132, s100
	v_readlane_b32 s100, v253, 13
	s_nop 1
	v_mov_b32_e32 v133, s100
	v_lshl_add_u64 v[130:131], s[26:27], 0, v[136:137]
	v_add_co_u32_e32 v154, vcc, 0x1000, v130
	v_add_f32_e32 v132, v1, v132
	v_max_f32_e32 v1, v133, v133
	v_max_f32_e32 v1, v132, v1
	v_sub_f32_e32 v132, v132, v1
	v_sub_f32_e32 v133, v133, v1
	v_mul_f32_e32 v152, 0x3fb8aa3b, v132
	v_mul_f32_e32 v132, 0x3fb8aa3b, v133
	v_exp_f32_e32 v132, v132
	v_exp_f32_e32 v152, v152
	v_addc_co_u32_e32 v155, vcc, 0, v131, vcc
	v_pk_mul_f32 v[156:157], v[42:43], v[132:133] op_sel_hi:[1,0]
	v_pk_mul_f32 v[132:133], v[44:45], v[132:133] op_sel_hi:[1,0]
	v_pk_fma_f32 v[126:127], v[126:127], v[152:153], v[156:157] op_sel_hi:[1,0,1]
	v_pk_fma_f32 v[128:129], v[128:129], v[152:153], v[132:133] op_sel_hi:[1,0,1]
	global_store_dwordx4 v[154:155], v[126:129], off offset:3072
	s_and_saveexec_b64 s[14:15], s[10:11]
	s_cbranch_execz .LBB0_395
	s_ashr_i32 s25, s24, 31
	s_lshl_b64 s[28:29], s[24:25], 2
	s_add_u32 s28, s64, s28
	s_addc_u32 s29, s65, s29
	global_store_dword v137, v1, s[28:29] offset:56
.LBB0_395:
	s_or_b64 exec, exec, s[14:15]
	v_readlane_b32 s100, v252, 14
	s_nop 1
	v_mov_b32_e32 v132, s100
	v_readlane_b32 s100, v253, 14
	s_nop 1
	v_mov_b32_e32 v133, s100
	v_add_co_u32_e32 v130, vcc, 0x1000, v130
	v_add_f32_e32 v132, v1, v132
	v_max_f32_e32 v1, v133, v133
	v_max_f32_e32 v1, v132, v1
	v_sub_f32_e32 v132, v132, v1
	v_sub_f32_e32 v133, v133, v1
	v_mul_f32_e32 v152, 0x3fb8aa3b, v132
	v_mul_f32_e32 v132, 0x3fb8aa3b, v133
	v_exp_f32_e32 v132, v132
	v_exp_f32_e32 v152, v152
	v_addc_co_u32_e32 v131, vcc, 0, v131, vcc
	v_pk_mul_f32 v[154:155], v[38:39], v[132:133] op_sel_hi:[1,0]
	v_pk_mul_f32 v[132:133], v[40:41], v[132:133] op_sel_hi:[1,0]
	v_pk_fma_f32 v[126:127], v[126:127], v[152:153], v[154:155] op_sel_hi:[1,0,1]
	v_pk_fma_f32 v[128:129], v[128:129], v[152:153], v[132:133] op_sel_hi:[1,0,1]
	global_store_dwordx4 v[130:131], v[126:129], off offset:3584
	s_and_saveexec_b64 s[14:15], s[10:11]
	s_cbranch_execz .LBB0_397
	s_ashr_i32 s25, s24, 31
	s_lshl_b64 s[28:29], s[24:25], 2
	s_add_u32 s28, s64, s28
	s_addc_u32 s29, s65, s29
	global_store_dword v137, v1, s[28:29] offset:60
.LBB0_397:
	s_or_b64 exec, exec, s[14:15]
	v_readlane_b32 s100, v252, 15
	s_nop 1
	v_mov_b32_e32 v132, s100
	v_readlane_b32 s100, v253, 15
	s_nop 1
	v_mov_b32_e32 v133, s100
	v_lshl_add_u64 v[130:131], s[26:27], 0, v[136:137]
	v_add_co_u32_e32 v154, vcc, 0x2000, v130
	v_add_f32_e32 v132, v1, v132
	v_max_f32_e32 v1, v133, v133
	v_max_f32_e32 v1, v132, v1
	v_sub_f32_e32 v132, v132, v1
	v_sub_f32_e32 v133, v133, v1
	v_mul_f32_e32 v152, 0x3fb8aa3b, v132
	v_mul_f32_e32 v132, 0x3fb8aa3b, v133
	v_exp_f32_e32 v132, v132
	v_exp_f32_e32 v152, v152
	v_addc_co_u32_e32 v155, vcc, 0, v131, vcc
	v_pk_mul_f32 v[156:157], v[34:35], v[132:133] op_sel_hi:[1,0]
	v_pk_mul_f32 v[132:133], v[36:37], v[132:133] op_sel_hi:[1,0]
	v_pk_fma_f32 v[126:127], v[126:127], v[152:153], v[156:157] op_sel_hi:[1,0,1]
	v_pk_fma_f32 v[128:129], v[128:129], v[152:153], v[132:133] op_sel_hi:[1,0,1]
	global_store_dwordx4 v[154:155], v[126:129], off
	s_and_saveexec_b64 s[14:15], s[10:11]
	s_cbranch_execz .LBB0_399
	s_ashr_i32 s25, s24, 31
	s_lshl_b64 s[28:29], s[24:25], 2
	s_add_u32 s28, s64, s28
	s_addc_u32 s29, s65, s29
	global_store_dword v137, v1, s[28:29] offset:64
.LBB0_399:
	s_or_b64 exec, exec, s[14:15]
	v_readlane_b32 s100, v252, 16
	s_nop 1
	v_mov_b32_e32 v132, s100
	v_readlane_b32 s100, v253, 16
	s_nop 1
	v_mov_b32_e32 v133, s100
	v_add_co_u32_e32 v130, vcc, 0x2000, v130
	v_add_f32_e32 v132, v1, v132
	v_max_f32_e32 v1, v133, v133
	v_max_f32_e32 v1, v132, v1
	v_sub_f32_e32 v132, v132, v1
	v_sub_f32_e32 v133, v133, v1
	v_mul_f32_e32 v152, 0x3fb8aa3b, v132
	v_mul_f32_e32 v132, 0x3fb8aa3b, v133
	v_exp_f32_e32 v132, v132
	v_exp_f32_e32 v152, v152
	v_addc_co_u32_e32 v131, vcc, 0, v131, vcc
	v_pk_mul_f32 v[154:155], v[94:95], v[132:133] op_sel_hi:[1,0]
	v_pk_mul_f32 v[132:133], v[96:97], v[132:133] op_sel_hi:[1,0]
	v_pk_fma_f32 v[126:127], v[126:127], v[152:153], v[154:155] op_sel_hi:[1,0,1]
	v_pk_fma_f32 v[128:129], v[128:129], v[152:153], v[132:133] op_sel_hi:[1,0,1]
	global_store_dwordx4 v[130:131], v[126:129], off offset:512
	s_and_saveexec_b64 s[14:15], s[10:11]
	s_cbranch_execz .LBB0_401
	s_ashr_i32 s25, s24, 31
	s_lshl_b64 s[28:29], s[24:25], 2
	s_add_u32 s28, s64, s28
	s_addc_u32 s29, s65, s29
	global_store_dword v137, v1, s[28:29] offset:68
.LBB0_401:
	s_or_b64 exec, exec, s[14:15]
	v_readlane_b32 s100, v252, 17
	s_nop 1
	v_mov_b32_e32 v132, s100
	v_readlane_b32 s100, v253, 17
	s_nop 1
	v_mov_b32_e32 v133, s100
	v_lshl_add_u64 v[130:131], s[26:27], 0, v[136:137]
	v_add_co_u32_e32 v154, vcc, 0x2000, v130
	v_add_f32_e32 v132, v1, v132
	v_max_f32_e32 v1, v133, v133
	v_max_f32_e32 v1, v132, v1
	v_sub_f32_e32 v132, v132, v1
	v_sub_f32_e32 v133, v133, v1
	v_mul_f32_e32 v152, 0x3fb8aa3b, v132
	v_mul_f32_e32 v132, 0x3fb8aa3b, v133
	v_exp_f32_e32 v132, v132
	v_exp_f32_e32 v152, v152
	v_addc_co_u32_e32 v155, vcc, 0, v131, vcc
	v_pk_mul_f32 v[156:157], v[90:91], v[132:133] op_sel_hi:[1,0]
	v_pk_mul_f32 v[132:133], v[92:93], v[132:133] op_sel_hi:[1,0]
	v_pk_fma_f32 v[126:127], v[126:127], v[152:153], v[156:157] op_sel_hi:[1,0,1]
	v_pk_fma_f32 v[128:129], v[128:129], v[152:153], v[132:133] op_sel_hi:[1,0,1]
	global_store_dwordx4 v[154:155], v[126:129], off offset:1024
	s_and_saveexec_b64 s[14:15], s[10:11]
	s_cbranch_execz .LBB0_403
	s_ashr_i32 s25, s24, 31
	s_lshl_b64 s[28:29], s[24:25], 2
	s_add_u32 s28, s64, s28
	s_addc_u32 s29, s65, s29
	global_store_dword v137, v1, s[28:29] offset:72
; template <int GRP>
; __device__ __forceinline__ void y_phase(Frame& F, const MW& W) {
;     ...
;         if (nsc) {
;             f32x4 N = (f32x4){0.f, 0.f, 0.f, 0.f}; float mm = 0.f;
; #pragma unroll
;             for (int c = 0; c < 32; ++c) {
;                 *(f32x4*)(W.NP + ((size_t)bh * 32 + c) * 128 + g * 4) = N; if (g == 0) W.MP[bh * 32 + c] = mm;
;                 const float bl = sc[2 * c], am = sc[2 * c + 1], mn = fmaxf(bl + mm, am), dec = __expf(bl + mm - mn), inj = __expf(am - mn);
;                 N = N * dec + nv[c] * inj; mm = mn; }
.LBB0_403:
	s_or_b64 exec, exec, s[14:15]
	v_readlane_b32 s100, v252, 18
	s_nop 1
	v_mov_b32_e32 v132, s100
	v_readlane_b32 s100, v253, 18
	s_nop 1
	v_mov_b32_e32 v133, s100
	v_add_co_u32_e32 v130, vcc, 0x2000, v130
	v_add_f32_e32 v132, v1, v132
	v_max_f32_e32 v1, v133, v133
	v_max_f32_e32 v1, v132, v1
	v_sub_f32_e32 v132, v132, v1
	v_sub_f32_e32 v133, v133, v1
	v_mul_f32_e32 v152, 0x3fb8aa3b, v132
	v_mul_f32_e32 v132, 0x3fb8aa3b, v133
	v_exp_f32_e32 v132, v132
	v_exp_f32_e32 v152, v152
	v_addc_co_u32_e32 v131, vcc, 0, v131, vcc
	v_pk_mul_f32 v[154:155], v[86:87], v[132:133] op_sel_hi:[1,0]
	v_pk_mul_f32 v[132:133], v[88:89], v[132:133] op_sel_hi:[1,0]
	v_pk_fma_f32 v[126:127], v[126:127], v[152:153], v[154:155] op_sel_hi:[1,0,1]
	v_pk_fma_f32 v[128:129], v[128:129], v[152:153], v[132:133] op_sel_hi:[1,0,1]
	global_store_dwordx4 v[130:131], v[126:129], off offset:1536
	s_and_saveexec_b64 s[14:15], s[10:11]
	s_cbranch_execz .LBB0_405
	s_ashr_i32 s25, s24, 31
	s_lshl_b64 s[28:29], s[24:25], 2
	s_add_u32 s28, s64, s28
	s_addc_u32 s29, s65, s29
	global_store_dword v137, v1, s[28:29] offset:76
.LBB0_405:
	s_or_b64 exec, exec, s[14:15]
	v_readlane_b32 s100, v252, 19
	s_nop 1
	v_mov_b32_e32 v132, s100
	v_readlane_b32 s100, v253, 19
	s_nop 1
	v_mov_b32_e32 v133, s100
	v_lshl_add_u64 v[130:131], s[26:27], 0, v[136:137]
	v_add_co_u32_e32 v154, vcc, 0x2000, v130
	v_add_f32_e32 v132, v1, v132
	v_max_f32_e32 v1, v133, v133
	v_max_f32_e32 v1, v132, v1
	v_sub_f32_e32 v132, v132, v1
	v_sub_f32_e32 v133, v133, v1
	v_mul_f32_e32 v152, 0x3fb8aa3b, v132
	v_mul_f32_e32 v132, 0x3fb8aa3b, v133
	v_exp_f32_e32 v132, v132
	v_exp_f32_e32 v152, v152
	v_addc_co_u32_e32 v155, vcc, 0, v131, vcc
	v_pk_mul_f32 v[156:157], v[82:83], v[132:133] op_sel_hi:[1,0]
	v_pk_mul_f32 v[132:133], v[84:85], v[132:133] op_sel_hi:[1,0]
	v_pk_fma_f32 v[126:127], v[126:127], v[152:153], v[156:157] op_sel_hi:[1,0,1]
	v_pk_fma_f32 v[128:129], v[128:129], v[152:153], v[132:133] op_sel_hi:[1,0,1]
	global_store_dwordx4 v[154:155], v[126:129], off offset:2048
	s_and_saveexec_b64 s[14:15], s[10:11]
	s_cbranch_execz .LBB0_407
	s_ashr_i32 s25, s24, 31
	s_lshl_b64 s[28:29], s[24:25], 2
	s_add_u32 s28, s64, s28
	s_addc_u32 s29, s65, s29
	global_store_dword v137, v1, s[28:29] offset:80
.LBB0_407:
	s_or_b64 exec, exec, s[14:15]
	v_readlane_b32 s100, v252, 20
	s_nop 1
	v_mov_b32_e32 v132, s100
	v_readlane_b32 s100, v253, 20
	s_nop 1
	v_mov_b32_e32 v133, s100
	v_add_co_u32_e32 v130, vcc, 0x2000, v130
	v_add_f32_e32 v132, v1, v132
	v_max_f32_e32 v1, v133, v133
	v_max_f32_e32 v1, v132, v1
	v_sub_f32_e32 v132, v132, v1
	v_sub_f32_e32 v133, v133, v1
	v_mul_f32_e32 v152, 0x3fb8aa3b, v132
	v_mul_f32_e32 v132, 0x3fb8aa3b, v133
	v_exp_f32_e32 v132, v132
	v_exp_f32_e32 v152, v152
	v_addc_co_u32_e32 v131, vcc, 0, v131, vcc
	v_pk_mul_f32 v[154:155], v[78:79], v[132:133] op_sel_hi:[1,0]
	v_pk_mul_f32 v[132:133], v[80:81], v[132:133] op_sel_hi:[1,0]
	v_pk_fma_f32 v[126:127], v[126:127], v[152:153], v[154:155] op_sel_hi:[1,0,1]
	v_pk_fma_f32 v[128:129], v[128:129], v[152:153], v[132:133] op_sel_hi:[1,0,1]
	global_store_dwordx4 v[130:131], v[126:129], off offset:2560
	s_and_saveexec_b64 s[14:15], s[10:11]
	s_cbranch_execz .LBB0_409
	s_ashr_i32 s25, s24, 31
	s_lshl_b64 s[28:29], s[24:25], 2
	s_add_u32 s28, s64, s28
	s_addc_u32 s29, s65, s29
	global_store_dword v137, v1, s[28:29] offset:84
.LBB0_409:
	s_or_b64 exec, exec, s[14:15]
	v_readlane_b32 s100, v252, 21
	s_nop 1
	v_mov_b32_e32 v132, s100
	v_readlane_b32 s100, v253, 21
	s_nop 1
	v_mov_b32_e32 v133, s100
	v_lshl_add_u64 v[130:131], s[26:27], 0, v[136:137]
	v_add_co_u32_e32 v154, vcc, 0x2000, v130
	v_add_f32_e32 v132, v1, v132
	v_max_f32_e32 v1, v133, v133
	v_max_f32_e32 v1, v132, v1
	v_sub_f32_e32 v132, v132, v1
	v_sub_f32_e32 v133, v133, v1
	v_mul_f32_e32 v152, 0x3fb8aa3b, v132
	v_mul_f32_e32 v132, 0x3fb8aa3b, v133
	v_exp_f32_e32 v132, v132
	v_exp_f32_e32 v152, v152
	v_addc_co_u32_e32 v155, vcc, 0, v131, vcc
	v_pk_mul_f32 v[156:157], v[74:75], v[132:133] op_sel_hi:[1,0]
	v_pk_mul_f32 v[132:133], v[76:77], v[132:133] op_sel_hi:[1,0]
	v_pk_fma_f32 v[126:127], v[126:127], v[152:153], v[156:157] op_sel_hi:[1,0,1]
	v_pk_fma_f32 v[128:129], v[128:129], v[152:153], v[132:133] op_sel_hi:[1,0,1]
	global_store_dwordx4 v[154:155], v[126:129], off offset:3072
	s_and_saveexec_b64 s[14:15], s[10:11]
	s_cbranch_execz .LBB0_411
	s_ashr_i32 s25, s24, 31
	s_lshl_b64 s[28:29], s[24:25], 2
	s_add_u32 s28, s64, s28
	s_addc_u32 s29, s65, s29
	global_store_dword v137, v1, s[28:29] offset:88
.LBB0_411:
	s_or_b64 exec, exec, s[14:15]
	v_readlane_b32 s100, v252, 22
	s_nop 1
	v_mov_b32_e32 v132, s100
	v_readlane_b32 s100, v253, 22
	s_nop 1
	v_mov_b32_e32 v133, s100
	v_add_co_u32_e32 v130, vcc, 0x2000, v130
	v_add_f32_e32 v132, v1, v132
	v_max_f32_e32 v1, v133, v133
	v_max_f32_e32 v1, v132, v1
	v_sub_f32_e32 v132, v132, v1
	v_sub_f32_e32 v133, v133, v1
	v_mul_f32_e32 v152, 0x3fb8aa3b, v132
	v_mul_f32_e32 v132, 0x3fb8aa3b, v133
	v_exp_f32_e32 v132, v132
	v_exp_f32_e32 v152, v152
	v_addc_co_u32_e32 v131, vcc, 0, v131, vcc
	v_pk_mul_f32 v[154:155], v[70:71], v[132:133] op_sel_hi:[1,0]
	v_pk_mul_f32 v[132:133], v[72:73], v[132:133] op_sel_hi:[1,0]
	v_pk_fma_f32 v[126:127], v[126:127], v[152:153], v[154:155] op_sel_hi:[1,0,1]
	v_pk_fma_f32 v[128:129], v[128:129], v[152:153], v[132:133] op_sel_hi:[1,0,1]
	global_store_dwordx4 v[130:131], v[126:129], off offset:3584
	s_and_saveexec_b64 s[14:15], s[10:11]
	s_cbranch_execz .LBB0_413
	s_ashr_i32 s25, s24, 31
	s_lshl_b64 s[28:29], s[24:25], 2
	s_add_u32 s28, s64, s28
	s_addc_u32 s29, s65, s29
	global_store_dword v137, v1, s[28:29] offset:92
; template <int GRP>
; __device__ __forceinline__ void y_phase(Frame& F, const MW& W) {
;     ...
;         if (nsc) {
;             f32x4 N = (f32x4){0.f, 0.f, 0.f, 0.f}; float mm = 0.f;
; #pragma unroll
;             for (int c = 0; c < 32; ++c) {
;                 *(f32x4*)(W.NP + ((size_t)bh * 32 + c) * 128 + g * 4) = N; if (g == 0) W.MP[bh * 32 + c] = mm;
;                 const float bl = sc[2 * c], am = sc[2 * c + 1], mn = fmaxf(bl + mm, am), dec = __expf(bl + mm - mn), inj = __expf(am - mn);
;                 N = N * dec + nv[c] * inj; mm = mn; }
.LBB0_413:
	s_or_b64 exec, exec, s[14:15]
	v_readlane_b32 s100, v252, 23
	s_nop 1
	v_mov_b32_e32 v132, s100
	v_readlane_b32 s100, v253, 23
	s_nop 1
	v_mov_b32_e32 v133, s100
	v_lshl_add_u64 v[130:131], s[26:27], 0, v[136:137]
	v_add_co_u32_e32 v154, vcc, 0x3000, v130
	v_add_f32_e32 v132, v1, v132
	v_max_f32_e32 v1, v133, v133
	v_max_f32_e32 v1, v132, v1
	v_sub_f32_e32 v132, v132, v1
	v_sub_f32_e32 v133, v133, v1
	v_mul_f32_e32 v152, 0x3fb8aa3b, v132
	v_mul_f32_e32 v132, 0x3fb8aa3b, v133
	v_exp_f32_e32 v132, v132
	v_exp_f32_e32 v152, v152
	v_addc_co_u32_e32 v155, vcc, 0, v131, vcc
	v_pk_mul_f32 v[156:157], v[66:67], v[132:133] op_sel_hi:[1,0]
	v_pk_mul_f32 v[132:133], v[68:69], v[132:133] op_sel_hi:[1,0]
	v_pk_fma_f32 v[126:127], v[126:127], v[152:153], v[156:157] op_sel_hi:[1,0,1]
	v_pk_fma_f32 v[128:129], v[128:129], v[152:153], v[132:133] op_sel_hi:[1,0,1]
	global_store_dwordx4 v[154:155], v[126:129], off
	s_and_saveexec_b64 s[14:15], s[10:11]
	s_cbranch_execz .LBB0_415
	s_ashr_i32 s25, s24, 31
	s_lshl_b64 s[28:29], s[24:25], 2
	s_add_u32 s28, s64, s28
	s_addc_u32 s29, s65, s29
	global_store_dword v137, v1, s[28:29] offset:96
.LBB0_415:
	s_or_b64 exec, exec, s[14:15]
	v_readlane_b32 s100, v252, 24
	s_nop 1
	v_mov_b32_e32 v132, s100
	v_readlane_b32 s100, v253, 24
	s_nop 1
	v_mov_b32_e32 v133, s100
	v_add_co_u32_e32 v130, vcc, 0x3000, v130
	v_add_f32_e32 v132, v1, v132
	v_max_f32_e32 v1, v133, v133
	v_max_f32_e32 v1, v132, v1
	v_sub_f32_e32 v132, v132, v1
	v_sub_f32_e32 v133, v133, v1
	v_mul_f32_e32 v152, 0x3fb8aa3b, v132
	v_mul_f32_e32 v132, 0x3fb8aa3b, v133
	v_exp_f32_e32 v132, v132
	v_exp_f32_e32 v152, v152
	v_addc_co_u32_e32 v131, vcc, 0, v131, vcc
	v_pk_mul_f32 v[154:155], v[122:123], v[132:133] op_sel_hi:[1,0]
	v_pk_mul_f32 v[132:133], v[124:125], v[132:133] op_sel_hi:[1,0]
	v_pk_fma_f32 v[126:127], v[126:127], v[152:153], v[154:155] op_sel_hi:[1,0,1]
	v_pk_fma_f32 v[128:129], v[128:129], v[152:153], v[132:133] op_sel_hi:[1,0,1]
	global_store_dwordx4 v[130:131], v[126:129], off offset:512
	s_and_saveexec_b64 s[14:15], s[10:11]
	s_cbranch_execz .LBB0_417
	s_ashr_i32 s25, s24, 31
	s_lshl_b64 s[28:29], s[24:25], 2
	s_add_u32 s28, s64, s28
	s_addc_u32 s29, s65, s29
	global_store_dword v137, v1, s[28:29] offset:100
.LBB0_417:
	s_or_b64 exec, exec, s[14:15]
	v_readlane_b32 s100, v252, 25
	s_nop 1
	v_mov_b32_e32 v132, s100
	v_readlane_b32 s100, v253, 25
	s_nop 1
	v_mov_b32_e32 v133, s100
	v_lshl_add_u64 v[130:131], s[26:27], 0, v[136:137]
	v_add_co_u32_e32 v154, vcc, 0x3000, v130
	v_add_f32_e32 v132, v1, v132
	v_max_f32_e32 v1, v133, v133
	v_max_f32_e32 v1, v132, v1
	v_sub_f32_e32 v132, v132, v1
	v_sub_f32_e32 v133, v133, v1
	v_mul_f32_e32 v152, 0x3fb8aa3b, v132
	v_mul_f32_e32 v132, 0x3fb8aa3b, v133
	v_exp_f32_e32 v132, v132
	v_exp_f32_e32 v152, v152
	v_addc_co_u32_e32 v155, vcc, 0, v131, vcc
	v_pk_mul_f32 v[156:157], v[118:119], v[132:133] op_sel_hi:[1,0]
	v_pk_mul_f32 v[132:133], v[120:121], v[132:133] op_sel_hi:[1,0]
	v_pk_fma_f32 v[126:127], v[126:127], v[152:153], v[156:157] op_sel_hi:[1,0,1]
	v_pk_fma_f32 v[128:129], v[128:129], v[152:153], v[132:133] op_sel_hi:[1,0,1]
	global_store_dwordx4 v[154:155], v[126:129], off offset:1024
	s_and_saveexec_b64 s[14:15], s[10:11]
	s_cbranch_execz .LBB0_419
	s_ashr_i32 s25, s24, 31
	s_lshl_b64 s[28:29], s[24:25], 2
	s_add_u32 s28, s64, s28
	s_addc_u32 s29, s65, s29
	global_store_dword v137, v1, s[28:29] offset:104
.LBB0_419:
	s_or_b64 exec, exec, s[14:15]
	v_readlane_b32 s100, v252, 26
	s_nop 1
	v_mov_b32_e32 v132, s100
	v_readlane_b32 s100, v253, 26
	s_nop 1
	v_mov_b32_e32 v133, s100
	v_add_co_u32_e32 v130, vcc, 0x3000, v130
	v_add_f32_e32 v132, v1, v132
	v_max_f32_e32 v1, v133, v133
	v_max_f32_e32 v1, v132, v1
	v_sub_f32_e32 v132, v132, v1
	v_sub_f32_e32 v133, v133, v1
	v_mul_f32_e32 v152, 0x3fb8aa3b, v132
	v_mul_f32_e32 v132, 0x3fb8aa3b, v133
	v_exp_f32_e32 v132, v132
	v_exp_f32_e32 v152, v152
	v_addc_co_u32_e32 v131, vcc, 0, v131, vcc
	v_pk_mul_f32 v[154:155], v[114:115], v[132:133] op_sel_hi:[1,0]
	v_pk_mul_f32 v[132:133], v[116:117], v[132:133] op_sel_hi:[1,0]
	v_pk_fma_f32 v[126:127], v[126:127], v[152:153], v[154:155] op_sel_hi:[1,0,1]
	v_pk_fma_f32 v[128:129], v[128:129], v[152:153], v[132:133] op_sel_hi:[1,0,1]
	global_store_dwordx4 v[130:131], v[126:129], off offset:1536
	s_and_saveexec_b64 s[14:15], s[10:11]
	s_cbranch_execz .LBB0_421
	s_ashr_i32 s25, s24, 31
	s_lshl_b64 s[28:29], s[24:25], 2
	s_add_u32 s28, s64, s28
	s_addc_u32 s29, s65, s29
	global_store_dword v137, v1, s[28:29] offset:108
; template <int GRP>
; __device__ __forceinline__ void y_phase(Frame& F, const MW& W) {
;     ...
;         if (nsc) {
;             f32x4 N = (f32x4){0.f, 0.f, 0.f, 0.f}; float mm = 0.f;
; #pragma unroll
;             for (int c = 0; c < 32; ++c) {
;                 *(f32x4*)(W.NP + ((size_t)bh * 32 + c) * 128 + g * 4) = N; if (g == 0) W.MP[bh * 32 + c] = mm;
;                 const float bl = sc[2 * c], am = sc[2 * c + 1], mn = fmaxf(bl + mm, am), dec = __expf(bl + mm - mn), inj = __expf(am - mn);
;                 N = N * dec + nv[c] * inj; mm = mn; }
.LBB0_421:
	s_or_b64 exec, exec, s[14:15]
	v_readlane_b32 s100, v252, 27
	s_nop 1
	v_mov_b32_e32 v132, s100
	v_readlane_b32 s100, v253, 27
	s_nop 1
	v_mov_b32_e32 v133, s100
	v_lshl_add_u64 v[130:131], s[26:27], 0, v[136:137]
	v_add_co_u32_e32 v154, vcc, 0x3000, v130
	v_add_f32_e32 v132, v1, v132
	v_max_f32_e32 v1, v133, v133
	v_max_f32_e32 v1, v132, v1
	v_sub_f32_e32 v132, v132, v1
	v_sub_f32_e32 v133, v133, v1
	v_mul_f32_e32 v152, 0x3fb8aa3b, v132
	v_mul_f32_e32 v132, 0x3fb8aa3b, v133
	v_exp_f32_e32 v132, v132
	v_exp_f32_e32 v152, v152
	v_addc_co_u32_e32 v155, vcc, 0, v131, vcc
	v_pk_mul_f32 v[156:157], v[110:111], v[132:133] op_sel_hi:[1,0]
	v_pk_mul_f32 v[132:133], v[112:113], v[132:133] op_sel_hi:[1,0]
	v_pk_fma_f32 v[126:127], v[126:127], v[152:153], v[156:157] op_sel_hi:[1,0,1]
	v_pk_fma_f32 v[128:129], v[128:129], v[152:153], v[132:133] op_sel_hi:[1,0,1]
	global_store_dwordx4 v[154:155], v[126:129], off offset:2048
	s_and_saveexec_b64 s[14:15], s[10:11]
	s_cbranch_execz .LBB0_423
	s_ashr_i32 s25, s24, 31
	s_lshl_b64 s[28:29], s[24:25], 2
	s_add_u32 s28, s64, s28
	s_addc_u32 s29, s65, s29
	global_store_dword v137, v1, s[28:29] offset:112
.LBB0_423:
	s_or_b64 exec, exec, s[14:15]
	v_readlane_b32 s100, v252, 28
	s_nop 1
	v_mov_b32_e32 v132, s100
	v_readlane_b32 s100, v253, 28
	s_nop 1
	v_mov_b32_e32 v133, s100
	v_add_co_u32_e32 v130, vcc, 0x3000, v130
	v_add_f32_e32 v132, v1, v132
	v_max_f32_e32 v1, v133, v133
	v_max_f32_e32 v1, v132, v1
	v_sub_f32_e32 v132, v132, v1
	v_sub_f32_e32 v133, v133, v1
	v_mul_f32_e32 v152, 0x3fb8aa3b, v132
	v_mul_f32_e32 v132, 0x3fb8aa3b, v133
	v_exp_f32_e32 v132, v132
	v_exp_f32_e32 v152, v152
	v_addc_co_u32_e32 v131, vcc, 0, v131, vcc
	v_pk_mul_f32 v[154:155], v[106:107], v[132:133] op_sel_hi:[1,0]
	v_pk_mul_f32 v[132:133], v[108:109], v[132:133] op_sel_hi:[1,0]
	v_pk_fma_f32 v[126:127], v[126:127], v[152:153], v[154:155] op_sel_hi:[1,0,1]
	v_pk_fma_f32 v[128:129], v[128:129], v[152:153], v[132:133] op_sel_hi:[1,0,1]
	global_store_dwordx4 v[130:131], v[126:129], off offset:2560
	s_and_saveexec_b64 s[14:15], s[10:11]
	s_cbranch_execz .LBB0_425
	s_ashr_i32 s25, s24, 31
	s_lshl_b64 s[28:29], s[24:25], 2
	s_add_u32 s28, s64, s28
	s_addc_u32 s29, s65, s29
	global_store_dword v137, v1, s[28:29] offset:116
.LBB0_425:
	s_or_b64 exec, exec, s[14:15]
	v_readlane_b32 s100, v252, 29
	s_nop 1
	v_mov_b32_e32 v132, s100
	v_readlane_b32 s100, v253, 29
	s_nop 1
	v_mov_b32_e32 v133, s100
	v_lshl_add_u64 v[130:131], s[26:27], 0, v[136:137]
	v_add_co_u32_e32 v152, vcc, 0x3000, v130
	v_add_f32_e32 v132, v1, v132
	v_max_f32_e32 v1, v133, v133
	v_max_f32_e32 v1, v132, v1
	v_sub_f32_e32 v132, v132, v1
	v_sub_f32_e32 v133, v133, v1
	v_mul_f32_e32 v136, 0x3fb8aa3b, v132
	v_mul_f32_e32 v132, 0x3fb8aa3b, v133
	v_exp_f32_e32 v132, v132
	v_exp_f32_e32 v136, v136
	v_addc_co_u32_e32 v153, vcc, 0, v131, vcc
	v_pk_mul_f32 v[154:155], v[102:103], v[132:133] op_sel_hi:[1,0]
	v_pk_mul_f32 v[132:133], v[104:105], v[132:133] op_sel_hi:[1,0]
	v_pk_fma_f32 v[126:127], v[126:127], v[136:137], v[154:155] op_sel_hi:[1,0,1]
	v_pk_fma_f32 v[128:129], v[128:129], v[136:137], v[132:133] op_sel_hi:[1,0,1]
	global_store_dwordx4 v[152:153], v[126:129], off offset:3072
	s_and_saveexec_b64 s[14:15], s[10:11]
	s_cbranch_execz .LBB0_427
	s_ashr_i32 s25, s24, 31
	s_lshl_b64 s[26:27], s[24:25], 2
	s_add_u32 s26, s64, s26
	s_addc_u32 s27, s65, s27
	global_store_dword v137, v1, s[26:27] offset:120
.LBB0_427:
	s_or_b64 exec, exec, s[14:15]
	v_readlane_b32 s100, v252, 30
	s_nop 1
	v_mov_b32_e32 v132, s100
	v_readlane_b32 s100, v253, 30
	s_nop 1
	v_mov_b32_e32 v133, s100
	v_add_co_u32_e32 v130, vcc, 0x3000, v130
	v_add_f32_e32 v132, v1, v132
	v_max_f32_e32 v1, v133, v133
	v_max_f32_e32 v1, v132, v1
	v_sub_f32_e32 v132, v132, v1
	v_sub_f32_e32 v133, v133, v1
	v_mul_f32_e32 v136, 0x3fb8aa3b, v132
	v_mul_f32_e32 v132, 0x3fb8aa3b, v133
	v_exp_f32_e32 v132, v132
	v_exp_f32_e32 v136, v136
	v_addc_co_u32_e32 v131, vcc, 0, v131, vcc
	v_pk_mul_f32 v[152:153], v[98:99], v[132:133] op_sel_hi:[1,0]
	v_pk_mul_f32 v[132:133], v[100:101], v[132:133] op_sel_hi:[1,0]
	v_pk_fma_f32 v[126:127], v[126:127], v[136:137], v[152:153] op_sel_hi:[1,0,1]
	v_pk_fma_f32 v[128:129], v[128:129], v[136:137], v[132:133] op_sel_hi:[1,0,1]
	global_store_dwordx4 v[130:131], v[126:129], off offset:3584
	s_and_b64 exec, exec, s[10:11]
	s_cbranch_execz .LBB0_429
	s_ashr_i32 s25, s24, 31
	s_lshl_b64 s[10:11], s[24:25], 2
	s_add_u32 s10, s64, s10
	s_addc_u32 s11, s65, s11
	global_store_dword v137, v1, s[10:11] offset:124

; __device__ __forceinline__ int cslot(int bh, int c) { return (c + bh) & 31; }
; template <int GRP>
; __device__ __forceinline__ void y_phase(Frame& F, const MW& W) {
;     ...
; #pragma unroll
;         for (int c = 0; c < 32; ++c) {
;             u32x2 o; o.x = pg8::pack_fp8x4(C[0], C[1], C[2], C[3]); o.y = pg8::pack_fp8x4(C[4], C[5], C[6], C[7]); *(u32x2*)(W.CP + off + (size_t)cslot(bh, c) * 16384) = o;
;             const float bl = sc[2 * c], am = sc[2 * c + 1], mn = fmaxf(bl + m, am), dec = __expf(bl + m - mn), inj = __expf(am - mn);
;             const auto x0 = __builtin_amdgcn_cvt_pk_f32_fp8((int)v[c].x, false), x1 = __builtin_amdgcn_cvt_pk_f32_fp8((int)v[c].x, true), x2 = __builtin_amdgcn_cvt_pk_f32_fp8((int)v[c].y, false), x3 = __builtin_amdgcn_cvt_pk_f32_fp8((int)v[c].y, true);
;             C[0] = C[0] * dec + x0[0] * inj; C[1] = C[1] * dec + x0[1] * inj; C[2] = C[2] * dec + x1[0] * inj; C[3] = C[3] * dec + x1[1] * inj;
;             C[4] = C[4] * dec + x2[0] * inj; C[5] = C[5] * dec + x2[1] * inj; C[6] = C[6] * dec + x3[0] * inj; C[7] = C[7] * dec + x3[1] * inj; m = mn; }
.LBB0_1547:
	s_or_b64 exec, exec, s[12:13]
	v_mov_b32_e32 v202, v133
	v_cvt_pk_fp8_f32 v202, 0, 0
	v_readlane_b32 vcc_lo, v255, 21
	v_readlane_b32 vcc_hi, v255, 22
	s_lshl_b64 s[12:13], s[18:19], 8
	v_cvt_pk_fp8_f32 v202, 0, 0 op_sel:[0,0,1]
	v_readlane_b32 s19, v255, 19
	v_lshl_add_u64 v[126:127], vcc, 0, v[126:127]
	s_add_u32 s12, s19, s12
	v_readlane_b32 s19, v255, 20
	v_mov_b32_e32 v203, v202
	v_lshl_add_u64 v[204:205], v[126:127], 0, s[16:17]
	s_addc_u32 s13, s19, s13
	global_store_dwordx2 v[204:205], v[202:203], off
	v_and_b32_e32 v254, 31, v194
	v_lshlrev_b32_e32 v254, 3, v254
	global_load_dwordx2 v[252:253], v254, s[12:13]
	global_load_dwordx2 v[202:203], v133, s[12:13]
	s_waitcnt vmcnt(32)
	v_cvt_pk_f32_fp8_sdwa v[210:211], v200 src0_sel:WORD_1
	v_cvt_pk_f32_fp8_e32 v[212:213], v201
	v_mov_b32_e32 v230, v133
	s_waitcnt vmcnt(31)
	v_cvt_pk_f32_fp8_sdwa v[232:233], v198 src0_sel:WORD_1
	v_cvt_pk_f32_fp8_e32 v[234:235], v199
	v_cvt_pk_f32_fp8_sdwa v[236:237], v199 src0_sel:WORD_1
	s_add_i32 s76, s76, 0x7c000
	s_and_b32 s16, s76, 0x7c000
	s_waitcnt vmcnt(0)
	v_add_f32_e32 v1, 0, v202
	v_max_f32_e32 v195, v203, v203
	v_max_f32_e32 v195, v1, v195
	v_sub_f32_e32 v1, v1, v195
	v_mul_f32_e32 v1, 0x3fb8aa3b, v1
	v_exp_f32_e32 v228, v1
	v_sub_f32_e32 v1, v203, v195
	v_mul_f32_e32 v1, 0x3fb8aa3b, v1
	v_cvt_pk_f32_fp8_e32 v[202:203], v200
	v_cvt_pk_f32_fp8_sdwa v[200:201], v201 src0_sel:WORD_1
	v_exp_f32_e32 v229, v1
	v_mov_b32_e32 v231, v200
	v_pk_mul_f32 v[208:209], v[228:229], v[230:231]
	s_nop 0
	v_fma_f32 v206, v202, v229, v208
	v_fma_f32 v204, v203, v229, v208
	v_fma_f32 v202, v210, v229, v208
	v_fma_f32 v200, v211, v229, v208
	v_fma_f32 v214, v229, v212, v208
	v_fma_f32 v212, v229, v213, v208
	v_pk_fma_f32 v[210:211], v[228:229], v[230:231], v[208:209] op_sel:[0,0,1] op_sel_hi:[1,1,0]
	v_fmac_f32_e32 v208, v229, v201
	v_med3_f32 v1, v206, s14, v221
	v_med3_f32 v201, v204, s14, v221
	v_mov_b32_e32 v228, v133
	v_cvt_pk_fp8_f32 v228, v1, v201
	v_med3_f32 v1, v214, s14, v221
	v_med3_f32 v201, v212, s14, v221
	v_mov_b32_e32 v229, v133
	v_cvt_pk_fp8_f32 v229, v1, v201
	v_med3_f32 v203, v202, s14, v221
	v_med3_f32 v205, v200, s14, v221
	v_cvt_pk_fp8_f32 v228, v203, v205 op_sel:[0,0,1]
	v_med3_f32 v203, v210, s14, v221
	v_med3_f32 v205, v208, s14, v221
	v_cvt_pk_fp8_f32 v229, v203, v205 op_sel:[0,0,1]
	v_lshl_add_u64 v[230:231], v[126:127], 0, s[62:63]
	v_mov_b32_e32 v203, v232
	v_mov_b32_e32 v201, v233
	global_store_dwordx2 v[230:231], v[228:229], off
	v_readlane_b32 s100, v252, 1
	s_nop 1
	v_mov_b32_e32 v228, s100
	v_readlane_b32 s100, v253, 1
	s_nop 1
	v_mov_b32_e32 v229, s100
	v_cvt_pk_f32_fp8_e32 v[230:231], v198
	v_mov_b32_e32 v207, v230
	v_mov_b32_e32 v205, v231
	v_add_f32_e32 v1, v195, v228
	v_max_f32_e32 v195, v229, v229
	v_max_f32_e32 v195, v1, v195
	v_sub_f32_e32 v1, v1, v195
	v_mul_f32_e32 v1, 0x3fb8aa3b, v1
	v_exp_f32_e32 v228, v1
	v_sub_f32_e32 v1, v229, v195
	v_mul_f32_e32 v1, 0x3fb8aa3b, v1
	v_exp_f32_e32 v229, v1
	s_nop 0
	v_mul_f32_e32 v198, v230, v229
	v_pk_fma_f32 v[206:207], v[206:207], v[228:229], v[198:199] op_sel_hi:[1,1,0]
	v_mul_f32_e32 v198, v231, v229
	v_pk_fma_f32 v[204:205], v[204:205], v[228:229], v[198:199] op_sel_hi:[1,1,0]
	v_mul_f32_e32 v198, v232, v229
	v_pk_fma_f32 v[202:203], v[202:203], v[228:229], v[198:199] op_sel_hi:[1,1,0]
	v_mul_f32_e32 v198, v233, v229
	v_pk_fma_f32 v[200:201], v[200:201], v[228:229], v[198:199] op_sel_hi:[1,1,0]
	v_mov_b32_e32 v215, v229
	v_mov_b32_e32 v198, v228
	v_mov_b32_e32 v199, v234
	v_mul_f32_e32 v230, v229, v234
	v_pk_fma_f32 v[198:199], v[214:215], v[198:199], v[230:231] op_sel_hi:[1,1,0]
	v_mov_b32_e32 v213, v229
	v_mov_b32_e32 v234, v228
	v_mul_f32_e32 v214, v229, v235
	v_pk_fma_f32 v[212:213], v[212:213], v[234:235], v[214:215] op_sel_hi:[1,1,0]
	v_mov_b32_e32 v211, v229
	v_mov_b32_e32 v214, v228
	v_mov_b32_e32 v215, v236
	v_mul_f32_e32 v230, v229, v236
	v_pk_fma_f32 v[210:211], v[210:211], v[214:215], v[230:231] op_sel_hi:[1,1,0]
	v_mov_b32_e32 v209, v229
	v_mov_b32_e32 v236, v228
	v_mul_f32_e32 v214, v229, v237
	v_pk_fma_f32 v[208:209], v[208:209], v[236:237], v[214:215] op_sel_hi:[1,1,0]
	v_med3_f32 v1, v206, s14, v221
	v_med3_f32 v199, v204, s14, v221
	v_mov_b32_e32 v214, v133
	v_cvt_pk_fp8_f32 v214, v1, v199
	v_med3_f32 v1, v198, s14, v221
	v_med3_f32 v199, v212, s14, v221
	v_mov_b32_e32 v215, v133
	v_cvt_pk_fp8_f32 v215, v1, v199
	v_med3_f32 v201, v202, s14, v221
	v_med3_f32 v203, v200, s14, v221
	v_cvt_pk_fp8_f32 v214, v201, v203 op_sel:[0,0,1]
	v_med3_f32 v201, v210, s14, v221
	v_med3_f32 v203, v208, s14, v221
	v_cvt_pk_fp8_f32 v215, v201, v203 op_sel:[0,0,1]
	v_lshl_add_u64 v[228:229], v[126:127], 0, s[70:71]
	v_cvt_pk_f32_fp8_sdwa v[230:231], v196 src0_sel:WORD_1
	v_cvt_pk_f32_fp8_e32 v[232:233], v197
	global_store_dwordx2 v[228:229], v[214:215], off
	v_readlane_b32 s100, v252, 2
	s_nop 1
	v_mov_b32_e32 v214, s100
	v_readlane_b32 s100, v253, 2
	s_nop 1
	v_mov_b32_e32 v215, s100
	v_cvt_pk_f32_fp8_e32 v[228:229], v196
	v_cvt_pk_f32_fp8_sdwa v[234:235], v197 src0_sel:WORD_1
	v_mov_b32_e32 v203, v230
	v_mov_b32_e32 v201, v231
	v_mov_b32_e32 v207, v228
	v_mov_b32_e32 v205, v229
	v_add_f32_e32 v1, v195, v214
	v_max_f32_e32 v195, v215, v215
	v_max_f32_e32 v195, v1, v195
	v_sub_f32_e32 v1, v1, v195
	v_mul_f32_e32 v1, 0x3fb8aa3b, v1
	v_exp_f32_e32 v214, v1
	v_sub_f32_e32 v1, v215, v195
	v_mul_f32_e32 v1, 0x3fb8aa3b, v1
	v_exp_f32_e32 v215, v1
	s_nop 0
	v_mul_f32_e32 v196, v228, v215
	v_pk_fma_f32 v[206:207], v[206:207], v[214:215], v[196:197] op_sel_hi:[1,1,0]
	v_mul_f32_e32 v196, v229, v215
	v_pk_fma_f32 v[204:205], v[204:205], v[214:215], v[196:197] op_sel_hi:[1,1,0]
; __device__ __forceinline__ int cslot(int bh, int c) { return (c + bh) & 31; }
; template <int GRP>
; __device__ __forceinline__ void y_phase(Frame& F, const MW& W) {
;     ...
;         for (int c = 0; c < 32; ++c) {
;             u32x2 o; o.x = pg8::pack_fp8x4(C[0], C[1], C[2], C[3]); o.y = pg8::pack_fp8x4(C[4], C[5], C[6], C[7]); *(u32x2*)(W.CP + off + (size_t)cslot(bh, c) * 16384) = o;
;             const float bl = sc[2 * c], am = sc[2 * c + 1], mn = fmaxf(bl + m, am), dec = __expf(bl + m - mn), inj = __expf(am - mn);
;             const auto x0 = __builtin_amdgcn_cvt_pk_f32_fp8((int)v[c].x, false), x1 = __builtin_amdgcn_cvt_pk_f32_fp8((int)v[c].x, true), x2 = __builtin_amdgcn_cvt_pk_f32_fp8((int)v[c].y, false), x3 = __builtin_amdgcn_cvt_pk_f32_fp8((int)v[c].y, true);
;             C[0] = C[0] * dec + x0[0] * inj; C[1] = C[1] * dec + x0[1] * inj; C[2] = C[2] * dec + x1[0] * inj; C[3] = C[3] * dec + x1[1] * inj;
;             C[4] = C[4] * dec + x2[0] * inj; C[5] = C[5] * dec + x2[1] * inj; C[6] = C[6] * dec + x3[0] * inj; C[7] = C[7] * dec + x3[1] * inj; m = mn; }
	v_mul_f32_e32 v196, v230, v215
	v_pk_fma_f32 v[202:203], v[202:203], v[214:215], v[196:197] op_sel_hi:[1,1,0]
	v_mul_f32_e32 v196, v231, v215
	v_pk_fma_f32 v[200:201], v[200:201], v[214:215], v[196:197] op_sel_hi:[1,1,0]
	v_mov_b32_e32 v199, v215
	v_mov_b32_e32 v196, v214
	v_mov_b32_e32 v197, v232
	v_mul_f32_e32 v228, v215, v232
	v_pk_fma_f32 v[198:199], v[198:199], v[196:197], v[228:229] op_sel_hi:[1,1,0]
	v_mov_b32_e32 v213, v215
	v_mov_b32_e32 v232, v214
	v_mul_f32_e32 v196, v215, v233
	v_pk_fma_f32 v[196:197], v[212:213], v[232:233], v[196:197] op_sel_hi:[1,1,0]
	v_mov_b32_e32 v211, v215
	v_mov_b32_e32 v212, v214
	v_mov_b32_e32 v213, v234
	v_mul_f32_e32 v228, v215, v234
	v_pk_fma_f32 v[210:211], v[210:211], v[212:213], v[228:229] op_sel_hi:[1,1,0]
	v_mov_b32_e32 v209, v215
	v_mov_b32_e32 v234, v214
	v_mul_f32_e32 v212, v215, v235
	v_pk_fma_f32 v[208:209], v[208:209], v[234:235], v[212:213] op_sel_hi:[1,1,0]
	v_med3_f32 v1, v206, s14, v221
	v_med3_f32 v197, v204, s14, v221
	v_mov_b32_e32 v212, v133
	v_cvt_pk_fp8_f32 v212, v1, v197
	v_med3_f32 v1, v198, s14, v221
	v_med3_f32 v197, v196, s14, v221
	v_mov_b32_e32 v213, v133
	v_cvt_pk_fp8_f32 v213, v1, v197
	v_med3_f32 v199, v202, s14, v221
	v_med3_f32 v201, v200, s14, v221
	v_cvt_pk_fp8_f32 v212, v199, v201 op_sel:[0,0,1]
	v_med3_f32 v199, v210, s14, v221
	v_med3_f32 v201, v208, s14, v221
	v_cvt_pk_fp8_f32 v213, v199, v201 op_sel:[0,0,1]
	v_lshl_add_u64 v[214:215], v[126:127], 0, s[52:53]
	v_cvt_pk_f32_fp8_sdwa v[228:229], v192 src0_sel:WORD_1
	v_cvt_pk_f32_fp8_e32 v[230:231], v193
	global_store_dwordx2 v[214:215], v[212:213], off
	v_readlane_b32 s100, v252, 3
	s_nop 1
	v_mov_b32_e32 v212, s100
	v_readlane_b32 s100, v253, 3
	s_nop 1
	v_mov_b32_e32 v213, s100
	v_cvt_pk_f32_fp8_e32 v[214:215], v192
	v_cvt_pk_f32_fp8_sdwa v[232:233], v193 src0_sel:WORD_1
	v_mov_b32_e32 v203, v228
	v_mov_b32_e32 v201, v229
	v_mov_b32_e32 v207, v214
	v_mov_b32_e32 v205, v215
	v_add_f32_e32 v1, v195, v212
	v_max_f32_e32 v195, v213, v213
	v_max_f32_e32 v195, v1, v195
	v_sub_f32_e32 v1, v1, v195
	v_mul_f32_e32 v1, 0x3fb8aa3b, v1
	v_exp_f32_e32 v212, v1
	v_sub_f32_e32 v1, v213, v195
	v_mul_f32_e32 v1, 0x3fb8aa3b, v1
	v_exp_f32_e32 v213, v1
	s_nop 0
	v_mul_f32_e32 v192, v214, v213
	v_pk_fma_f32 v[206:207], v[206:207], v[212:213], v[192:193] op_sel_hi:[1,1,0]
	v_mul_f32_e32 v192, v215, v213
	v_pk_fma_f32 v[204:205], v[204:205], v[212:213], v[192:193] op_sel_hi:[1,1,0]
	v_mul_f32_e32 v192, v228, v213
	v_pk_fma_f32 v[202:203], v[202:203], v[212:213], v[192:193] op_sel_hi:[1,1,0]
	v_mul_f32_e32 v192, v229, v213
	v_pk_fma_f32 v[200:201], v[200:201], v[212:213], v[192:193] op_sel_hi:[1,1,0]
	v_mov_b32_e32 v199, v213
	v_mov_b32_e32 v192, v212
	v_mov_b32_e32 v193, v230
	v_mul_f32_e32 v214, v213, v230
	v_pk_fma_f32 v[198:199], v[198:199], v[192:193], v[214:215] op_sel_hi:[1,1,0]
	v_mov_b32_e32 v197, v213
	v_mov_b32_e32 v230, v212
	v_mul_f32_e32 v192, v213, v231
	v_pk_fma_f32 v[196:197], v[196:197], v[230:231], v[192:193] op_sel_hi:[1,1,0]
	v_mov_b32_e32 v211, v213
	v_mov_b32_e32 v192, v212
	v_mov_b32_e32 v193, v232
	v_mul_f32_e32 v214, v213, v232
	v_pk_fma_f32 v[192:193], v[210:211], v[192:193], v[214:215] op_sel_hi:[1,1,0]
	v_mov_b32_e32 v209, v213
	v_mov_b32_e32 v232, v212
	v_mul_f32_e32 v210, v213, v233
	v_pk_fma_f32 v[208:209], v[208:209], v[232:233], v[210:211] op_sel_hi:[1,1,0]
	v_med3_f32 v1, v206, s14, v221
	v_med3_f32 v193, v204, s14, v221
	v_mov_b32_e32 v210, v133
	v_cvt_pk_fp8_f32 v210, v1, v193
	v_med3_f32 v1, v198, s14, v221
	v_med3_f32 v193, v196, s14, v221
	v_mov_b32_e32 v211, v133
	v_cvt_pk_fp8_f32 v211, v1, v193
	v_med3_f32 v197, v202, s14, v221
	v_med3_f32 v199, v200, s14, v221
	v_cvt_pk_fp8_f32 v210, v197, v199 op_sel:[0,0,1]
	v_med3_f32 v197, v192, s14, v221
	v_med3_f32 v199, v208, s14, v221
	v_cvt_pk_fp8_f32 v211, v197, v199 op_sel:[0,0,1]
	v_lshl_add_u64 v[212:213], v[126:127], 0, s[68:69]
	v_cvt_pk_f32_fp8_sdwa v[214:215], v190 src0_sel:WORD_1
	v_cvt_pk_f32_fp8_e32 v[228:229], v191
	global_store_dwordx2 v[212:213], v[210:211], off
	v_readlane_b32 s100, v252, 4
	s_nop 1
	v_mov_b32_e32 v210, s100
	v_readlane_b32 s100, v253, 4
	s_nop 1
	v_mov_b32_e32 v211, s100
	v_cvt_pk_f32_fp8_e32 v[212:213], v190
	v_cvt_pk_f32_fp8_sdwa v[190:191], v191 src0_sel:WORD_1
	v_mov_b32_e32 v203, v214
	v_mov_b32_e32 v201, v215
	v_mov_b32_e32 v207, v212
	v_mov_b32_e32 v205, v213
	v_add_f32_e32 v1, v195, v210
	v_max_f32_e32 v193, v211, v211
	v_max_f32_e32 v195, v1, v193
	v_sub_f32_e32 v1, v1, v195
	v_mul_f32_e32 v1, 0x3fb8aa3b, v1
	v_exp_f32_e32 v210, v1
	v_sub_f32_e32 v1, v211, v195
	v_mul_f32_e32 v1, 0x3fb8aa3b, v1
	v_exp_f32_e32 v211, v1
	s_nop 0
	v_mul_f32_e32 v212, v212, v211
	v_pk_fma_f32 v[206:207], v[206:207], v[210:211], v[212:213] op_sel_hi:[1,1,0]
	v_mul_f32_e32 v212, v213, v211
	v_pk_fma_f32 v[204:205], v[204:205], v[210:211], v[212:213] op_sel_hi:[1,1,0]
	v_mul_f32_e32 v212, v214, v211
	v_pk_fma_f32 v[202:203], v[202:203], v[210:211], v[212:213] op_sel_hi:[1,1,0]
	v_mul_f32_e32 v212, v215, v211
	v_pk_fma_f32 v[200:201], v[200:201], v[210:211], v[212:213] op_sel_hi:[1,1,0]
	v_mov_b32_e32 v199, v211
	v_mov_b32_e32 v212, v210
	v_mov_b32_e32 v213, v228
	v_mul_f32_e32 v214, v211, v228
	v_pk_fma_f32 v[198:199], v[198:199], v[212:213], v[214:215] op_sel_hi:[1,1,0]
	v_mov_b32_e32 v197, v211
	v_mov_b32_e32 v228, v210
	v_mul_f32_e32 v212, v211, v229
	v_pk_fma_f32 v[196:197], v[196:197], v[228:229], v[212:213] op_sel_hi:[1,1,0]
	v_mov_b32_e32 v193, v211
	v_mov_b32_e32 v212, v210
	v_mov_b32_e32 v213, v190
	v_mul_f32_e32 v190, v211, v190
	v_pk_fma_f32 v[192:193], v[192:193], v[212:213], v[190:191] op_sel_hi:[1,1,0]
; __device__ __forceinline__ int cslot(int bh, int c) { return (c + bh) & 31; }
; template <int GRP>
; __device__ __forceinline__ void y_phase(Frame& F, const MW& W) {
;     ...
;         for (int c = 0; c < 32; ++c) {
;             u32x2 o; o.x = pg8::pack_fp8x4(C[0], C[1], C[2], C[3]); o.y = pg8::pack_fp8x4(C[4], C[5], C[6], C[7]); *(u32x2*)(W.CP + off + (size_t)cslot(bh, c) * 16384) = o;
;             const float bl = sc[2 * c], am = sc[2 * c + 1], mn = fmaxf(bl + m, am), dec = __expf(bl + m - mn), inj = __expf(am - mn);
;             const auto x0 = __builtin_amdgcn_cvt_pk_f32_fp8((int)v[c].x, false), x1 = __builtin_amdgcn_cvt_pk_f32_fp8((int)v[c].x, true), x2 = __builtin_amdgcn_cvt_pk_f32_fp8((int)v[c].y, false), x3 = __builtin_amdgcn_cvt_pk_f32_fp8((int)v[c].y, true);
;             C[0] = C[0] * dec + x0[0] * inj; C[1] = C[1] * dec + x0[1] * inj; C[2] = C[2] * dec + x1[0] * inj; C[3] = C[3] * dec + x1[1] * inj;
;             C[4] = C[4] * dec + x2[0] * inj; C[5] = C[5] * dec + x2[1] * inj; C[6] = C[6] * dec + x3[0] * inj; C[7] = C[7] * dec + x3[1] * inj; m = mn; }
	v_mov_b32_e32 v209, v211
	v_mov_b32_e32 v190, v210
	v_mul_f32_e32 v210, v211, v191
	v_pk_fma_f32 v[190:191], v[208:209], v[190:191], v[210:211] op_sel_hi:[1,1,0]
	v_med3_f32 v1, v206, s14, v221
	v_med3_f32 v191, v204, s14, v221
	v_mov_b32_e32 v208, v133
	v_cvt_pk_fp8_f32 v208, v1, v191
	v_med3_f32 v1, v198, s14, v221
	v_med3_f32 v191, v196, s14, v221
	v_mov_b32_e32 v209, v133
	v_cvt_pk_fp8_f32 v209, v1, v191
	v_med3_f32 v193, v202, s14, v221
	v_med3_f32 v197, v200, s14, v221
	v_cvt_pk_fp8_f32 v208, v193, v197 op_sel:[0,0,1]
	v_med3_f32 v193, v192, s14, v221
	v_med3_f32 v197, v190, s14, v221
	v_cvt_pk_fp8_f32 v209, v193, v197 op_sel:[0,0,1]
	v_lshl_add_u64 v[210:211], v[126:127], 0, s[54:55]
	v_cvt_pk_f32_fp8_sdwa v[212:213], v188 src0_sel:WORD_1
	v_cvt_pk_f32_fp8_e32 v[214:215], v189
	global_store_dwordx2 v[210:211], v[208:209], off
	v_readlane_b32 s100, v252, 5
	s_nop 1
	v_mov_b32_e32 v208, s100
	v_readlane_b32 s100, v253, 5
	s_nop 1
	v_mov_b32_e32 v209, s100
	v_cvt_pk_f32_fp8_e32 v[210:211], v188
	v_cvt_pk_f32_fp8_sdwa v[228:229], v189 src0_sel:WORD_1
	v_mov_b32_e32 v203, v212
	v_mov_b32_e32 v201, v213
	v_mov_b32_e32 v207, v210
	v_mov_b32_e32 v205, v211
	v_add_f32_e32 v1, v195, v208
	v_max_f32_e32 v191, v209, v209
	v_max_f32_e32 v195, v1, v191
	v_sub_f32_e32 v1, v1, v195
	v_mul_f32_e32 v1, 0x3fb8aa3b, v1
	v_exp_f32_e32 v208, v1
	v_sub_f32_e32 v1, v209, v195
	v_mul_f32_e32 v1, 0x3fb8aa3b, v1
	v_exp_f32_e32 v209, v1
	s_nop 0
	v_mul_f32_e32 v188, v210, v209
	v_pk_fma_f32 v[188:189], v[206:207], v[208:209], v[188:189] op_sel_hi:[1,1,0]
	v_mul_f32_e32 v206, v211, v209
	v_pk_fma_f32 v[204:205], v[204:205], v[208:209], v[206:207] op_sel_hi:[1,1,0]
	v_mul_f32_e32 v206, v212, v209
	v_pk_fma_f32 v[202:203], v[202:203], v[208:209], v[206:207] op_sel_hi:[1,1,0]
	v_mul_f32_e32 v206, v213, v209
	v_pk_fma_f32 v[200:201], v[200:201], v[208:209], v[206:207] op_sel_hi:[1,1,0]
	v_mov_b32_e32 v199, v209
	v_mov_b32_e32 v206, v208
	v_mov_b32_e32 v207, v214
	v_mul_f32_e32 v210, v209, v214
	v_pk_fma_f32 v[198:199], v[198:199], v[206:207], v[210:211] op_sel_hi:[1,1,0]
	v_mov_b32_e32 v197, v209
	v_mov_b32_e32 v214, v208
	v_mul_f32_e32 v206, v209, v215
	v_pk_fma_f32 v[196:197], v[196:197], v[214:215], v[206:207] op_sel_hi:[1,1,0]
	v_mov_b32_e32 v193, v209
	v_mov_b32_e32 v206, v208
	v_mov_b32_e32 v207, v228
	v_mul_f32_e32 v210, v209, v228
	v_pk_fma_f32 v[192:193], v[192:193], v[206:207], v[210:211] op_sel_hi:[1,1,0]
	v_mov_b32_e32 v191, v209
	v_mov_b32_e32 v228, v208
	v_mul_f32_e32 v206, v209, v229
	v_pk_fma_f32 v[190:191], v[190:191], v[228:229], v[206:207] op_sel_hi:[1,1,0]
	v_med3_f32 v1, v188, s14, v221
	v_med3_f32 v189, v204, s14, v221
	v_mov_b32_e32 v206, v133
	v_cvt_pk_fp8_f32 v206, v1, v189
	v_med3_f32 v1, v198, s14, v221
	v_med3_f32 v189, v196, s14, v221
	v_mov_b32_e32 v207, v133
	v_cvt_pk_fp8_f32 v207, v1, v189
	v_med3_f32 v191, v202, s14, v221
	v_med3_f32 v193, v200, s14, v221
	v_cvt_pk_fp8_f32 v206, v191, v193 op_sel:[0,0,1]
	v_med3_f32 v191, v192, s14, v221
	v_med3_f32 v193, v190, s14, v221
	v_cvt_pk_fp8_f32 v207, v191, v193 op_sel:[0,0,1]
	v_lshl_add_u64 v[208:209], v[126:127], 0, s[94:95]
	v_cvt_pk_f32_fp8_sdwa v[210:211], v186 src0_sel:WORD_1
	v_cvt_pk_f32_fp8_e32 v[212:213], v187
	global_store_dwordx2 v[208:209], v[206:207], off
	v_readlane_b32 s100, v252, 6
	s_nop 1
	v_mov_b32_e32 v206, s100
	v_readlane_b32 s100, v253, 6
	s_nop 1
	v_mov_b32_e32 v207, s100
	v_cvt_pk_f32_fp8_e32 v[208:209], v186
	v_cvt_pk_f32_fp8_sdwa v[214:215], v187 src0_sel:WORD_1
	v_mov_b32_e32 v203, v210
	v_mov_b32_e32 v201, v211
	v_mov_b32_e32 v205, v209
	v_add_f32_e32 v1, v195, v206
	v_max_f32_e32 v189, v207, v207
	v_max_f32_e32 v195, v1, v189
	v_sub_f32_e32 v1, v1, v195
	v_mul_f32_e32 v1, 0x3fb8aa3b, v1
	v_exp_f32_e32 v206, v1
	v_sub_f32_e32 v1, v207, v195
	v_mul_f32_e32 v1, 0x3fb8aa3b, v1
	v_exp_f32_e32 v207, v1
	v_mov_b32_e32 v189, v208
	v_mul_f32_e32 v186, v208, v207
	v_pk_fma_f32 v[188:189], v[188:189], v[206:207], v[186:187] op_sel_hi:[1,1,0]
	v_mul_f32_e32 v186, v209, v207
	v_pk_fma_f32 v[186:187], v[204:205], v[206:207], v[186:187] op_sel_hi:[1,1,0]
	v_mul_f32_e32 v204, v210, v207
	v_pk_fma_f32 v[202:203], v[202:203], v[206:207], v[204:205] op_sel_hi:[1,1,0]
	v_mul_f32_e32 v204, v211, v207
	v_pk_fma_f32 v[200:201], v[200:201], v[206:207], v[204:205] op_sel_hi:[1,1,0]
	v_mov_b32_e32 v199, v207
	v_mov_b32_e32 v204, v206
	v_mov_b32_e32 v205, v212
	v_mul_f32_e32 v208, v207, v212
	v_pk_fma_f32 v[198:199], v[198:199], v[204:205], v[208:209] op_sel_hi:[1,1,0]
	v_mov_b32_e32 v197, v207
	v_mov_b32_e32 v212, v206
	v_mul_f32_e32 v204, v207, v213
	v_pk_fma_f32 v[196:197], v[196:197], v[212:213], v[204:205] op_sel_hi:[1,1,0]
	v_mov_b32_e32 v193, v207
	v_mov_b32_e32 v204, v206
	v_mov_b32_e32 v205, v214
	v_mul_f32_e32 v208, v207, v214
	v_pk_fma_f32 v[192:193], v[192:193], v[204:205], v[208:209] op_sel_hi:[1,1,0]
	v_mov_b32_e32 v191, v207
	v_mov_b32_e32 v214, v206
	v_mul_f32_e32 v204, v207, v215
	v_pk_fma_f32 v[190:191], v[190:191], v[214:215], v[204:205] op_sel_hi:[1,1,0]
	v_med3_f32 v1, v188, s14, v221
	v_med3_f32 v187, v186, s14, v221
	v_mov_b32_e32 v204, v133
	v_cvt_pk_fp8_f32 v204, v1, v187
	v_med3_f32 v1, v198, s14, v221
	v_med3_f32 v187, v196, s14, v221
	v_mov_b32_e32 v205, v133
	v_cvt_pk_fp8_f32 v205, v1, v187
	v_med3_f32 v189, v202, s14, v221
	v_med3_f32 v191, v200, s14, v221
	v_cvt_pk_fp8_f32 v204, v189, v191 op_sel:[0,0,1]
	v_med3_f32 v189, v192, s14, v221
	v_med3_f32 v191, v190, s14, v221
	v_cvt_pk_fp8_f32 v205, v189, v191 op_sel:[0,0,1]
	v_lshl_add_u64 v[206:207], v[126:127], 0, s[92:93]
	v_cvt_pk_f32_fp8_sdwa v[208:209], v184 src0_sel:WORD_1
	v_cvt_pk_f32_fp8_e32 v[210:211], v185
; __device__ __forceinline__ int cslot(int bh, int c) { return (c + bh) & 31; }
; template <int GRP>
; __device__ __forceinline__ void y_phase(Frame& F, const MW& W) {
;     ...
;         for (int c = 0; c < 32; ++c) {
;             u32x2 o; o.x = pg8::pack_fp8x4(C[0], C[1], C[2], C[3]); o.y = pg8::pack_fp8x4(C[4], C[5], C[6], C[7]); *(u32x2*)(W.CP + off + (size_t)cslot(bh, c) * 16384) = o;
;             const float bl = sc[2 * c], am = sc[2 * c + 1], mn = fmaxf(bl + m, am), dec = __expf(bl + m - mn), inj = __expf(am - mn);
;             const auto x0 = __builtin_amdgcn_cvt_pk_f32_fp8((int)v[c].x, false), x1 = __builtin_amdgcn_cvt_pk_f32_fp8((int)v[c].x, true), x2 = __builtin_amdgcn_cvt_pk_f32_fp8((int)v[c].y, false), x3 = __builtin_amdgcn_cvt_pk_f32_fp8((int)v[c].y, true);
;             C[0] = C[0] * dec + x0[0] * inj; C[1] = C[1] * dec + x0[1] * inj; C[2] = C[2] * dec + x1[0] * inj; C[3] = C[3] * dec + x1[1] * inj;
;             C[4] = C[4] * dec + x2[0] * inj; C[5] = C[5] * dec + x2[1] * inj; C[6] = C[6] * dec + x3[0] * inj; C[7] = C[7] * dec + x3[1] * inj; m = mn; }
	global_store_dwordx2 v[206:207], v[204:205], off
	v_readlane_b32 s100, v252, 7
	s_nop 1
	v_mov_b32_e32 v204, s100
	v_readlane_b32 s100, v253, 7
	s_nop 1
	v_mov_b32_e32 v205, s100
	v_cvt_pk_f32_fp8_e32 v[206:207], v184
	v_cvt_pk_f32_fp8_sdwa v[212:213], v185 src0_sel:WORD_1
	v_mov_b32_e32 v203, v208
	v_mov_b32_e32 v201, v209
	v_mov_b32_e32 v189, v206
	v_add_f32_e32 v1, v195, v204
	v_max_f32_e32 v187, v205, v205
	v_max_f32_e32 v195, v1, v187
	v_sub_f32_e32 v1, v1, v195
	v_mul_f32_e32 v1, 0x3fb8aa3b, v1
	v_exp_f32_e32 v204, v1
	v_sub_f32_e32 v1, v205, v195
	v_mul_f32_e32 v1, 0x3fb8aa3b, v1
	v_exp_f32_e32 v205, v1
	v_mov_b32_e32 v187, v207
	v_mul_f32_e32 v184, v206, v205
	v_pk_fma_f32 v[188:189], v[188:189], v[204:205], v[184:185] op_sel_hi:[1,1,0]
	v_mul_f32_e32 v184, v207, v205
	v_pk_fma_f32 v[186:187], v[186:187], v[204:205], v[184:185] op_sel_hi:[1,1,0]
	v_mul_f32_e32 v184, v208, v205
	v_pk_fma_f32 v[184:185], v[202:203], v[204:205], v[184:185] op_sel_hi:[1,1,0]
	v_mul_f32_e32 v202, v209, v205
	v_pk_fma_f32 v[200:201], v[200:201], v[204:205], v[202:203] op_sel_hi:[1,1,0]
	v_mov_b32_e32 v199, v205
	v_mov_b32_e32 v202, v204
	v_mov_b32_e32 v203, v210
	v_mul_f32_e32 v206, v205, v210
	v_pk_fma_f32 v[198:199], v[198:199], v[202:203], v[206:207] op_sel_hi:[1,1,0]
	v_mov_b32_e32 v197, v205
	v_mov_b32_e32 v210, v204
	v_mul_f32_e32 v202, v205, v211
	v_pk_fma_f32 v[196:197], v[196:197], v[210:211], v[202:203] op_sel_hi:[1,1,0]
	v_mov_b32_e32 v193, v205
	v_mov_b32_e32 v202, v204
	v_mov_b32_e32 v203, v212
	v_mul_f32_e32 v206, v205, v212
	v_pk_fma_f32 v[192:193], v[192:193], v[202:203], v[206:207] op_sel_hi:[1,1,0]
	v_mov_b32_e32 v191, v205
	v_mov_b32_e32 v212, v204
	v_mul_f32_e32 v202, v205, v213
	v_pk_fma_f32 v[190:191], v[190:191], v[212:213], v[202:203] op_sel_hi:[1,1,0]
	v_med3_f32 v1, v188, s14, v221
	v_med3_f32 v185, v186, s14, v221
	v_mov_b32_e32 v202, v133
	v_cvt_pk_fp8_f32 v202, v1, v185
	v_med3_f32 v1, v198, s14, v221
	v_med3_f32 v185, v196, s14, v221
	v_mov_b32_e32 v203, v133
	v_cvt_pk_fp8_f32 v203, v1, v185
	v_med3_f32 v187, v184, s14, v221
	v_med3_f32 v189, v200, s14, v221
	v_cvt_pk_fp8_f32 v202, v187, v189 op_sel:[0,0,1]
	v_med3_f32 v187, v192, s14, v221
	v_med3_f32 v189, v190, s14, v221
	v_cvt_pk_fp8_f32 v203, v187, v189 op_sel:[0,0,1]
	v_lshl_add_u64 v[204:205], v[126:127], 0, s[0:1]
	v_cvt_pk_f32_fp8_sdwa v[206:207], v182 src0_sel:WORD_1
	v_cvt_pk_f32_fp8_e32 v[208:209], v183
	global_store_dwordx2 v[204:205], v[202:203], off
	v_readlane_b32 s100, v252, 8
	s_nop 1
	v_mov_b32_e32 v202, s100
	v_readlane_b32 s100, v253, 8
	s_nop 1
	v_mov_b32_e32 v203, s100
	v_cvt_pk_f32_fp8_e32 v[204:205], v182
	v_cvt_pk_f32_fp8_sdwa v[210:211], v183 src0_sel:WORD_1
	v_mov_b32_e32 v201, v207
	v_mov_b32_e32 v189, v204
	v_mov_b32_e32 v187, v205
	v_add_f32_e32 v1, v195, v202
	v_max_f32_e32 v185, v203, v203
	v_max_f32_e32 v195, v1, v185
	v_sub_f32_e32 v1, v1, v195
	v_mul_f32_e32 v1, 0x3fb8aa3b, v1
	v_exp_f32_e32 v202, v1
	v_sub_f32_e32 v1, v203, v195
	v_mul_f32_e32 v1, 0x3fb8aa3b, v1
	v_exp_f32_e32 v203, v1
	v_mov_b32_e32 v185, v206
	v_mul_f32_e32 v182, v204, v203
	v_pk_fma_f32 v[188:189], v[188:189], v[202:203], v[182:183] op_sel_hi:[1,1,0]
	v_mul_f32_e32 v182, v205, v203
	v_pk_fma_f32 v[186:187], v[186:187], v[202:203], v[182:183] op_sel_hi:[1,1,0]
	v_mul_f32_e32 v182, v206, v203
	v_pk_fma_f32 v[184:185], v[184:185], v[202:203], v[182:183] op_sel_hi:[1,1,0]
	v_mul_f32_e32 v182, v207, v203
	v_pk_fma_f32 v[182:183], v[200:201], v[202:203], v[182:183] op_sel_hi:[1,1,0]
	v_mov_b32_e32 v199, v203
	v_mov_b32_e32 v200, v202
	v_mov_b32_e32 v201, v208
	v_mul_f32_e32 v204, v203, v208
	v_pk_fma_f32 v[198:199], v[198:199], v[200:201], v[204:205] op_sel_hi:[1,1,0]
	v_mov_b32_e32 v197, v203
	v_mov_b32_e32 v208, v202
	v_mul_f32_e32 v200, v203, v209
	v_pk_fma_f32 v[196:197], v[196:197], v[208:209], v[200:201] op_sel_hi:[1,1,0]
	v_mov_b32_e32 v193, v203
	v_mov_b32_e32 v200, v202
	v_mov_b32_e32 v201, v210
	v_mul_f32_e32 v204, v203, v210
	v_pk_fma_f32 v[192:193], v[192:193], v[200:201], v[204:205] op_sel_hi:[1,1,0]
	v_mov_b32_e32 v191, v203
	v_mov_b32_e32 v210, v202
	v_mul_f32_e32 v200, v203, v211
	v_pk_fma_f32 v[190:191], v[190:191], v[210:211], v[200:201] op_sel_hi:[1,1,0]
	v_med3_f32 v1, v188, s14, v221
	v_med3_f32 v183, v186, s14, v221
	v_mov_b32_e32 v200, v133
	v_cvt_pk_fp8_f32 v200, v1, v183
	v_med3_f32 v1, v198, s14, v221
	v_med3_f32 v183, v196, s14, v221
	v_mov_b32_e32 v201, v133
	v_cvt_pk_fp8_f32 v201, v1, v183
	v_med3_f32 v185, v184, s14, v221
	v_med3_f32 v187, v182, s14, v221
	v_cvt_pk_fp8_f32 v200, v185, v187 op_sel:[0,0,1]
	v_med3_f32 v185, v192, s14, v221
	v_med3_f32 v187, v190, s14, v221
	v_cvt_pk_fp8_f32 v201, v185, v187 op_sel:[0,0,1]
	v_lshl_add_u64 v[202:203], v[126:127], 0, s[56:57]
	v_cvt_pk_f32_fp8_sdwa v[204:205], v180 src0_sel:WORD_1
	v_cvt_pk_f32_fp8_e32 v[206:207], v181
	global_store_dwordx2 v[202:203], v[200:201], off
	v_readlane_b32 s100, v252, 9
	s_nop 1
	v_mov_b32_e32 v200, s100
	v_readlane_b32 s100, v253, 9
	s_nop 1
	v_mov_b32_e32 v201, s100
	v_cvt_pk_f32_fp8_e32 v[202:203], v180
	v_cvt_pk_f32_fp8_sdwa v[208:209], v181 src0_sel:WORD_1
	v_mov_b32_e32 v185, v204
	v_mov_b32_e32 v189, v202
	v_mov_b32_e32 v187, v203
	v_add_f32_e32 v1, v195, v200
	v_max_f32_e32 v183, v201, v201
	v_max_f32_e32 v195, v1, v183
	v_sub_f32_e32 v1, v1, v195
	v_mul_f32_e32 v1, 0x3fb8aa3b, v1
	v_exp_f32_e32 v200, v1
	v_sub_f32_e32 v1, v201, v195
	v_mul_f32_e32 v1, 0x3fb8aa3b, v1
	v_exp_f32_e32 v201, v1
	v_mov_b32_e32 v183, v205
	v_mul_f32_e32 v180, v202, v201
	v_pk_fma_f32 v[188:189], v[188:189], v[200:201], v[180:181] op_sel_hi:[1,1,0]
	v_mul_f32_e32 v180, v203, v201
; __device__ __forceinline__ int cslot(int bh, int c) { return (c + bh) & 31; }
; template <int GRP>
; __device__ __forceinline__ void y_phase(Frame& F, const MW& W) {
;     ...
;         for (int c = 0; c < 32; ++c) {
;             u32x2 o; o.x = pg8::pack_fp8x4(C[0], C[1], C[2], C[3]); o.y = pg8::pack_fp8x4(C[4], C[5], C[6], C[7]); *(u32x2*)(W.CP + off + (size_t)cslot(bh, c) * 16384) = o;
;             const float bl = sc[2 * c], am = sc[2 * c + 1], mn = fmaxf(bl + m, am), dec = __expf(bl + m - mn), inj = __expf(am - mn);
;             const auto x0 = __builtin_amdgcn_cvt_pk_f32_fp8((int)v[c].x, false), x1 = __builtin_amdgcn_cvt_pk_f32_fp8((int)v[c].x, true), x2 = __builtin_amdgcn_cvt_pk_f32_fp8((int)v[c].y, false), x3 = __builtin_amdgcn_cvt_pk_f32_fp8((int)v[c].y, true);
;             C[0] = C[0] * dec + x0[0] * inj; C[1] = C[1] * dec + x0[1] * inj; C[2] = C[2] * dec + x1[0] * inj; C[3] = C[3] * dec + x1[1] * inj;
;             C[4] = C[4] * dec + x2[0] * inj; C[5] = C[5] * dec + x2[1] * inj; C[6] = C[6] * dec + x3[0] * inj; C[7] = C[7] * dec + x3[1] * inj; m = mn; }
	v_pk_fma_f32 v[186:187], v[186:187], v[200:201], v[180:181] op_sel_hi:[1,1,0]
	v_mul_f32_e32 v180, v204, v201
	v_pk_fma_f32 v[184:185], v[184:185], v[200:201], v[180:181] op_sel_hi:[1,1,0]
	v_mul_f32_e32 v180, v205, v201
	v_pk_fma_f32 v[182:183], v[182:183], v[200:201], v[180:181] op_sel_hi:[1,1,0]
	v_mov_b32_e32 v199, v201
	v_mov_b32_e32 v180, v200
	v_mov_b32_e32 v181, v206
	v_mul_f32_e32 v202, v201, v206
	v_pk_fma_f32 v[180:181], v[198:199], v[180:181], v[202:203] op_sel_hi:[1,1,0]
	v_mov_b32_e32 v197, v201
	v_mov_b32_e32 v206, v200
	v_mul_f32_e32 v198, v201, v207
	v_pk_fma_f32 v[196:197], v[196:197], v[206:207], v[198:199] op_sel_hi:[1,1,0]
	v_mov_b32_e32 v193, v201
	v_mov_b32_e32 v198, v200
	v_mov_b32_e32 v199, v208
	v_mul_f32_e32 v202, v201, v208
	v_pk_fma_f32 v[192:193], v[192:193], v[198:199], v[202:203] op_sel_hi:[1,1,0]
	v_mov_b32_e32 v191, v201
	v_mov_b32_e32 v208, v200
	v_mul_f32_e32 v198, v201, v209
	v_pk_fma_f32 v[190:191], v[190:191], v[208:209], v[198:199] op_sel_hi:[1,1,0]
	v_med3_f32 v1, v188, s14, v221
	v_med3_f32 v181, v186, s14, v221
	v_mov_b32_e32 v198, v133
	v_cvt_pk_fp8_f32 v198, v1, v181
	v_med3_f32 v1, v180, s14, v221
	v_med3_f32 v181, v196, s14, v221
	v_mov_b32_e32 v199, v133
	v_cvt_pk_fp8_f32 v199, v1, v181
	v_med3_f32 v183, v184, s14, v221
	v_med3_f32 v185, v182, s14, v221
	v_cvt_pk_fp8_f32 v198, v183, v185 op_sel:[0,0,1]
	v_med3_f32 v183, v192, s14, v221
	v_med3_f32 v185, v190, s14, v221
	v_cvt_pk_fp8_f32 v199, v183, v185 op_sel:[0,0,1]
	v_lshl_add_u64 v[200:201], v[126:127], 0, s[66:67]
	v_cvt_pk_f32_fp8_sdwa v[202:203], v178 src0_sel:WORD_1
	v_cvt_pk_f32_fp8_e32 v[204:205], v179
	global_store_dwordx2 v[200:201], v[198:199], off
	v_readlane_b32 s100, v252, 10
	s_nop 1
	v_mov_b32_e32 v198, s100
	v_readlane_b32 s100, v253, 10
	s_nop 1
	v_mov_b32_e32 v199, s100
	v_cvt_pk_f32_fp8_e32 v[200:201], v178
	v_cvt_pk_f32_fp8_sdwa v[206:207], v179 src0_sel:WORD_1
	v_mov_b32_e32 v185, v202
	v_mov_b32_e32 v183, v203
	v_mov_b32_e32 v189, v200
	v_mov_b32_e32 v187, v201
	v_add_f32_e32 v1, v195, v198
	v_max_f32_e32 v181, v199, v199
	v_max_f32_e32 v195, v1, v181
	v_sub_f32_e32 v1, v1, v195
	v_mul_f32_e32 v1, 0x3fb8aa3b, v1
	v_exp_f32_e32 v198, v1
	v_sub_f32_e32 v1, v199, v195
	v_mul_f32_e32 v1, 0x3fb8aa3b, v1
	v_exp_f32_e32 v199, v1
	s_nop 0
	v_mul_f32_e32 v178, v200, v199
	v_pk_fma_f32 v[188:189], v[188:189], v[198:199], v[178:179] op_sel_hi:[1,1,0]
	v_mul_f32_e32 v178, v201, v199
	v_pk_fma_f32 v[186:187], v[186:187], v[198:199], v[178:179] op_sel_hi:[1,1,0]
	v_mul_f32_e32 v178, v202, v199
	v_pk_fma_f32 v[184:185], v[184:185], v[198:199], v[178:179] op_sel_hi:[1,1,0]
	v_mul_f32_e32 v178, v203, v199
	v_pk_fma_f32 v[182:183], v[182:183], v[198:199], v[178:179] op_sel_hi:[1,1,0]
	v_mov_b32_e32 v181, v199
	v_mov_b32_e32 v178, v198
	v_mov_b32_e32 v179, v204
	v_mul_f32_e32 v200, v199, v204
	v_pk_fma_f32 v[180:181], v[180:181], v[178:179], v[200:201] op_sel_hi:[1,1,0]
	v_mov_b32_e32 v197, v199
	v_mov_b32_e32 v204, v198
	v_mul_f32_e32 v178, v199, v205
	v_pk_fma_f32 v[178:179], v[196:197], v[204:205], v[178:179] op_sel_hi:[1,1,0]
	v_mov_b32_e32 v193, v199
	v_mov_b32_e32 v196, v198
	v_mov_b32_e32 v197, v206
	v_mul_f32_e32 v200, v199, v206
	v_pk_fma_f32 v[192:193], v[192:193], v[196:197], v[200:201] op_sel_hi:[1,1,0]
	v_mov_b32_e32 v191, v199
	v_mov_b32_e32 v206, v198
	v_mul_f32_e32 v196, v199, v207
	v_pk_fma_f32 v[190:191], v[190:191], v[206:207], v[196:197] op_sel_hi:[1,1,0]
	v_med3_f32 v1, v188, s14, v221
	v_med3_f32 v179, v186, s14, v221
	v_mov_b32_e32 v196, v133
	v_cvt_pk_fp8_f32 v196, v1, v179
	v_med3_f32 v1, v180, s14, v221
	v_med3_f32 v179, v178, s14, v221
	v_mov_b32_e32 v197, v133
	v_cvt_pk_fp8_f32 v197, v1, v179
	v_med3_f32 v181, v184, s14, v221
	v_med3_f32 v183, v182, s14, v221
	v_cvt_pk_fp8_f32 v196, v181, v183 op_sel:[0,0,1]
	v_med3_f32 v181, v192, s14, v221
	v_med3_f32 v183, v190, s14, v221
	v_cvt_pk_fp8_f32 v197, v181, v183 op_sel:[0,0,1]
	v_lshl_add_u64 v[198:199], v[126:127], 0, s[90:91]
	v_cvt_pk_f32_fp8_sdwa v[200:201], v176 src0_sel:WORD_1
	v_cvt_pk_f32_fp8_e32 v[202:203], v177
	global_store_dwordx2 v[198:199], v[196:197], off
	v_readlane_b32 s100, v252, 11
	s_nop 1
	v_mov_b32_e32 v196, s100
	v_readlane_b32 s100, v253, 11
	s_nop 1
	v_mov_b32_e32 v197, s100
	v_cvt_pk_f32_fp8_e32 v[198:199], v176
	v_cvt_pk_f32_fp8_sdwa v[204:205], v177 src0_sel:WORD_1
	v_mov_b32_e32 v185, v200
	v_mov_b32_e32 v183, v201
	v_mov_b32_e32 v189, v198
	v_mov_b32_e32 v187, v199
	v_add_f32_e32 v1, v195, v196
	v_max_f32_e32 v179, v197, v197
	v_max_f32_e32 v195, v1, v179
	v_sub_f32_e32 v1, v1, v195
	v_mul_f32_e32 v1, 0x3fb8aa3b, v1
	v_exp_f32_e32 v196, v1
	v_sub_f32_e32 v1, v197, v195
	v_mul_f32_e32 v1, 0x3fb8aa3b, v1
	v_exp_f32_e32 v197, v1
	s_nop 0
	v_mul_f32_e32 v176, v198, v197
	v_pk_fma_f32 v[188:189], v[188:189], v[196:197], v[176:177] op_sel_hi:[1,1,0]
	v_mul_f32_e32 v176, v199, v197
	v_pk_fma_f32 v[186:187], v[186:187], v[196:197], v[176:177] op_sel_hi:[1,1,0]
	v_mul_f32_e32 v176, v200, v197
	v_pk_fma_f32 v[184:185], v[184:185], v[196:197], v[176:177] op_sel_hi:[1,1,0]
	v_mul_f32_e32 v176, v201, v197
	v_pk_fma_f32 v[182:183], v[182:183], v[196:197], v[176:177] op_sel_hi:[1,1,0]
	v_mov_b32_e32 v181, v197
	v_mov_b32_e32 v176, v196
	v_mov_b32_e32 v177, v202
	v_mul_f32_e32 v198, v197, v202
	v_pk_fma_f32 v[180:181], v[180:181], v[176:177], v[198:199] op_sel_hi:[1,1,0]
	v_mov_b32_e32 v179, v197
	v_mov_b32_e32 v202, v196
	v_mul_f32_e32 v176, v197, v203
	v_pk_fma_f32 v[178:179], v[178:179], v[202:203], v[176:177] op_sel_hi:[1,1,0]
	v_mov_b32_e32 v193, v197
	v_mov_b32_e32 v176, v196
	v_mov_b32_e32 v177, v204
	v_mul_f32_e32 v198, v197, v204
; __device__ __forceinline__ int cslot(int bh, int c) { return (c + bh) & 31; }
; template <int GRP>
; __device__ __forceinline__ void y_phase(Frame& F, const MW& W) {
;     ...
;         for (int c = 0; c < 32; ++c) {
;             u32x2 o; o.x = pg8::pack_fp8x4(C[0], C[1], C[2], C[3]); o.y = pg8::pack_fp8x4(C[4], C[5], C[6], C[7]); *(u32x2*)(W.CP + off + (size_t)cslot(bh, c) * 16384) = o;
;             const float bl = sc[2 * c], am = sc[2 * c + 1], mn = fmaxf(bl + m, am), dec = __expf(bl + m - mn), inj = __expf(am - mn);
;             const auto x0 = __builtin_amdgcn_cvt_pk_f32_fp8((int)v[c].x, false), x1 = __builtin_amdgcn_cvt_pk_f32_fp8((int)v[c].x, true), x2 = __builtin_amdgcn_cvt_pk_f32_fp8((int)v[c].y, false), x3 = __builtin_amdgcn_cvt_pk_f32_fp8((int)v[c].y, true);
;             C[0] = C[0] * dec + x0[0] * inj; C[1] = C[1] * dec + x0[1] * inj; C[2] = C[2] * dec + x1[0] * inj; C[3] = C[3] * dec + x1[1] * inj;
;             C[4] = C[4] * dec + x2[0] * inj; C[5] = C[5] * dec + x2[1] * inj; C[6] = C[6] * dec + x3[0] * inj; C[7] = C[7] * dec + x3[1] * inj; m = mn; }
	v_pk_fma_f32 v[176:177], v[192:193], v[176:177], v[198:199] op_sel_hi:[1,1,0]
	v_mov_b32_e32 v191, v197
	v_mov_b32_e32 v204, v196
	v_mul_f32_e32 v192, v197, v205
	v_pk_fma_f32 v[190:191], v[190:191], v[204:205], v[192:193] op_sel_hi:[1,1,0]
	v_med3_f32 v1, v188, s14, v221
	v_med3_f32 v177, v186, s14, v221
	v_mov_b32_e32 v192, v133
	v_cvt_pk_fp8_f32 v192, v1, v177
	v_med3_f32 v1, v180, s14, v221
	v_med3_f32 v177, v178, s14, v221
	v_mov_b32_e32 v193, v133
	v_cvt_pk_fp8_f32 v193, v1, v177
	v_med3_f32 v179, v184, s14, v221
	v_med3_f32 v181, v182, s14, v221
	v_cvt_pk_fp8_f32 v192, v179, v181 op_sel:[0,0,1]
	v_med3_f32 v179, v176, s14, v221
	v_med3_f32 v181, v190, s14, v221
	v_cvt_pk_fp8_f32 v193, v179, v181 op_sel:[0,0,1]
	v_lshl_add_u64 v[196:197], v[126:127], 0, s[88:89]
	v_cvt_pk_f32_fp8_sdwa v[198:199], v174 src0_sel:WORD_1
	v_cvt_pk_f32_fp8_e32 v[200:201], v175
	global_store_dwordx2 v[196:197], v[192:193], off
	v_readlane_b32 s100, v252, 12
	s_nop 1
	v_mov_b32_e32 v192, s100
	v_readlane_b32 s100, v253, 12
	s_nop 1
	v_mov_b32_e32 v193, s100
	v_cvt_pk_f32_fp8_e32 v[196:197], v174
	v_cvt_pk_f32_fp8_sdwa v[174:175], v175 src0_sel:WORD_1
	v_mov_b32_e32 v185, v198
	v_mov_b32_e32 v183, v199
	v_mov_b32_e32 v189, v196
	v_mov_b32_e32 v187, v197
	v_add_f32_e32 v1, v195, v192
	v_max_f32_e32 v177, v193, v193
	v_max_f32_e32 v195, v1, v177
	v_sub_f32_e32 v1, v1, v195
	v_mul_f32_e32 v1, 0x3fb8aa3b, v1
	v_exp_f32_e32 v192, v1
	v_sub_f32_e32 v1, v193, v195
	v_mul_f32_e32 v1, 0x3fb8aa3b, v1
	v_exp_f32_e32 v193, v1
	s_nop 0
	v_mul_f32_e32 v196, v196, v193
	v_pk_fma_f32 v[188:189], v[188:189], v[192:193], v[196:197] op_sel_hi:[1,1,0]
	v_mul_f32_e32 v196, v197, v193
	v_pk_fma_f32 v[186:187], v[186:187], v[192:193], v[196:197] op_sel_hi:[1,1,0]
	v_mul_f32_e32 v196, v198, v193
	v_pk_fma_f32 v[184:185], v[184:185], v[192:193], v[196:197] op_sel_hi:[1,1,0]
	v_mul_f32_e32 v196, v199, v193
	v_pk_fma_f32 v[182:183], v[182:183], v[192:193], v[196:197] op_sel_hi:[1,1,0]
	v_mov_b32_e32 v181, v193
	v_mov_b32_e32 v196, v192
	v_mov_b32_e32 v197, v200
	v_mul_f32_e32 v198, v193, v200
	v_pk_fma_f32 v[180:181], v[180:181], v[196:197], v[198:199] op_sel_hi:[1,1,0]
	v_mov_b32_e32 v179, v193
	v_mov_b32_e32 v200, v192
	v_mul_f32_e32 v196, v193, v201
	v_pk_fma_f32 v[178:179], v[178:179], v[200:201], v[196:197] op_sel_hi:[1,1,0]
	v_mov_b32_e32 v177, v193
	v_mov_b32_e32 v196, v192
	v_mov_b32_e32 v197, v174
	v_mul_f32_e32 v174, v193, v174
	v_pk_fma_f32 v[176:177], v[176:177], v[196:197], v[174:175] op_sel_hi:[1,1,0]
	v_mov_b32_e32 v191, v193
	v_mov_b32_e32 v174, v192
	v_mul_f32_e32 v192, v193, v175
	v_pk_fma_f32 v[174:175], v[190:191], v[174:175], v[192:193] op_sel_hi:[1,1,0]
	v_med3_f32 v1, v188, s14, v221
	v_med3_f32 v175, v186, s14, v221
	v_mov_b32_e32 v190, v133
	v_cvt_pk_fp8_f32 v190, v1, v175
	v_med3_f32 v1, v180, s14, v221
	v_med3_f32 v175, v178, s14, v221
	v_mov_b32_e32 v191, v133
	v_cvt_pk_fp8_f32 v191, v1, v175
	v_med3_f32 v177, v184, s14, v221
	v_med3_f32 v179, v182, s14, v221
	v_cvt_pk_fp8_f32 v190, v177, v179 op_sel:[0,0,1]
	v_med3_f32 v177, v176, s14, v221
	v_med3_f32 v179, v174, s14, v221
	v_cvt_pk_fp8_f32 v191, v177, v179 op_sel:[0,0,1]
	v_lshl_add_u64 v[192:193], v[126:127], 0, s[86:87]
	v_cvt_pk_f32_fp8_sdwa v[196:197], v172 src0_sel:WORD_1
	v_cvt_pk_f32_fp8_e32 v[198:199], v173
	global_store_dwordx2 v[192:193], v[190:191], off
	v_readlane_b32 s100, v252, 13
	s_nop 1
	v_mov_b32_e32 v190, s100
	v_readlane_b32 s100, v253, 13
	s_nop 1
	v_mov_b32_e32 v191, s100
	v_cvt_pk_f32_fp8_e32 v[192:193], v172
	v_cvt_pk_f32_fp8_sdwa v[200:201], v173 src0_sel:WORD_1
	v_mov_b32_e32 v185, v196
	v_mov_b32_e32 v183, v197
	v_mov_b32_e32 v189, v192
	v_mov_b32_e32 v187, v193
	v_add_f32_e32 v1, v195, v190
	v_max_f32_e32 v175, v191, v191
	v_max_f32_e32 v195, v1, v175
	v_sub_f32_e32 v1, v1, v195
	v_mul_f32_e32 v1, 0x3fb8aa3b, v1
	v_exp_f32_e32 v190, v1
	v_sub_f32_e32 v1, v191, v195
	v_mul_f32_e32 v1, 0x3fb8aa3b, v1
	v_exp_f32_e32 v191, v1
	s_nop 0
	v_mul_f32_e32 v172, v192, v191
	v_pk_fma_f32 v[172:173], v[188:189], v[190:191], v[172:173] op_sel_hi:[1,1,0]
	v_mul_f32_e32 v188, v193, v191
	v_pk_fma_f32 v[186:187], v[186:187], v[190:191], v[188:189] op_sel_hi:[1,1,0]
	v_mul_f32_e32 v188, v196, v191
	v_pk_fma_f32 v[184:185], v[184:185], v[190:191], v[188:189] op_sel_hi:[1,1,0]
	v_mul_f32_e32 v188, v197, v191
	v_pk_fma_f32 v[182:183], v[182:183], v[190:191], v[188:189] op_sel_hi:[1,1,0]
	v_mov_b32_e32 v181, v191
	v_mov_b32_e32 v188, v190
	v_mov_b32_e32 v189, v198
	v_mul_f32_e32 v192, v191, v198
	v_pk_fma_f32 v[180:181], v[180:181], v[188:189], v[192:193] op_sel_hi:[1,1,0]
	v_mov_b32_e32 v179, v191
	v_mov_b32_e32 v198, v190
	v_mul_f32_e32 v188, v191, v199
	v_pk_fma_f32 v[178:179], v[178:179], v[198:199], v[188:189] op_sel_hi:[1,1,0]
	v_mov_b32_e32 v177, v191
	v_mov_b32_e32 v188, v190
	v_mov_b32_e32 v189, v200
	v_mul_f32_e32 v192, v191, v200
	v_pk_fma_f32 v[176:177], v[176:177], v[188:189], v[192:193] op_sel_hi:[1,1,0]
	v_mov_b32_e32 v175, v191
	v_mov_b32_e32 v200, v190
	v_mul_f32_e32 v188, v191, v201
	v_pk_fma_f32 v[174:175], v[174:175], v[200:201], v[188:189] op_sel_hi:[1,1,0]
	v_med3_f32 v1, v172, s14, v221
	v_med3_f32 v173, v186, s14, v221
	v_mov_b32_e32 v188, v133
	v_cvt_pk_fp8_f32 v188, v1, v173
	v_med3_f32 v1, v180, s14, v221
	v_med3_f32 v173, v178, s14, v221
	v_mov_b32_e32 v189, v133
	v_cvt_pk_fp8_f32 v189, v1, v173
	v_med3_f32 v175, v184, s14, v221
	v_med3_f32 v177, v182, s14, v221
	v_cvt_pk_fp8_f32 v188, v175, v177 op_sel:[0,0,1]
	v_med3_f32 v175, v176, s14, v221
	v_med3_f32 v177, v174, s14, v221
	v_cvt_pk_fp8_f32 v189, v175, v177 op_sel:[0,0,1]
	v_lshl_add_u64 v[190:191], v[126:127], 0, s[84:85]
; __device__ __forceinline__ int cslot(int bh, int c) { return (c + bh) & 31; }
; template <int GRP>
; __device__ __forceinline__ void y_phase(Frame& F, const MW& W) {
;     ...
;         for (int c = 0; c < 32; ++c) {
;             u32x2 o; o.x = pg8::pack_fp8x4(C[0], C[1], C[2], C[3]); o.y = pg8::pack_fp8x4(C[4], C[5], C[6], C[7]); *(u32x2*)(W.CP + off + (size_t)cslot(bh, c) * 16384) = o;
;             const float bl = sc[2 * c], am = sc[2 * c + 1], mn = fmaxf(bl + m, am), dec = __expf(bl + m - mn), inj = __expf(am - mn);
;             const auto x0 = __builtin_amdgcn_cvt_pk_f32_fp8((int)v[c].x, false), x1 = __builtin_amdgcn_cvt_pk_f32_fp8((int)v[c].x, true), x2 = __builtin_amdgcn_cvt_pk_f32_fp8((int)v[c].y, false), x3 = __builtin_amdgcn_cvt_pk_f32_fp8((int)v[c].y, true);
;             C[0] = C[0] * dec + x0[0] * inj; C[1] = C[1] * dec + x0[1] * inj; C[2] = C[2] * dec + x1[0] * inj; C[3] = C[3] * dec + x1[1] * inj;
;             C[4] = C[4] * dec + x2[0] * inj; C[5] = C[5] * dec + x2[1] * inj; C[6] = C[6] * dec + x3[0] * inj; C[7] = C[7] * dec + x3[1] * inj; m = mn; }
	v_cvt_pk_f32_fp8_sdwa v[192:193], v170 src0_sel:WORD_1
	v_cvt_pk_f32_fp8_e32 v[196:197], v171
	global_store_dwordx2 v[190:191], v[188:189], off
	v_readlane_b32 s100, v252, 14
	s_nop 1
	v_mov_b32_e32 v188, s100
	v_readlane_b32 s100, v253, 14
	s_nop 1
	v_mov_b32_e32 v189, s100
	v_cvt_pk_f32_fp8_e32 v[190:191], v170
	v_cvt_pk_f32_fp8_sdwa v[198:199], v171 src0_sel:WORD_1
	v_mov_b32_e32 v185, v192
	v_mov_b32_e32 v183, v193
	v_mov_b32_e32 v187, v191
	v_add_f32_e32 v1, v195, v188
	v_max_f32_e32 v173, v189, v189
	v_max_f32_e32 v195, v1, v173
	v_sub_f32_e32 v1, v1, v195
	v_mul_f32_e32 v1, 0x3fb8aa3b, v1
	v_exp_f32_e32 v188, v1
	v_sub_f32_e32 v1, v189, v195
	v_mul_f32_e32 v1, 0x3fb8aa3b, v1
	v_exp_f32_e32 v189, v1
	v_mov_b32_e32 v173, v190
	v_mul_f32_e32 v170, v190, v189
	v_pk_fma_f32 v[172:173], v[172:173], v[188:189], v[170:171] op_sel_hi:[1,1,0]
	v_mul_f32_e32 v170, v191, v189
	v_pk_fma_f32 v[170:171], v[186:187], v[188:189], v[170:171] op_sel_hi:[1,1,0]
	v_mul_f32_e32 v186, v192, v189
	v_pk_fma_f32 v[184:185], v[184:185], v[188:189], v[186:187] op_sel_hi:[1,1,0]
	v_mul_f32_e32 v186, v193, v189
	v_pk_fma_f32 v[182:183], v[182:183], v[188:189], v[186:187] op_sel_hi:[1,1,0]
	v_mov_b32_e32 v181, v189
	v_mov_b32_e32 v186, v188
	v_mov_b32_e32 v187, v196
	v_mul_f32_e32 v190, v189, v196
	v_pk_fma_f32 v[180:181], v[180:181], v[186:187], v[190:191] op_sel_hi:[1,1,0]
	v_mov_b32_e32 v179, v189
	v_mov_b32_e32 v196, v188
	v_mul_f32_e32 v186, v189, v197
	v_pk_fma_f32 v[178:179], v[178:179], v[196:197], v[186:187] op_sel_hi:[1,1,0]
	v_mov_b32_e32 v177, v189
	v_mov_b32_e32 v186, v188
	v_mov_b32_e32 v187, v198
	v_mul_f32_e32 v190, v189, v198
	v_pk_fma_f32 v[176:177], v[176:177], v[186:187], v[190:191] op_sel_hi:[1,1,0]
	v_mov_b32_e32 v175, v189
	v_mov_b32_e32 v198, v188
	v_mul_f32_e32 v186, v189, v199
	v_pk_fma_f32 v[174:175], v[174:175], v[198:199], v[186:187] op_sel_hi:[1,1,0]
	v_med3_f32 v1, v172, s14, v221
	v_med3_f32 v171, v170, s14, v221
	v_mov_b32_e32 v186, v133
	v_cvt_pk_fp8_f32 v186, v1, v171
	v_med3_f32 v1, v180, s14, v221
	v_med3_f32 v171, v178, s14, v221
	v_mov_b32_e32 v187, v133
	v_cvt_pk_fp8_f32 v187, v1, v171
	v_med3_f32 v173, v184, s14, v221
	v_med3_f32 v175, v182, s14, v221
	v_cvt_pk_fp8_f32 v186, v173, v175 op_sel:[0,0,1]
	v_med3_f32 v173, v176, s14, v221
	v_med3_f32 v175, v174, s14, v221
	v_cvt_pk_fp8_f32 v187, v173, v175 op_sel:[0,0,1]
	v_lshl_add_u64 v[188:189], v[126:127], 0, s[82:83]
	v_cvt_pk_f32_fp8_sdwa v[190:191], v168 src0_sel:WORD_1
	v_cvt_pk_f32_fp8_e32 v[192:193], v169
	global_store_dwordx2 v[188:189], v[186:187], off
	v_readlane_b32 s100, v252, 15
	s_nop 1
	v_mov_b32_e32 v186, s100
	v_readlane_b32 s100, v253, 15
	s_nop 1
	v_mov_b32_e32 v187, s100
	v_cvt_pk_f32_fp8_e32 v[188:189], v168
	v_cvt_pk_f32_fp8_sdwa v[196:197], v169 src0_sel:WORD_1
	v_mov_b32_e32 v185, v190
	v_mov_b32_e32 v183, v191
	v_mov_b32_e32 v173, v188
	v_add_f32_e32 v1, v195, v186
	v_max_f32_e32 v171, v187, v187
	v_max_f32_e32 v195, v1, v171
	v_sub_f32_e32 v1, v1, v195
	v_mul_f32_e32 v1, 0x3fb8aa3b, v1
	v_exp_f32_e32 v186, v1
	v_sub_f32_e32 v1, v187, v195
	v_mul_f32_e32 v1, 0x3fb8aa3b, v1
	v_exp_f32_e32 v187, v1
	v_mov_b32_e32 v171, v189
	v_mul_f32_e32 v168, v188, v187
	v_pk_fma_f32 v[172:173], v[172:173], v[186:187], v[168:169] op_sel_hi:[1,1,0]
	v_mul_f32_e32 v168, v189, v187
	v_pk_fma_f32 v[170:171], v[170:171], v[186:187], v[168:169] op_sel_hi:[1,1,0]
	v_mul_f32_e32 v168, v190, v187
	v_pk_fma_f32 v[168:169], v[184:185], v[186:187], v[168:169] op_sel_hi:[1,1,0]
	v_mul_f32_e32 v184, v191, v187
	v_pk_fma_f32 v[182:183], v[182:183], v[186:187], v[184:185] op_sel_hi:[1,1,0]
	v_mov_b32_e32 v181, v187
	v_mov_b32_e32 v184, v186
	v_mov_b32_e32 v185, v192
	v_mul_f32_e32 v188, v187, v192
	v_pk_fma_f32 v[180:181], v[180:181], v[184:185], v[188:189] op_sel_hi:[1,1,0]
	v_mov_b32_e32 v179, v187
	v_mov_b32_e32 v192, v186
	v_mul_f32_e32 v184, v187, v193
	v_pk_fma_f32 v[178:179], v[178:179], v[192:193], v[184:185] op_sel_hi:[1,1,0]
	v_mov_b32_e32 v177, v187
	v_mov_b32_e32 v184, v186
	v_mov_b32_e32 v185, v196
	v_mul_f32_e32 v188, v187, v196
	v_pk_fma_f32 v[176:177], v[176:177], v[184:185], v[188:189] op_sel_hi:[1,1,0]
	v_mov_b32_e32 v175, v187
	v_mov_b32_e32 v196, v186
	v_mul_f32_e32 v184, v187, v197
	v_pk_fma_f32 v[174:175], v[174:175], v[196:197], v[184:185] op_sel_hi:[1,1,0]
	v_med3_f32 v1, v172, s14, v221
	v_med3_f32 v169, v170, s14, v221
	v_mov_b32_e32 v184, v133
	v_cvt_pk_fp8_f32 v184, v1, v169
	v_med3_f32 v1, v180, s14, v221
	v_med3_f32 v169, v178, s14, v221
	v_mov_b32_e32 v185, v133
	v_cvt_pk_fp8_f32 v185, v1, v169
	v_med3_f32 v171, v168, s14, v221
	v_med3_f32 v173, v182, s14, v221
	v_cvt_pk_fp8_f32 v184, v171, v173 op_sel:[0,0,1]
	v_med3_f32 v171, v176, s14, v221
	v_med3_f32 v173, v174, s14, v221
	v_cvt_pk_fp8_f32 v185, v171, v173 op_sel:[0,0,1]
	v_lshl_add_u64 v[186:187], v[126:127], 0, s[80:81]
	v_cvt_pk_f32_fp8_sdwa v[188:189], v166 src0_sel:WORD_1
	v_cvt_pk_f32_fp8_e32 v[190:191], v167
	global_store_dwordx2 v[186:187], v[184:185], off
	v_readlane_b32 s100, v252, 16
	s_nop 1
	v_mov_b32_e32 v184, s100
	v_readlane_b32 s100, v253, 16
	s_nop 1
	v_mov_b32_e32 v185, s100
	v_cvt_pk_f32_fp8_e32 v[186:187], v166
	v_cvt_pk_f32_fp8_sdwa v[192:193], v167 src0_sel:WORD_1
	v_mov_b32_e32 v183, v189
	v_mov_b32_e32 v173, v186
	v_mov_b32_e32 v171, v187
	v_add_f32_e32 v1, v195, v184
	v_max_f32_e32 v169, v185, v185
	v_max_f32_e32 v195, v1, v169
	v_sub_f32_e32 v1, v1, v195
	v_mul_f32_e32 v1, 0x3fb8aa3b, v1
	v_exp_f32_e32 v184, v1
	v_sub_f32_e32 v1, v185, v195
	v_mul_f32_e32 v1, 0x3fb8aa3b, v1
	v_exp_f32_e32 v185, v1
	v_mov_b32_e32 v169, v188
	v_mul_f32_e32 v166, v186, v185
; __device__ __forceinline__ int cslot(int bh, int c) { return (c + bh) & 31; }
; template <int GRP>
; __device__ __forceinline__ void y_phase(Frame& F, const MW& W) {
;     ...
;         for (int c = 0; c < 32; ++c) {
;             u32x2 o; o.x = pg8::pack_fp8x4(C[0], C[1], C[2], C[3]); o.y = pg8::pack_fp8x4(C[4], C[5], C[6], C[7]); *(u32x2*)(W.CP + off + (size_t)cslot(bh, c) * 16384) = o;
;             const float bl = sc[2 * c], am = sc[2 * c + 1], mn = fmaxf(bl + m, am), dec = __expf(bl + m - mn), inj = __expf(am - mn);
;             const auto x0 = __builtin_amdgcn_cvt_pk_f32_fp8((int)v[c].x, false), x1 = __builtin_amdgcn_cvt_pk_f32_fp8((int)v[c].x, true), x2 = __builtin_amdgcn_cvt_pk_f32_fp8((int)v[c].y, false), x3 = __builtin_amdgcn_cvt_pk_f32_fp8((int)v[c].y, true);
;             C[0] = C[0] * dec + x0[0] * inj; C[1] = C[1] * dec + x0[1] * inj; C[2] = C[2] * dec + x1[0] * inj; C[3] = C[3] * dec + x1[1] * inj;
;             C[4] = C[4] * dec + x2[0] * inj; C[5] = C[5] * dec + x2[1] * inj; C[6] = C[6] * dec + x3[0] * inj; C[7] = C[7] * dec + x3[1] * inj; m = mn; }
	v_pk_fma_f32 v[172:173], v[172:173], v[184:185], v[166:167] op_sel_hi:[1,1,0]
	v_mul_f32_e32 v166, v187, v185
	v_pk_fma_f32 v[170:171], v[170:171], v[184:185], v[166:167] op_sel_hi:[1,1,0]
	v_mul_f32_e32 v166, v188, v185
	v_pk_fma_f32 v[168:169], v[168:169], v[184:185], v[166:167] op_sel_hi:[1,1,0]
	v_mul_f32_e32 v166, v189, v185
	v_pk_fma_f32 v[166:167], v[182:183], v[184:185], v[166:167] op_sel_hi:[1,1,0]
	v_mov_b32_e32 v181, v185
	v_mov_b32_e32 v182, v184
	v_mov_b32_e32 v183, v190
	v_mul_f32_e32 v186, v185, v190
	v_pk_fma_f32 v[180:181], v[180:181], v[182:183], v[186:187] op_sel_hi:[1,1,0]
	v_mov_b32_e32 v179, v185
	v_mov_b32_e32 v190, v184
	v_mul_f32_e32 v182, v185, v191
	v_pk_fma_f32 v[178:179], v[178:179], v[190:191], v[182:183] op_sel_hi:[1,1,0]
	v_mov_b32_e32 v177, v185
	v_mov_b32_e32 v182, v184
	v_mov_b32_e32 v183, v192
	v_mul_f32_e32 v186, v185, v192
	v_pk_fma_f32 v[176:177], v[176:177], v[182:183], v[186:187] op_sel_hi:[1,1,0]
	v_mov_b32_e32 v175, v185
	v_mov_b32_e32 v192, v184
	v_mul_f32_e32 v182, v185, v193
	v_pk_fma_f32 v[174:175], v[174:175], v[192:193], v[182:183] op_sel_hi:[1,1,0]
	v_med3_f32 v1, v172, s14, v221
	v_med3_f32 v167, v170, s14, v221
	v_mov_b32_e32 v182, v133
	v_cvt_pk_fp8_f32 v182, v1, v167
	v_med3_f32 v1, v180, s14, v221
	v_med3_f32 v167, v178, s14, v221
	v_mov_b32_e32 v183, v133
	v_cvt_pk_fp8_f32 v183, v1, v167
	v_med3_f32 v169, v168, s14, v221
	v_med3_f32 v171, v166, s14, v221
	v_cvt_pk_fp8_f32 v182, v169, v171 op_sel:[0,0,1]
	v_med3_f32 v169, v176, s14, v221
	v_med3_f32 v171, v174, s14, v221
	v_cvt_pk_fp8_f32 v183, v169, v171 op_sel:[0,0,1]
	v_lshl_add_u64 v[184:185], v[126:127], 0, s[78:79]
	v_cvt_pk_f32_fp8_sdwa v[186:187], v164 src0_sel:WORD_1
	v_cvt_pk_f32_fp8_e32 v[188:189], v165
	global_store_dwordx2 v[184:185], v[182:183], off
	v_readlane_b32 s100, v252, 17
	s_nop 1
	v_mov_b32_e32 v182, s100
	v_readlane_b32 s100, v253, 17
	s_nop 1
	v_mov_b32_e32 v183, s100
	v_cvt_pk_f32_fp8_e32 v[184:185], v164
	v_cvt_pk_f32_fp8_sdwa v[190:191], v165 src0_sel:WORD_1
	v_mov_b32_e32 v169, v186
	v_mov_b32_e32 v173, v184
	v_mov_b32_e32 v171, v185
	v_add_f32_e32 v1, v195, v182
	v_max_f32_e32 v167, v183, v183
	v_max_f32_e32 v192, v1, v167
	v_sub_f32_e32 v1, v1, v192
	v_mul_f32_e32 v1, 0x3fb8aa3b, v1
	v_exp_f32_e32 v182, v1
	v_sub_f32_e32 v1, v183, v192
	v_mul_f32_e32 v1, 0x3fb8aa3b, v1
	v_exp_f32_e32 v183, v1
	v_mov_b32_e32 v167, v187
	v_mul_f32_e32 v164, v184, v183
	v_pk_fma_f32 v[172:173], v[172:173], v[182:183], v[164:165] op_sel_hi:[1,1,0]
	v_mul_f32_e32 v164, v185, v183
	v_pk_fma_f32 v[170:171], v[170:171], v[182:183], v[164:165] op_sel_hi:[1,1,0]
	v_mul_f32_e32 v164, v186, v183
	v_pk_fma_f32 v[168:169], v[168:169], v[182:183], v[164:165] op_sel_hi:[1,1,0]
	v_mul_f32_e32 v164, v187, v183
	v_pk_fma_f32 v[166:167], v[166:167], v[182:183], v[164:165] op_sel_hi:[1,1,0]
	v_mov_b32_e32 v181, v183
	v_mov_b32_e32 v164, v182
	v_mov_b32_e32 v165, v188
	v_mul_f32_e32 v184, v183, v188
	v_pk_fma_f32 v[164:165], v[180:181], v[164:165], v[184:185] op_sel_hi:[1,1,0]
	v_mov_b32_e32 v179, v183
	v_mov_b32_e32 v188, v182
	v_mul_f32_e32 v180, v183, v189
	v_pk_fma_f32 v[178:179], v[178:179], v[188:189], v[180:181] op_sel_hi:[1,1,0]
	v_mov_b32_e32 v177, v183
	v_mov_b32_e32 v180, v182
	v_mov_b32_e32 v181, v190
	v_mul_f32_e32 v184, v183, v190
	v_pk_fma_f32 v[176:177], v[176:177], v[180:181], v[184:185] op_sel_hi:[1,1,0]
	v_mov_b32_e32 v175, v183
	v_mov_b32_e32 v190, v182
	v_mul_f32_e32 v180, v183, v191
	v_pk_fma_f32 v[174:175], v[174:175], v[190:191], v[180:181] op_sel_hi:[1,1,0]
	v_med3_f32 v1, v172, s14, v221
	v_med3_f32 v165, v170, s14, v221
	v_mov_b32_e32 v180, v133
	v_cvt_pk_fp8_f32 v180, v1, v165
	v_med3_f32 v1, v164, s14, v221
	v_med3_f32 v165, v178, s14, v221
	v_mov_b32_e32 v181, v133
	v_cvt_pk_fp8_f32 v181, v1, v165
	v_med3_f32 v167, v168, s14, v221
	v_med3_f32 v169, v166, s14, v221
	v_cvt_pk_fp8_f32 v180, v167, v169 op_sel:[0,0,1]
	v_med3_f32 v167, v176, s14, v221
	v_med3_f32 v169, v174, s14, v221
	v_cvt_pk_fp8_f32 v181, v167, v169 op_sel:[0,0,1]
	v_lshl_add_u64 v[182:183], v[126:127], 0, s[74:75]
	v_cvt_pk_f32_fp8_sdwa v[184:185], v162 src0_sel:WORD_1
	v_cvt_pk_f32_fp8_e32 v[186:187], v163
	global_store_dwordx2 v[182:183], v[180:181], off
	v_readlane_b32 s100, v252, 18
	s_nop 1
	v_mov_b32_e32 v180, s100
	v_readlane_b32 s100, v253, 18
	s_nop 1
	v_mov_b32_e32 v181, s100
	v_cvt_pk_f32_fp8_e32 v[182:183], v162
	v_cvt_pk_f32_fp8_sdwa v[188:189], v163 src0_sel:WORD_1
	v_mov_b32_e32 v169, v184
	v_mov_b32_e32 v167, v185
	v_mov_b32_e32 v173, v182
	v_mov_b32_e32 v171, v183
	v_add_f32_e32 v1, v192, v180
	v_max_f32_e32 v165, v181, v181
	v_max_f32_e32 v190, v1, v165
	v_sub_f32_e32 v1, v1, v190
	v_mul_f32_e32 v1, 0x3fb8aa3b, v1
	v_exp_f32_e32 v180, v1
	v_sub_f32_e32 v1, v181, v190
	v_mul_f32_e32 v1, 0x3fb8aa3b, v1
	v_exp_f32_e32 v181, v1
	s_nop 0
	v_mul_f32_e32 v162, v182, v181
	v_pk_fma_f32 v[172:173], v[172:173], v[180:181], v[162:163] op_sel_hi:[1,1,0]
	v_mul_f32_e32 v162, v183, v181
	v_pk_fma_f32 v[170:171], v[170:171], v[180:181], v[162:163] op_sel_hi:[1,1,0]
	v_mul_f32_e32 v162, v184, v181
	v_pk_fma_f32 v[168:169], v[168:169], v[180:181], v[162:163] op_sel_hi:[1,1,0]
	v_mul_f32_e32 v162, v185, v181
	v_pk_fma_f32 v[166:167], v[166:167], v[180:181], v[162:163] op_sel_hi:[1,1,0]
	v_mov_b32_e32 v165, v181
	v_mov_b32_e32 v162, v180
	v_mov_b32_e32 v163, v186
	v_mul_f32_e32 v182, v181, v186
	v_pk_fma_f32 v[164:165], v[164:165], v[162:163], v[182:183] op_sel_hi:[1,1,0]
	v_mov_b32_e32 v179, v181
	v_mov_b32_e32 v186, v180
	v_mul_f32_e32 v162, v181, v187
	v_pk_fma_f32 v[162:163], v[178:179], v[186:187], v[162:163] op_sel_hi:[1,1,0]
; __device__ __forceinline__ int cslot(int bh, int c) { return (c + bh) & 31; }
; template <int GRP>
; __device__ __forceinline__ void y_phase(Frame& F, const MW& W) {
;     ...
;         for (int c = 0; c < 32; ++c) {
;             u32x2 o; o.x = pg8::pack_fp8x4(C[0], C[1], C[2], C[3]); o.y = pg8::pack_fp8x4(C[4], C[5], C[6], C[7]); *(u32x2*)(W.CP + off + (size_t)cslot(bh, c) * 16384) = o;
;             const float bl = sc[2 * c], am = sc[2 * c + 1], mn = fmaxf(bl + m, am), dec = __expf(bl + m - mn), inj = __expf(am - mn);
;             const auto x0 = __builtin_amdgcn_cvt_pk_f32_fp8((int)v[c].x, false), x1 = __builtin_amdgcn_cvt_pk_f32_fp8((int)v[c].x, true), x2 = __builtin_amdgcn_cvt_pk_f32_fp8((int)v[c].y, false), x3 = __builtin_amdgcn_cvt_pk_f32_fp8((int)v[c].y, true);
;             C[0] = C[0] * dec + x0[0] * inj; C[1] = C[1] * dec + x0[1] * inj; C[2] = C[2] * dec + x1[0] * inj; C[3] = C[3] * dec + x1[1] * inj;
;             C[4] = C[4] * dec + x2[0] * inj; C[5] = C[5] * dec + x2[1] * inj; C[6] = C[6] * dec + x3[0] * inj; C[7] = C[7] * dec + x3[1] * inj; m = mn; }
	v_mov_b32_e32 v177, v181
	v_mov_b32_e32 v178, v180
	v_mov_b32_e32 v179, v188
	v_mul_f32_e32 v182, v181, v188
	v_pk_fma_f32 v[176:177], v[176:177], v[178:179], v[182:183] op_sel_hi:[1,1,0]
	v_mov_b32_e32 v175, v181
	v_mov_b32_e32 v188, v180
	v_mul_f32_e32 v178, v181, v189
	v_pk_fma_f32 v[174:175], v[174:175], v[188:189], v[178:179] op_sel_hi:[1,1,0]
	v_med3_f32 v1, v172, s14, v221
	v_med3_f32 v163, v170, s14, v221
	v_mov_b32_e32 v178, v133
	v_cvt_pk_fp8_f32 v178, v1, v163
	v_med3_f32 v1, v164, s14, v221
	v_med3_f32 v163, v162, s14, v221
	v_mov_b32_e32 v179, v133
	v_cvt_pk_fp8_f32 v179, v1, v163
	v_med3_f32 v165, v168, s14, v221
	v_med3_f32 v167, v166, s14, v221
	v_cvt_pk_fp8_f32 v178, v165, v167 op_sel:[0,0,1]
	v_med3_f32 v165, v176, s14, v221
	v_med3_f32 v167, v174, s14, v221
	v_cvt_pk_fp8_f32 v179, v165, v167 op_sel:[0,0,1]
	v_lshl_add_u64 v[180:181], v[126:127], 0, s[46:47]
	v_cvt_pk_f32_fp8_sdwa v[182:183], v160 src0_sel:WORD_1
	v_cvt_pk_f32_fp8_e32 v[184:185], v161
	global_store_dwordx2 v[180:181], v[178:179], off
	v_readlane_b32 s100, v252, 19
	s_nop 1
	v_mov_b32_e32 v178, s100
	v_readlane_b32 s100, v253, 19
	s_nop 1
	v_mov_b32_e32 v179, s100
	v_cvt_pk_f32_fp8_e32 v[180:181], v160
	v_cvt_pk_f32_fp8_sdwa v[186:187], v161 src0_sel:WORD_1
	v_mov_b32_e32 v169, v182
	v_mov_b32_e32 v167, v183
	v_mov_b32_e32 v173, v180
	v_mov_b32_e32 v171, v181
	v_add_f32_e32 v1, v190, v178
	v_max_f32_e32 v163, v179, v179
	v_max_f32_e32 v188, v1, v163
	v_sub_f32_e32 v1, v1, v188
	v_mul_f32_e32 v1, 0x3fb8aa3b, v1
	v_exp_f32_e32 v178, v1
	v_sub_f32_e32 v1, v179, v188
	v_mul_f32_e32 v1, 0x3fb8aa3b, v1
	v_exp_f32_e32 v179, v1
	s_nop 0
	v_mul_f32_e32 v160, v180, v179
	v_pk_fma_f32 v[172:173], v[172:173], v[178:179], v[160:161] op_sel_hi:[1,1,0]
	v_mul_f32_e32 v160, v181, v179
	v_pk_fma_f32 v[170:171], v[170:171], v[178:179], v[160:161] op_sel_hi:[1,1,0]
	v_mul_f32_e32 v160, v182, v179
	v_pk_fma_f32 v[168:169], v[168:169], v[178:179], v[160:161] op_sel_hi:[1,1,0]
	v_mul_f32_e32 v160, v183, v179
	v_pk_fma_f32 v[166:167], v[166:167], v[178:179], v[160:161] op_sel_hi:[1,1,0]
	v_mov_b32_e32 v165, v179
	v_mov_b32_e32 v160, v178
	v_mov_b32_e32 v161, v184
	v_mul_f32_e32 v180, v179, v184
	v_pk_fma_f32 v[164:165], v[164:165], v[160:161], v[180:181] op_sel_hi:[1,1,0]
	v_mov_b32_e32 v163, v179
	v_mov_b32_e32 v184, v178
	v_mul_f32_e32 v160, v179, v185
	v_pk_fma_f32 v[162:163], v[162:163], v[184:185], v[160:161] op_sel_hi:[1,1,0]
	v_mov_b32_e32 v177, v179
	v_mov_b32_e32 v160, v178
	v_mov_b32_e32 v161, v186
	v_mul_f32_e32 v180, v179, v186
	v_pk_fma_f32 v[160:161], v[176:177], v[160:161], v[180:181] op_sel_hi:[1,1,0]
	v_mov_b32_e32 v175, v179
	v_mov_b32_e32 v186, v178
	v_mul_f32_e32 v176, v179, v187
	v_pk_fma_f32 v[174:175], v[174:175], v[186:187], v[176:177] op_sel_hi:[1,1,0]
	v_med3_f32 v1, v172, s14, v221
	v_med3_f32 v161, v170, s14, v221
	v_mov_b32_e32 v176, v133
	v_cvt_pk_fp8_f32 v176, v1, v161
	v_med3_f32 v1, v164, s14, v221
	v_med3_f32 v161, v162, s14, v221
	v_mov_b32_e32 v177, v133
	v_cvt_pk_fp8_f32 v177, v1, v161
	v_med3_f32 v163, v168, s14, v221
	v_med3_f32 v165, v166, s14, v221
	v_cvt_pk_fp8_f32 v176, v163, v165 op_sel:[0,0,1]
	v_med3_f32 v163, v160, s14, v221
	v_med3_f32 v165, v174, s14, v221
	v_cvt_pk_fp8_f32 v177, v163, v165 op_sel:[0,0,1]
	v_lshl_add_u64 v[178:179], v[126:127], 0, s[44:45]
	v_cvt_pk_f32_fp8_sdwa v[180:181], v158 src0_sel:WORD_1
	v_cvt_pk_f32_fp8_e32 v[182:183], v159
	global_store_dwordx2 v[178:179], v[176:177], off
	v_readlane_b32 s100, v252, 20
	s_nop 1
	v_mov_b32_e32 v176, s100
	v_readlane_b32 s100, v253, 20
	s_nop 1
	v_mov_b32_e32 v177, s100
	v_cvt_pk_f32_fp8_e32 v[178:179], v158
	v_cvt_pk_f32_fp8_sdwa v[158:159], v159 src0_sel:WORD_1
	v_mov_b32_e32 v169, v180
	v_mov_b32_e32 v167, v181
	v_mov_b32_e32 v173, v178
	v_mov_b32_e32 v171, v179
	v_add_f32_e32 v1, v188, v176
	v_max_f32_e32 v161, v177, v177
	v_max_f32_e32 v184, v1, v161
	v_sub_f32_e32 v1, v1, v184
	v_mul_f32_e32 v1, 0x3fb8aa3b, v1
	v_exp_f32_e32 v176, v1
	v_sub_f32_e32 v1, v177, v184
	v_mul_f32_e32 v1, 0x3fb8aa3b, v1
	v_exp_f32_e32 v177, v1
	s_nop 0
	v_mul_f32_e32 v178, v178, v177
	v_pk_fma_f32 v[172:173], v[172:173], v[176:177], v[178:179] op_sel_hi:[1,1,0]
	v_mul_f32_e32 v178, v179, v177
	v_pk_fma_f32 v[170:171], v[170:171], v[176:177], v[178:179] op_sel_hi:[1,1,0]
	v_mul_f32_e32 v178, v180, v177
	v_pk_fma_f32 v[168:169], v[168:169], v[176:177], v[178:179] op_sel_hi:[1,1,0]
	v_mul_f32_e32 v178, v181, v177
	v_pk_fma_f32 v[166:167], v[166:167], v[176:177], v[178:179] op_sel_hi:[1,1,0]
	v_mov_b32_e32 v165, v177
	v_mov_b32_e32 v178, v176
	v_mov_b32_e32 v179, v182
	v_mul_f32_e32 v180, v177, v182
	v_pk_fma_f32 v[164:165], v[164:165], v[178:179], v[180:181] op_sel_hi:[1,1,0]
	v_mov_b32_e32 v163, v177
	v_mov_b32_e32 v182, v176
	v_mul_f32_e32 v178, v177, v183
	v_pk_fma_f32 v[162:163], v[162:163], v[182:183], v[178:179] op_sel_hi:[1,1,0]
	v_mov_b32_e32 v161, v177
	v_mov_b32_e32 v178, v176
	v_mov_b32_e32 v179, v158
	v_mul_f32_e32 v158, v177, v158
	v_pk_fma_f32 v[160:161], v[160:161], v[178:179], v[158:159] op_sel_hi:[1,1,0]
	v_mov_b32_e32 v175, v177
	v_mov_b32_e32 v158, v176
	v_mul_f32_e32 v176, v177, v159
	v_pk_fma_f32 v[158:159], v[174:175], v[158:159], v[176:177] op_sel_hi:[1,1,0]
	v_med3_f32 v1, v172, s14, v221
	v_med3_f32 v159, v170, s14, v221
	v_mov_b32_e32 v174, v133
	v_cvt_pk_fp8_f32 v174, v1, v159
	v_med3_f32 v1, v164, s14, v221
	v_med3_f32 v159, v162, s14, v221
	v_mov_b32_e32 v175, v133
	v_cvt_pk_fp8_f32 v175, v1, v159
	v_med3_f32 v161, v168, s14, v221
	v_med3_f32 v163, v166, s14, v221
	v_cvt_pk_fp8_f32 v174, v161, v163 op_sel:[0,0,1]
	v_med3_f32 v161, v160, s14, v221
; __device__ __forceinline__ int cslot(int bh, int c) { return (c + bh) & 31; }
; template <int GRP>
; __device__ __forceinline__ void y_phase(Frame& F, const MW& W) {
;     ...
;         for (int c = 0; c < 32; ++c) {
;             u32x2 o; o.x = pg8::pack_fp8x4(C[0], C[1], C[2], C[3]); o.y = pg8::pack_fp8x4(C[4], C[5], C[6], C[7]); *(u32x2*)(W.CP + off + (size_t)cslot(bh, c) * 16384) = o;
;             const float bl = sc[2 * c], am = sc[2 * c + 1], mn = fmaxf(bl + m, am), dec = __expf(bl + m - mn), inj = __expf(am - mn);
;             const auto x0 = __builtin_amdgcn_cvt_pk_f32_fp8((int)v[c].x, false), x1 = __builtin_amdgcn_cvt_pk_f32_fp8((int)v[c].x, true), x2 = __builtin_amdgcn_cvt_pk_f32_fp8((int)v[c].y, false), x3 = __builtin_amdgcn_cvt_pk_f32_fp8((int)v[c].y, true);
;             C[0] = C[0] * dec + x0[0] * inj; C[1] = C[1] * dec + x0[1] * inj; C[2] = C[2] * dec + x1[0] * inj; C[3] = C[3] * dec + x1[1] * inj;
;             C[4] = C[4] * dec + x2[0] * inj; C[5] = C[5] * dec + x2[1] * inj; C[6] = C[6] * dec + x3[0] * inj; C[7] = C[7] * dec + x3[1] * inj; m = mn; }
	v_med3_f32 v163, v158, s14, v221
	v_cvt_pk_fp8_f32 v175, v161, v163 op_sel:[0,0,1]
	v_lshl_add_u64 v[176:177], v[126:127], 0, s[42:43]
	v_cvt_pk_f32_fp8_sdwa v[178:179], v156 src0_sel:WORD_1
	v_cvt_pk_f32_fp8_e32 v[180:181], v157
	global_store_dwordx2 v[176:177], v[174:175], off
	v_readlane_b32 s100, v252, 21
	s_nop 1
	v_mov_b32_e32 v174, s100
	v_readlane_b32 s100, v253, 21
	s_nop 1
	v_mov_b32_e32 v175, s100
	v_cvt_pk_f32_fp8_e32 v[176:177], v156
	v_cvt_pk_f32_fp8_sdwa v[182:183], v157 src0_sel:WORD_1
	v_mov_b32_e32 v169, v178
	v_mov_b32_e32 v167, v179
	v_mov_b32_e32 v173, v176
	v_mov_b32_e32 v171, v177
	v_add_f32_e32 v1, v184, v174
	v_max_f32_e32 v159, v175, v175
	v_max_f32_e32 v184, v1, v159
	v_sub_f32_e32 v1, v1, v184
	v_mul_f32_e32 v1, 0x3fb8aa3b, v1
	v_exp_f32_e32 v174, v1
	v_sub_f32_e32 v1, v175, v184
	v_mul_f32_e32 v1, 0x3fb8aa3b, v1
	v_exp_f32_e32 v175, v1
	s_nop 0
	v_mul_f32_e32 v156, v176, v175
	v_pk_fma_f32 v[156:157], v[172:173], v[174:175], v[156:157] op_sel_hi:[1,1,0]
	v_mul_f32_e32 v172, v177, v175
	v_pk_fma_f32 v[170:171], v[170:171], v[174:175], v[172:173] op_sel_hi:[1,1,0]
	v_mul_f32_e32 v172, v178, v175
	v_pk_fma_f32 v[168:169], v[168:169], v[174:175], v[172:173] op_sel_hi:[1,1,0]
	v_mul_f32_e32 v172, v179, v175
	v_pk_fma_f32 v[166:167], v[166:167], v[174:175], v[172:173] op_sel_hi:[1,1,0]
	v_mov_b32_e32 v165, v175
	v_mov_b32_e32 v172, v174
	v_mov_b32_e32 v173, v180
	v_mul_f32_e32 v176, v175, v180
	v_pk_fma_f32 v[164:165], v[164:165], v[172:173], v[176:177] op_sel_hi:[1,1,0]
	v_mov_b32_e32 v163, v175
	v_mov_b32_e32 v180, v174
	v_mul_f32_e32 v172, v175, v181
	v_pk_fma_f32 v[162:163], v[162:163], v[180:181], v[172:173] op_sel_hi:[1,1,0]
	v_mov_b32_e32 v161, v175
	v_mov_b32_e32 v172, v174
	v_mov_b32_e32 v173, v182
	v_mul_f32_e32 v176, v175, v182
	v_pk_fma_f32 v[160:161], v[160:161], v[172:173], v[176:177] op_sel_hi:[1,1,0]
	v_mov_b32_e32 v159, v175
	v_mov_b32_e32 v182, v174
	v_mul_f32_e32 v172, v175, v183
	v_pk_fma_f32 v[158:159], v[158:159], v[182:183], v[172:173] op_sel_hi:[1,1,0]
	v_med3_f32 v1, v156, s14, v221
	v_med3_f32 v157, v170, s14, v221
	v_mov_b32_e32 v172, v133
	v_cvt_pk_fp8_f32 v172, v1, v157
	v_med3_f32 v1, v164, s14, v221
	v_med3_f32 v157, v162, s14, v221
	v_mov_b32_e32 v173, v133
	v_cvt_pk_fp8_f32 v173, v1, v157
	v_med3_f32 v159, v168, s14, v221
	v_med3_f32 v161, v166, s14, v221
	v_cvt_pk_fp8_f32 v172, v159, v161 op_sel:[0,0,1]
	v_med3_f32 v159, v160, s14, v221
	v_med3_f32 v161, v158, s14, v221
	v_cvt_pk_fp8_f32 v173, v159, v161 op_sel:[0,0,1]
	v_lshl_add_u64 v[174:175], v[126:127], 0, s[40:41]
	v_cvt_pk_f32_fp8_sdwa v[176:177], v154 src0_sel:WORD_1
	v_cvt_pk_f32_fp8_e32 v[178:179], v155
	global_store_dwordx2 v[174:175], v[172:173], off
	v_readlane_b32 s100, v252, 22
	s_nop 1
	v_mov_b32_e32 v172, s100
	v_readlane_b32 s100, v253, 22
	s_nop 1
	v_mov_b32_e32 v173, s100
	v_cvt_pk_f32_fp8_e32 v[174:175], v154
	v_cvt_pk_f32_fp8_sdwa v[180:181], v155 src0_sel:WORD_1
	v_mov_b32_e32 v169, v176
	v_mov_b32_e32 v167, v177
	v_mov_b32_e32 v171, v175
	v_add_f32_e32 v1, v184, v172
	v_max_f32_e32 v157, v173, v173
	v_max_f32_e32 v182, v1, v157
	v_sub_f32_e32 v1, v1, v182
	v_mul_f32_e32 v1, 0x3fb8aa3b, v1
	v_exp_f32_e32 v172, v1
	v_sub_f32_e32 v1, v173, v182
	v_mul_f32_e32 v1, 0x3fb8aa3b, v1
	v_exp_f32_e32 v173, v1
	v_mov_b32_e32 v157, v174
	v_mul_f32_e32 v154, v174, v173
	v_pk_fma_f32 v[156:157], v[156:157], v[172:173], v[154:155] op_sel_hi:[1,1,0]
	v_mul_f32_e32 v154, v175, v173
	v_pk_fma_f32 v[154:155], v[170:171], v[172:173], v[154:155] op_sel_hi:[1,1,0]
	v_mul_f32_e32 v170, v176, v173
	v_pk_fma_f32 v[168:169], v[168:169], v[172:173], v[170:171] op_sel_hi:[1,1,0]
	v_mul_f32_e32 v170, v177, v173
	v_pk_fma_f32 v[166:167], v[166:167], v[172:173], v[170:171] op_sel_hi:[1,1,0]
	v_mov_b32_e32 v165, v173
	v_mov_b32_e32 v170, v172
	v_mov_b32_e32 v171, v178
	v_mul_f32_e32 v174, v173, v178
	v_pk_fma_f32 v[164:165], v[164:165], v[170:171], v[174:175] op_sel_hi:[1,1,0]
	v_mov_b32_e32 v163, v173
	v_mov_b32_e32 v178, v172
	v_mul_f32_e32 v170, v173, v179
	v_pk_fma_f32 v[162:163], v[162:163], v[178:179], v[170:171] op_sel_hi:[1,1,0]
	v_mov_b32_e32 v161, v173
	v_mov_b32_e32 v170, v172
	v_mov_b32_e32 v171, v180
	v_mul_f32_e32 v174, v173, v180
	v_pk_fma_f32 v[160:161], v[160:161], v[170:171], v[174:175] op_sel_hi:[1,1,0]
	v_mov_b32_e32 v159, v173
	v_mov_b32_e32 v180, v172
	v_mul_f32_e32 v170, v173, v181
	v_pk_fma_f32 v[158:159], v[158:159], v[180:181], v[170:171] op_sel_hi:[1,1,0]
	v_med3_f32 v1, v156, s14, v221
	v_med3_f32 v155, v154, s14, v221
	v_mov_b32_e32 v170, v133
	v_cvt_pk_fp8_f32 v170, v1, v155
	v_med3_f32 v1, v164, s14, v221
	v_med3_f32 v155, v162, s14, v221
	v_mov_b32_e32 v171, v133
	v_cvt_pk_fp8_f32 v171, v1, v155
	v_med3_f32 v157, v168, s14, v221
	v_med3_f32 v159, v166, s14, v221
	v_cvt_pk_fp8_f32 v170, v157, v159 op_sel:[0,0,1]
	v_med3_f32 v157, v160, s14, v221
	v_med3_f32 v159, v158, s14, v221
	v_cvt_pk_fp8_f32 v171, v157, v159 op_sel:[0,0,1]
	v_lshl_add_u64 v[172:173], v[126:127], 0, s[38:39]
	v_cvt_pk_f32_fp8_sdwa v[174:175], v152 src0_sel:WORD_1
	v_cvt_pk_f32_fp8_e32 v[176:177], v153
	global_store_dwordx2 v[172:173], v[170:171], off
	v_readlane_b32 s100, v252, 23
	s_nop 1
	v_mov_b32_e32 v170, s100
	v_readlane_b32 s100, v253, 23
	s_nop 1
	v_mov_b32_e32 v171, s100
	v_cvt_pk_f32_fp8_e32 v[172:173], v152
	v_cvt_pk_f32_fp8_sdwa v[178:179], v153 src0_sel:WORD_1
	v_mov_b32_e32 v169, v174
	v_mov_b32_e32 v167, v175
	v_mov_b32_e32 v157, v172
	v_add_f32_e32 v1, v182, v170
	v_max_f32_e32 v155, v171, v171
	v_max_f32_e32 v180, v1, v155
	v_sub_f32_e32 v1, v1, v180
	v_mul_f32_e32 v1, 0x3fb8aa3b, v1
	v_exp_f32_e32 v170, v1
; __device__ __forceinline__ int cslot(int bh, int c) { return (c + bh) & 31; }
; template <int GRP>
; __device__ __forceinline__ void y_phase(Frame& F, const MW& W) {
;     ...
;         for (int c = 0; c < 32; ++c) {
;             u32x2 o; o.x = pg8::pack_fp8x4(C[0], C[1], C[2], C[3]); o.y = pg8::pack_fp8x4(C[4], C[5], C[6], C[7]); *(u32x2*)(W.CP + off + (size_t)cslot(bh, c) * 16384) = o;
;             const float bl = sc[2 * c], am = sc[2 * c + 1], mn = fmaxf(bl + m, am), dec = __expf(bl + m - mn), inj = __expf(am - mn);
;             const auto x0 = __builtin_amdgcn_cvt_pk_f32_fp8((int)v[c].x, false), x1 = __builtin_amdgcn_cvt_pk_f32_fp8((int)v[c].x, true), x2 = __builtin_amdgcn_cvt_pk_f32_fp8((int)v[c].y, false), x3 = __builtin_amdgcn_cvt_pk_f32_fp8((int)v[c].y, true);
;             C[0] = C[0] * dec + x0[0] * inj; C[1] = C[1] * dec + x0[1] * inj; C[2] = C[2] * dec + x1[0] * inj; C[3] = C[3] * dec + x1[1] * inj;
;             C[4] = C[4] * dec + x2[0] * inj; C[5] = C[5] * dec + x2[1] * inj; C[6] = C[6] * dec + x3[0] * inj; C[7] = C[7] * dec + x3[1] * inj; m = mn; }
	v_sub_f32_e32 v1, v171, v180
	v_mul_f32_e32 v1, 0x3fb8aa3b, v1
	v_exp_f32_e32 v171, v1
	v_mov_b32_e32 v155, v173
	v_mul_f32_e32 v152, v172, v171
	v_pk_fma_f32 v[156:157], v[156:157], v[170:171], v[152:153] op_sel_hi:[1,1,0]
	v_mul_f32_e32 v152, v173, v171
	v_pk_fma_f32 v[154:155], v[154:155], v[170:171], v[152:153] op_sel_hi:[1,1,0]
	v_mul_f32_e32 v152, v174, v171
	v_pk_fma_f32 v[152:153], v[168:169], v[170:171], v[152:153] op_sel_hi:[1,1,0]
	v_mul_f32_e32 v168, v175, v171
	v_pk_fma_f32 v[166:167], v[166:167], v[170:171], v[168:169] op_sel_hi:[1,1,0]
	v_mov_b32_e32 v165, v171
	v_mov_b32_e32 v168, v170
	v_mov_b32_e32 v169, v176
	v_mul_f32_e32 v172, v171, v176
	v_pk_fma_f32 v[164:165], v[164:165], v[168:169], v[172:173] op_sel_hi:[1,1,0]
	v_mov_b32_e32 v163, v171
	v_mov_b32_e32 v176, v170
	v_mul_f32_e32 v168, v171, v177
	v_pk_fma_f32 v[162:163], v[162:163], v[176:177], v[168:169] op_sel_hi:[1,1,0]
	v_mov_b32_e32 v161, v171
	v_mov_b32_e32 v168, v170
	v_mov_b32_e32 v169, v178
	v_mul_f32_e32 v172, v171, v178
	v_pk_fma_f32 v[160:161], v[160:161], v[168:169], v[172:173] op_sel_hi:[1,1,0]
	v_mov_b32_e32 v159, v171
	v_mov_b32_e32 v178, v170
	v_mul_f32_e32 v168, v171, v179
	v_pk_fma_f32 v[158:159], v[158:159], v[178:179], v[168:169] op_sel_hi:[1,1,0]
	v_med3_f32 v1, v156, s14, v221
	v_med3_f32 v153, v154, s14, v221
	v_mov_b32_e32 v168, v133
	v_cvt_pk_fp8_f32 v168, v1, v153
	v_med3_f32 v1, v164, s14, v221
	v_med3_f32 v153, v162, s14, v221
	v_mov_b32_e32 v169, v133
	v_cvt_pk_fp8_f32 v169, v1, v153
	v_med3_f32 v155, v152, s14, v221
	v_med3_f32 v157, v166, s14, v221
	v_cvt_pk_fp8_f32 v168, v155, v157 op_sel:[0,0,1]
	v_med3_f32 v155, v160, s14, v221
	v_med3_f32 v157, v158, s14, v221
	v_cvt_pk_fp8_f32 v169, v155, v157 op_sel:[0,0,1]
	v_lshl_add_u64 v[170:171], v[126:127], 0, s[36:37]
	v_cvt_pk_f32_fp8_sdwa v[172:173], v150 src0_sel:WORD_1
	v_cvt_pk_f32_fp8_e32 v[174:175], v151
	global_store_dwordx2 v[170:171], v[168:169], off
	v_readlane_b32 s100, v252, 24
	s_nop 1
	v_mov_b32_e32 v168, s100
	v_readlane_b32 s100, v253, 24
	s_nop 1
	v_mov_b32_e32 v169, s100
	v_cvt_pk_f32_fp8_e32 v[170:171], v150
	v_cvt_pk_f32_fp8_sdwa v[176:177], v151 src0_sel:WORD_1
	v_mov_b32_e32 v167, v173
	v_mov_b32_e32 v157, v170
	v_mov_b32_e32 v155, v171
	v_add_f32_e32 v1, v180, v168
	v_max_f32_e32 v153, v169, v169
	v_max_f32_e32 v178, v1, v153
	v_sub_f32_e32 v1, v1, v178
	v_mul_f32_e32 v1, 0x3fb8aa3b, v1
	v_exp_f32_e32 v168, v1
	v_sub_f32_e32 v1, v169, v178
	v_mul_f32_e32 v1, 0x3fb8aa3b, v1
	v_exp_f32_e32 v169, v1
	v_mov_b32_e32 v153, v172
	v_mul_f32_e32 v150, v170, v169
	v_pk_fma_f32 v[156:157], v[156:157], v[168:169], v[150:151] op_sel_hi:[1,1,0]
	v_mul_f32_e32 v150, v171, v169
	v_pk_fma_f32 v[154:155], v[154:155], v[168:169], v[150:151] op_sel_hi:[1,1,0]
	v_mul_f32_e32 v150, v172, v169
	v_pk_fma_f32 v[152:153], v[152:153], v[168:169], v[150:151] op_sel_hi:[1,1,0]
	v_mul_f32_e32 v150, v173, v169
	v_pk_fma_f32 v[150:151], v[166:167], v[168:169], v[150:151] op_sel_hi:[1,1,0]
	v_mov_b32_e32 v165, v169
	v_mov_b32_e32 v166, v168
	v_mov_b32_e32 v167, v174
	v_mul_f32_e32 v170, v169, v174
	v_pk_fma_f32 v[164:165], v[164:165], v[166:167], v[170:171] op_sel_hi:[1,1,0]
	v_mov_b32_e32 v163, v169
	v_mov_b32_e32 v174, v168
	v_mul_f32_e32 v166, v169, v175
	v_pk_fma_f32 v[162:163], v[162:163], v[174:175], v[166:167] op_sel_hi:[1,1,0]
	v_mov_b32_e32 v161, v169
	v_mov_b32_e32 v166, v168
	v_mov_b32_e32 v167, v176
	v_mul_f32_e32 v170, v169, v176
	v_pk_fma_f32 v[160:161], v[160:161], v[166:167], v[170:171] op_sel_hi:[1,1,0]
	v_mov_b32_e32 v159, v169
	v_mov_b32_e32 v176, v168
	v_mul_f32_e32 v166, v169, v177
	v_pk_fma_f32 v[158:159], v[158:159], v[176:177], v[166:167] op_sel_hi:[1,1,0]
	v_med3_f32 v1, v156, s14, v221
	v_med3_f32 v151, v154, s14, v221
	v_mov_b32_e32 v166, v133
	v_cvt_pk_fp8_f32 v166, v1, v151
	v_med3_f32 v1, v164, s14, v221
	v_med3_f32 v151, v162, s14, v221
	v_mov_b32_e32 v167, v133
	v_cvt_pk_fp8_f32 v167, v1, v151
	v_med3_f32 v153, v152, s14, v221
	v_med3_f32 v155, v150, s14, v221
	v_cvt_pk_fp8_f32 v166, v153, v155 op_sel:[0,0,1]
	v_med3_f32 v153, v160, s14, v221
	v_med3_f32 v155, v158, s14, v221
	v_cvt_pk_fp8_f32 v167, v153, v155 op_sel:[0,0,1]
	v_lshl_add_u64 v[168:169], v[126:127], 0, s[34:35]
	v_cvt_pk_f32_fp8_sdwa v[170:171], v148 src0_sel:WORD_1
	v_cvt_pk_f32_fp8_e32 v[172:173], v149
	global_store_dwordx2 v[168:169], v[166:167], off
	v_readlane_b32 s100, v252, 25
	s_nop 1
	v_mov_b32_e32 v166, s100
	v_readlane_b32 s100, v253, 25
	s_nop 1
	v_mov_b32_e32 v167, s100
	v_cvt_pk_f32_fp8_e32 v[168:169], v148
	v_cvt_pk_f32_fp8_sdwa v[174:175], v149 src0_sel:WORD_1
	v_mov_b32_e32 v153, v170
	v_mov_b32_e32 v157, v168
	v_mov_b32_e32 v155, v169
	v_add_f32_e32 v1, v178, v166
	v_max_f32_e32 v151, v167, v167
	v_max_f32_e32 v176, v1, v151
	v_sub_f32_e32 v1, v1, v176
	v_mul_f32_e32 v1, 0x3fb8aa3b, v1
	v_exp_f32_e32 v166, v1
	v_sub_f32_e32 v1, v167, v176
	v_mul_f32_e32 v1, 0x3fb8aa3b, v1
	v_exp_f32_e32 v167, v1
	v_mov_b32_e32 v151, v171
	v_mul_f32_e32 v148, v168, v167
	v_pk_fma_f32 v[156:157], v[156:157], v[166:167], v[148:149] op_sel_hi:[1,1,0]
	v_mul_f32_e32 v148, v169, v167
	v_pk_fma_f32 v[154:155], v[154:155], v[166:167], v[148:149] op_sel_hi:[1,1,0]
	v_mul_f32_e32 v148, v170, v167
	v_pk_fma_f32 v[152:153], v[152:153], v[166:167], v[148:149] op_sel_hi:[1,1,0]
	v_mul_f32_e32 v148, v171, v167
	v_pk_fma_f32 v[150:151], v[150:151], v[166:167], v[148:149] op_sel_hi:[1,1,0]
	v_mov_b32_e32 v165, v167
	v_mov_b32_e32 v148, v166
	v_mov_b32_e32 v149, v172
	v_mul_f32_e32 v168, v167, v172
	v_pk_fma_f32 v[148:149], v[164:165], v[148:149], v[168:169] op_sel_hi:[1,1,0]
	v_mov_b32_e32 v163, v167
; __device__ __forceinline__ int cslot(int bh, int c) { return (c + bh) & 31; }
; template <int GRP>
; __device__ __forceinline__ void y_phase(Frame& F, const MW& W) {
;     ...
;         for (int c = 0; c < 32; ++c) {
;             u32x2 o; o.x = pg8::pack_fp8x4(C[0], C[1], C[2], C[3]); o.y = pg8::pack_fp8x4(C[4], C[5], C[6], C[7]); *(u32x2*)(W.CP + off + (size_t)cslot(bh, c) * 16384) = o;
;             const float bl = sc[2 * c], am = sc[2 * c + 1], mn = fmaxf(bl + m, am), dec = __expf(bl + m - mn), inj = __expf(am - mn);
;             const auto x0 = __builtin_amdgcn_cvt_pk_f32_fp8((int)v[c].x, false), x1 = __builtin_amdgcn_cvt_pk_f32_fp8((int)v[c].x, true), x2 = __builtin_amdgcn_cvt_pk_f32_fp8((int)v[c].y, false), x3 = __builtin_amdgcn_cvt_pk_f32_fp8((int)v[c].y, true);
;             C[0] = C[0] * dec + x0[0] * inj; C[1] = C[1] * dec + x0[1] * inj; C[2] = C[2] * dec + x1[0] * inj; C[3] = C[3] * dec + x1[1] * inj;
;             C[4] = C[4] * dec + x2[0] * inj; C[5] = C[5] * dec + x2[1] * inj; C[6] = C[6] * dec + x3[0] * inj; C[7] = C[7] * dec + x3[1] * inj; m = mn; }
	v_mov_b32_e32 v172, v166
	v_mul_f32_e32 v164, v167, v173
	v_pk_fma_f32 v[162:163], v[162:163], v[172:173], v[164:165] op_sel_hi:[1,1,0]
	v_mov_b32_e32 v161, v167
	v_mov_b32_e32 v164, v166
	v_mov_b32_e32 v165, v174
	v_mul_f32_e32 v168, v167, v174
	v_pk_fma_f32 v[160:161], v[160:161], v[164:165], v[168:169] op_sel_hi:[1,1,0]
	v_mov_b32_e32 v159, v167
	v_mov_b32_e32 v174, v166
	v_mul_f32_e32 v164, v167, v175
	v_pk_fma_f32 v[158:159], v[158:159], v[174:175], v[164:165] op_sel_hi:[1,1,0]
	v_med3_f32 v1, v156, s14, v221
	v_med3_f32 v149, v154, s14, v221
	v_mov_b32_e32 v164, v133
	v_cvt_pk_fp8_f32 v164, v1, v149
	v_med3_f32 v1, v148, s14, v221
	v_med3_f32 v149, v162, s14, v221
	v_mov_b32_e32 v165, v133
	v_cvt_pk_fp8_f32 v165, v1, v149
	v_med3_f32 v151, v152, s14, v221
	v_med3_f32 v153, v150, s14, v221
	v_cvt_pk_fp8_f32 v164, v151, v153 op_sel:[0,0,1]
	v_med3_f32 v151, v160, s14, v221
	v_med3_f32 v153, v158, s14, v221
	v_cvt_pk_fp8_f32 v165, v151, v153 op_sel:[0,0,1]
	v_lshl_add_u64 v[166:167], v[126:127], 0, s[30:31]
	v_cvt_pk_f32_fp8_sdwa v[168:169], v146 src0_sel:WORD_1
	v_cvt_pk_f32_fp8_e32 v[170:171], v147
	global_store_dwordx2 v[166:167], v[164:165], off
	v_readlane_b32 s100, v252, 26
	s_nop 1
	v_mov_b32_e32 v164, s100
	v_readlane_b32 s100, v253, 26
	s_nop 1
	v_mov_b32_e32 v165, s100
	v_cvt_pk_f32_fp8_e32 v[166:167], v146
	v_cvt_pk_f32_fp8_sdwa v[172:173], v147 src0_sel:WORD_1
	v_mov_b32_e32 v153, v168
	v_mov_b32_e32 v151, v169
	v_mov_b32_e32 v157, v166
	v_mov_b32_e32 v155, v167
	v_add_f32_e32 v1, v176, v164
	v_max_f32_e32 v149, v165, v165
	v_max_f32_e32 v174, v1, v149
	v_sub_f32_e32 v1, v1, v174
	v_mul_f32_e32 v1, 0x3fb8aa3b, v1
	v_exp_f32_e32 v164, v1
	v_sub_f32_e32 v1, v165, v174
	v_mul_f32_e32 v1, 0x3fb8aa3b, v1
	v_exp_f32_e32 v165, v1
	s_nop 0
	v_mul_f32_e32 v146, v166, v165
	v_pk_fma_f32 v[156:157], v[156:157], v[164:165], v[146:147] op_sel_hi:[1,1,0]
	v_mul_f32_e32 v146, v167, v165
	v_pk_fma_f32 v[154:155], v[154:155], v[164:165], v[146:147] op_sel_hi:[1,1,0]
	v_mul_f32_e32 v146, v168, v165
	v_pk_fma_f32 v[152:153], v[152:153], v[164:165], v[146:147] op_sel_hi:[1,1,0]
	v_mul_f32_e32 v146, v169, v165
	v_pk_fma_f32 v[150:151], v[150:151], v[164:165], v[146:147] op_sel_hi:[1,1,0]
	v_mov_b32_e32 v149, v165
	v_mov_b32_e32 v146, v164
	v_mov_b32_e32 v147, v170
	v_mul_f32_e32 v166, v165, v170
	v_pk_fma_f32 v[148:149], v[148:149], v[146:147], v[166:167] op_sel_hi:[1,1,0]
	v_mov_b32_e32 v163, v165
	v_mov_b32_e32 v170, v164
	v_mul_f32_e32 v146, v165, v171
	v_pk_fma_f32 v[146:147], v[162:163], v[170:171], v[146:147] op_sel_hi:[1,1,0]
	v_mov_b32_e32 v161, v165
	v_mov_b32_e32 v162, v164
	v_mov_b32_e32 v163, v172
	v_mul_f32_e32 v166, v165, v172
	v_pk_fma_f32 v[160:161], v[160:161], v[162:163], v[166:167] op_sel_hi:[1,1,0]
	v_mov_b32_e32 v159, v165
	v_mov_b32_e32 v172, v164
	v_mul_f32_e32 v162, v165, v173
	v_pk_fma_f32 v[158:159], v[158:159], v[172:173], v[162:163] op_sel_hi:[1,1,0]
	v_med3_f32 v1, v156, s14, v221
	v_med3_f32 v147, v154, s14, v221
	v_mov_b32_e32 v162, v133
	v_cvt_pk_fp8_f32 v162, v1, v147
	v_med3_f32 v1, v148, s14, v221
	v_med3_f32 v147, v146, s14, v221
	v_mov_b32_e32 v163, v133
	v_cvt_pk_fp8_f32 v163, v1, v147
	v_med3_f32 v149, v152, s14, v221
	v_med3_f32 v151, v150, s14, v221
	v_cvt_pk_fp8_f32 v162, v149, v151 op_sel:[0,0,1]
	v_med3_f32 v149, v160, s14, v221
	v_med3_f32 v151, v158, s14, v221
	v_cvt_pk_fp8_f32 v163, v149, v151 op_sel:[0,0,1]
	v_lshl_add_u64 v[164:165], v[126:127], 0, s[28:29]
	v_cvt_pk_f32_fp8_sdwa v[166:167], v144 src0_sel:WORD_1
	v_cvt_pk_f32_fp8_e32 v[168:169], v145
	global_store_dwordx2 v[164:165], v[162:163], off
	v_readlane_b32 s100, v252, 27
	s_nop 1
	v_mov_b32_e32 v162, s100
	v_readlane_b32 s100, v253, 27
	s_nop 1
	v_mov_b32_e32 v163, s100
	v_cvt_pk_f32_fp8_e32 v[164:165], v144
	v_cvt_pk_f32_fp8_sdwa v[170:171], v145 src0_sel:WORD_1
	v_mov_b32_e32 v153, v166
	v_mov_b32_e32 v151, v167
	v_mov_b32_e32 v157, v164
	v_mov_b32_e32 v155, v165
	v_add_f32_e32 v1, v174, v162
	v_max_f32_e32 v147, v163, v163
	v_max_f32_e32 v172, v1, v147
	v_sub_f32_e32 v1, v1, v172
	v_mul_f32_e32 v1, 0x3fb8aa3b, v1
	v_exp_f32_e32 v162, v1
	v_sub_f32_e32 v1, v163, v172
	v_mul_f32_e32 v1, 0x3fb8aa3b, v1
	v_exp_f32_e32 v163, v1
	s_nop 0
	v_mul_f32_e32 v144, v164, v163
	v_pk_fma_f32 v[156:157], v[156:157], v[162:163], v[144:145] op_sel_hi:[1,1,0]
	v_mul_f32_e32 v144, v165, v163
	v_pk_fma_f32 v[154:155], v[154:155], v[162:163], v[144:145] op_sel_hi:[1,1,0]
	v_mul_f32_e32 v144, v166, v163
	v_pk_fma_f32 v[152:153], v[152:153], v[162:163], v[144:145] op_sel_hi:[1,1,0]
	v_mul_f32_e32 v144, v167, v163
	v_pk_fma_f32 v[150:151], v[150:151], v[162:163], v[144:145] op_sel_hi:[1,1,0]
	v_mov_b32_e32 v149, v163
	v_mov_b32_e32 v144, v162
	v_mov_b32_e32 v145, v168
	v_mul_f32_e32 v164, v163, v168
	v_pk_fma_f32 v[148:149], v[148:149], v[144:145], v[164:165] op_sel_hi:[1,1,0]
	v_mov_b32_e32 v147, v163
	v_mov_b32_e32 v168, v162
	v_mul_f32_e32 v144, v163, v169
	v_pk_fma_f32 v[146:147], v[146:147], v[168:169], v[144:145] op_sel_hi:[1,1,0]
	v_mov_b32_e32 v161, v163
	v_mov_b32_e32 v144, v162
	v_mov_b32_e32 v145, v170
	v_mul_f32_e32 v164, v163, v170
	v_pk_fma_f32 v[144:145], v[160:161], v[144:145], v[164:165] op_sel_hi:[1,1,0]
	v_mov_b32_e32 v159, v163
	v_mov_b32_e32 v170, v162
	v_mul_f32_e32 v160, v163, v171
	v_pk_fma_f32 v[158:159], v[158:159], v[170:171], v[160:161] op_sel_hi:[1,1,0]
	v_med3_f32 v1, v156, s14, v221
	v_med3_f32 v145, v154, s14, v221
	v_mov_b32_e32 v160, v133
	v_cvt_pk_fp8_f32 v160, v1, v145
	v_med3_f32 v1, v148, s14, v221
	v_med3_f32 v145, v146, s14, v221
	v_mov_b32_e32 v161, v133
	v_cvt_pk_fp8_f32 v161, v1, v145
	v_med3_f32 v147, v152, s14, v221
; __device__ __forceinline__ int cslot(int bh, int c) { return (c + bh) & 31; }
; template <int GRP>
; __device__ __forceinline__ void y_phase(Frame& F, const MW& W) {
;     ...
;         for (int c = 0; c < 32; ++c) {
;             u32x2 o; o.x = pg8::pack_fp8x4(C[0], C[1], C[2], C[3]); o.y = pg8::pack_fp8x4(C[4], C[5], C[6], C[7]); *(u32x2*)(W.CP + off + (size_t)cslot(bh, c) * 16384) = o;
;             const float bl = sc[2 * c], am = sc[2 * c + 1], mn = fmaxf(bl + m, am), dec = __expf(bl + m - mn), inj = __expf(am - mn);
;             const auto x0 = __builtin_amdgcn_cvt_pk_f32_fp8((int)v[c].x, false), x1 = __builtin_amdgcn_cvt_pk_f32_fp8((int)v[c].x, true), x2 = __builtin_amdgcn_cvt_pk_f32_fp8((int)v[c].y, false), x3 = __builtin_amdgcn_cvt_pk_f32_fp8((int)v[c].y, true);
;             C[0] = C[0] * dec + x0[0] * inj; C[1] = C[1] * dec + x0[1] * inj; C[2] = C[2] * dec + x1[0] * inj; C[3] = C[3] * dec + x1[1] * inj;
;             C[4] = C[4] * dec + x2[0] * inj; C[5] = C[5] * dec + x2[1] * inj; C[6] = C[6] * dec + x3[0] * inj; C[7] = C[7] * dec + x3[1] * inj; m = mn; }
	v_med3_f32 v149, v150, s14, v221
	v_cvt_pk_fp8_f32 v160, v147, v149 op_sel:[0,0,1]
	v_med3_f32 v147, v144, s14, v221
	v_med3_f32 v149, v158, s14, v221
	v_cvt_pk_fp8_f32 v161, v147, v149 op_sel:[0,0,1]
	v_lshl_add_u64 v[162:163], v[126:127], 0, s[26:27]
	v_cvt_pk_f32_fp8_sdwa v[164:165], v142 src0_sel:WORD_1
	v_cvt_pk_f32_fp8_e32 v[166:167], v143
	global_store_dwordx2 v[162:163], v[160:161], off
	v_readlane_b32 s100, v252, 28
	s_nop 1
	v_mov_b32_e32 v160, s100
	v_readlane_b32 s100, v253, 28
	s_nop 1
	v_mov_b32_e32 v161, s100
	v_cvt_pk_f32_fp8_e32 v[162:163], v142
	v_cvt_pk_f32_fp8_sdwa v[142:143], v143 src0_sel:WORD_1
	v_mov_b32_e32 v153, v164
	v_mov_b32_e32 v151, v165
	v_mov_b32_e32 v157, v162
	v_mov_b32_e32 v155, v163
	v_add_f32_e32 v1, v172, v160
	v_max_f32_e32 v145, v161, v161
	v_max_f32_e32 v168, v1, v145
	v_sub_f32_e32 v1, v1, v168
	v_mul_f32_e32 v1, 0x3fb8aa3b, v1
	v_exp_f32_e32 v160, v1
	v_sub_f32_e32 v1, v161, v168
	v_mul_f32_e32 v1, 0x3fb8aa3b, v1
	v_exp_f32_e32 v161, v1
	s_nop 0
	v_mul_f32_e32 v162, v162, v161
	v_pk_fma_f32 v[156:157], v[156:157], v[160:161], v[162:163] op_sel_hi:[1,1,0]
	v_mul_f32_e32 v162, v163, v161
	v_pk_fma_f32 v[154:155], v[154:155], v[160:161], v[162:163] op_sel_hi:[1,1,0]
	v_mul_f32_e32 v162, v164, v161
	v_pk_fma_f32 v[152:153], v[152:153], v[160:161], v[162:163] op_sel_hi:[1,1,0]
	v_mul_f32_e32 v162, v165, v161
	v_pk_fma_f32 v[150:151], v[150:151], v[160:161], v[162:163] op_sel_hi:[1,1,0]
	v_mov_b32_e32 v149, v161
	v_mov_b32_e32 v162, v160
	v_mov_b32_e32 v163, v166
	v_mul_f32_e32 v164, v161, v166
	v_pk_fma_f32 v[148:149], v[148:149], v[162:163], v[164:165] op_sel_hi:[1,1,0]
	v_mov_b32_e32 v147, v161
	v_mov_b32_e32 v166, v160
	v_mul_f32_e32 v162, v161, v167
	v_pk_fma_f32 v[146:147], v[146:147], v[166:167], v[162:163] op_sel_hi:[1,1,0]
	v_mov_b32_e32 v145, v161
	v_mov_b32_e32 v162, v160
	v_mov_b32_e32 v163, v142
	v_mul_f32_e32 v142, v161, v142
	v_pk_fma_f32 v[144:145], v[144:145], v[162:163], v[142:143] op_sel_hi:[1,1,0]
	v_mov_b32_e32 v159, v161
	v_mov_b32_e32 v142, v160
	v_mul_f32_e32 v160, v161, v143
	v_pk_fma_f32 v[142:143], v[158:159], v[142:143], v[160:161] op_sel_hi:[1,1,0]
	v_med3_f32 v1, v156, s14, v221
	v_med3_f32 v143, v154, s14, v221
	v_mov_b32_e32 v158, v133
	v_cvt_pk_fp8_f32 v158, v1, v143
	v_med3_f32 v1, v148, s14, v221
	v_med3_f32 v143, v146, s14, v221
	v_mov_b32_e32 v159, v133
	v_cvt_pk_fp8_f32 v159, v1, v143
	v_med3_f32 v145, v152, s14, v221
	v_med3_f32 v147, v150, s14, v221
	v_cvt_pk_fp8_f32 v158, v145, v147 op_sel:[0,0,1]
	v_med3_f32 v145, v144, s14, v221
	v_med3_f32 v147, v142, s14, v221
	v_cvt_pk_fp8_f32 v159, v145, v147 op_sel:[0,0,1]
	v_lshl_add_u64 v[160:161], v[126:127], 0, s[24:25]
	v_cvt_pk_f32_fp8_sdwa v[162:163], v140 src0_sel:WORD_1
	v_cvt_pk_f32_fp8_e32 v[164:165], v141
	global_store_dwordx2 v[160:161], v[158:159], off
	v_readlane_b32 s100, v252, 29
	s_nop 1
	v_mov_b32_e32 v158, s100
	v_readlane_b32 s100, v253, 29
	s_nop 1
	v_mov_b32_e32 v159, s100
	v_cvt_pk_f32_fp8_e32 v[160:161], v140
	v_cvt_pk_f32_fp8_sdwa v[140:141], v141 src0_sel:WORD_1
	v_mov_b32_e32 v153, v162
	v_mov_b32_e32 v151, v163
	v_mov_b32_e32 v157, v160
	v_mov_b32_e32 v155, v161
	v_add_f32_e32 v1, v168, v158
	v_max_f32_e32 v143, v159, v159
	v_max_f32_e32 v166, v1, v143
	v_sub_f32_e32 v1, v1, v166
	v_mul_f32_e32 v1, 0x3fb8aa3b, v1
	v_exp_f32_e32 v158, v1
	v_sub_f32_e32 v1, v159, v166
	v_mul_f32_e32 v1, 0x3fb8aa3b, v1
	v_exp_f32_e32 v159, v1
	s_nop 0
	v_mul_f32_e32 v160, v160, v159
	v_pk_fma_f32 v[156:157], v[156:157], v[158:159], v[160:161] op_sel_hi:[1,1,0]
	v_mul_f32_e32 v160, v161, v159
	v_pk_fma_f32 v[154:155], v[154:155], v[158:159], v[160:161] op_sel_hi:[1,1,0]
	v_mul_f32_e32 v160, v162, v159
	v_pk_fma_f32 v[152:153], v[152:153], v[158:159], v[160:161] op_sel_hi:[1,1,0]
	v_mul_f32_e32 v160, v163, v159
	v_pk_fma_f32 v[150:151], v[150:151], v[158:159], v[160:161] op_sel_hi:[1,1,0]
	v_mov_b32_e32 v149, v159
	v_mov_b32_e32 v160, v158
	v_mov_b32_e32 v161, v164
	v_mul_f32_e32 v162, v159, v164
	v_pk_fma_f32 v[148:149], v[148:149], v[160:161], v[162:163] op_sel_hi:[1,1,0]
	v_mov_b32_e32 v147, v159
	v_mov_b32_e32 v164, v158
	v_mul_f32_e32 v160, v159, v165
	v_pk_fma_f32 v[146:147], v[146:147], v[164:165], v[160:161] op_sel_hi:[1,1,0]
	v_mov_b32_e32 v145, v159
	v_mov_b32_e32 v160, v158
	v_mov_b32_e32 v161, v140
	v_mul_f32_e32 v140, v159, v140
	v_pk_fma_f32 v[144:145], v[144:145], v[160:161], v[140:141] op_sel_hi:[1,1,0]
	v_mov_b32_e32 v143, v159
	v_mov_b32_e32 v140, v158
	v_mul_f32_e32 v158, v159, v141
	v_pk_fma_f32 v[140:141], v[142:143], v[140:141], v[158:159] op_sel_hi:[1,1,0]
	v_med3_f32 v1, v156, s14, v221
	v_med3_f32 v141, v154, s14, v221
	v_mov_b32_e32 v142, v133
	v_cvt_pk_fp8_f32 v142, v1, v141
	v_med3_f32 v143, v152, s14, v221
	v_med3_f32 v145, v150, s14, v221
	v_med3_f32 v1, v148, s14, v221
	v_cvt_pk_fp8_f32 v142, v143, v145 op_sel:[0,0,1]
	v_med3_f32 v141, v146, s14, v221
	v_mov_b32_e32 v143, v133
	v_cvt_pk_fp8_f32 v143, v1, v141
	v_med3_f32 v145, v144, s14, v221
	v_med3_f32 v147, v140, s14, v221
	v_lshl_add_u64 v[158:159], v[126:127], 0, s[22:23]
	v_cvt_pk_fp8_f32 v143, v145, v147 op_sel:[0,0,1]
	v_cvt_pk_f32_fp8_sdwa v[160:161], v128 src0_sel:WORD_1
	v_cvt_pk_f32_fp8_e32 v[162:163], v129
	v_lshl_add_u64 v[126:127], v[126:127], 0, s[16:17]
	global_store_dwordx2 v[158:159], v[142:143], off
	v_readlane_b32 s100, v252, 30
	s_nop 1
	v_mov_b32_e32 v142, s100
	v_readlane_b32 s100, v253, 30
	s_nop 1
	v_mov_b32_e32 v143, s100
	v_cvt_pk_f32_fp8_e32 v[158:159], v128
	v_cvt_pk_f32_fp8_sdwa v[128:129], v129 src0_sel:WORD_1
	v_mov_b32_e32 v153, v160
	v_mov_b32_e32 v151, v161
	v_mov_b32_e32 v157, v158
; __device__ __forceinline__ int cslot(int bh, int c) { return (c + bh) & 31; }
; template <int GRP>
; __device__ __forceinline__ void y_phase(Frame& F, const MW& W) {
;     ...
;         for (int c = 0; c < 32; ++c) {
;             u32x2 o; o.x = pg8::pack_fp8x4(C[0], C[1], C[2], C[3]); o.y = pg8::pack_fp8x4(C[4], C[5], C[6], C[7]); *(u32x2*)(W.CP + off + (size_t)cslot(bh, c) * 16384) = o;
;             const float bl = sc[2 * c], am = sc[2 * c + 1], mn = fmaxf(bl + m, am), dec = __expf(bl + m - mn), inj = __expf(am - mn);
;             const auto x0 = __builtin_amdgcn_cvt_pk_f32_fp8((int)v[c].x, false), x1 = __builtin_amdgcn_cvt_pk_f32_fp8((int)v[c].x, true), x2 = __builtin_amdgcn_cvt_pk_f32_fp8((int)v[c].y, false), x3 = __builtin_amdgcn_cvt_pk_f32_fp8((int)v[c].y, true);
;             C[0] = C[0] * dec + x0[0] * inj; C[1] = C[1] * dec + x0[1] * inj; C[2] = C[2] * dec + x1[0] * inj; C[3] = C[3] * dec + x1[1] * inj;
;             C[4] = C[4] * dec + x2[0] * inj; C[5] = C[5] * dec + x2[1] * inj; C[6] = C[6] * dec + x3[0] * inj; C[7] = C[7] * dec + x3[1] * inj; m = mn; }
;         if (nsc) {
;             f32x4 N = (f32x4){0.f, 0.f, 0.f, 0.f}; float mm = 0.f;
; #pragma unroll
;             for (int c = 0; c < 32; ++c) {
;                 *(f32x4*)(W.NP + ((size_t)bh * 32 + c) * 128 + g * 4) = N; if (g == 0) W.MP[bh * 32 + c] = mm;
;                 const float bl = sc[2 * c], am = sc[2 * c + 1], mn = fmaxf(bl + mm, am), dec = __expf(bl + mm - mn), inj = __expf(am - mn);
;                 N = N * dec + nv[c] * inj; mm = mn; }
	v_mov_b32_e32 v155, v159
	v_add_f32_e32 v1, v166, v142
	v_max_f32_e32 v141, v143, v143
	v_max_f32_e32 v141, v1, v141
	v_sub_f32_e32 v1, v1, v141
	v_mul_f32_e32 v1, 0x3fb8aa3b, v1
	v_exp_f32_e32 v142, v1
	v_sub_f32_e32 v1, v143, v141
	v_mul_f32_e32 v1, 0x3fb8aa3b, v1
	v_exp_f32_e32 v143, v1
	s_nop 0
	v_pk_mul_f32 v[152:153], v[152:153], v[142:143]
	v_pk_mul_f32 v[150:151], v[150:151], v[142:143]
	v_add_f32_e32 v152, v152, v153
	v_add_f32_e32 v153, v150, v151
	v_mov_b32_e32 v149, v143
	v_mov_b32_e32 v150, v142
	v_mov_b32_e32 v151, v162
	v_mov_b32_e32 v147, v143
	v_mov_b32_e32 v162, v142
	v_pk_mul_f32 v[156:157], v[156:157], v[142:143]
	v_pk_mul_f32 v[154:155], v[154:155], v[142:143]
	v_pk_mul_f32 v[148:149], v[148:149], v[150:151]
	v_pk_mul_f32 v[146:147], v[146:147], v[162:163]
	v_mov_b32_e32 v145, v143
	v_mov_b32_e32 v141, v143
	v_mov_b32_e32 v143, v129
	v_add_f32_e32 v1, v156, v157
	v_add_f32_e32 v154, v154, v155
	v_add_f32_e32 v148, v148, v149
	v_add_f32_e32 v149, v146, v147
	v_mov_b32_e32 v147, v128
	v_pk_mul_f32 v[128:129], v[140:141], v[142:143]
	v_med3_f32 v1, v1, s14, v221
	v_add_f32_e32 v129, v128, v129
	v_med3_f32 v140, v154, s14, v221
	v_mov_b32_e32 v128, v133
	v_cvt_pk_fp8_f32 v128, v1, v140
	v_mov_b32_e32 v146, v142
	v_med3_f32 v141, v152, s14, v221
	v_med3_f32 v142, v153, s14, v221
	v_cvt_pk_fp8_f32 v128, v141, v142 op_sel:[0,0,1]
	v_med3_f32 v1, v148, s14, v221
	v_med3_f32 v140, v149, s14, v221
	v_med3_f32 v142, v129, s14, v221
	v_mov_b32_e32 v129, v133
	v_cvt_pk_fp8_f32 v129, v1, v140
	v_pk_mul_f32 v[144:145], v[144:145], v[146:147]
	s_nop 0
	v_add_f32_e32 v144, v144, v145
	v_med3_f32 v141, v144, s14, v221
	v_cvt_pk_fp8_f32 v129, v141, v142 op_sel:[0,0,1]
	global_store_dwordx2 v[126:127], v[128:129], off
	s_and_saveexec_b64 s[0:1], s[8:9]
	s_cbranch_execz .LBB0_1612
	s_lshl_b32 s18, s18, 5
	v_readlane_b32 s22, v255, 25
	v_readlane_b32 s23, v255, 26
	s_add_u32 s20, s22, s20
	v_cmp_eq_u32_e64 s[8:9], 0, v223
	s_addc_u32 s21, s23, s21
	v_lshlrev_b32_e32 v140, 2, v134
	global_store_dwordx4 v140, v[224:227], s[20:21]
	s_and_saveexec_b64 s[22:23], s[8:9]
	s_cbranch_execz .LBB0_1550
	s_ashr_i32 s19, s18, 31
	s_lshl_b64 s[24:25], s[18:19], 2
	s_add_u32 s24, s64, s24
	s_addc_u32 s25, s65, s25
	global_store_dword v133, v133, s[24:25]
.LBB0_1550:
	s_or_b64 exec, exec, s[22:23]
	v_readlane_b32 s100, v252, 0
	s_nop 1
	v_mov_b32_e32 v126, s100
	v_readlane_b32 s100, v253, 0
	s_nop 1
	v_mov_b32_e32 v127, s100
	v_mov_b32_e32 v141, v133
	v_lshl_add_u64 v[142:143], s[20:21], 0, v[140:141]
	v_add_f32_e32 v126, 0, v126
	v_max_f32_e32 v1, v127, v127
	v_max_f32_e32 v1, v126, v1
	v_sub_f32_e32 v126, v126, v1
	v_sub_f32_e32 v127, v127, v1
	v_mul_f32_e32 v126, 0x3fb8aa3b, v126
	v_mul_f32_e32 v127, 0x3fb8aa3b, v127
	v_exp_f32_e32 v128, v126
	v_exp_f32_e32 v126, v127
	v_mul_f32_e32 v144, 0, v128
	v_pk_fma_f32 v[128:129], v[32:33], v[126:127], v[144:145] op_sel_hi:[1,0,0]
	v_pk_fma_f32 v[126:127], v[30:31], v[126:127], v[144:145] op_sel_hi:[1,0,0]
	global_store_dwordx4 v[142:143], v[126:129], off offset:512
	s_and_saveexec_b64 s[22:23], s[8:9]
	s_cbranch_execz .LBB0_1552
	s_ashr_i32 s19, s18, 31
	s_lshl_b64 s[24:25], s[18:19], 2
	s_add_u32 s24, s64, s24
	s_addc_u32 s25, s65, s25
	global_store_dword v133, v1, s[24:25] offset:4
.LBB0_1552:
	s_or_b64 exec, exec, s[22:23]
	v_readlane_b32 s100, v252, 1
	s_nop 1
	v_mov_b32_e32 v144, s100
	v_readlane_b32 s100, v253, 1
	s_nop 1
	v_mov_b32_e32 v145, s100
	v_add_f32_e32 v141, v1, v144
	v_max_f32_e32 v1, v145, v145
	v_max_f32_e32 v1, v141, v1
	v_sub_f32_e32 v144, v145, v1
	v_sub_f32_e32 v141, v141, v1
	v_mul_f32_e32 v144, 0x3fb8aa3b, v144
	v_exp_f32_e32 v144, v144
	v_mul_f32_e32 v141, 0x3fb8aa3b, v141
	v_exp_f32_e32 v146, v141
	v_pk_mul_f32 v[148:149], v[26:27], v[144:145] op_sel_hi:[1,0]
	v_pk_mul_f32 v[144:145], v[28:29], v[144:145] op_sel_hi:[1,0]
	v_pk_fma_f32 v[126:127], v[126:127], v[146:147], v[148:149] op_sel_hi:[1,0,1]
	v_pk_fma_f32 v[128:129], v[128:129], v[146:147], v[144:145] op_sel_hi:[1,0,1]
	global_store_dwordx4 v[142:143], v[126:129], off offset:1024
	s_and_saveexec_b64 s[22:23], s[8:9]
	s_cbranch_execz .LBB0_1554
	s_ashr_i32 s19, s18, 31
	s_lshl_b64 s[24:25], s[18:19], 2
	s_add_u32 s24, s64, s24
	s_addc_u32 s25, s65, s25
	global_store_dword v133, v1, s[24:25] offset:8
.LBB0_1554:
	s_or_b64 exec, exec, s[22:23]
	v_readlane_b32 s100, v252, 2
	s_nop 1
	v_mov_b32_e32 v144, s100
	v_readlane_b32 s100, v253, 2
	s_nop 1
	v_mov_b32_e32 v145, s100
	v_add_f32_e32 v141, v1, v144
	v_max_f32_e32 v1, v145, v145
	v_max_f32_e32 v1, v141, v1
	v_sub_f32_e32 v144, v145, v1
	v_sub_f32_e32 v141, v141, v1
	v_mul_f32_e32 v144, 0x3fb8aa3b, v144
	v_exp_f32_e32 v144, v144
	v_mul_f32_e32 v141, 0x3fb8aa3b, v141
	v_exp_f32_e32 v146, v141
	v_pk_mul_f32 v[148:149], v[22:23], v[144:145] op_sel_hi:[1,0]
	v_pk_mul_f32 v[144:145], v[24:25], v[144:145] op_sel_hi:[1,0]
	v_pk_fma_f32 v[126:127], v[126:127], v[146:147], v[148:149] op_sel_hi:[1,0,1]
	v_pk_fma_f32 v[128:129], v[128:129], v[146:147], v[144:145] op_sel_hi:[1,0,1]
	global_store_dwordx4 v[142:143], v[126:129], off offset:1536
	s_and_saveexec_b64 s[22:23], s[8:9]
	s_cbranch_execz .LBB0_1556
	s_ashr_i32 s19, s18, 31
	s_lshl_b64 s[24:25], s[18:19], 2
	s_add_u32 s24, s64, s24
	s_addc_u32 s25, s65, s25
	global_store_dword v133, v1, s[24:25] offset:12
; template <int GRP>
; __device__ __forceinline__ void y_phase(Frame& F, const MW& W) {
;     ...
; #pragma unroll
;             for (int c = 0; c < 32; ++c) {
;                 *(f32x4*)(W.NP + ((size_t)bh * 32 + c) * 128 + g * 4) = N; if (g == 0) W.MP[bh * 32 + c] = mm;
;                 const float bl = sc[2 * c], am = sc[2 * c + 1], mn = fmaxf(bl + mm, am), dec = __expf(bl + mm - mn), inj = __expf(am - mn);
;                 N = N * dec + nv[c] * inj; mm = mn; }
.LBB0_1556:
	s_or_b64 exec, exec, s[22:23]
	v_readlane_b32 s100, v252, 3
	s_nop 1
	v_mov_b32_e32 v144, s100
	v_readlane_b32 s100, v253, 3
	s_nop 1
	v_mov_b32_e32 v145, s100
	v_add_f32_e32 v141, v1, v144
	v_max_f32_e32 v1, v145, v145
	v_max_f32_e32 v1, v141, v1
	v_sub_f32_e32 v144, v145, v1
	v_sub_f32_e32 v141, v141, v1
	v_mul_f32_e32 v144, 0x3fb8aa3b, v144
	v_exp_f32_e32 v144, v144
	v_mul_f32_e32 v141, 0x3fb8aa3b, v141
	v_exp_f32_e32 v146, v141
	v_pk_mul_f32 v[148:149], v[18:19], v[144:145] op_sel_hi:[1,0]
	v_pk_mul_f32 v[144:145], v[20:21], v[144:145] op_sel_hi:[1,0]
	v_pk_fma_f32 v[126:127], v[126:127], v[146:147], v[148:149] op_sel_hi:[1,0,1]
	v_pk_fma_f32 v[128:129], v[128:129], v[146:147], v[144:145] op_sel_hi:[1,0,1]
	global_store_dwordx4 v[142:143], v[126:129], off offset:2048
	s_and_saveexec_b64 s[22:23], s[8:9]
	s_cbranch_execz .LBB0_1558
	s_ashr_i32 s19, s18, 31
	s_lshl_b64 s[24:25], s[18:19], 2
	s_add_u32 s24, s64, s24
	s_addc_u32 s25, s65, s25
	global_store_dword v133, v1, s[24:25] offset:16
.LBB0_1558:
	s_or_b64 exec, exec, s[22:23]
	v_readlane_b32 s100, v252, 4
	s_nop 1
	v_mov_b32_e32 v144, s100
	v_readlane_b32 s100, v253, 4
	s_nop 1
	v_mov_b32_e32 v145, s100
	v_add_f32_e32 v141, v1, v144
	v_max_f32_e32 v1, v145, v145
	v_max_f32_e32 v1, v141, v1
	v_sub_f32_e32 v144, v145, v1
	v_sub_f32_e32 v141, v141, v1
	v_mul_f32_e32 v144, 0x3fb8aa3b, v144
	v_exp_f32_e32 v144, v144
	v_mul_f32_e32 v141, 0x3fb8aa3b, v141
	v_exp_f32_e32 v146, v141
	v_pk_mul_f32 v[148:149], v[14:15], v[144:145] op_sel_hi:[1,0]
	v_pk_mul_f32 v[144:145], v[16:17], v[144:145] op_sel_hi:[1,0]
	v_pk_fma_f32 v[126:127], v[126:127], v[146:147], v[148:149] op_sel_hi:[1,0,1]
	v_pk_fma_f32 v[128:129], v[128:129], v[146:147], v[144:145] op_sel_hi:[1,0,1]
	global_store_dwordx4 v[142:143], v[126:129], off offset:2560
	s_and_saveexec_b64 s[22:23], s[8:9]
	s_cbranch_execz .LBB0_1560
	s_ashr_i32 s19, s18, 31
	s_lshl_b64 s[24:25], s[18:19], 2
	s_add_u32 s24, s64, s24
	s_addc_u32 s25, s65, s25
	global_store_dword v133, v1, s[24:25] offset:20
.LBB0_1560:
	s_or_b64 exec, exec, s[22:23]
	v_readlane_b32 s100, v252, 5
	s_nop 1
	v_mov_b32_e32 v144, s100
	v_readlane_b32 s100, v253, 5
	s_nop 1
	v_mov_b32_e32 v145, s100
	v_add_f32_e32 v141, v1, v144
	v_max_f32_e32 v1, v145, v145
	v_max_f32_e32 v1, v141, v1
	v_sub_f32_e32 v144, v145, v1
	v_sub_f32_e32 v141, v141, v1
	v_mul_f32_e32 v144, 0x3fb8aa3b, v144
	v_exp_f32_e32 v144, v144
	v_mul_f32_e32 v141, 0x3fb8aa3b, v141
	v_exp_f32_e32 v146, v141
	v_pk_mul_f32 v[148:149], v[10:11], v[144:145] op_sel_hi:[1,0]
	v_pk_mul_f32 v[144:145], v[12:13], v[144:145] op_sel_hi:[1,0]
	v_pk_fma_f32 v[126:127], v[126:127], v[146:147], v[148:149] op_sel_hi:[1,0,1]
	v_pk_fma_f32 v[128:129], v[128:129], v[146:147], v[144:145] op_sel_hi:[1,0,1]
	global_store_dwordx4 v[142:143], v[126:129], off offset:3072
	s_and_saveexec_b64 s[22:23], s[8:9]
	s_cbranch_execz .LBB0_1562
	s_ashr_i32 s19, s18, 31
	s_lshl_b64 s[24:25], s[18:19], 2
	s_add_u32 s24, s64, s24
	s_addc_u32 s25, s65, s25
	global_store_dword v133, v1, s[24:25] offset:24
.LBB0_1562:
	s_or_b64 exec, exec, s[22:23]
	v_readlane_b32 s100, v252, 6
	s_nop 1
	v_mov_b32_e32 v144, s100
	v_readlane_b32 s100, v253, 6
	s_nop 1
	v_mov_b32_e32 v145, s100
	v_add_f32_e32 v141, v1, v144
	v_max_f32_e32 v1, v145, v145
	v_max_f32_e32 v1, v141, v1
	v_sub_f32_e32 v144, v145, v1
	v_sub_f32_e32 v141, v141, v1
	v_mul_f32_e32 v144, 0x3fb8aa3b, v144
	v_exp_f32_e32 v144, v144
	v_mul_f32_e32 v141, 0x3fb8aa3b, v141
	v_exp_f32_e32 v146, v141
	s_waitcnt lgkmcnt(1)
	v_pk_mul_f32 v[148:149], v[6:7], v[144:145] op_sel_hi:[1,0]
	s_waitcnt lgkmcnt(0)
	v_pk_mul_f32 v[144:145], v[8:9], v[144:145] op_sel_hi:[1,0]
	v_pk_fma_f32 v[126:127], v[126:127], v[146:147], v[148:149] op_sel_hi:[1,0,1]
	v_pk_fma_f32 v[128:129], v[128:129], v[146:147], v[144:145] op_sel_hi:[1,0,1]
	global_store_dwordx4 v[142:143], v[126:129], off offset:3584
	s_and_saveexec_b64 s[22:23], s[8:9]
	s_cbranch_execz .LBB0_1564
	s_ashr_i32 s19, s18, 31
	s_lshl_b64 s[24:25], s[18:19], 2
	s_add_u32 s24, s64, s24
	s_addc_u32 s25, s65, s25
	global_store_dword v133, v1, s[24:25] offset:28
.LBB0_1564:
	s_or_b64 exec, exec, s[22:23]
	v_readlane_b32 s100, v252, 7
	s_nop 1
	v_mov_b32_e32 v144, s100
	v_readlane_b32 s100, v253, 7
	s_nop 1
	v_mov_b32_e32 v145, s100
	v_mov_b32_e32 v141, v133
	v_lshl_add_u64 v[142:143], s[20:21], 0, v[140:141]
	v_add_co_u32_e32 v148, vcc, 0x1000, v142
	v_add_f32_e32 v141, v1, v144
	v_max_f32_e32 v1, v145, v145
	v_max_f32_e32 v1, v141, v1
	v_sub_f32_e32 v144, v145, v1
	v_sub_f32_e32 v141, v141, v1
	v_mul_f32_e32 v144, 0x3fb8aa3b, v144
	v_mul_f32_e32 v141, 0x3fb8aa3b, v141
	v_exp_f32_e32 v144, v144
	v_exp_f32_e32 v146, v141
	v_addc_co_u32_e32 v149, vcc, 0, v143, vcc
	v_pk_mul_f32 v[150:151], v[2:3], v[144:145] op_sel_hi:[1,0]
	v_pk_mul_f32 v[144:145], v[4:5], v[144:145] op_sel_hi:[1,0]
	v_pk_fma_f32 v[126:127], v[126:127], v[146:147], v[150:151] op_sel_hi:[1,0,1]
	v_pk_fma_f32 v[128:129], v[128:129], v[146:147], v[144:145] op_sel_hi:[1,0,1]
	global_store_dwordx4 v[148:149], v[126:129], off
	s_and_saveexec_b64 s[22:23], s[8:9]
	s_cbranch_execz .LBB0_1566
	s_ashr_i32 s19, s18, 31
	s_lshl_b64 s[24:25], s[18:19], 2
	s_add_u32 s24, s64, s24
	s_addc_u32 s25, s65, s25
	global_store_dword v133, v1, s[24:25] offset:32
; template <int GRP>
; __device__ __forceinline__ void y_phase(Frame& F, const MW& W) {
;     ...
; #pragma unroll
;             for (int c = 0; c < 32; ++c) {
;                 *(f32x4*)(W.NP + ((size_t)bh * 32 + c) * 128 + g * 4) = N; if (g == 0) W.MP[bh * 32 + c] = mm;
;                 const float bl = sc[2 * c], am = sc[2 * c + 1], mn = fmaxf(bl + mm, am), dec = __expf(bl + mm - mn), inj = __expf(am - mn);
;                 N = N * dec + nv[c] * inj; mm = mn; }
.LBB0_1566:
	s_or_b64 exec, exec, s[22:23]
	v_readlane_b32 s100, v252, 8
	s_nop 1
	v_mov_b32_e32 v144, s100
	v_readlane_b32 s100, v253, 8
	s_nop 1
	v_mov_b32_e32 v145, s100
	v_add_co_u32_e32 v142, vcc, 0x1000, v142
	v_add_f32_e32 v141, v1, v144
	v_max_f32_e32 v1, v145, v145
	v_max_f32_e32 v1, v141, v1
	v_sub_f32_e32 v144, v145, v1
	v_sub_f32_e32 v141, v141, v1
	v_mul_f32_e32 v144, 0x3fb8aa3b, v144
	v_mul_f32_e32 v141, 0x3fb8aa3b, v141
	v_exp_f32_e32 v144, v144
	v_exp_f32_e32 v146, v141
	v_addc_co_u32_e32 v143, vcc, 0, v143, vcc
	v_pk_mul_f32 v[148:149], v[62:63], v[144:145] op_sel_hi:[1,0]
	v_pk_mul_f32 v[144:145], v[64:65], v[144:145] op_sel_hi:[1,0]
	v_pk_fma_f32 v[126:127], v[126:127], v[146:147], v[148:149] op_sel_hi:[1,0,1]
	v_pk_fma_f32 v[128:129], v[128:129], v[146:147], v[144:145] op_sel_hi:[1,0,1]
	global_store_dwordx4 v[142:143], v[126:129], off offset:512
	s_and_saveexec_b64 s[22:23], s[8:9]
	s_cbranch_execz .LBB0_1568
	s_ashr_i32 s19, s18, 31
	s_lshl_b64 s[24:25], s[18:19], 2
	s_add_u32 s24, s64, s24
	s_addc_u32 s25, s65, s25
	global_store_dword v133, v1, s[24:25] offset:36
.LBB0_1568:
	s_or_b64 exec, exec, s[22:23]
	v_readlane_b32 s100, v252, 9
	s_nop 1
	v_mov_b32_e32 v144, s100
	v_readlane_b32 s100, v253, 9
	s_nop 1
	v_mov_b32_e32 v145, s100
	v_mov_b32_e32 v141, v133
	v_lshl_add_u64 v[142:143], s[20:21], 0, v[140:141]
	v_add_co_u32_e32 v148, vcc, 0x1000, v142
	v_add_f32_e32 v141, v1, v144
	v_max_f32_e32 v1, v145, v145
	v_max_f32_e32 v1, v141, v1
	v_sub_f32_e32 v144, v145, v1
	v_sub_f32_e32 v141, v141, v1
	v_mul_f32_e32 v144, 0x3fb8aa3b, v144
	v_mul_f32_e32 v141, 0x3fb8aa3b, v141
	v_exp_f32_e32 v144, v144
	v_exp_f32_e32 v146, v141
	v_addc_co_u32_e32 v149, vcc, 0, v143, vcc
	v_pk_mul_f32 v[150:151], v[58:59], v[144:145] op_sel_hi:[1,0]
	v_pk_mul_f32 v[144:145], v[60:61], v[144:145] op_sel_hi:[1,0]
	v_pk_fma_f32 v[126:127], v[126:127], v[146:147], v[150:151] op_sel_hi:[1,0,1]
	v_pk_fma_f32 v[128:129], v[128:129], v[146:147], v[144:145] op_sel_hi:[1,0,1]
	global_store_dwordx4 v[148:149], v[126:129], off offset:1024
	s_and_saveexec_b64 s[22:23], s[8:9]
	s_cbranch_execz .LBB0_1570
	s_ashr_i32 s19, s18, 31
	s_lshl_b64 s[24:25], s[18:19], 2
	s_add_u32 s24, s64, s24
	s_addc_u32 s25, s65, s25
	global_store_dword v133, v1, s[24:25] offset:40
.LBB0_1570:
	s_or_b64 exec, exec, s[22:23]
	v_readlane_b32 s100, v252, 10
	s_nop 1
	v_mov_b32_e32 v144, s100
	v_readlane_b32 s100, v253, 10
	s_nop 1
	v_mov_b32_e32 v145, s100
	v_add_co_u32_e32 v142, vcc, 0x1000, v142
	v_add_f32_e32 v141, v1, v144
	v_max_f32_e32 v1, v145, v145
	v_max_f32_e32 v1, v141, v1
	v_sub_f32_e32 v144, v145, v1
	v_sub_f32_e32 v141, v141, v1
	v_mul_f32_e32 v144, 0x3fb8aa3b, v144
	v_mul_f32_e32 v141, 0x3fb8aa3b, v141
	v_exp_f32_e32 v144, v144
	v_exp_f32_e32 v146, v141
	v_addc_co_u32_e32 v143, vcc, 0, v143, vcc
	v_pk_mul_f32 v[148:149], v[54:55], v[144:145] op_sel_hi:[1,0]
	v_pk_mul_f32 v[144:145], v[56:57], v[144:145] op_sel_hi:[1,0]
	v_pk_fma_f32 v[126:127], v[126:127], v[146:147], v[148:149] op_sel_hi:[1,0,1]
	v_pk_fma_f32 v[128:129], v[128:129], v[146:147], v[144:145] op_sel_hi:[1,0,1]
	global_store_dwordx4 v[142:143], v[126:129], off offset:1536
	s_and_saveexec_b64 s[22:23], s[8:9]
	s_cbranch_execz .LBB0_1572
	s_ashr_i32 s19, s18, 31
	s_lshl_b64 s[24:25], s[18:19], 2
	s_add_u32 s24, s64, s24
	s_addc_u32 s25, s65, s25
	global_store_dword v133, v1, s[24:25] offset:44
.LBB0_1572:
	s_or_b64 exec, exec, s[22:23]
	v_readlane_b32 s100, v252, 11
	s_nop 1
	v_mov_b32_e32 v144, s100
	v_readlane_b32 s100, v253, 11
	s_nop 1
	v_mov_b32_e32 v145, s100
	v_mov_b32_e32 v141, v133
	v_lshl_add_u64 v[142:143], s[20:21], 0, v[140:141]
	v_add_co_u32_e32 v148, vcc, 0x1000, v142
	v_add_f32_e32 v141, v1, v144
	v_max_f32_e32 v1, v145, v145
	v_max_f32_e32 v1, v141, v1
	v_sub_f32_e32 v144, v145, v1
	v_sub_f32_e32 v141, v141, v1
	v_mul_f32_e32 v144, 0x3fb8aa3b, v144
	v_mul_f32_e32 v141, 0x3fb8aa3b, v141
	v_exp_f32_e32 v144, v144
	v_exp_f32_e32 v146, v141
	v_addc_co_u32_e32 v149, vcc, 0, v143, vcc
	v_pk_mul_f32 v[150:151], v[50:51], v[144:145] op_sel_hi:[1,0]
	v_pk_mul_f32 v[144:145], v[52:53], v[144:145] op_sel_hi:[1,0]
	v_pk_fma_f32 v[126:127], v[126:127], v[146:147], v[150:151] op_sel_hi:[1,0,1]
	v_pk_fma_f32 v[128:129], v[128:129], v[146:147], v[144:145] op_sel_hi:[1,0,1]
	global_store_dwordx4 v[148:149], v[126:129], off offset:2048
	s_and_saveexec_b64 s[22:23], s[8:9]
	s_cbranch_execz .LBB0_1574
	s_ashr_i32 s19, s18, 31
	s_lshl_b64 s[24:25], s[18:19], 2
	s_add_u32 s24, s64, s24
	s_addc_u32 s25, s65, s25
	global_store_dword v133, v1, s[24:25] offset:48
.LBB0_1574:
	s_or_b64 exec, exec, s[22:23]
	v_readlane_b32 s100, v252, 12
	s_nop 1
	v_mov_b32_e32 v144, s100
	v_readlane_b32 s100, v253, 12
	s_nop 1
	v_mov_b32_e32 v145, s100
	v_add_co_u32_e32 v142, vcc, 0x1000, v142
	v_add_f32_e32 v141, v1, v144
	v_max_f32_e32 v1, v145, v145
	v_max_f32_e32 v1, v141, v1
	v_sub_f32_e32 v144, v145, v1
	v_sub_f32_e32 v141, v141, v1
	v_mul_f32_e32 v144, 0x3fb8aa3b, v144
	v_mul_f32_e32 v141, 0x3fb8aa3b, v141
	v_exp_f32_e32 v144, v144
	v_exp_f32_e32 v146, v141
	v_addc_co_u32_e32 v143, vcc, 0, v143, vcc
	v_pk_mul_f32 v[148:149], v[46:47], v[144:145] op_sel_hi:[1,0]
	v_pk_mul_f32 v[144:145], v[48:49], v[144:145] op_sel_hi:[1,0]
	v_pk_fma_f32 v[126:127], v[126:127], v[146:147], v[148:149] op_sel_hi:[1,0,1]
	v_pk_fma_f32 v[128:129], v[128:129], v[146:147], v[144:145] op_sel_hi:[1,0,1]
	global_store_dwordx4 v[142:143], v[126:129], off offset:2560
	s_and_saveexec_b64 s[22:23], s[8:9]
	s_cbranch_execz .LBB0_1576
	s_ashr_i32 s19, s18, 31
	s_lshl_b64 s[24:25], s[18:19], 2
	s_add_u32 s24, s64, s24
	s_addc_u32 s25, s65, s25
	global_store_dword v133, v1, s[24:25] offset:52
; template <int GRP>
; __device__ __forceinline__ void y_phase(Frame& F, const MW& W) {
;     ...
; #pragma unroll
;             for (int c = 0; c < 32; ++c) {
;                 *(f32x4*)(W.NP + ((size_t)bh * 32 + c) * 128 + g * 4) = N; if (g == 0) W.MP[bh * 32 + c] = mm;
;                 const float bl = sc[2 * c], am = sc[2 * c + 1], mn = fmaxf(bl + mm, am), dec = __expf(bl + mm - mn), inj = __expf(am - mn);
;                 N = N * dec + nv[c] * inj; mm = mn; }
.LBB0_1576:
	s_or_b64 exec, exec, s[22:23]
	v_readlane_b32 s100, v252, 13
	s_nop 1
	v_mov_b32_e32 v144, s100
	v_readlane_b32 s100, v253, 13
	s_nop 1
	v_mov_b32_e32 v145, s100
	v_mov_b32_e32 v141, v133
	v_lshl_add_u64 v[142:143], s[20:21], 0, v[140:141]
	v_add_co_u32_e32 v148, vcc, 0x1000, v142
	v_add_f32_e32 v141, v1, v144
	v_max_f32_e32 v1, v145, v145
	v_max_f32_e32 v1, v141, v1
	v_sub_f32_e32 v144, v145, v1
	v_sub_f32_e32 v141, v141, v1
	v_mul_f32_e32 v144, 0x3fb8aa3b, v144
	v_mul_f32_e32 v141, 0x3fb8aa3b, v141
	v_exp_f32_e32 v144, v144
	v_exp_f32_e32 v146, v141
	v_addc_co_u32_e32 v149, vcc, 0, v143, vcc
	v_pk_mul_f32 v[150:151], v[42:43], v[144:145] op_sel_hi:[1,0]
	v_pk_mul_f32 v[144:145], v[44:45], v[144:145] op_sel_hi:[1,0]
	v_pk_fma_f32 v[126:127], v[126:127], v[146:147], v[150:151] op_sel_hi:[1,0,1]
	v_pk_fma_f32 v[128:129], v[128:129], v[146:147], v[144:145] op_sel_hi:[1,0,1]
	global_store_dwordx4 v[148:149], v[126:129], off offset:3072
	s_and_saveexec_b64 s[22:23], s[8:9]
	s_cbranch_execz .LBB0_1578
	s_ashr_i32 s19, s18, 31
	s_lshl_b64 s[24:25], s[18:19], 2
	s_add_u32 s24, s64, s24
	s_addc_u32 s25, s65, s25
	global_store_dword v133, v1, s[24:25] offset:56
.LBB0_1578:
	s_or_b64 exec, exec, s[22:23]
	v_readlane_b32 s100, v252, 14
	s_nop 1
	v_mov_b32_e32 v144, s100
	v_readlane_b32 s100, v253, 14
	s_nop 1
	v_mov_b32_e32 v145, s100
	v_add_co_u32_e32 v142, vcc, 0x1000, v142
	v_add_f32_e32 v141, v1, v144
	v_max_f32_e32 v1, v145, v145
	v_max_f32_e32 v1, v141, v1
	v_sub_f32_e32 v144, v145, v1
	v_sub_f32_e32 v141, v141, v1
	v_mul_f32_e32 v144, 0x3fb8aa3b, v144
	v_mul_f32_e32 v141, 0x3fb8aa3b, v141
	v_exp_f32_e32 v144, v144
	v_exp_f32_e32 v146, v141
	v_addc_co_u32_e32 v143, vcc, 0, v143, vcc
	v_pk_mul_f32 v[148:149], v[38:39], v[144:145] op_sel_hi:[1,0]
	v_pk_mul_f32 v[144:145], v[40:41], v[144:145] op_sel_hi:[1,0]
	v_pk_fma_f32 v[126:127], v[126:127], v[146:147], v[148:149] op_sel_hi:[1,0,1]
	v_pk_fma_f32 v[128:129], v[128:129], v[146:147], v[144:145] op_sel_hi:[1,0,1]
	global_store_dwordx4 v[142:143], v[126:129], off offset:3584
	s_and_saveexec_b64 s[22:23], s[8:9]
	s_cbranch_execz .LBB0_1580
	s_ashr_i32 s19, s18, 31
	s_lshl_b64 s[24:25], s[18:19], 2
	s_add_u32 s24, s64, s24
	s_addc_u32 s25, s65, s25
	global_store_dword v133, v1, s[24:25] offset:60
.LBB0_1580:
	s_or_b64 exec, exec, s[22:23]
	v_readlane_b32 s100, v252, 15
	s_nop 1
	v_mov_b32_e32 v144, s100
	v_readlane_b32 s100, v253, 15
	s_nop 1
	v_mov_b32_e32 v145, s100
	v_mov_b32_e32 v141, v133
	v_lshl_add_u64 v[142:143], s[20:21], 0, v[140:141]
	v_add_co_u32_e32 v148, vcc, 0x2000, v142
	v_add_f32_e32 v141, v1, v144
	v_max_f32_e32 v1, v145, v145
	v_max_f32_e32 v1, v141, v1
	v_sub_f32_e32 v144, v145, v1
	v_sub_f32_e32 v141, v141, v1
	v_mul_f32_e32 v144, 0x3fb8aa3b, v144
	v_mul_f32_e32 v141, 0x3fb8aa3b, v141
	v_exp_f32_e32 v144, v144
	v_exp_f32_e32 v146, v141
	v_addc_co_u32_e32 v149, vcc, 0, v143, vcc
	v_pk_mul_f32 v[150:151], v[34:35], v[144:145] op_sel_hi:[1,0]
	v_pk_mul_f32 v[144:145], v[36:37], v[144:145] op_sel_hi:[1,0]
	v_pk_fma_f32 v[126:127], v[126:127], v[146:147], v[150:151] op_sel_hi:[1,0,1]
	v_pk_fma_f32 v[128:129], v[128:129], v[146:147], v[144:145] op_sel_hi:[1,0,1]
	global_store_dwordx4 v[148:149], v[126:129], off
	s_and_saveexec_b64 s[22:23], s[8:9]
	s_cbranch_execz .LBB0_1582
	s_ashr_i32 s19, s18, 31
	s_lshl_b64 s[24:25], s[18:19], 2
	s_add_u32 s24, s64, s24
	s_addc_u32 s25, s65, s25
	global_store_dword v133, v1, s[24:25] offset:64
.LBB0_1582:
	s_or_b64 exec, exec, s[22:23]
	v_readlane_b32 s100, v252, 16
	s_nop 1
	v_mov_b32_e32 v144, s100
	v_readlane_b32 s100, v253, 16
	s_nop 1
	v_mov_b32_e32 v145, s100
	v_add_co_u32_e32 v142, vcc, 0x2000, v142
	v_add_f32_e32 v141, v1, v144
	v_max_f32_e32 v1, v145, v145
	v_max_f32_e32 v1, v141, v1
	v_sub_f32_e32 v144, v145, v1
	v_sub_f32_e32 v141, v141, v1
	v_mul_f32_e32 v144, 0x3fb8aa3b, v144
	v_mul_f32_e32 v141, 0x3fb8aa3b, v141
	v_exp_f32_e32 v144, v144
	v_exp_f32_e32 v146, v141
	v_addc_co_u32_e32 v143, vcc, 0, v143, vcc
	v_pk_mul_f32 v[148:149], v[94:95], v[144:145] op_sel_hi:[1,0]
	v_pk_mul_f32 v[144:145], v[96:97], v[144:145] op_sel_hi:[1,0]
	v_pk_fma_f32 v[126:127], v[126:127], v[146:147], v[148:149] op_sel_hi:[1,0,1]
	v_pk_fma_f32 v[128:129], v[128:129], v[146:147], v[144:145] op_sel_hi:[1,0,1]
	global_store_dwordx4 v[142:143], v[126:129], off offset:512
	s_and_saveexec_b64 s[22:23], s[8:9]
	s_cbranch_execz .LBB0_1584
	s_ashr_i32 s19, s18, 31
	s_lshl_b64 s[24:25], s[18:19], 2
	s_add_u32 s24, s64, s24
	s_addc_u32 s25, s65, s25
	global_store_dword v133, v1, s[24:25] offset:68
.LBB0_1584:
	s_or_b64 exec, exec, s[22:23]
	v_readlane_b32 s100, v252, 17
	s_nop 1
	v_mov_b32_e32 v144, s100
	v_readlane_b32 s100, v253, 17
	s_nop 1
	v_mov_b32_e32 v145, s100
	v_mov_b32_e32 v141, v133
	v_lshl_add_u64 v[142:143], s[20:21], 0, v[140:141]
	v_add_co_u32_e32 v148, vcc, 0x2000, v142
	v_add_f32_e32 v141, v1, v144
	v_max_f32_e32 v1, v145, v145
	v_max_f32_e32 v1, v141, v1
	v_sub_f32_e32 v144, v145, v1
	v_sub_f32_e32 v141, v141, v1
	v_mul_f32_e32 v144, 0x3fb8aa3b, v144
	v_mul_f32_e32 v141, 0x3fb8aa3b, v141
	v_exp_f32_e32 v144, v144
	v_exp_f32_e32 v146, v141
	v_addc_co_u32_e32 v149, vcc, 0, v143, vcc
	v_pk_mul_f32 v[150:151], v[90:91], v[144:145] op_sel_hi:[1,0]
	v_pk_mul_f32 v[144:145], v[92:93], v[144:145] op_sel_hi:[1,0]
	v_pk_fma_f32 v[126:127], v[126:127], v[146:147], v[150:151] op_sel_hi:[1,0,1]
	v_pk_fma_f32 v[128:129], v[128:129], v[146:147], v[144:145] op_sel_hi:[1,0,1]
	global_store_dwordx4 v[148:149], v[126:129], off offset:1024
	s_and_saveexec_b64 s[22:23], s[8:9]
	s_cbranch_execz .LBB0_1586
	s_ashr_i32 s19, s18, 31
	s_lshl_b64 s[24:25], s[18:19], 2
	s_add_u32 s24, s64, s24
	s_addc_u32 s25, s65, s25
	global_store_dword v133, v1, s[24:25] offset:72
; template <int GRP>
; __device__ __forceinline__ void y_phase(Frame& F, const MW& W) {
;     ...
; #pragma unroll
;             for (int c = 0; c < 32; ++c) {
;                 *(f32x4*)(W.NP + ((size_t)bh * 32 + c) * 128 + g * 4) = N; if (g == 0) W.MP[bh * 32 + c] = mm;
;                 const float bl = sc[2 * c], am = sc[2 * c + 1], mn = fmaxf(bl + mm, am), dec = __expf(bl + mm - mn), inj = __expf(am - mn);
;                 N = N * dec + nv[c] * inj; mm = mn; }
.LBB0_1586:
	s_or_b64 exec, exec, s[22:23]
	v_readlane_b32 s100, v252, 18
	s_nop 1
	v_mov_b32_e32 v144, s100
	v_readlane_b32 s100, v253, 18
	s_nop 1
	v_mov_b32_e32 v145, s100
	v_add_co_u32_e32 v142, vcc, 0x2000, v142
	v_add_f32_e32 v141, v1, v144
	v_max_f32_e32 v1, v145, v145
	v_max_f32_e32 v1, v141, v1
	v_sub_f32_e32 v144, v145, v1
	v_sub_f32_e32 v141, v141, v1
	v_mul_f32_e32 v144, 0x3fb8aa3b, v144
	v_mul_f32_e32 v141, 0x3fb8aa3b, v141
	v_exp_f32_e32 v144, v144
	v_exp_f32_e32 v146, v141
	v_addc_co_u32_e32 v143, vcc, 0, v143, vcc
	v_pk_mul_f32 v[148:149], v[86:87], v[144:145] op_sel_hi:[1,0]
	v_pk_mul_f32 v[144:145], v[88:89], v[144:145] op_sel_hi:[1,0]
	v_pk_fma_f32 v[126:127], v[126:127], v[146:147], v[148:149] op_sel_hi:[1,0,1]
	v_pk_fma_f32 v[128:129], v[128:129], v[146:147], v[144:145] op_sel_hi:[1,0,1]
	global_store_dwordx4 v[142:143], v[126:129], off offset:1536
	s_and_saveexec_b64 s[22:23], s[8:9]
	s_cbranch_execz .LBB0_1588
	s_ashr_i32 s19, s18, 31
	s_lshl_b64 s[24:25], s[18:19], 2
	s_add_u32 s24, s64, s24
	s_addc_u32 s25, s65, s25
	global_store_dword v133, v1, s[24:25] offset:76
.LBB0_1588:
	s_or_b64 exec, exec, s[22:23]
	v_readlane_b32 s100, v252, 19
	s_nop 1
	v_mov_b32_e32 v144, s100
	v_readlane_b32 s100, v253, 19
	s_nop 1
	v_mov_b32_e32 v145, s100
	v_mov_b32_e32 v141, v133
	v_lshl_add_u64 v[142:143], s[20:21], 0, v[140:141]
	v_add_co_u32_e32 v148, vcc, 0x2000, v142
	v_add_f32_e32 v141, v1, v144
	v_max_f32_e32 v1, v145, v145
	v_max_f32_e32 v1, v141, v1
	v_sub_f32_e32 v144, v145, v1
	v_sub_f32_e32 v141, v141, v1
	v_mul_f32_e32 v144, 0x3fb8aa3b, v144
	v_mul_f32_e32 v141, 0x3fb8aa3b, v141
	v_exp_f32_e32 v144, v144
	v_exp_f32_e32 v146, v141
	v_addc_co_u32_e32 v149, vcc, 0, v143, vcc
	v_pk_mul_f32 v[150:151], v[82:83], v[144:145] op_sel_hi:[1,0]
	v_pk_mul_f32 v[144:145], v[84:85], v[144:145] op_sel_hi:[1,0]
	v_pk_fma_f32 v[126:127], v[126:127], v[146:147], v[150:151] op_sel_hi:[1,0,1]
	v_pk_fma_f32 v[128:129], v[128:129], v[146:147], v[144:145] op_sel_hi:[1,0,1]
	global_store_dwordx4 v[148:149], v[126:129], off offset:2048
	s_and_saveexec_b64 s[22:23], s[8:9]
	s_cbranch_execz .LBB0_1590
	s_ashr_i32 s19, s18, 31
	s_lshl_b64 s[24:25], s[18:19], 2
	s_add_u32 s24, s64, s24
	s_addc_u32 s25, s65, s25
	global_store_dword v133, v1, s[24:25] offset:80
.LBB0_1590:
	s_or_b64 exec, exec, s[22:23]
	v_readlane_b32 s100, v252, 20
	s_nop 1
	v_mov_b32_e32 v144, s100
	v_readlane_b32 s100, v253, 20
	s_nop 1
	v_mov_b32_e32 v145, s100
	v_add_co_u32_e32 v142, vcc, 0x2000, v142
	v_add_f32_e32 v141, v1, v144
	v_max_f32_e32 v1, v145, v145
	v_max_f32_e32 v1, v141, v1
	v_sub_f32_e32 v144, v145, v1
	v_sub_f32_e32 v141, v141, v1
	v_mul_f32_e32 v144, 0x3fb8aa3b, v144
	v_mul_f32_e32 v141, 0x3fb8aa3b, v141
	v_exp_f32_e32 v144, v144
	v_exp_f32_e32 v146, v141
	v_addc_co_u32_e32 v143, vcc, 0, v143, vcc
	v_pk_mul_f32 v[148:149], v[78:79], v[144:145] op_sel_hi:[1,0]
	v_pk_mul_f32 v[144:145], v[80:81], v[144:145] op_sel_hi:[1,0]
	v_pk_fma_f32 v[126:127], v[126:127], v[146:147], v[148:149] op_sel_hi:[1,0,1]
	v_pk_fma_f32 v[128:129], v[128:129], v[146:147], v[144:145] op_sel_hi:[1,0,1]
	global_store_dwordx4 v[142:143], v[126:129], off offset:2560
	s_and_saveexec_b64 s[22:23], s[8:9]
	s_cbranch_execz .LBB0_1592
	s_ashr_i32 s19, s18, 31
	s_lshl_b64 s[24:25], s[18:19], 2
	s_add_u32 s24, s64, s24
	s_addc_u32 s25, s65, s25
	global_store_dword v133, v1, s[24:25] offset:84
.LBB0_1592:
	s_or_b64 exec, exec, s[22:23]
	v_readlane_b32 s100, v252, 21
	s_nop 1
	v_mov_b32_e32 v144, s100
	v_readlane_b32 s100, v253, 21
	s_nop 1
	v_mov_b32_e32 v145, s100
	v_mov_b32_e32 v141, v133
	v_lshl_add_u64 v[142:143], s[20:21], 0, v[140:141]
	v_add_co_u32_e32 v148, vcc, 0x2000, v142
	v_add_f32_e32 v141, v1, v144
	v_max_f32_e32 v1, v145, v145
	v_max_f32_e32 v1, v141, v1
	v_sub_f32_e32 v144, v145, v1
	v_sub_f32_e32 v141, v141, v1
	v_mul_f32_e32 v144, 0x3fb8aa3b, v144
	v_mul_f32_e32 v141, 0x3fb8aa3b, v141
	v_exp_f32_e32 v144, v144
	v_exp_f32_e32 v146, v141
	v_addc_co_u32_e32 v149, vcc, 0, v143, vcc
	v_pk_mul_f32 v[150:151], v[74:75], v[144:145] op_sel_hi:[1,0]
	v_pk_mul_f32 v[144:145], v[76:77], v[144:145] op_sel_hi:[1,0]
	v_pk_fma_f32 v[126:127], v[126:127], v[146:147], v[150:151] op_sel_hi:[1,0,1]
	v_pk_fma_f32 v[128:129], v[128:129], v[146:147], v[144:145] op_sel_hi:[1,0,1]
	global_store_dwordx4 v[148:149], v[126:129], off offset:3072
	s_and_saveexec_b64 s[22:23], s[8:9]
	s_cbranch_execz .LBB0_1594
	s_ashr_i32 s19, s18, 31
	s_lshl_b64 s[24:25], s[18:19], 2
	s_add_u32 s24, s64, s24
	s_addc_u32 s25, s65, s25
	global_store_dword v133, v1, s[24:25] offset:88
.LBB0_1594:
	s_or_b64 exec, exec, s[22:23]
	v_readlane_b32 s100, v252, 22
	s_nop 1
	v_mov_b32_e32 v144, s100
	v_readlane_b32 s100, v253, 22
	s_nop 1
	v_mov_b32_e32 v145, s100
	v_add_co_u32_e32 v142, vcc, 0x2000, v142
	v_add_f32_e32 v141, v1, v144
	v_max_f32_e32 v1, v145, v145
	v_max_f32_e32 v1, v141, v1
	v_sub_f32_e32 v144, v145, v1
	v_sub_f32_e32 v141, v141, v1
	v_mul_f32_e32 v144, 0x3fb8aa3b, v144
	v_mul_f32_e32 v141, 0x3fb8aa3b, v141
	v_exp_f32_e32 v144, v144
	v_exp_f32_e32 v146, v141
	v_addc_co_u32_e32 v143, vcc, 0, v143, vcc
	v_pk_mul_f32 v[148:149], v[70:71], v[144:145] op_sel_hi:[1,0]
	v_pk_mul_f32 v[144:145], v[72:73], v[144:145] op_sel_hi:[1,0]
	v_pk_fma_f32 v[126:127], v[126:127], v[146:147], v[148:149] op_sel_hi:[1,0,1]
	v_pk_fma_f32 v[128:129], v[128:129], v[146:147], v[144:145] op_sel_hi:[1,0,1]
	global_store_dwordx4 v[142:143], v[126:129], off offset:3584
	s_and_saveexec_b64 s[22:23], s[8:9]
	s_cbranch_execz .LBB0_1596
	s_ashr_i32 s19, s18, 31
	s_lshl_b64 s[24:25], s[18:19], 2
	s_add_u32 s24, s64, s24
	s_addc_u32 s25, s65, s25
	global_store_dword v133, v1, s[24:25] offset:92
; template <int GRP>
; __device__ __forceinline__ void y_phase(Frame& F, const MW& W) {
;     ...
; #pragma unroll
;             for (int c = 0; c < 32; ++c) {
;                 *(f32x4*)(W.NP + ((size_t)bh * 32 + c) * 128 + g * 4) = N; if (g == 0) W.MP[bh * 32 + c] = mm;
;                 const float bl = sc[2 * c], am = sc[2 * c + 1], mn = fmaxf(bl + mm, am), dec = __expf(bl + mm - mn), inj = __expf(am - mn);
;                 N = N * dec + nv[c] * inj; mm = mn; }
.LBB0_1596:
	s_or_b64 exec, exec, s[22:23]
	v_readlane_b32 s100, v252, 23
	s_nop 1
	v_mov_b32_e32 v144, s100
	v_readlane_b32 s100, v253, 23
	s_nop 1
	v_mov_b32_e32 v145, s100
	v_mov_b32_e32 v141, v133
	v_lshl_add_u64 v[142:143], s[20:21], 0, v[140:141]
	v_add_co_u32_e32 v148, vcc, 0x3000, v142
	v_add_f32_e32 v141, v1, v144
	v_max_f32_e32 v1, v145, v145
	v_max_f32_e32 v1, v141, v1
	v_sub_f32_e32 v144, v145, v1
	v_sub_f32_e32 v141, v141, v1
	v_mul_f32_e32 v144, 0x3fb8aa3b, v144
	v_mul_f32_e32 v141, 0x3fb8aa3b, v141
	v_exp_f32_e32 v144, v144
	v_exp_f32_e32 v146, v141
	v_addc_co_u32_e32 v149, vcc, 0, v143, vcc
	v_pk_mul_f32 v[150:151], v[66:67], v[144:145] op_sel_hi:[1,0]
	v_pk_mul_f32 v[144:145], v[68:69], v[144:145] op_sel_hi:[1,0]
	v_pk_fma_f32 v[126:127], v[126:127], v[146:147], v[150:151] op_sel_hi:[1,0,1]
	v_pk_fma_f32 v[128:129], v[128:129], v[146:147], v[144:145] op_sel_hi:[1,0,1]
	global_store_dwordx4 v[148:149], v[126:129], off
	s_and_saveexec_b64 s[22:23], s[8:9]
	s_cbranch_execz .LBB0_1598
	s_ashr_i32 s19, s18, 31
	s_lshl_b64 s[24:25], s[18:19], 2
	s_add_u32 s24, s64, s24
	s_addc_u32 s25, s65, s25
	global_store_dword v133, v1, s[24:25] offset:96
.LBB0_1598:
	s_or_b64 exec, exec, s[22:23]
	v_readlane_b32 s100, v252, 24
	s_nop 1
	v_mov_b32_e32 v144, s100
	v_readlane_b32 s100, v253, 24
	s_nop 1
	v_mov_b32_e32 v145, s100
	v_add_co_u32_e32 v142, vcc, 0x3000, v142
	v_add_f32_e32 v141, v1, v144
	v_max_f32_e32 v1, v145, v145
	v_max_f32_e32 v1, v141, v1
	v_sub_f32_e32 v144, v145, v1
	v_sub_f32_e32 v141, v141, v1
	v_mul_f32_e32 v144, 0x3fb8aa3b, v144
	v_mul_f32_e32 v141, 0x3fb8aa3b, v141
	v_exp_f32_e32 v144, v144
	v_exp_f32_e32 v146, v141
	v_addc_co_u32_e32 v143, vcc, 0, v143, vcc
	v_pk_mul_f32 v[148:149], v[122:123], v[144:145] op_sel_hi:[1,0]
	v_pk_mul_f32 v[144:145], v[124:125], v[144:145] op_sel_hi:[1,0]
	v_pk_fma_f32 v[126:127], v[126:127], v[146:147], v[148:149] op_sel_hi:[1,0,1]
	v_pk_fma_f32 v[128:129], v[128:129], v[146:147], v[144:145] op_sel_hi:[1,0,1]
	global_store_dwordx4 v[142:143], v[126:129], off offset:512
	s_and_saveexec_b64 s[22:23], s[8:9]
	s_cbranch_execz .LBB0_1600
	s_ashr_i32 s19, s18, 31
	s_lshl_b64 s[24:25], s[18:19], 2
	s_add_u32 s24, s64, s24
	s_addc_u32 s25, s65, s25
	global_store_dword v133, v1, s[24:25] offset:100
.LBB0_1600:
	s_or_b64 exec, exec, s[22:23]
	v_readlane_b32 s100, v252, 25
	s_nop 1
	v_mov_b32_e32 v144, s100
	v_readlane_b32 s100, v253, 25
	s_nop 1
	v_mov_b32_e32 v145, s100
	v_mov_b32_e32 v141, v133
	v_lshl_add_u64 v[142:143], s[20:21], 0, v[140:141]
	v_add_co_u32_e32 v148, vcc, 0x3000, v142
	v_add_f32_e32 v141, v1, v144
	v_max_f32_e32 v1, v145, v145
	v_max_f32_e32 v1, v141, v1
	v_sub_f32_e32 v144, v145, v1
	v_sub_f32_e32 v141, v141, v1
	v_mul_f32_e32 v144, 0x3fb8aa3b, v144
	v_mul_f32_e32 v141, 0x3fb8aa3b, v141
	v_exp_f32_e32 v144, v144
	v_exp_f32_e32 v146, v141
	v_addc_co_u32_e32 v149, vcc, 0, v143, vcc
	v_pk_mul_f32 v[150:151], v[118:119], v[144:145] op_sel_hi:[1,0]
	v_pk_mul_f32 v[144:145], v[120:121], v[144:145] op_sel_hi:[1,0]
	v_pk_fma_f32 v[126:127], v[126:127], v[146:147], v[150:151] op_sel_hi:[1,0,1]
	v_pk_fma_f32 v[128:129], v[128:129], v[146:147], v[144:145] op_sel_hi:[1,0,1]
	global_store_dwordx4 v[148:149], v[126:129], off offset:1024
	s_and_saveexec_b64 s[22:23], s[8:9]
	s_cbranch_execz .LBB0_1602
	s_ashr_i32 s19, s18, 31
	s_lshl_b64 s[24:25], s[18:19], 2
	s_add_u32 s24, s64, s24
	s_addc_u32 s25, s65, s25
	global_store_dword v133, v1, s[24:25] offset:104
.LBB0_1602:
	s_or_b64 exec, exec, s[22:23]
	v_readlane_b32 s100, v252, 26
	s_nop 1
	v_mov_b32_e32 v144, s100
	v_readlane_b32 s100, v253, 26
	s_nop 1
	v_mov_b32_e32 v145, s100
	v_add_co_u32_e32 v142, vcc, 0x3000, v142
	v_add_f32_e32 v141, v1, v144
	v_max_f32_e32 v1, v145, v145
	v_max_f32_e32 v1, v141, v1
	v_sub_f32_e32 v144, v145, v1
	v_sub_f32_e32 v141, v141, v1
	v_mul_f32_e32 v144, 0x3fb8aa3b, v144
	v_mul_f32_e32 v141, 0x3fb8aa3b, v141
	v_exp_f32_e32 v144, v144
	v_exp_f32_e32 v146, v141
	v_addc_co_u32_e32 v143, vcc, 0, v143, vcc
	v_pk_mul_f32 v[148:149], v[114:115], v[144:145] op_sel_hi:[1,0]
	v_pk_mul_f32 v[144:145], v[116:117], v[144:145] op_sel_hi:[1,0]
	v_pk_fma_f32 v[126:127], v[126:127], v[146:147], v[148:149] op_sel_hi:[1,0,1]
	v_pk_fma_f32 v[128:129], v[128:129], v[146:147], v[144:145] op_sel_hi:[1,0,1]
	global_store_dwordx4 v[142:143], v[126:129], off offset:1536
	s_and_saveexec_b64 s[22:23], s[8:9]
	s_cbranch_execz .LBB0_1604
	s_ashr_i32 s19, s18, 31
	s_lshl_b64 s[24:25], s[18:19], 2
	s_add_u32 s24, s64, s24
	s_addc_u32 s25, s65, s25
	global_store_dword v133, v1, s[24:25] offset:108
; template <int GRP>
; __device__ __forceinline__ void y_phase(Frame& F, const MW& W) {
;     ...
; #pragma unroll
;             for (int c = 0; c < 32; ++c) {
;                 *(f32x4*)(W.NP + ((size_t)bh * 32 + c) * 128 + g * 4) = N; if (g == 0) W.MP[bh * 32 + c] = mm;
;                 const float bl = sc[2 * c], am = sc[2 * c + 1], mn = fmaxf(bl + mm, am), dec = __expf(bl + mm - mn), inj = __expf(am - mn);
;                 N = N * dec + nv[c] * inj; mm = mn; }
.LBB0_1604:
	s_or_b64 exec, exec, s[22:23]
	v_readlane_b32 s100, v252, 27
	s_nop 1
	v_mov_b32_e32 v144, s100
	v_readlane_b32 s100, v253, 27
	s_nop 1
	v_mov_b32_e32 v145, s100
	v_mov_b32_e32 v141, v133
	v_lshl_add_u64 v[142:143], s[20:21], 0, v[140:141]
	v_add_co_u32_e32 v148, vcc, 0x3000, v142
	v_add_f32_e32 v141, v1, v144
	v_max_f32_e32 v1, v145, v145
	v_max_f32_e32 v1, v141, v1
	v_sub_f32_e32 v144, v145, v1
	v_sub_f32_e32 v141, v141, v1
	v_mul_f32_e32 v144, 0x3fb8aa3b, v144
	v_mul_f32_e32 v141, 0x3fb8aa3b, v141
	v_exp_f32_e32 v144, v144
	v_exp_f32_e32 v146, v141
	v_addc_co_u32_e32 v149, vcc, 0, v143, vcc
	v_pk_mul_f32 v[150:151], v[110:111], v[144:145] op_sel_hi:[1,0]
	v_pk_mul_f32 v[144:145], v[112:113], v[144:145] op_sel_hi:[1,0]
	v_pk_fma_f32 v[126:127], v[126:127], v[146:147], v[150:151] op_sel_hi:[1,0,1]
	v_pk_fma_f32 v[128:129], v[128:129], v[146:147], v[144:145] op_sel_hi:[1,0,1]
	global_store_dwordx4 v[148:149], v[126:129], off offset:2048
	s_and_saveexec_b64 s[22:23], s[8:9]
	s_cbranch_execz .LBB0_1606
	s_ashr_i32 s19, s18, 31
	s_lshl_b64 s[24:25], s[18:19], 2
	s_add_u32 s24, s64, s24
	s_addc_u32 s25, s65, s25
	global_store_dword v133, v1, s[24:25] offset:112
.LBB0_1606:
	s_or_b64 exec, exec, s[22:23]
	v_readlane_b32 s100, v252, 28
	s_nop 1
	v_mov_b32_e32 v144, s100
	v_readlane_b32 s100, v253, 28
	s_nop 1
	v_mov_b32_e32 v145, s100
	v_add_co_u32_e32 v142, vcc, 0x3000, v142
	v_add_f32_e32 v141, v1, v144
	v_max_f32_e32 v1, v145, v145
	v_max_f32_e32 v1, v141, v1
	v_sub_f32_e32 v144, v145, v1
	v_sub_f32_e32 v141, v141, v1
	v_mul_f32_e32 v144, 0x3fb8aa3b, v144
	v_mul_f32_e32 v141, 0x3fb8aa3b, v141
	v_exp_f32_e32 v144, v144
	v_exp_f32_e32 v146, v141
	v_addc_co_u32_e32 v143, vcc, 0, v143, vcc
	v_pk_mul_f32 v[148:149], v[106:107], v[144:145] op_sel_hi:[1,0]
	v_pk_mul_f32 v[144:145], v[108:109], v[144:145] op_sel_hi:[1,0]
	v_pk_fma_f32 v[126:127], v[126:127], v[146:147], v[148:149] op_sel_hi:[1,0,1]
	v_pk_fma_f32 v[128:129], v[128:129], v[146:147], v[144:145] op_sel_hi:[1,0,1]
	global_store_dwordx4 v[142:143], v[126:129], off offset:2560
	s_and_saveexec_b64 s[22:23], s[8:9]
	s_cbranch_execz .LBB0_1608
	s_ashr_i32 s19, s18, 31
	s_lshl_b64 s[24:25], s[18:19], 2
	s_add_u32 s24, s64, s24
	s_addc_u32 s25, s65, s25
	global_store_dword v133, v1, s[24:25] offset:116
.LBB0_1608:
	s_or_b64 exec, exec, s[22:23]
	v_readlane_b32 s100, v252, 29
	s_nop 1
	v_mov_b32_e32 v142, s100
	v_readlane_b32 s100, v253, 29
	s_nop 1
	v_mov_b32_e32 v143, s100
	v_mov_b32_e32 v141, v133
	v_lshl_add_u64 v[140:141], s[20:21], 0, v[140:141]
	v_add_co_u32_e32 v146, vcc, 0x3000, v140
	v_add_f32_e32 v142, v1, v142
	v_max_f32_e32 v1, v143, v143
	v_max_f32_e32 v1, v142, v1
	v_sub_f32_e32 v142, v142, v1
	v_sub_f32_e32 v143, v143, v1
	v_mul_f32_e32 v144, 0x3fb8aa3b, v142
	v_mul_f32_e32 v142, 0x3fb8aa3b, v143
	v_exp_f32_e32 v142, v142
	v_exp_f32_e32 v144, v144
	v_addc_co_u32_e32 v147, vcc, 0, v141, vcc
	v_pk_mul_f32 v[148:149], v[102:103], v[142:143] op_sel_hi:[1,0]
	v_pk_mul_f32 v[142:143], v[104:105], v[142:143] op_sel_hi:[1,0]
	v_pk_fma_f32 v[126:127], v[126:127], v[144:145], v[148:149] op_sel_hi:[1,0,1]
	v_pk_fma_f32 v[128:129], v[128:129], v[144:145], v[142:143] op_sel_hi:[1,0,1]
	global_store_dwordx4 v[146:147], v[126:129], off offset:3072
	s_and_saveexec_b64 s[20:21], s[8:9]
	s_cbranch_execz .LBB0_1610
	s_ashr_i32 s19, s18, 31
	s_lshl_b64 s[22:23], s[18:19], 2
	s_add_u32 s22, s64, s22
	s_addc_u32 s23, s65, s23
	global_store_dword v133, v1, s[22:23] offset:120
.LBB0_1610:
	s_or_b64 exec, exec, s[20:21]
	v_readlane_b32 s100, v252, 30
	s_nop 1
	v_mov_b32_e32 v142, s100
	v_readlane_b32 s100, v253, 30
	s_nop 1
	v_mov_b32_e32 v143, s100
	v_add_co_u32_e32 v140, vcc, 0x3000, v140
	v_add_f32_e32 v142, v1, v142
	v_max_f32_e32 v1, v143, v143
	v_max_f32_e32 v1, v142, v1
	v_sub_f32_e32 v142, v142, v1
	v_sub_f32_e32 v143, v143, v1
	v_mul_f32_e32 v144, 0x3fb8aa3b, v142
	v_mul_f32_e32 v142, 0x3fb8aa3b, v143
	v_exp_f32_e32 v142, v142
	v_exp_f32_e32 v144, v144
	v_addc_co_u32_e32 v141, vcc, 0, v141, vcc
	v_pk_mul_f32 v[146:147], v[98:99], v[142:143] op_sel_hi:[1,0]
	v_pk_mul_f32 v[142:143], v[100:101], v[142:143] op_sel_hi:[1,0]
	v_pk_fma_f32 v[126:127], v[126:127], v[144:145], v[146:147] op_sel_hi:[1,0,1]
	v_pk_fma_f32 v[128:129], v[128:129], v[144:145], v[142:143] op_sel_hi:[1,0,1]
	global_store_dwordx4 v[140:141], v[126:129], off offset:3584
	s_and_b64 exec, exec, s[8:9]
	s_cbranch_execz .LBB0_1612
	s_ashr_i32 s19, s18, 31
	s_lshl_b64 s[8:9], s[18:19], 2
	s_add_u32 s8, s64, s8
	s_addc_u32 s9, s65, s9
	global_store_dword v133, v1, s[8:9] offset:124
